# opt26: opt24 + all 471 16-byte global stores marked sc1 (write-through) so less dirty L2 data remains for the barrier release flush; correctness does not depend on it
# speedup vs baseline: 1.0048x; 1.0048x over previous
.LBB0_34:
	s_mul_hi_i32 s10, s6, 0x15390949
	s_lshr_b32 s11, s10, 31
	s_ashr_i32 s10, s10, 9
	s_add_i32 s10, s10, s11
	s_mul_i32 s11, s10, 0xffffe7e0
	s_mul_hi_i32 s13, s10, 0x6080000
	s_mul_i32 s14, s10, 0x6080000
	s_add_i32 s10, s6, s11
	s_mul_i32 s11, s10, 0xffffa9c9
	s_lshr_b32 s11, s11, 16
	s_add_i32 s11, s11, s10
	s_sext_i32_i16 s12, s11
	s_bfe_u32 s11, s11, 0x1000f
	s_ashr_i32 s12, s12, 7
	s_add_i32 s11, s12, s11
	s_sext_i32_i16 s12, s11
	s_mulk_i32 s11, 0xc1
	s_sub_i32 s11, s10, s11
	s_sext_i32_i16 s16, s11
	s_lshl_b32 s10, s12, 6
	s_mul_i32 s15, s12, 0x304000
	s_lshl_b32 s12, s16, 6
	s_waitcnt lgkmcnt(0)
	s_add_u32 s14, s2, s14
	s_addc_u32 s13, s3, s13
	s_ashr_i32 s11, s10, 31
	s_mul_hi_i32 s17, s10, 0xc100
	s_add_u32 s18, s14, s15
	s_addc_u32 s17, s13, s17
	s_ashr_i32 s13, s12, 31
	s_lshl_b64 s[14:15], s[12:13], 2
	s_add_u32 s14, s18, s14
	s_addc_u32 s15, s17, s15
	v_lshl_add_u64 v[56:57], s[14:15], 0, v[2:3]
	v_lshl_add_u64 v[112:113], v[56:57], 0, v[4:5]
	v_lshl_add_u64 v[64:65], v[56:57], 0, v[6:7]
	v_lshl_add_u64 v[66:67], v[56:57], 0, v[8:9]
	v_lshl_add_u64 v[68:69], v[56:57], 0, v[10:11]
	v_lshl_add_u64 v[70:71], v[56:57], 0, v[12:13]
	v_lshl_add_u64 v[72:73], v[56:57], 0, v[14:15]
	v_lshl_add_u64 v[76:77], v[56:57], 0, v[16:17]
	v_lshl_add_u64 v[80:81], v[56:57], 0, v[18:19]
	v_lshl_add_u64 v[84:85], v[56:57], 0, v[20:21]
	v_lshl_add_u64 v[88:89], v[56:57], 0, v[22:23]
	v_lshl_add_u64 v[92:93], v[56:57], 0, v[24:25]
	v_lshl_add_u64 v[96:97], v[56:57], 0, v[26:27]
	v_lshl_add_u64 v[100:101], v[56:57], 0, v[28:29]
	v_lshl_add_u64 v[104:105], v[56:57], 0, v[30:31]
	v_lshl_add_u64 v[108:109], v[56:57], 0, v[32:33]
	v_lshl_add_u64 v[116:117], v[56:57], 0, v[34:35]
	flat_load_dwordx4 v[56:59], v[64:65] nt
	flat_load_dwordx4 v[60:63], v[66:67] nt
	s_nop 0
	flat_load_dwordx4 v[64:67], v[68:69] nt
	s_nop 0
	flat_load_dwordx4 v[68:71], v[70:71] nt
	s_nop 0
	flat_load_dwordx4 v[72:75], v[72:73] nt
	s_nop 0
	flat_load_dwordx4 v[76:79], v[76:77] nt
	s_nop 0
	flat_load_dwordx4 v[80:83], v[80:81] nt
	s_nop 0
	flat_load_dwordx4 v[84:87], v[84:85] nt
	s_nop 0
	flat_load_dwordx4 v[88:91], v[88:89] nt
	s_nop 0
	flat_load_dwordx4 v[92:95], v[92:93] nt
	s_nop 0
	flat_load_dwordx4 v[96:99], v[96:97] nt
	s_nop 0
	flat_load_dwordx4 v[100:103], v[100:101] nt
	s_nop 0
	flat_load_dwordx4 v[104:107], v[104:105] nt
	s_nop 0
	flat_load_dwordx4 v[108:111], v[108:109] nt
	s_nop 0
	flat_load_dwordx4 v[112:115], v[112:113] nt
	s_nop 0
	flat_load_dwordx4 v[116:119], v[116:117] nt
	s_add_i32 s13, s12, 0xc0
	s_cmpk_lt_i32 s16, 0x61
	v_add_u32_e32 v136, 0x410, v55
	s_cselect_b32 s12, s12, s13
	v_add_u32_e32 v137, 0x418, v55
	v_add_u32_e32 v138, 0x820, v55
	v_add_u32_e32 v139, 0x828, v55
	v_add_u32_e32 v140, 0xc30, v55
	v_add_u32_e32 v141, 0xc38, v55
	v_add_u32_e32 v142, 0x1040, v55
	v_add_u32_e32 v143, 0x1048, v55
	v_add_u32_e32 v144, 0x1450, v55
	v_add_u32_e32 v145, 0x1458, v55
	v_add_u32_e32 v146, 0x1860, v55
	v_add_u32_e32 v147, 0x1868, v55
	v_add_u32_e32 v148, 0x1c70, v55
	v_add_u32_e32 v149, 0x1c78, v55
	v_add_u32_e32 v150, 0x2080, v55
	v_add_u32_e32 v151, 0x2088, v55
	v_add_u32_e32 v152, 0x2490, v55
	v_add_u32_e32 v153, 0x2498, v55
	v_add_u32_e32 v154, 0x28a0, v55
	v_add_u32_e32 v155, 0x28a8, v55
	v_add_u32_e32 v156, 0x2cb0, v55
	v_add_u32_e32 v157, 0x2cb8, v55
	v_add_u32_e32 v158, 0x30c0, v55
	v_add_u32_e32 v159, 0x30c8, v55
	v_add_u32_e32 v160, 0x34d0, v55
	v_add_u32_e32 v161, 0x34d8, v55
	v_add_u32_e32 v162, 0x38e0, v55
	v_add_u32_e32 v163, 0x38e8, v55
	v_add_u32_e32 v164, 0x3cf0, v55
	v_add_u32_e32 v165, 0x3cf8, v55
	s_ashr_i32 s13, s12, 31
	s_lshl_b64 s[12:13], s[12:13], 12
	s_add_u32 s12, s7, s12
	v_add_u32_e32 v166, 0x400, v54
	s_addc_u32 s13, s9, s13
	s_lshl_b64 s[10:11], s[10:11], 1
	s_add_u32 s10, s12, s10
	v_mov_b32_e32 v53, v3
	s_addc_u32 s11, s13, s11
	v_lshl_add_u64 v[120:121], s[10:11], 0, v[52:53]
	v_lshl_add_u64 v[122:123], v[120:121], 0, v[36:37]
	v_lshl_add_u64 v[124:125], v[120:121], 0, v[38:39]
	v_lshl_add_u64 v[126:127], v[120:121], 0, v[40:41]
	v_lshl_add_u64 v[128:129], v[120:121], 0, v[42:43]
	v_lshl_add_u64 v[130:131], v[120:121], 0, v[44:45]
	v_lshl_add_u64 v[132:133], v[120:121], 0, v[46:47]
	v_lshl_add_u64 v[134:135], v[120:121], 0, v[48:49]
	v_lshl_add_u64 v[120:121], v[120:121], 0, v[50:51]
	s_add_i32 s6, s6, s80
	s_cmpk_lt_i32 s6, 0x1820
	s_waitcnt vmcnt(0) lgkmcnt(0)
	ds_write2_b32 v136, v56, v57 offset1:1
	ds_write2_b32 v137, v58, v59 offset1:1
	ds_write2_b32 v138, v60, v61 offset1:1
	ds_write2_b32 v139, v62, v63 offset1:1
	ds_write2_b32 v140, v64, v65 offset1:1
	ds_write2_b32 v141, v66, v67 offset1:1
	ds_write2_b32 v142, v68, v69 offset1:1
	ds_write2_b32 v143, v70, v71 offset1:1
	ds_write2_b32 v144, v72, v73 offset1:1
	ds_write2_b32 v145, v74, v75 offset1:1
	ds_write2_b32 v146, v76, v77 offset1:1
	ds_write2_b32 v147, v78, v79 offset1:1
	ds_write2_b32 v148, v80, v81 offset1:1
	ds_write2_b32 v149, v82, v83 offset1:1
	ds_write2_b32 v150, v84, v85 offset1:1
	ds_write2_b32 v151, v86, v87 offset1:1
	ds_write2_b32 v152, v88, v89 offset1:1
	ds_write2_b32 v153, v90, v91 offset1:1
	ds_write2_b32 v154, v92, v93 offset1:1
	ds_write2_b32 v155, v94, v95 offset1:1
	ds_write2_b32 v156, v96, v97 offset1:1
	ds_write2_b32 v157, v98, v99 offset1:1
	ds_write2_b32 v158, v100, v101 offset1:1
	ds_write2_b32 v159, v102, v103 offset1:1
	ds_write2_b32 v160, v104, v105 offset1:1
	ds_write2_b32 v161, v106, v107 offset1:1
	ds_write2_b32 v162, v108, v109 offset1:1
	ds_write2_b32 v163, v110, v111 offset1:1
	ds_write2_b32 v55, v112, v113 offset1:1
	ds_write2_b32 v55, v114, v115 offset0:2 offset1:3
	ds_write2_b32 v164, v116, v117 offset1:1
	ds_write2_b32 v165, v118, v119 offset1:1
	s_waitcnt lgkmcnt(0)
	ds_read2_b32 v[60:61], v54 offset0:65 offset1:73
	ds_read2_b32 v[62:63], v54 offset1:8
	ds_read2_b32 v[64:65], v54 offset0:130 offset1:138
	ds_read2_b32 v[66:67], v54 offset0:195 offset1:203
	ds_read2_b32 v[68:69], v166 offset0:4 offset1:12
	ds_read2_b32 v[70:71], v166 offset0:69 offset1:77
	ds_read2_b32 v[72:73], v166 offset0:134 offset1:142
	ds_read2_b32 v[74:75], v166 offset0:199 offset1:207
	ds_read2_b32 v[76:77], v54 offset0:81 offset1:89
	ds_read2_b32 v[78:79], v54 offset0:16 offset1:24
	ds_read2_b32 v[80:81], v54 offset0:146 offset1:154
	ds_read2_b32 v[82:83], v54 offset0:211 offset1:219
	ds_read2_b32 v[84:85], v166 offset0:20 offset1:28
	ds_read2_b32 v[86:87], v166 offset0:85 offset1:93
	ds_read2_b32 v[88:89], v166 offset0:150 offset1:158
	ds_read2_b32 v[90:91], v166 offset0:215 offset1:223
	ds_read2_b32 v[92:93], v54 offset0:32 offset1:40
	ds_read2_b32 v[94:95], v54 offset0:97 offset1:105
	ds_read2_b32 v[96:97], v54 offset0:162 offset1:170
	ds_read2_b32 v[98:99], v54 offset0:227 offset1:235
	ds_read2_b32 v[100:101], v166 offset0:36 offset1:44
	ds_read2_b32 v[102:103], v166 offset0:101 offset1:109
	ds_read2_b32 v[104:105], v166 offset0:166 offset1:174
	ds_read2_b32 v[106:107], v166 offset0:231 offset1:239
	ds_read2_b32 v[108:109], v54 offset0:48 offset1:56
	ds_read2_b32 v[110:111], v54 offset0:113 offset1:121
	ds_read2_b32 v[112:113], v54 offset0:178 offset1:186
	ds_read2_b32 v[114:115], v54 offset0:243 offset1:251
	ds_read2_b32 v[116:117], v166 offset0:52 offset1:60
	ds_read2_b32 v[118:119], v166 offset0:117 offset1:125
	ds_read2_b32 v[136:137], v166 offset0:182 offset1:190
	ds_read2_b32 v[138:139], v166 offset0:247 offset1:255
	s_waitcnt lgkmcnt(14)
	v_cvt_pk_bf16_f32 v56, v62, v60
	v_cvt_pk_bf16_f32 v57, v64, v66
	v_cvt_pk_bf16_f32 v58, v68, v70
	v_cvt_pk_bf16_f32 v59, v72, v74
	v_cvt_pk_bf16_f32 v60, v63, v61
	v_cvt_pk_bf16_f32 v61, v65, v67
	v_cvt_pk_bf16_f32 v62, v69, v71
	v_cvt_pk_bf16_f32 v63, v73, v75
	v_cvt_pk_bf16_f32 v64, v78, v76
	v_cvt_pk_bf16_f32 v65, v80, v82
	v_cvt_pk_bf16_f32 v66, v84, v86
	v_cvt_pk_bf16_f32 v67, v88, v90
	v_cvt_pk_bf16_f32 v68, v79, v77
	v_cvt_pk_bf16_f32 v69, v81, v83
	v_cvt_pk_bf16_f32 v70, v85, v87
	v_cvt_pk_bf16_f32 v71, v89, v91
	v_cvt_pk_bf16_f32 v72, v92, v94
	s_waitcnt lgkmcnt(12)
	v_cvt_pk_bf16_f32 v73, v96, v98
	s_waitcnt lgkmcnt(10)
	v_cvt_pk_bf16_f32 v74, v100, v102
	s_waitcnt lgkmcnt(8)
	v_cvt_pk_bf16_f32 v75, v104, v106
	v_cvt_pk_bf16_f32 v76, v93, v95
	v_cvt_pk_bf16_f32 v77, v97, v99
	v_cvt_pk_bf16_f32 v78, v101, v103
	v_cvt_pk_bf16_f32 v79, v105, v107
	s_waitcnt lgkmcnt(6)
	v_cvt_pk_bf16_f32 v80, v108, v110
	s_waitcnt lgkmcnt(4)
	v_cvt_pk_bf16_f32 v81, v112, v114
	s_waitcnt lgkmcnt(2)
	v_cvt_pk_bf16_f32 v82, v116, v118
	s_waitcnt lgkmcnt(0)
	v_cvt_pk_bf16_f32 v83, v136, v138
	v_cvt_pk_bf16_f32 v84, v109, v111
	v_cvt_pk_bf16_f32 v85, v113, v115
	v_cvt_pk_bf16_f32 v86, v117, v119
	v_cvt_pk_bf16_f32 v87, v137, v139
	global_store_dwordx4 v[122:123], v[56:59], off sc1
	global_store_dwordx4 v[124:125], v[60:63], off sc1
	global_store_dwordx4 v[126:127], v[64:67], off sc1
	global_store_dwordx4 v[128:129], v[68:71], off sc1
	global_store_dwordx4 v[130:131], v[72:75], off sc1
	global_store_dwordx4 v[132:133], v[76:79], off sc1
	global_store_dwordx4 v[134:135], v[80:83], off sc1
	global_store_dwordx4 v[120:121], v[84:87], off sc1
	s_waitcnt lgkmcnt(0)
	s_cbranch_scc1 .LBB0_34

.LBB0_37:
	s_ashr_i32 s10, s6, 31
	s_lshr_b32 s10, s10, 23
	s_add_i32 s11, s6, s10
	s_ashr_i32 s10, s11, 9
	s_and_b32 s11, s11, 0xfe00
	s_sub_i32 s12, s6, s11
	s_sext_i32_i16 s13, s12
	s_bfe_u32 s13, s13, 0x5001a
	s_add_i32 s13, s12, s13
	s_sext_i32_i16 s14, s13
	s_and_b32 s13, s13, 0xffe0
	s_sub_i32 s12, s12, s13
	s_ashr_i32 s11, s10, 31
	s_lshl_b32 s13, s14, 1
	s_sext_i32_i16 s14, s12
	s_lshl_b64 s[10:11], s[10:11], 23
	s_and_b32 s12, s13, 0xffffffc0
	s_lshl_b32 s14, s14, 6
	s_waitcnt lgkmcnt(0)
	s_add_u32 s15, s2, s10
	s_addc_u32 s16, s3, s11
	s_ashr_i32 s13, s12, 31
	s_lshl_b64 s[10:11], s[12:13], 13
	s_add_u32 s17, s15, s10
	s_addc_u32 s16, s16, s11
	s_ashr_i32 s15, s14, 31
	s_lshl_b64 s[10:11], s[14:15], 2
	s_add_u32 s10, s17, s10
	s_addc_u32 s11, s16, s11
	v_lshl_add_u64 v[56:57], s[10:11], 0, v[52:53]
	v_lshl_add_u64 v[72:73], v[56:57], 0, v[4:5]
	v_lshl_add_u64 v[64:65], v[56:57], 0, v[6:7]
	v_lshl_add_u64 v[66:67], v[56:57], 0, v[8:9]
	v_lshl_add_u64 v[68:69], v[56:57], 0, v[10:11]
	v_lshl_add_u64 v[70:71], v[56:57], 0, v[12:13]
	v_lshl_add_u64 v[76:77], v[56:57], 0, v[14:15]
	v_lshl_add_u64 v[80:81], v[56:57], 0, v[16:17]
	v_lshl_add_u64 v[84:85], v[56:57], 0, v[18:19]
	v_lshl_add_u64 v[88:89], v[56:57], 0, v[20:21]
	v_lshl_add_u64 v[92:93], v[56:57], 0, v[22:23]
	v_lshl_add_u64 v[96:97], v[56:57], 0, v[24:25]
	v_lshl_add_u64 v[100:101], v[56:57], 0, v[26:27]
	v_lshl_add_u64 v[104:105], v[56:57], 0, v[28:29]
	v_lshl_add_u64 v[108:109], v[56:57], 0, v[30:31]
	v_lshl_add_u64 v[112:113], v[56:57], 0, v[32:33]
	v_lshl_add_u64 v[116:117], v[56:57], 0, v[34:35]
	flat_load_dwordx4 v[56:59], v[64:65] nt
	flat_load_dwordx4 v[60:63], v[66:67] nt
	s_nop 0
	flat_load_dwordx4 v[64:67], v[68:69] nt
	s_nop 0
	flat_load_dwordx4 v[68:71], v[70:71] nt
	s_nop 0
	flat_load_dwordx4 v[72:75], v[72:73] nt
	s_nop 0
	flat_load_dwordx4 v[76:79], v[76:77] nt
	s_nop 0
	flat_load_dwordx4 v[80:83], v[80:81] nt
	s_nop 0
	flat_load_dwordx4 v[84:87], v[84:85] nt
	s_nop 0
	flat_load_dwordx4 v[88:91], v[88:89] nt
	s_nop 0
	flat_load_dwordx4 v[92:95], v[92:93] nt
	s_nop 0
	flat_load_dwordx4 v[96:99], v[96:97] nt
	s_nop 0
	flat_load_dwordx4 v[100:103], v[100:101] nt
	s_nop 0
	flat_load_dwordx4 v[104:107], v[104:105] nt
	s_nop 0
	flat_load_dwordx4 v[108:111], v[108:109] nt
	s_nop 0
	flat_load_dwordx4 v[112:115], v[112:113] nt
	s_nop 0
	flat_load_dwordx4 v[116:119], v[116:117] nt
	v_add_u32_e32 v136, 0x410, v55
	v_add_u32_e32 v137, 0x418, v55
	v_add_u32_e32 v138, 0x820, v55
	v_add_u32_e32 v139, 0x828, v55
	v_add_u32_e32 v140, 0xc30, v55
	v_add_u32_e32 v141, 0xc38, v55
	v_add_u32_e32 v142, 0x1040, v55
	v_add_u32_e32 v143, 0x1048, v55
	v_add_u32_e32 v144, 0x1450, v55
	v_add_u32_e32 v145, 0x1458, v55
	v_add_u32_e32 v146, 0x1860, v55
	v_add_u32_e32 v147, 0x1868, v55
	v_add_u32_e32 v148, 0x1c70, v55
	v_add_u32_e32 v149, 0x1c78, v55
	v_add_u32_e32 v150, 0x2080, v55
	v_add_u32_e32 v151, 0x2088, v55
	v_add_u32_e32 v152, 0x2490, v55
	v_add_u32_e32 v153, 0x2498, v55
	v_add_u32_e32 v154, 0x28a0, v55
	v_add_u32_e32 v155, 0x28a8, v55
	v_add_u32_e32 v156, 0x2cb0, v55
	v_add_u32_e32 v157, 0x2cb8, v55
	v_add_u32_e32 v158, 0x30c0, v55
	v_add_u32_e32 v159, 0x30c8, v55
	v_add_u32_e32 v160, 0x34d0, v55
	v_add_u32_e32 v161, 0x34d8, v55
	v_add_u32_e32 v162, 0x38e0, v55
	v_add_u32_e32 v163, 0x38e8, v55
	v_add_u32_e32 v164, 0x3cf0, v55
	v_add_u32_e32 v165, 0x3cf8, v55
	s_lshl_b64 s[14:15], s[14:15], 11
	s_add_u32 s14, s7, s14
	v_add_u32_e32 v166, 0x400, v54
	s_addc_u32 s15, s9, s15
	s_lshl_b64 s[10:11], s[12:13], 1
	s_add_u32 s10, s14, s10
	s_addc_u32 s11, s15, s11
	v_lshl_add_u64 v[120:121], s[10:11], 0, v[2:3]
	v_lshl_add_u64 v[122:123], v[120:121], 0, v[36:37]
	v_lshl_add_u64 v[124:125], v[120:121], 0, v[38:39]
	v_lshl_add_u64 v[126:127], v[120:121], 0, v[40:41]
	v_lshl_add_u64 v[128:129], v[120:121], 0, v[42:43]
	v_lshl_add_u64 v[130:131], v[120:121], 0, v[44:45]
	v_lshl_add_u64 v[132:133], v[120:121], 0, v[46:47]
	v_lshl_add_u64 v[134:135], v[120:121], 0, v[48:49]
	v_lshl_add_u64 v[120:121], v[120:121], 0, v[50:51]
	s_add_i32 s6, s6, s80
	s_cmpk_lt_i32 s6, 0x200
	s_waitcnt vmcnt(0) lgkmcnt(0)
	ds_write2_b32 v136, v56, v57 offset1:1
	ds_write2_b32 v137, v58, v59 offset1:1
	ds_write2_b32 v138, v60, v61 offset1:1
	ds_write2_b32 v139, v62, v63 offset1:1
	ds_write2_b32 v140, v64, v65 offset1:1
	ds_write2_b32 v141, v66, v67 offset1:1
	ds_write2_b32 v142, v68, v69 offset1:1
	ds_write2_b32 v143, v70, v71 offset1:1
	ds_write2_b32 v55, v72, v73 offset1:1
	ds_write2_b32 v55, v74, v75 offset0:2 offset1:3
	ds_write2_b32 v144, v76, v77 offset1:1
	ds_write2_b32 v145, v78, v79 offset1:1
	ds_write2_b32 v146, v80, v81 offset1:1
	ds_write2_b32 v147, v82, v83 offset1:1
	ds_write2_b32 v148, v84, v85 offset1:1
	ds_write2_b32 v149, v86, v87 offset1:1
	ds_write2_b32 v150, v88, v89 offset1:1
	ds_write2_b32 v151, v90, v91 offset1:1
	ds_write2_b32 v152, v92, v93 offset1:1
	ds_write2_b32 v153, v94, v95 offset1:1
	ds_write2_b32 v154, v96, v97 offset1:1
	ds_write2_b32 v155, v98, v99 offset1:1
	ds_write2_b32 v156, v100, v101 offset1:1
	ds_write2_b32 v157, v102, v103 offset1:1
	ds_write2_b32 v158, v104, v105 offset1:1
	ds_write2_b32 v159, v106, v107 offset1:1
	ds_write2_b32 v160, v108, v109 offset1:1
	ds_write2_b32 v161, v110, v111 offset1:1
	ds_write2_b32 v162, v112, v113 offset1:1
	ds_write2_b32 v163, v114, v115 offset1:1
	ds_write2_b32 v164, v116, v117 offset1:1
	ds_write2_b32 v165, v118, v119 offset1:1
	s_waitcnt lgkmcnt(0)
	ds_read2_b32 v[58:59], v54 offset0:65 offset1:73
	ds_read2_b32 v[60:61], v54 offset1:8
	ds_read2_b32 v[62:63], v54 offset0:130 offset1:138
	ds_read2_b32 v[64:65], v54 offset0:195 offset1:203
	ds_read2_b32 v[66:67], v166 offset0:4 offset1:12
	ds_read2_b32 v[68:69], v166 offset0:69 offset1:77
	ds_read2_b32 v[70:71], v166 offset0:134 offset1:142
	ds_read2_b32 v[72:73], v166 offset0:199 offset1:207
	ds_read2_b32 v[74:75], v54 offset0:81 offset1:89
	ds_read2_b32 v[76:77], v54 offset0:16 offset1:24
	ds_read2_b32 v[78:79], v54 offset0:146 offset1:154
	ds_read2_b32 v[80:81], v54 offset0:211 offset1:219
	ds_read2_b32 v[82:83], v166 offset0:20 offset1:28
	ds_read2_b32 v[84:85], v166 offset0:85 offset1:93
	ds_read2_b32 v[86:87], v166 offset0:150 offset1:158
	ds_read2_b32 v[88:89], v166 offset0:215 offset1:223
	ds_read2_b32 v[90:91], v54 offset0:32 offset1:40
	ds_read2_b32 v[92:93], v54 offset0:97 offset1:105
	ds_read2_b32 v[94:95], v54 offset0:162 offset1:170
	ds_read2_b32 v[96:97], v54 offset0:227 offset1:235
	ds_read2_b32 v[98:99], v166 offset0:36 offset1:44
	ds_read2_b32 v[100:101], v166 offset0:101 offset1:109
	ds_read2_b32 v[102:103], v166 offset0:166 offset1:174
	ds_read2_b32 v[104:105], v166 offset0:231 offset1:239
	ds_read2_b32 v[106:107], v54 offset0:48 offset1:56
	ds_read2_b32 v[108:109], v54 offset0:113 offset1:121
	ds_read2_b32 v[110:111], v54 offset0:178 offset1:186
	ds_read2_b32 v[112:113], v54 offset0:243 offset1:251
	ds_read2_b32 v[114:115], v166 offset0:52 offset1:60
	ds_read2_b32 v[116:117], v166 offset0:117 offset1:125
	ds_read2_b32 v[118:119], v166 offset0:182 offset1:190
	ds_read2_b32 v[136:137], v166 offset0:247 offset1:255
	s_waitcnt lgkmcnt(14)
	v_cvt_pk_bf16_f32 v56, v60, v58
	v_cvt_pk_bf16_f32 v57, v62, v64
	v_cvt_pk_bf16_f32 v60, v61, v59
	v_cvt_pk_bf16_f32 v58, v66, v68
	v_cvt_pk_bf16_f32 v59, v70, v72
	v_cvt_pk_bf16_f32 v61, v63, v65
	v_cvt_pk_bf16_f32 v62, v67, v69
	v_cvt_pk_bf16_f32 v63, v71, v73
	v_cvt_pk_bf16_f32 v64, v76, v74
	v_cvt_pk_bf16_f32 v65, v78, v80
	v_cvt_pk_bf16_f32 v68, v77, v75
	v_cvt_pk_bf16_f32 v69, v79, v81
	v_cvt_pk_bf16_f32 v66, v82, v84
	v_cvt_pk_bf16_f32 v70, v83, v85
	v_cvt_pk_bf16_f32 v67, v86, v88
	v_cvt_pk_bf16_f32 v71, v87, v89
	v_cvt_pk_bf16_f32 v72, v90, v92
	s_waitcnt lgkmcnt(12)
	v_cvt_pk_bf16_f32 v73, v94, v96
	s_waitcnt lgkmcnt(10)
	v_cvt_pk_bf16_f32 v74, v98, v100
	s_waitcnt lgkmcnt(8)
	v_cvt_pk_bf16_f32 v75, v102, v104
	v_cvt_pk_bf16_f32 v76, v91, v93
	v_cvt_pk_bf16_f32 v77, v95, v97
	v_cvt_pk_bf16_f32 v78, v99, v101
	v_cvt_pk_bf16_f32 v79, v103, v105
	s_waitcnt lgkmcnt(6)
	v_cvt_pk_bf16_f32 v80, v106, v108
	s_waitcnt lgkmcnt(4)
	v_cvt_pk_bf16_f32 v81, v110, v112
	s_waitcnt lgkmcnt(2)
	v_cvt_pk_bf16_f32 v82, v114, v116
	s_waitcnt lgkmcnt(0)
	v_cvt_pk_bf16_f32 v83, v118, v136
	v_cvt_pk_bf16_f32 v84, v107, v109
	v_cvt_pk_bf16_f32 v85, v111, v113
	v_cvt_pk_bf16_f32 v86, v115, v117
	v_cvt_pk_bf16_f32 v87, v119, v137
	global_store_dwordx4 v[122:123], v[56:59], off sc1
	global_store_dwordx4 v[124:125], v[60:63], off sc1
	global_store_dwordx4 v[126:127], v[64:67], off sc1
	global_store_dwordx4 v[128:129], v[68:71], off sc1
	global_store_dwordx4 v[130:131], v[72:75], off sc1
	global_store_dwordx4 v[132:133], v[76:79], off sc1
	global_store_dwordx4 v[134:135], v[80:83], off sc1
	global_store_dwordx4 v[120:121], v[84:87], off sc1
	s_waitcnt lgkmcnt(0)
	s_cbranch_scc1 .LBB0_37

.LBB0_46:
	s_ashr_i32 s10, s6, 31
	s_lshr_b32 s10, s10, 22
	s_add_i32 s11, s6, s10
	s_ashr_i32 s10, s11, 10
	s_and_b32 s11, s11, 0xfc00
	s_sub_i32 s12, s6, s11
	s_sext_i32_i16 s13, s12
	s_bfe_u32 s13, s13, 0x5001a
	s_add_i32 s13, s12, s13
	s_sext_i32_i16 s14, s13
	s_and_b32 s13, s13, 0xffe0
	s_sub_i32 s12, s12, s13
	s_ashr_i32 s11, s10, 31
	s_lshl_b32 s13, s14, 1
	s_sext_i32_i16 s14, s12
	s_lshl_b64 s[10:11], s[10:11], 24
	s_and_b32 s12, s13, 0xffffffc0
	s_lshl_b32 s14, s14, 6
	s_waitcnt lgkmcnt(0)
	s_add_u32 s15, s2, s10
	s_addc_u32 s16, s3, s11
	s_ashr_i32 s13, s12, 31
	s_lshl_b64 s[10:11], s[12:13], 13
	s_add_u32 s17, s15, s10
	s_addc_u32 s16, s16, s11
	s_ashr_i32 s15, s14, 31
	s_lshl_b64 s[10:11], s[14:15], 2
	s_add_u32 s10, s17, s10
	s_addc_u32 s11, s16, s11
	v_lshl_add_u64 v[56:57], s[10:11], 0, v[52:53]
	v_lshl_add_u64 v[72:73], v[56:57], 0, v[4:5]
	v_lshl_add_u64 v[64:65], v[56:57], 0, v[6:7]
	v_lshl_add_u64 v[66:67], v[56:57], 0, v[8:9]
	v_lshl_add_u64 v[68:69], v[56:57], 0, v[10:11]
	v_lshl_add_u64 v[70:71], v[56:57], 0, v[12:13]
	v_lshl_add_u64 v[76:77], v[56:57], 0, v[14:15]
	v_lshl_add_u64 v[80:81], v[56:57], 0, v[16:17]
	v_lshl_add_u64 v[84:85], v[56:57], 0, v[18:19]
	v_lshl_add_u64 v[88:89], v[56:57], 0, v[20:21]
	v_lshl_add_u64 v[92:93], v[56:57], 0, v[22:23]
	v_lshl_add_u64 v[96:97], v[56:57], 0, v[24:25]
	v_lshl_add_u64 v[100:101], v[56:57], 0, v[26:27]
	v_lshl_add_u64 v[104:105], v[56:57], 0, v[28:29]
	v_lshl_add_u64 v[108:109], v[56:57], 0, v[30:31]
	v_lshl_add_u64 v[112:113], v[56:57], 0, v[32:33]
	v_lshl_add_u64 v[116:117], v[56:57], 0, v[34:35]
	flat_load_dwordx4 v[56:59], v[64:65] nt
	flat_load_dwordx4 v[60:63], v[66:67] nt
	s_nop 0
	flat_load_dwordx4 v[64:67], v[68:69] nt
	s_nop 0
	flat_load_dwordx4 v[68:71], v[70:71] nt
	s_nop 0
	flat_load_dwordx4 v[72:75], v[72:73] nt
	s_nop 0
	flat_load_dwordx4 v[76:79], v[76:77] nt
	s_nop 0
	flat_load_dwordx4 v[80:83], v[80:81] nt
	s_nop 0
	flat_load_dwordx4 v[84:87], v[84:85] nt
	s_nop 0
	flat_load_dwordx4 v[88:91], v[88:89] nt
	s_nop 0
	flat_load_dwordx4 v[92:95], v[92:93] nt
	s_nop 0
	flat_load_dwordx4 v[96:99], v[96:97] nt
	s_nop 0
	flat_load_dwordx4 v[100:103], v[100:101] nt
	s_nop 0
	flat_load_dwordx4 v[104:107], v[104:105] nt
	s_nop 0
	flat_load_dwordx4 v[108:111], v[108:109] nt
	s_nop 0
	flat_load_dwordx4 v[112:115], v[112:113] nt
	s_nop 0
	flat_load_dwordx4 v[116:119], v[116:117] nt
	v_add_u32_e32 v136, 0x410, v55
	v_add_u32_e32 v137, 0x418, v55
	v_add_u32_e32 v138, 0x820, v55
	v_add_u32_e32 v139, 0x828, v55
	v_add_u32_e32 v140, 0xc30, v55
	v_add_u32_e32 v141, 0xc38, v55
	v_add_u32_e32 v142, 0x1040, v55
	v_add_u32_e32 v143, 0x1048, v55
	v_add_u32_e32 v144, 0x1450, v55
	v_add_u32_e32 v145, 0x1458, v55
	v_add_u32_e32 v146, 0x1860, v55
	v_add_u32_e32 v147, 0x1868, v55
	v_add_u32_e32 v148, 0x1c70, v55
	v_add_u32_e32 v149, 0x1c78, v55
	v_add_u32_e32 v150, 0x2080, v55
	v_add_u32_e32 v151, 0x2088, v55
	v_add_u32_e32 v152, 0x2490, v55
	v_add_u32_e32 v153, 0x2498, v55
	v_add_u32_e32 v154, 0x28a0, v55
	v_add_u32_e32 v155, 0x28a8, v55
	v_add_u32_e32 v156, 0x2cb0, v55
	v_add_u32_e32 v157, 0x2cb8, v55
	v_add_u32_e32 v158, 0x30c0, v55
	v_add_u32_e32 v159, 0x30c8, v55
	v_add_u32_e32 v160, 0x34d0, v55
	v_add_u32_e32 v161, 0x34d8, v55
	v_add_u32_e32 v162, 0x38e0, v55
	v_add_u32_e32 v163, 0x38e8, v55
	v_add_u32_e32 v164, 0x3cf0, v55
	v_add_u32_e32 v165, 0x3cf8, v55
	s_lshl_b64 s[14:15], s[14:15], 12
	s_add_u32 s14, s7, s14
	v_add_u32_e32 v166, 0x400, v54
	s_addc_u32 s15, s9, s15
	s_lshl_b64 s[10:11], s[12:13], 1
	s_add_u32 s10, s14, s10
	s_addc_u32 s11, s15, s11
	v_lshl_add_u64 v[120:121], s[10:11], 0, v[2:3]
	v_lshl_add_u64 v[122:123], v[120:121], 0, v[36:37]
	v_lshl_add_u64 v[124:125], v[120:121], 0, v[38:39]
	v_lshl_add_u64 v[126:127], v[120:121], 0, v[40:41]
	v_lshl_add_u64 v[128:129], v[120:121], 0, v[42:43]
	v_lshl_add_u64 v[130:131], v[120:121], 0, v[44:45]
	v_lshl_add_u64 v[132:133], v[120:121], 0, v[46:47]
	v_lshl_add_u64 v[134:135], v[120:121], 0, v[48:49]
	v_lshl_add_u64 v[120:121], v[120:121], 0, v[50:51]
	s_add_i32 s6, s6, s80
	s_cmpk_lt_i32 s6, 0x400
	s_waitcnt vmcnt(0) lgkmcnt(0)
	ds_write2_b32 v136, v56, v57 offset1:1
	ds_write2_b32 v137, v58, v59 offset1:1
	ds_write2_b32 v138, v60, v61 offset1:1
	ds_write2_b32 v139, v62, v63 offset1:1
	ds_write2_b32 v140, v64, v65 offset1:1
	ds_write2_b32 v141, v66, v67 offset1:1
	ds_write2_b32 v142, v68, v69 offset1:1
	ds_write2_b32 v143, v70, v71 offset1:1
	ds_write2_b32 v55, v72, v73 offset1:1
	ds_write2_b32 v55, v74, v75 offset0:2 offset1:3
	ds_write2_b32 v144, v76, v77 offset1:1
	ds_write2_b32 v145, v78, v79 offset1:1
	ds_write2_b32 v146, v80, v81 offset1:1
	ds_write2_b32 v147, v82, v83 offset1:1
	ds_write2_b32 v148, v84, v85 offset1:1
	ds_write2_b32 v149, v86, v87 offset1:1
	ds_write2_b32 v150, v88, v89 offset1:1
	ds_write2_b32 v151, v90, v91 offset1:1
	ds_write2_b32 v152, v92, v93 offset1:1
	ds_write2_b32 v153, v94, v95 offset1:1
	ds_write2_b32 v154, v96, v97 offset1:1
	ds_write2_b32 v155, v98, v99 offset1:1
	ds_write2_b32 v156, v100, v101 offset1:1
	ds_write2_b32 v157, v102, v103 offset1:1
	ds_write2_b32 v158, v104, v105 offset1:1
	ds_write2_b32 v159, v106, v107 offset1:1
	ds_write2_b32 v160, v108, v109 offset1:1
	ds_write2_b32 v161, v110, v111 offset1:1
	ds_write2_b32 v162, v112, v113 offset1:1
	ds_write2_b32 v163, v114, v115 offset1:1
	ds_write2_b32 v164, v116, v117 offset1:1
	ds_write2_b32 v165, v118, v119 offset1:1
	s_waitcnt lgkmcnt(0)
	ds_read2_b32 v[58:59], v54 offset0:65 offset1:73
	ds_read2_b32 v[60:61], v54 offset1:8
	ds_read2_b32 v[62:63], v54 offset0:130 offset1:138
	ds_read2_b32 v[64:65], v54 offset0:195 offset1:203
	ds_read2_b32 v[66:67], v166 offset0:4 offset1:12
	ds_read2_b32 v[68:69], v166 offset0:69 offset1:77
	ds_read2_b32 v[70:71], v166 offset0:134 offset1:142
	ds_read2_b32 v[72:73], v166 offset0:199 offset1:207
	ds_read2_b32 v[74:75], v54 offset0:81 offset1:89
	ds_read2_b32 v[76:77], v54 offset0:16 offset1:24
	ds_read2_b32 v[78:79], v54 offset0:146 offset1:154
	ds_read2_b32 v[80:81], v54 offset0:211 offset1:219
	ds_read2_b32 v[82:83], v166 offset0:20 offset1:28
	ds_read2_b32 v[84:85], v166 offset0:85 offset1:93
	ds_read2_b32 v[86:87], v166 offset0:150 offset1:158
	ds_read2_b32 v[88:89], v166 offset0:215 offset1:223
	ds_read2_b32 v[90:91], v54 offset0:32 offset1:40
	ds_read2_b32 v[92:93], v54 offset0:97 offset1:105
	ds_read2_b32 v[94:95], v54 offset0:162 offset1:170
	ds_read2_b32 v[96:97], v54 offset0:227 offset1:235
	ds_read2_b32 v[98:99], v166 offset0:36 offset1:44
	ds_read2_b32 v[100:101], v166 offset0:101 offset1:109
	ds_read2_b32 v[102:103], v166 offset0:166 offset1:174
	ds_read2_b32 v[104:105], v166 offset0:231 offset1:239
	ds_read2_b32 v[106:107], v54 offset0:48 offset1:56
	ds_read2_b32 v[108:109], v54 offset0:113 offset1:121
	ds_read2_b32 v[110:111], v54 offset0:178 offset1:186
	ds_read2_b32 v[112:113], v54 offset0:243 offset1:251
	ds_read2_b32 v[114:115], v166 offset0:52 offset1:60
	ds_read2_b32 v[116:117], v166 offset0:117 offset1:125
	ds_read2_b32 v[118:119], v166 offset0:182 offset1:190
	ds_read2_b32 v[136:137], v166 offset0:247 offset1:255
	s_waitcnt lgkmcnt(14)
	v_cvt_pk_bf16_f32 v56, v60, v58
	v_cvt_pk_bf16_f32 v57, v62, v64
	v_cvt_pk_bf16_f32 v60, v61, v59
	v_cvt_pk_bf16_f32 v58, v66, v68
	v_cvt_pk_bf16_f32 v59, v70, v72
	v_cvt_pk_bf16_f32 v61, v63, v65
	v_cvt_pk_bf16_f32 v62, v67, v69
	v_cvt_pk_bf16_f32 v63, v71, v73
	v_cvt_pk_bf16_f32 v64, v76, v74
	v_cvt_pk_bf16_f32 v65, v78, v80
	v_cvt_pk_bf16_f32 v68, v77, v75
	v_cvt_pk_bf16_f32 v69, v79, v81
	v_cvt_pk_bf16_f32 v66, v82, v84
	v_cvt_pk_bf16_f32 v70, v83, v85
	v_cvt_pk_bf16_f32 v67, v86, v88
	v_cvt_pk_bf16_f32 v71, v87, v89
	v_cvt_pk_bf16_f32 v72, v90, v92
	s_waitcnt lgkmcnt(12)
	v_cvt_pk_bf16_f32 v73, v94, v96
	s_waitcnt lgkmcnt(10)
	v_cvt_pk_bf16_f32 v74, v98, v100
	s_waitcnt lgkmcnt(8)
	v_cvt_pk_bf16_f32 v75, v102, v104
	v_cvt_pk_bf16_f32 v76, v91, v93
	v_cvt_pk_bf16_f32 v77, v95, v97
	v_cvt_pk_bf16_f32 v78, v99, v101
	v_cvt_pk_bf16_f32 v79, v103, v105
	s_waitcnt lgkmcnt(6)
	v_cvt_pk_bf16_f32 v80, v106, v108
	s_waitcnt lgkmcnt(4)
	v_cvt_pk_bf16_f32 v81, v110, v112
	s_waitcnt lgkmcnt(2)
	v_cvt_pk_bf16_f32 v82, v114, v116
	s_waitcnt lgkmcnt(0)
	v_cvt_pk_bf16_f32 v83, v118, v136
	v_cvt_pk_bf16_f32 v84, v107, v109
	v_cvt_pk_bf16_f32 v85, v111, v113
	v_cvt_pk_bf16_f32 v86, v115, v117
	v_cvt_pk_bf16_f32 v87, v119, v137
	global_store_dwordx4 v[122:123], v[56:59], off sc1
	global_store_dwordx4 v[124:125], v[60:63], off sc1
	global_store_dwordx4 v[126:127], v[64:67], off sc1
	global_store_dwordx4 v[128:129], v[68:71], off sc1
	global_store_dwordx4 v[130:131], v[72:75], off sc1
	global_store_dwordx4 v[132:133], v[76:79], off sc1
	global_store_dwordx4 v[134:135], v[80:83], off sc1
	global_store_dwordx4 v[120:121], v[84:87], off sc1
	s_waitcnt lgkmcnt(0)
	s_cbranch_scc1 .LBB0_46

.LBB0_49:
	s_ashr_i32 s10, s6, 31
	s_lshr_b32 s10, s10, 28
	s_add_i32 s11, s6, s10
	s_ashr_i32 s10, s11, 4
	s_and_b32 s11, s11, 0xfff0
	s_sub_i32 s14, s6, s11
	s_bfe_i32 s15, s14, 0x80000
	s_bfe_u32 s15, s15, 0x2000d
	s_add_i32 s15, s14, s15
	s_bfe_i32 s16, s15, 0x80000
	s_and_b32 s15, s15, 0xfc
	s_sext_i32_i16 s16, s16
	s_sub_i32 s14, s14, s15
	s_ashr_i32 s11, s10, 31
	s_sext_i32_i8 s15, s14
	s_lshl_b32 s14, s16, 4
	s_lshl_b64 s[12:13], s[10:11], 18
	s_andn2_b32 s14, s14, 63
	s_lshl_b32 s16, s15, 6
	s_waitcnt lgkmcnt(0)
	s_add_u32 s17, s2, s12
	s_addc_u32 s18, s3, s13
	s_ashr_i32 s15, s14, 31
	s_lshl_b64 s[12:13], s[14:15], 10
	s_add_u32 s19, s17, s12
	s_addc_u32 s18, s18, s13
	s_ashr_i32 s17, s16, 31
	s_lshl_b64 s[12:13], s[16:17], 2
	s_add_u32 s12, s19, s12
	s_addc_u32 s13, s18, s13
	v_lshl_add_u64 v[56:57], s[12:13], 0, v[52:53]
	v_lshl_add_u64 v[72:73], v[56:57], 0, v[4:5]
	v_lshl_add_u64 v[64:65], v[56:57], 0, v[6:7]
	v_lshl_add_u64 v[66:67], v[56:57], 0, v[8:9]
	v_lshl_add_u64 v[68:69], v[56:57], 0, v[10:11]
	v_lshl_add_u64 v[70:71], v[56:57], 0, v[12:13]
	v_lshl_add_u64 v[76:77], v[56:57], 0, v[14:15]
	v_lshl_add_u64 v[80:81], v[56:57], 0, v[16:17]
	v_lshl_add_u64 v[84:85], v[56:57], 0, v[18:19]
	v_lshl_add_u64 v[88:89], v[56:57], 0, v[20:21]
	v_lshl_add_u64 v[92:93], v[56:57], 0, v[22:23]
	v_lshl_add_u64 v[96:97], v[56:57], 0, v[24:25]
	v_lshl_add_u64 v[100:101], v[56:57], 0, v[26:27]
	v_lshl_add_u64 v[104:105], v[56:57], 0, v[28:29]
	v_lshl_add_u64 v[108:109], v[56:57], 0, v[30:31]
	v_lshl_add_u64 v[112:113], v[56:57], 0, v[32:33]
	v_lshl_add_u64 v[116:117], v[56:57], 0, v[34:35]
	flat_load_dwordx4 v[56:59], v[64:65] nt
	flat_load_dwordx4 v[60:63], v[66:67] nt
	s_nop 0
	flat_load_dwordx4 v[64:67], v[68:69] nt
	s_nop 0
	flat_load_dwordx4 v[68:71], v[70:71] nt
	s_nop 0
	flat_load_dwordx4 v[72:75], v[72:73] nt
	s_nop 0
	flat_load_dwordx4 v[76:79], v[76:77] nt
	s_nop 0
	flat_load_dwordx4 v[80:83], v[80:81] nt
	s_nop 0
	flat_load_dwordx4 v[84:87], v[84:85] nt
	s_nop 0
	flat_load_dwordx4 v[88:91], v[88:89] nt
	s_nop 0
	flat_load_dwordx4 v[92:95], v[92:93] nt
	s_nop 0
	flat_load_dwordx4 v[96:99], v[96:97] nt
	s_nop 0
	flat_load_dwordx4 v[100:103], v[100:101] nt
	s_nop 0
	flat_load_dwordx4 v[104:107], v[104:105] nt
	s_nop 0
	flat_load_dwordx4 v[108:111], v[108:109] nt
	s_nop 0
	flat_load_dwordx4 v[112:115], v[112:113] nt
	s_nop 0
	flat_load_dwordx4 v[116:119], v[116:117] nt
	v_add_u32_e32 v136, 0x410, v55
	s_lshl_b64 s[10:11], s[10:11], 17
	v_add_u32_e32 v137, 0x418, v55
	v_add_u32_e32 v138, 0x820, v55
	v_add_u32_e32 v139, 0x828, v55
	v_add_u32_e32 v140, 0xc30, v55
	v_add_u32_e32 v141, 0xc38, v55
	v_add_u32_e32 v142, 0x1040, v55
	v_add_u32_e32 v143, 0x1048, v55
	v_add_u32_e32 v144, 0x1450, v55
	v_add_u32_e32 v145, 0x1458, v55
	v_add_u32_e32 v146, 0x1860, v55
	v_add_u32_e32 v147, 0x1868, v55
	v_add_u32_e32 v148, 0x1c70, v55
	v_add_u32_e32 v149, 0x1c78, v55
	v_add_u32_e32 v150, 0x2080, v55
	v_add_u32_e32 v151, 0x2088, v55
	v_add_u32_e32 v152, 0x2490, v55
	v_add_u32_e32 v153, 0x2498, v55
	v_add_u32_e32 v154, 0x28a0, v55
	v_add_u32_e32 v155, 0x28a8, v55
	v_add_u32_e32 v156, 0x2cb0, v55
	v_add_u32_e32 v157, 0x2cb8, v55
	v_add_u32_e32 v158, 0x30c0, v55
	v_add_u32_e32 v159, 0x30c8, v55
	v_add_u32_e32 v160, 0x34d0, v55
	v_add_u32_e32 v161, 0x34d8, v55
	v_add_u32_e32 v162, 0x38e0, v55
	v_add_u32_e32 v163, 0x38e8, v55
	v_add_u32_e32 v164, 0x3cf0, v55
	v_add_u32_e32 v165, 0x3cf8, v55
	s_add_u32 s12, s7, s10
	s_addc_u32 s13, s9, s11
	s_lshl_b64 s[10:11], s[16:17], 9
	s_add_u32 s12, s12, s10
	v_add_u32_e32 v166, 0x400, v54
	s_addc_u32 s13, s13, s11
	s_lshl_b64 s[10:11], s[14:15], 1
	s_add_u32 s10, s12, s10
	s_addc_u32 s11, s13, s11
	v_lshl_add_u64 v[120:121], s[10:11], 0, v[2:3]
	v_lshl_add_u64 v[122:123], v[120:121], 0, v[36:37]
	v_lshl_add_u64 v[124:125], v[120:121], 0, v[38:39]
	v_lshl_add_u64 v[126:127], v[120:121], 0, v[40:41]
	v_lshl_add_u64 v[128:129], v[120:121], 0, v[42:43]
	v_lshl_add_u64 v[130:131], v[120:121], 0, v[44:45]
	v_lshl_add_u64 v[132:133], v[120:121], 0, v[46:47]
	v_lshl_add_u64 v[134:135], v[120:121], 0, v[48:49]
	v_lshl_add_u64 v[120:121], v[120:121], 0, v[50:51]
	s_add_i32 s6, s6, s80
	s_cmp_lt_i32 s6, 64
	s_waitcnt vmcnt(0) lgkmcnt(0)
	ds_write2_b32 v136, v56, v57 offset1:1
	ds_write2_b32 v137, v58, v59 offset1:1
	ds_write2_b32 v138, v60, v61 offset1:1
	ds_write2_b32 v139, v62, v63 offset1:1
	ds_write2_b32 v140, v64, v65 offset1:1
	ds_write2_b32 v141, v66, v67 offset1:1
	ds_write2_b32 v142, v68, v69 offset1:1
	ds_write2_b32 v143, v70, v71 offset1:1
	ds_write2_b32 v55, v72, v73 offset1:1
	ds_write2_b32 v55, v74, v75 offset0:2 offset1:3
	ds_write2_b32 v144, v76, v77 offset1:1
	ds_write2_b32 v145, v78, v79 offset1:1
	ds_write2_b32 v146, v80, v81 offset1:1
	ds_write2_b32 v147, v82, v83 offset1:1
	ds_write2_b32 v148, v84, v85 offset1:1
	ds_write2_b32 v149, v86, v87 offset1:1
	ds_write2_b32 v150, v88, v89 offset1:1
	ds_write2_b32 v151, v90, v91 offset1:1
	ds_write2_b32 v152, v92, v93 offset1:1
	ds_write2_b32 v153, v94, v95 offset1:1
	ds_write2_b32 v154, v96, v97 offset1:1
	ds_write2_b32 v155, v98, v99 offset1:1
	ds_write2_b32 v156, v100, v101 offset1:1
	ds_write2_b32 v157, v102, v103 offset1:1
	ds_write2_b32 v158, v104, v105 offset1:1
	ds_write2_b32 v159, v106, v107 offset1:1
	ds_write2_b32 v160, v108, v109 offset1:1
	ds_write2_b32 v161, v110, v111 offset1:1
	ds_write2_b32 v162, v112, v113 offset1:1
	ds_write2_b32 v163, v114, v115 offset1:1
	ds_write2_b32 v164, v116, v117 offset1:1
	ds_write2_b32 v165, v118, v119 offset1:1
	s_waitcnt lgkmcnt(0)
	ds_read2_b32 v[58:59], v54 offset0:65 offset1:73
	ds_read2_b32 v[60:61], v54 offset1:8
	ds_read2_b32 v[62:63], v54 offset0:130 offset1:138
	ds_read2_b32 v[64:65], v54 offset0:195 offset1:203
	ds_read2_b32 v[66:67], v166 offset0:4 offset1:12
	ds_read2_b32 v[68:69], v166 offset0:69 offset1:77
	ds_read2_b32 v[70:71], v166 offset0:134 offset1:142
	ds_read2_b32 v[72:73], v166 offset0:199 offset1:207
	ds_read2_b32 v[74:75], v54 offset0:81 offset1:89
	ds_read2_b32 v[76:77], v54 offset0:16 offset1:24
	ds_read2_b32 v[78:79], v54 offset0:146 offset1:154
	ds_read2_b32 v[80:81], v54 offset0:211 offset1:219
	ds_read2_b32 v[82:83], v166 offset0:20 offset1:28
	ds_read2_b32 v[84:85], v166 offset0:85 offset1:93
	ds_read2_b32 v[86:87], v166 offset0:150 offset1:158
	ds_read2_b32 v[88:89], v166 offset0:215 offset1:223
	ds_read2_b32 v[90:91], v54 offset0:97 offset1:105
	ds_read2_b32 v[92:93], v54 offset0:32 offset1:40
	ds_read2_b32 v[94:95], v54 offset0:162 offset1:170
	ds_read2_b32 v[96:97], v54 offset0:227 offset1:235
	ds_read2_b32 v[98:99], v166 offset0:36 offset1:44
	ds_read2_b32 v[100:101], v166 offset0:101 offset1:109
	ds_read2_b32 v[102:103], v166 offset0:166 offset1:174
	ds_read2_b32 v[104:105], v166 offset0:231 offset1:239
	ds_read2_b32 v[106:107], v54 offset0:48 offset1:56
	ds_read2_b32 v[108:109], v54 offset0:113 offset1:121
	ds_read2_b32 v[110:111], v54 offset0:178 offset1:186
	ds_read2_b32 v[112:113], v54 offset0:243 offset1:251
	ds_read2_b32 v[114:115], v166 offset0:52 offset1:60
	ds_read2_b32 v[116:117], v166 offset0:117 offset1:125
	ds_read2_b32 v[118:119], v166 offset0:182 offset1:190
	ds_read2_b32 v[136:137], v166 offset0:247 offset1:255
	s_waitcnt lgkmcnt(14)
	v_cvt_pk_bf16_f32 v56, v60, v58
	v_cvt_pk_bf16_f32 v57, v62, v64
	v_cvt_pk_bf16_f32 v60, v61, v59
	v_cvt_pk_bf16_f32 v58, v66, v68
	v_cvt_pk_bf16_f32 v59, v70, v72
	v_cvt_pk_bf16_f32 v61, v63, v65
	v_cvt_pk_bf16_f32 v62, v67, v69
	v_cvt_pk_bf16_f32 v63, v71, v73
	v_cvt_pk_bf16_f32 v64, v76, v74
	v_cvt_pk_bf16_f32 v65, v78, v80
	v_cvt_pk_bf16_f32 v68, v77, v75
	v_cvt_pk_bf16_f32 v69, v79, v81
	v_cvt_pk_bf16_f32 v66, v82, v84
	v_cvt_pk_bf16_f32 v70, v83, v85
	v_cvt_pk_bf16_f32 v67, v86, v88
	v_cvt_pk_bf16_f32 v71, v87, v89
	v_cvt_pk_bf16_f32 v72, v92, v90
	s_waitcnt lgkmcnt(12)
	v_cvt_pk_bf16_f32 v73, v94, v96
	s_waitcnt lgkmcnt(10)
	v_cvt_pk_bf16_f32 v74, v98, v100
	s_waitcnt lgkmcnt(8)
	v_cvt_pk_bf16_f32 v75, v102, v104
	v_cvt_pk_bf16_f32 v76, v93, v91
	v_cvt_pk_bf16_f32 v77, v95, v97
	v_cvt_pk_bf16_f32 v78, v99, v101
	v_cvt_pk_bf16_f32 v79, v103, v105
	s_waitcnt lgkmcnt(6)
	v_cvt_pk_bf16_f32 v80, v106, v108
	s_waitcnt lgkmcnt(4)
	v_cvt_pk_bf16_f32 v81, v110, v112
	s_waitcnt lgkmcnt(2)
	v_cvt_pk_bf16_f32 v82, v114, v116
	s_waitcnt lgkmcnt(0)
	v_cvt_pk_bf16_f32 v83, v118, v136
	v_cvt_pk_bf16_f32 v84, v107, v109
	v_cvt_pk_bf16_f32 v85, v111, v113
	v_cvt_pk_bf16_f32 v86, v115, v117
	v_cvt_pk_bf16_f32 v87, v119, v137
	global_store_dwordx4 v[122:123], v[56:59], off sc1
	global_store_dwordx4 v[124:125], v[60:63], off sc1
	global_store_dwordx4 v[126:127], v[64:67], off sc1
	global_store_dwordx4 v[128:129], v[68:71], off sc1
	global_store_dwordx4 v[130:131], v[72:75], off sc1
	global_store_dwordx4 v[132:133], v[76:79], off sc1
	global_store_dwordx4 v[134:135], v[80:83], off sc1
	global_store_dwordx4 v[120:121], v[84:87], off sc1
	s_waitcnt lgkmcnt(0)
	s_cbranch_scc1 .LBB0_49

.LBB0_52:
	s_ashr_i32 s6, s9, 31
	s_lshr_b32 s6, s6, 28
	s_add_i32 s6, s9, s6
	s_ashr_i32 s6, s6, 4
	s_lshl_b32 s14, s6, 10
	s_ashr_i32 s7, s6, 31
	s_sub_i32 s14, s12, s14
	s_lshl_b64 s[16:17], s[6:7], 18
	s_waitcnt lgkmcnt(0)
	s_add_u32 s18, s2, s16
	s_addc_u32 s19, s3, s17
	s_ashr_i32 s15, s14, 31
	s_lshl_b64 s[16:17], s[14:15], 2
	s_add_u32 s16, s18, s16
	s_addc_u32 s17, s19, s17
	v_lshl_add_u64 v[56:57], s[16:17], 0, v[52:53]
	v_lshl_add_u64 v[72:73], v[56:57], 0, v[4:5]
	v_lshl_add_u64 v[64:65], v[56:57], 0, v[6:7]
	v_lshl_add_u64 v[66:67], v[56:57], 0, v[8:9]
	v_lshl_add_u64 v[68:69], v[56:57], 0, v[10:11]
	v_lshl_add_u64 v[70:71], v[56:57], 0, v[12:13]
	v_lshl_add_u64 v[76:77], v[56:57], 0, v[14:15]
	v_lshl_add_u64 v[80:81], v[56:57], 0, v[16:17]
	v_lshl_add_u64 v[84:85], v[56:57], 0, v[18:19]
	v_lshl_add_u64 v[88:89], v[56:57], 0, v[20:21]
	v_lshl_add_u64 v[92:93], v[56:57], 0, v[22:23]
	v_lshl_add_u64 v[96:97], v[56:57], 0, v[24:25]
	v_lshl_add_u64 v[100:101], v[56:57], 0, v[26:27]
	v_lshl_add_u64 v[104:105], v[56:57], 0, v[28:29]
	v_lshl_add_u64 v[108:109], v[56:57], 0, v[30:31]
	v_lshl_add_u64 v[112:113], v[56:57], 0, v[32:33]
	v_lshl_add_u64 v[116:117], v[56:57], 0, v[34:35]
	flat_load_dwordx4 v[56:59], v[64:65] nt
	flat_load_dwordx4 v[60:63], v[66:67] nt
	s_nop 0
	flat_load_dwordx4 v[64:67], v[68:69] nt
	s_nop 0
	flat_load_dwordx4 v[68:71], v[70:71] nt
	s_nop 0
	flat_load_dwordx4 v[72:75], v[72:73] nt
	s_nop 0
	flat_load_dwordx4 v[76:79], v[76:77] nt
	s_nop 0
	flat_load_dwordx4 v[80:83], v[80:81] nt
	s_nop 0
	flat_load_dwordx4 v[84:87], v[84:85] nt
	s_nop 0
	flat_load_dwordx4 v[88:91], v[88:89] nt
	s_nop 0
	flat_load_dwordx4 v[92:95], v[92:93] nt
	s_nop 0
	flat_load_dwordx4 v[96:99], v[96:97] nt
	s_nop 0
	flat_load_dwordx4 v[100:103], v[100:101] nt
	s_nop 0
	flat_load_dwordx4 v[104:107], v[104:105] nt
	s_nop 0
	flat_load_dwordx4 v[108:111], v[108:109] nt
	s_nop 0
	flat_load_dwordx4 v[112:115], v[112:113] nt
	s_nop 0
	flat_load_dwordx4 v[116:119], v[116:117] nt
	v_add_u32_e32 v136, 0x410, v55
	v_add_u32_e32 v137, 0x418, v55
	v_add_u32_e32 v138, 0x820, v55
	v_add_u32_e32 v139, 0x828, v55
	v_add_u32_e32 v140, 0xc30, v55
	v_add_u32_e32 v141, 0xc38, v55
	v_add_u32_e32 v142, 0x1040, v55
	v_add_u32_e32 v143, 0x1048, v55
	v_add_u32_e32 v144, 0x1450, v55
	v_add_u32_e32 v145, 0x1458, v55
	v_add_u32_e32 v146, 0x1860, v55
	v_add_u32_e32 v147, 0x1868, v55
	v_add_u32_e32 v148, 0x1c70, v55
	v_add_u32_e32 v149, 0x1c78, v55
	v_add_u32_e32 v150, 0x2080, v55
	v_add_u32_e32 v151, 0x2088, v55
	v_add_u32_e32 v152, 0x2490, v55
	v_add_u32_e32 v153, 0x2498, v55
	v_add_u32_e32 v154, 0x28a0, v55
	v_add_u32_e32 v155, 0x28a8, v55
	v_add_u32_e32 v156, 0x2cb0, v55
	v_add_u32_e32 v157, 0x2cb8, v55
	v_add_u32_e32 v158, 0x30c0, v55
	v_add_u32_e32 v159, 0x30c8, v55
	v_add_u32_e32 v160, 0x34d0, v55
	v_add_u32_e32 v161, 0x34d8, v55
	v_add_u32_e32 v162, 0x38e0, v55
	v_add_u32_e32 v163, 0x38e8, v55
	v_add_u32_e32 v164, 0x3cf0, v55
	v_add_u32_e32 v165, 0x3cf8, v55
	s_lshl_b64 s[6:7], s[6:7], 17
	s_add_u32 s16, s10, s6
	v_add_u32_e32 v166, 0x400, v54
	s_addc_u32 s17, s11, s7
	s_lshl_b64 s[6:7], s[14:15], 7
	s_add_u32 s6, s16, s6
	s_addc_u32 s7, s17, s7
	v_lshl_add_u64 v[120:121], s[6:7], 0, v[2:3]
	v_lshl_add_u64 v[122:123], v[120:121], 0, v[36:37]
	v_lshl_add_u64 v[124:125], v[120:121], 0, v[38:39]
	v_lshl_add_u64 v[126:127], v[120:121], 0, v[40:41]
	v_lshl_add_u64 v[128:129], v[120:121], 0, v[42:43]
	v_lshl_add_u64 v[130:131], v[120:121], 0, v[44:45]
	v_lshl_add_u64 v[132:133], v[120:121], 0, v[46:47]
	v_lshl_add_u64 v[134:135], v[120:121], 0, v[48:49]
	v_lshl_add_u64 v[120:121], v[120:121], 0, v[50:51]
	s_add_i32 s9, s9, s80
	s_add_i32 s12, s12, s13
	s_cmp_lt_i32 s9, 32
	s_waitcnt vmcnt(0) lgkmcnt(0)
	ds_write2_b32 v136, v56, v57 offset1:1
	ds_write2_b32 v137, v58, v59 offset1:1
	ds_write2_b32 v138, v60, v61 offset1:1
	ds_write2_b32 v139, v62, v63 offset1:1
	ds_write2_b32 v140, v64, v65 offset1:1
	ds_write2_b32 v141, v66, v67 offset1:1
	ds_write2_b32 v142, v68, v69 offset1:1
	ds_write2_b32 v143, v70, v71 offset1:1
	ds_write2_b32 v55, v72, v73 offset1:1
	ds_write2_b32 v55, v74, v75 offset0:2 offset1:3
	ds_write2_b32 v144, v76, v77 offset1:1
	ds_write2_b32 v145, v78, v79 offset1:1
	ds_write2_b32 v146, v80, v81 offset1:1
	ds_write2_b32 v147, v82, v83 offset1:1
	ds_write2_b32 v148, v84, v85 offset1:1
	ds_write2_b32 v149, v86, v87 offset1:1
	ds_write2_b32 v150, v88, v89 offset1:1
	ds_write2_b32 v151, v90, v91 offset1:1
	ds_write2_b32 v152, v92, v93 offset1:1
	ds_write2_b32 v153, v94, v95 offset1:1
	ds_write2_b32 v154, v96, v97 offset1:1
	ds_write2_b32 v155, v98, v99 offset1:1
	ds_write2_b32 v156, v100, v101 offset1:1
	ds_write2_b32 v157, v102, v103 offset1:1
	ds_write2_b32 v158, v104, v105 offset1:1
	ds_write2_b32 v159, v106, v107 offset1:1
	ds_write2_b32 v160, v108, v109 offset1:1
	ds_write2_b32 v161, v110, v111 offset1:1
	ds_write2_b32 v162, v112, v113 offset1:1
	ds_write2_b32 v163, v114, v115 offset1:1
	ds_write2_b32 v164, v116, v117 offset1:1
	ds_write2_b32 v165, v118, v119 offset1:1
	s_waitcnt lgkmcnt(0)
	ds_read2_b32 v[58:59], v54 offset0:65 offset1:73
	ds_read2_b32 v[60:61], v54 offset1:8
	ds_read2_b32 v[62:63], v54 offset0:130 offset1:138
	ds_read2_b32 v[64:65], v54 offset0:195 offset1:203
	ds_read2_b32 v[66:67], v166 offset0:4 offset1:12
	ds_read2_b32 v[68:69], v166 offset0:69 offset1:77
	ds_read2_b32 v[70:71], v166 offset0:134 offset1:142
	ds_read2_b32 v[72:73], v166 offset0:199 offset1:207
	ds_read2_b32 v[74:75], v54 offset0:81 offset1:89
	ds_read2_b32 v[76:77], v54 offset0:16 offset1:24
	ds_read2_b32 v[78:79], v54 offset0:146 offset1:154
	ds_read2_b32 v[80:81], v54 offset0:211 offset1:219
	ds_read2_b32 v[82:83], v166 offset0:20 offset1:28
	ds_read2_b32 v[84:85], v166 offset0:85 offset1:93
	ds_read2_b32 v[86:87], v166 offset0:150 offset1:158
	ds_read2_b32 v[88:89], v166 offset0:215 offset1:223
	ds_read2_b32 v[90:91], v54 offset0:32 offset1:40
	ds_read2_b32 v[92:93], v54 offset0:97 offset1:105
	ds_read2_b32 v[94:95], v54 offset0:162 offset1:170
	ds_read2_b32 v[96:97], v54 offset0:227 offset1:235
	ds_read2_b32 v[98:99], v166 offset0:36 offset1:44
	ds_read2_b32 v[100:101], v166 offset0:101 offset1:109
	ds_read2_b32 v[102:103], v166 offset0:166 offset1:174
	ds_read2_b32 v[104:105], v166 offset0:231 offset1:239
	ds_read2_b32 v[106:107], v54 offset0:48 offset1:56
	ds_read2_b32 v[108:109], v54 offset0:113 offset1:121
	ds_read2_b32 v[110:111], v54 offset0:178 offset1:186
	ds_read2_b32 v[112:113], v54 offset0:243 offset1:251
	ds_read2_b32 v[114:115], v166 offset0:52 offset1:60
	ds_read2_b32 v[116:117], v166 offset0:117 offset1:125
	ds_read2_b32 v[118:119], v166 offset0:182 offset1:190
	ds_read2_b32 v[136:137], v166 offset0:247 offset1:255
	s_waitcnt lgkmcnt(14)
	v_cvt_pk_bf16_f32 v56, v60, v58
	v_cvt_pk_bf16_f32 v57, v62, v64
	v_cvt_pk_bf16_f32 v60, v61, v59
	v_cvt_pk_bf16_f32 v58, v66, v68
	v_cvt_pk_bf16_f32 v59, v70, v72
	v_cvt_pk_bf16_f32 v61, v63, v65
	v_cvt_pk_bf16_f32 v62, v67, v69
	v_cvt_pk_bf16_f32 v63, v71, v73
	v_cvt_pk_bf16_f32 v64, v76, v74
	v_cvt_pk_bf16_f32 v65, v78, v80
	v_cvt_pk_bf16_f32 v68, v77, v75
	v_cvt_pk_bf16_f32 v69, v79, v81
	v_cvt_pk_bf16_f32 v66, v82, v84
	v_cvt_pk_bf16_f32 v70, v83, v85
	v_cvt_pk_bf16_f32 v67, v86, v88
	v_cvt_pk_bf16_f32 v71, v87, v89
	v_cvt_pk_bf16_f32 v72, v90, v92
	s_waitcnt lgkmcnt(12)
	v_cvt_pk_bf16_f32 v73, v94, v96
	s_waitcnt lgkmcnt(10)
	v_cvt_pk_bf16_f32 v74, v98, v100
	s_waitcnt lgkmcnt(8)
	v_cvt_pk_bf16_f32 v75, v102, v104
	v_cvt_pk_bf16_f32 v76, v91, v93
	v_cvt_pk_bf16_f32 v77, v95, v97
	v_cvt_pk_bf16_f32 v78, v99, v101
	v_cvt_pk_bf16_f32 v79, v103, v105
	s_waitcnt lgkmcnt(6)
	v_cvt_pk_bf16_f32 v80, v106, v108
	s_waitcnt lgkmcnt(4)
	v_cvt_pk_bf16_f32 v81, v110, v112
	s_waitcnt lgkmcnt(2)
	v_cvt_pk_bf16_f32 v82, v114, v116
	s_waitcnt lgkmcnt(0)
	v_cvt_pk_bf16_f32 v83, v118, v136
	v_cvt_pk_bf16_f32 v84, v107, v109
	v_cvt_pk_bf16_f32 v85, v111, v113
	v_cvt_pk_bf16_f32 v86, v115, v117
	v_cvt_pk_bf16_f32 v87, v119, v137
	global_store_dwordx4 v[122:123], v[56:59], off sc1
	global_store_dwordx4 v[124:125], v[60:63], off sc1
	global_store_dwordx4 v[126:127], v[64:67], off sc1
	global_store_dwordx4 v[128:129], v[68:71], off sc1
	global_store_dwordx4 v[130:131], v[72:75], off sc1
	global_store_dwordx4 v[132:133], v[76:79], off sc1
	global_store_dwordx4 v[134:135], v[80:83], off sc1
	global_store_dwordx4 v[120:121], v[84:87], off sc1
	s_waitcnt lgkmcnt(0)
	s_cbranch_scc1 .LBB0_52

.LBB0_58:
	s_mul_hi_i32 s8, s1, 0x66666667
	s_lshr_b32 s9, s8, 31
	s_ashr_i32 s8, s8, 5
	s_add_i32 s8, s8, s9
	s_mul_i32 s9, s8, 0xffffffb0
	s_mul_hi_i32 s11, s8, 0x140000
	s_mul_i32 s12, s8, 0x140000
	s_add_i32 s8, s1, s9
	s_bfe_i32 s9, s8, 0x80000
	s_bfe_u32 s9, s9, 0x4000b
	s_add_i32 s9, s8, s9
	s_bfe_i32 s10, s9, 0x80000
	s_and_b32 s9, s9, 0xf0
	s_sext_i32_i16 s10, s10
	s_sub_i32 s8, s8, s9
	s_sext_i32_i8 s9, s8
	s_lshl_b32 s8, s10, 2
	s_andn2_b32 s8, s8, 63
	s_lshl_b32 s10, s9, 6
	s_waitcnt lgkmcnt(0)
	s_add_u32 s15, s2, s12
	s_mul_i32 s14, s9, 0xa000
	s_addc_u32 s11, s3, s11
	s_ashr_i32 s9, s8, 31
	s_lshl_b64 s[12:13], s[8:9], 12
	s_add_u32 s12, s15, s12
	s_addc_u32 s13, s11, s13
	s_ashr_i32 s11, s10, 31
	s_mul_hi_i32 s16, s10, 0x280
	s_lshl_b64 s[10:11], s[10:11], 2
	s_add_u32 s10, s12, s10
	s_addc_u32 s11, s13, s11
	v_lshl_add_u64 v[56:57], s[10:11], 0, v[2:3]
	v_lshl_add_u64 v[72:73], v[56:57], 0, v[4:5]
	v_lshl_add_u64 v[64:65], v[56:57], 0, v[6:7]
	v_lshl_add_u64 v[66:67], v[56:57], 0, v[8:9]
	v_lshl_add_u64 v[68:69], v[56:57], 0, v[10:11]
	v_lshl_add_u64 v[70:71], v[56:57], 0, v[12:13]
	v_lshl_add_u64 v[76:77], v[56:57], 0, v[14:15]
	v_lshl_add_u64 v[80:81], v[56:57], 0, v[16:17]
	v_lshl_add_u64 v[84:85], v[56:57], 0, v[18:19]
	v_lshl_add_u64 v[88:89], v[56:57], 0, v[20:21]
	v_lshl_add_u64 v[92:93], v[56:57], 0, v[22:23]
	v_lshl_add_u64 v[96:97], v[56:57], 0, v[24:25]
	v_lshl_add_u64 v[100:101], v[56:57], 0, v[26:27]
	v_lshl_add_u64 v[104:105], v[56:57], 0, v[28:29]
	v_lshl_add_u64 v[108:109], v[56:57], 0, v[30:31]
	v_lshl_add_u64 v[112:113], v[56:57], 0, v[32:33]
	v_lshl_add_u64 v[116:117], v[56:57], 0, v[34:35]
	flat_load_dwordx4 v[56:59], v[64:65] nt
	flat_load_dwordx4 v[60:63], v[66:67] nt
	s_nop 0
	flat_load_dwordx4 v[64:67], v[68:69] nt
	s_nop 0
	flat_load_dwordx4 v[68:71], v[70:71] nt
	s_nop 0
	flat_load_dwordx4 v[72:75], v[72:73] nt
	s_nop 0
	flat_load_dwordx4 v[76:79], v[76:77] nt
	s_nop 0
	flat_load_dwordx4 v[80:83], v[80:81] nt
	s_nop 0
	flat_load_dwordx4 v[84:87], v[84:85] nt
	s_nop 0
	flat_load_dwordx4 v[88:91], v[88:89] nt
	s_nop 0
	flat_load_dwordx4 v[92:95], v[92:93] nt
	s_nop 0
	flat_load_dwordx4 v[96:99], v[96:97] nt
	s_nop 0
	flat_load_dwordx4 v[100:103], v[100:101] nt
	s_nop 0
	flat_load_dwordx4 v[104:107], v[104:105] nt
	s_nop 0
	flat_load_dwordx4 v[108:111], v[108:109] nt
	s_nop 0
	flat_load_dwordx4 v[112:115], v[112:113] nt
	s_nop 0
	flat_load_dwordx4 v[116:119], v[116:117] nt
	v_add_u32_e32 v55, 0x410, v54
	v_add_u32_e32 v136, 0x418, v54
	v_add_u32_e32 v137, 0x820, v54
	v_add_u32_e32 v138, 0x828, v54
	v_add_u32_e32 v139, 0xc30, v54
	v_add_u32_e32 v140, 0xc38, v54
	v_add_u32_e32 v141, 0x1040, v54
	v_add_u32_e32 v142, 0x1048, v54
	v_add_u32_e32 v143, 0x1450, v54
	v_add_u32_e32 v144, 0x1458, v54
	v_add_u32_e32 v145, 0x1860, v54
	v_add_u32_e32 v146, 0x1868, v54
	v_add_u32_e32 v147, 0x1c70, v54
	v_add_u32_e32 v148, 0x1c78, v54
	v_add_u32_e32 v149, 0x2080, v54
	v_add_u32_e32 v150, 0x2088, v54
	v_add_u32_e32 v151, 0x2490, v54
	v_add_u32_e32 v152, 0x2498, v54
	v_add_u32_e32 v153, 0x28a0, v54
	v_add_u32_e32 v154, 0x28a8, v54
	v_add_u32_e32 v155, 0x2cb0, v54
	v_add_u32_e32 v156, 0x2cb8, v54
	v_add_u32_e32 v157, 0x30c0, v54
	v_add_u32_e32 v158, 0x30c8, v54
	v_add_u32_e32 v159, 0x34d0, v54
	v_add_u32_e32 v160, 0x34d8, v54
	v_add_u32_e32 v161, 0x38e0, v54
	v_add_u32_e32 v162, 0x38e8, v54
	v_add_u32_e32 v163, 0x3cf0, v54
	v_add_u32_e32 v164, 0x3cf8, v54
	s_add_u32 s10, s6, s14
	v_add_u32_e32 v165, 0x400, v1
	s_addc_u32 s11, s7, s16
	s_lshl_b64 s[8:9], s[8:9], 1
	s_add_u32 s8, s10, s8
	v_mov_b32_e32 v53, v3
	s_addc_u32 s9, s11, s9
	v_lshl_add_u64 v[120:121], s[8:9], 0, v[52:53]
	v_lshl_add_u64 v[122:123], v[120:121], 0, v[36:37]
	v_lshl_add_u64 v[124:125], v[120:121], 0, v[38:39]
	v_lshl_add_u64 v[126:127], v[120:121], 0, v[40:41]
	v_lshl_add_u64 v[128:129], v[120:121], 0, v[42:43]
	v_lshl_add_u64 v[130:131], v[120:121], 0, v[44:45]
	v_lshl_add_u64 v[132:133], v[120:121], 0, v[46:47]
	v_lshl_add_u64 v[134:135], v[120:121], 0, v[48:49]
	v_lshl_add_u64 v[120:121], v[120:121], 0, v[50:51]
	s_add_i32 s1, s1, s80
	s_cmpk_gt_i32 s1, 0x4f
	s_waitcnt vmcnt(0) lgkmcnt(0)
	ds_write2_b32 v55, v56, v57 offset1:1
	ds_write2_b32 v136, v58, v59 offset1:1
	ds_write2_b32 v137, v60, v61 offset1:1
	ds_write2_b32 v138, v62, v63 offset1:1
	ds_write2_b32 v139, v64, v65 offset1:1
	ds_write2_b32 v140, v66, v67 offset1:1
	ds_write2_b32 v141, v68, v69 offset1:1
	ds_write2_b32 v142, v70, v71 offset1:1
	ds_write2_b32 v54, v72, v73 offset1:1
	ds_write2_b32 v54, v74, v75 offset0:2 offset1:3
	ds_write2_b32 v143, v76, v77 offset1:1
	ds_write2_b32 v144, v78, v79 offset1:1
	ds_write2_b32 v145, v80, v81 offset1:1
	ds_write2_b32 v146, v82, v83 offset1:1
	ds_write2_b32 v147, v84, v85 offset1:1
	ds_write2_b32 v148, v86, v87 offset1:1
	ds_write2_b32 v149, v88, v89 offset1:1
	ds_write2_b32 v150, v90, v91 offset1:1
	ds_write2_b32 v151, v92, v93 offset1:1
	ds_write2_b32 v152, v94, v95 offset1:1
	ds_write2_b32 v153, v96, v97 offset1:1
	ds_write2_b32 v154, v98, v99 offset1:1
	ds_write2_b32 v155, v100, v101 offset1:1
	ds_write2_b32 v156, v102, v103 offset1:1
	ds_write2_b32 v157, v104, v105 offset1:1
	ds_write2_b32 v158, v106, v107 offset1:1
	ds_write2_b32 v159, v108, v109 offset1:1
	ds_write2_b32 v160, v110, v111 offset1:1
	ds_write2_b32 v161, v112, v113 offset1:1
	ds_write2_b32 v162, v114, v115 offset1:1
	ds_write2_b32 v163, v116, v117 offset1:1
	ds_write2_b32 v164, v118, v119 offset1:1
	s_waitcnt lgkmcnt(0)
	ds_read2_b32 v[58:59], v1 offset0:65 offset1:73
	ds_read2_b32 v[60:61], v1 offset1:8
	ds_read2_b32 v[62:63], v1 offset0:130 offset1:138
	ds_read2_b32 v[64:65], v1 offset0:195 offset1:203
	ds_read2_b32 v[66:67], v165 offset0:4 offset1:12
	ds_read2_b32 v[68:69], v165 offset0:69 offset1:77
	ds_read2_b32 v[70:71], v165 offset0:134 offset1:142
	ds_read2_b32 v[72:73], v165 offset0:199 offset1:207
	ds_read2_b32 v[74:75], v1 offset0:81 offset1:89
	ds_read2_b32 v[76:77], v1 offset0:16 offset1:24
	ds_read2_b32 v[78:79], v1 offset0:146 offset1:154
	ds_read2_b32 v[80:81], v1 offset0:211 offset1:219
	ds_read2_b32 v[82:83], v165 offset0:20 offset1:28
	ds_read2_b32 v[84:85], v165 offset0:85 offset1:93
	ds_read2_b32 v[86:87], v165 offset0:150 offset1:158
	ds_read2_b32 v[88:89], v165 offset0:215 offset1:223
	ds_read2_b32 v[90:91], v1 offset0:97 offset1:105
	ds_read2_b32 v[92:93], v1 offset0:32 offset1:40
	ds_read2_b32 v[94:95], v1 offset0:162 offset1:170
	ds_read2_b32 v[96:97], v1 offset0:227 offset1:235
	ds_read2_b32 v[98:99], v165 offset0:36 offset1:44
	ds_read2_b32 v[100:101], v165 offset0:101 offset1:109
	ds_read2_b32 v[102:103], v165 offset0:166 offset1:174
	ds_read2_b32 v[104:105], v165 offset0:231 offset1:239
	ds_read2_b32 v[106:107], v1 offset0:48 offset1:56
	ds_read2_b32 v[108:109], v1 offset0:113 offset1:121
	ds_read2_b32 v[110:111], v1 offset0:178 offset1:186
	ds_read2_b32 v[112:113], v1 offset0:243 offset1:251
	ds_read2_b32 v[114:115], v165 offset0:52 offset1:60
	ds_read2_b32 v[116:117], v165 offset0:117 offset1:125
	ds_read2_b32 v[118:119], v165 offset0:182 offset1:190
	ds_read2_b32 v[136:137], v165 offset0:247 offset1:255
	s_waitcnt lgkmcnt(14)
	v_cvt_pk_bf16_f32 v56, v60, v58
	v_cvt_pk_bf16_f32 v57, v62, v64
	v_cvt_pk_bf16_f32 v60, v61, v59
	v_cvt_pk_bf16_f32 v58, v66, v68
	v_cvt_pk_bf16_f32 v59, v70, v72
	v_cvt_pk_bf16_f32 v61, v63, v65
	v_cvt_pk_bf16_f32 v62, v67, v69
	v_cvt_pk_bf16_f32 v63, v71, v73
	v_cvt_pk_bf16_f32 v64, v76, v74
	v_cvt_pk_bf16_f32 v65, v78, v80
	v_cvt_pk_bf16_f32 v68, v77, v75
	v_cvt_pk_bf16_f32 v69, v79, v81
	v_cvt_pk_bf16_f32 v66, v82, v84
	v_cvt_pk_bf16_f32 v70, v83, v85
	v_cvt_pk_bf16_f32 v67, v86, v88
	v_cvt_pk_bf16_f32 v71, v87, v89
	v_cvt_pk_bf16_f32 v72, v92, v90
	s_waitcnt lgkmcnt(12)
	v_cvt_pk_bf16_f32 v73, v94, v96
	s_waitcnt lgkmcnt(10)
	v_cvt_pk_bf16_f32 v74, v98, v100
	s_waitcnt lgkmcnt(8)
	v_cvt_pk_bf16_f32 v75, v102, v104
	v_cvt_pk_bf16_f32 v76, v93, v91
	v_cvt_pk_bf16_f32 v77, v95, v97
	v_cvt_pk_bf16_f32 v78, v99, v101
	v_cvt_pk_bf16_f32 v79, v103, v105
	s_waitcnt lgkmcnt(6)
	v_cvt_pk_bf16_f32 v80, v106, v108
	s_waitcnt lgkmcnt(4)
	v_cvt_pk_bf16_f32 v81, v110, v112
	s_waitcnt lgkmcnt(2)
	v_cvt_pk_bf16_f32 v82, v114, v116
	s_waitcnt lgkmcnt(0)
	v_cvt_pk_bf16_f32 v83, v118, v136
	v_cvt_pk_bf16_f32 v84, v107, v109
	v_cvt_pk_bf16_f32 v85, v111, v113
	v_cvt_pk_bf16_f32 v86, v115, v117
	v_cvt_pk_bf16_f32 v87, v119, v137
	global_store_dwordx4 v[122:123], v[56:59], off sc1
	global_store_dwordx4 v[124:125], v[60:63], off sc1
	global_store_dwordx4 v[126:127], v[64:67], off sc1
	global_store_dwordx4 v[128:129], v[68:71], off sc1
	global_store_dwordx4 v[130:131], v[72:75], off sc1
	global_store_dwordx4 v[132:133], v[76:79], off sc1
	global_store_dwordx4 v[134:135], v[80:83], off sc1
	global_store_dwordx4 v[120:121], v[84:87], off sc1
	s_waitcnt lgkmcnt(0)
	s_cbranch_scc0 .LBB0_58

.LBB0_231:
	s_mul_hi_i32 s2, s6, 0x15390949
	s_lshr_b32 s3, s2, 31
	s_ashr_i32 s2, s2, 9
	s_add_i32 s3, s2, s3
	s_mul_i32 s2, s3, 0xffffe7e0
	s_add_i32 s2, s6, s2
	s_mul_i32 s4, s2, 0xffffa9c9
	s_lshr_b32 s4, s4, 16
	s_add_i32 s4, s4, s2
	s_sext_i32_i16 s5, s4
	s_ashr_i32 s5, s5, 7
	s_bfe_u32 s4, s4, 0x1000f
	s_add_i32 s4, s5, s4
	s_sext_i32_i16 s5, s4
	s_mulk_i32 s4, 0xc1
	s_sub_i32 s2, s2, s4
	s_sext_i32_i16 s15, s2
	s_lshl_b32 s2, s5, 6
	s_lshl_b32 s4, s15, 6
	s_mul_hi_i32 s16, s3, 0x6080000
	s_mul_i32 s3, s3, 0x6080000
	s_add_u32 s18, s7, s3
	s_addc_u32 s16, s14, s16
	s_ashr_i32 s3, s2, 31
	s_mul_i32 s5, s5, 0x304000
	s_mul_hi_i32 s19, s2, 0xc100
	s_add_u32 s20, s18, s5
	s_addc_u32 s16, s16, s19
	s_ashr_i32 s5, s4, 31
	s_lshl_b64 s[18:19], s[4:5], 2
	s_add_u32 s18, s20, s18
	s_addc_u32 s19, s16, s19
	v_lshl_add_u64 v[0:1], s[18:19], 0, v[96:97]
	v_lshl_add_u64 v[2:3], v[0:1], 0, v[60:61]
	flat_load_dwordx4 v[116:119], v[2:3] nt
	v_lshl_add_u64 v[2:3], v[0:1], 0, v[62:63]
	flat_load_dwordx4 v[56:59], v[2:3] nt
	v_lshl_add_u64 v[2:3], v[0:1], 0, v[64:65]
	flat_load_dwordx4 v[52:55], v[2:3] nt
	v_lshl_add_u64 v[2:3], v[0:1], 0, v[66:67]
	flat_load_dwordx4 v[48:51], v[2:3] nt
	v_lshl_add_u64 v[2:3], v[0:1], 0, v[68:69]
	flat_load_dwordx4 v[44:47], v[2:3] nt
	v_lshl_add_u64 v[2:3], v[0:1], 0, v[70:71]
	flat_load_dwordx4 v[40:43], v[2:3] nt
	v_lshl_add_u64 v[2:3], v[0:1], 0, v[72:73]
	flat_load_dwordx4 v[36:39], v[2:3] nt
	v_lshl_add_u64 v[2:3], v[0:1], 0, v[74:75]
	flat_load_dwordx4 v[32:35], v[2:3] nt
	v_lshl_add_u64 v[2:3], v[0:1], 0, v[76:77]
	flat_load_dwordx4 v[28:31], v[2:3] nt
	v_lshl_add_u64 v[2:3], v[0:1], 0, v[78:79]
	flat_load_dwordx4 v[24:27], v[2:3] nt
	v_lshl_add_u64 v[2:3], v[0:1], 0, v[80:81]
	flat_load_dwordx4 v[20:23], v[2:3] nt
	v_lshl_add_u64 v[2:3], v[0:1], 0, v[82:83]
	flat_load_dwordx4 v[16:19], v[2:3] nt
	v_lshl_add_u64 v[2:3], v[0:1], 0, v[84:85]
	flat_load_dwordx4 v[12:15], v[2:3] nt
	v_lshl_add_u64 v[2:3], v[0:1], 0, v[86:87]
	flat_load_dwordx4 v[8:11], v[2:3] nt
	v_lshl_add_u64 v[2:3], v[0:1], 0, v[88:89]
	flat_load_dwordx4 v[4:7], v[2:3] nt
	v_lshl_add_u64 v[0:1], v[0:1], 0, v[90:91]
	flat_load_dwordx4 v[0:3], v[0:1] nt
	v_add_u32_e32 v111, 0x410, v114
	s_add_i32 s5, s4, 0xc0
	s_cmpk_lt_i32 s15, 0x61
	s_cselect_b32 s4, s4, s5
	s_ashr_i32 s5, s4, 31
	s_lshl_b64 s[4:5], s[4:5], 12
	s_add_u32 s4, s21, s4
	s_addc_u32 s5, s22, s5
	s_lshl_b64 s[2:3], s[2:3], 1
	s_add_u32 s2, s4, s2
	s_addc_u32 s3, s5, s3
	s_add_i32 s6, s6, s80
	s_cmpk_lt_i32 s6, 0x1820
	s_waitcnt vmcnt(0) lgkmcnt(0)
	ds_write2_b32 v114, v116, v117 offset1:1
	ds_write2_b32 v114, v118, v119 offset0:2 offset1:3
	ds_write2_b32 v111, v56, v57 offset1:1
	v_add_u32_e32 v56, 0x418, v114
	ds_write2_b32 v56, v58, v59 offset1:1
	v_add_u32_e32 v56, 0x820, v114
	ds_write2_b32 v56, v52, v53 offset1:1
	v_add_u32_e32 v52, 0x828, v114
	ds_write2_b32 v52, v54, v55 offset1:1
	v_add_u32_e32 v52, 0xc30, v114
	ds_write2_b32 v52, v48, v49 offset1:1
	v_add_u32_e32 v48, 0xc38, v114
	ds_write2_b32 v48, v50, v51 offset1:1
	v_add_u32_e32 v48, 0x1040, v114
	ds_write2_b32 v48, v44, v45 offset1:1
	v_add_u32_e32 v44, 0x1048, v114
	ds_write2_b32 v44, v46, v47 offset1:1
	v_add_u32_e32 v44, 0x1450, v114
	ds_write2_b32 v44, v40, v41 offset1:1
	v_add_u32_e32 v40, 0x1458, v114
	ds_write2_b32 v40, v42, v43 offset1:1
	v_add_u32_e32 v40, 0x1860, v114
	ds_write2_b32 v40, v36, v37 offset1:1
	v_add_u32_e32 v36, 0x1868, v114
	ds_write2_b32 v36, v38, v39 offset1:1
	v_add_u32_e32 v36, 0x1c70, v114
	ds_write2_b32 v36, v32, v33 offset1:1
	v_add_u32_e32 v32, 0x1c78, v114
	ds_write2_b32 v32, v34, v35 offset1:1
	v_add_u32_e32 v32, 0x2080, v114
	ds_write2_b32 v32, v28, v29 offset1:1
	v_add_u32_e32 v28, 0x2088, v114
	ds_write2_b32 v28, v30, v31 offset1:1
	v_add_u32_e32 v28, 0x2490, v114
	ds_write2_b32 v28, v24, v25 offset1:1
	v_add_u32_e32 v24, 0x2498, v114
	ds_write2_b32 v24, v26, v27 offset1:1
	v_add_u32_e32 v24, 0x28a0, v114
	ds_write2_b32 v24, v20, v21 offset1:1
	v_add_u32_e32 v20, 0x28a8, v114
	ds_write2_b32 v20, v22, v23 offset1:1
	v_add_u32_e32 v20, 0x2cb0, v114
	ds_write2_b32 v20, v16, v17 offset1:1
	v_add_u32_e32 v16, 0x2cb8, v114
	ds_write2_b32 v16, v18, v19 offset1:1
	v_add_u32_e32 v16, 0x30c0, v114
	ds_write2_b32 v16, v12, v13 offset1:1
	v_add_u32_e32 v12, 0x30c8, v114
	ds_write2_b32 v12, v14, v15 offset1:1
	v_add_u32_e32 v12, 0x34d0, v114
	ds_write2_b32 v12, v8, v9 offset1:1
	v_add_u32_e32 v8, 0x34d8, v114
	ds_write2_b32 v8, v10, v11 offset1:1
	v_add_u32_e32 v8, 0x38e0, v114
	ds_write2_b32 v8, v4, v5 offset1:1
	v_add_u32_e32 v4, 0x38e8, v114
	ds_write2_b32 v4, v6, v7 offset1:1
	v_add_u32_e32 v4, 0x3cf0, v114
	ds_write2_b32 v4, v0, v1 offset1:1
	v_add_u32_e32 v0, 0x3cf8, v114
	ds_write2_b32 v0, v2, v3 offset1:1
	s_waitcnt lgkmcnt(0)
	ds_read2_b32 v[6:7], v113 offset0:65 offset1:73
	ds_read2_b32 v[8:9], v113 offset1:8
	ds_read2_b32 v[10:11], v113 offset0:130 offset1:138
	ds_read2_b32 v[12:13], v113 offset0:195 offset1:203
	v_mov_b32_e32 v111, v97
	v_lshl_add_u64 v[4:5], s[2:3], 0, v[110:111]
	v_lshl_add_u64 v[22:23], v[4:5], 0, v[92:93]
	s_waitcnt lgkmcnt(2)
	v_cvt_pk_bf16_f32 v0, v8, v6
	v_add_u32_e32 v6, 0x400, v113
	ds_read2_b32 v[14:15], v6 offset0:4 offset1:12
	ds_read2_b32 v[16:17], v6 offset0:69 offset1:77
	ds_read2_b32 v[18:19], v6 offset0:134 offset1:142
	ds_read2_b32 v[20:21], v6 offset0:199 offset1:207
	s_waitcnt lgkmcnt(4)
	v_cvt_pk_bf16_f32 v1, v10, v12
	v_lshl_add_u64 v[24:25], v[4:5], 0, v[98:99]
	s_waitcnt lgkmcnt(2)
	v_cvt_pk_bf16_f32 v2, v14, v16
	s_waitcnt lgkmcnt(0)
	v_cvt_pk_bf16_f32 v3, v18, v20
	global_store_dwordx4 v[22:23], v[0:3], off sc1
	s_nop 1
	v_cvt_pk_bf16_f32 v0, v9, v7
	v_cvt_pk_bf16_f32 v1, v11, v13
	v_cvt_pk_bf16_f32 v2, v15, v17
	v_cvt_pk_bf16_f32 v3, v19, v21
	v_lshl_add_u64 v[8:9], v[4:5], 0, v[94:95]
	global_store_dwordx4 v[8:9], v[0:3], off sc1
	ds_read2_b32 v[8:9], v113 offset0:81 offset1:89
	ds_read2_b32 v[10:11], v113 offset0:16 offset1:24
	ds_read2_b32 v[12:13], v113 offset0:146 offset1:154
	ds_read2_b32 v[14:15], v113 offset0:211 offset1:219
	ds_read2_b32 v[16:17], v6 offset0:20 offset1:28
	ds_read2_b32 v[18:19], v6 offset0:85 offset1:93
	ds_read2_b32 v[20:21], v6 offset0:150 offset1:158
	ds_read2_b32 v[22:23], v6 offset0:215 offset1:223
	s_waitcnt lgkmcnt(6)
	v_cvt_pk_bf16_f32 v0, v10, v8
	s_waitcnt lgkmcnt(4)
	v_cvt_pk_bf16_f32 v1, v12, v14
	s_waitcnt lgkmcnt(2)
	v_cvt_pk_bf16_f32 v2, v16, v18
	s_waitcnt lgkmcnt(0)
	v_cvt_pk_bf16_f32 v3, v20, v22
	global_store_dwordx4 v[24:25], v[0:3], off sc1
	v_lshl_add_u64 v[24:25], v[4:5], 0, v[102:103]
	s_nop 0
	v_cvt_pk_bf16_f32 v0, v11, v9
	v_cvt_pk_bf16_f32 v1, v13, v15
	v_cvt_pk_bf16_f32 v2, v17, v19
	v_cvt_pk_bf16_f32 v3, v21, v23
	v_lshl_add_u64 v[8:9], v[4:5], 0, v[100:101]
	global_store_dwordx4 v[8:9], v[0:3], off sc1
	ds_read2_b32 v[8:9], v113 offset0:32 offset1:40
	ds_read2_b32 v[10:11], v113 offset0:97 offset1:105
	ds_read2_b32 v[12:13], v113 offset0:162 offset1:170
	ds_read2_b32 v[14:15], v113 offset0:227 offset1:235
	ds_read2_b32 v[16:17], v6 offset0:36 offset1:44
	ds_read2_b32 v[18:19], v6 offset0:101 offset1:109
	ds_read2_b32 v[20:21], v6 offset0:166 offset1:174
	ds_read2_b32 v[22:23], v6 offset0:231 offset1:239
	s_waitcnt lgkmcnt(6)
	v_cvt_pk_bf16_f32 v0, v8, v10
	s_waitcnt lgkmcnt(4)
	v_cvt_pk_bf16_f32 v1, v12, v14
	s_waitcnt lgkmcnt(2)
	v_cvt_pk_bf16_f32 v2, v16, v18
	s_waitcnt lgkmcnt(0)
	v_cvt_pk_bf16_f32 v3, v20, v22
	global_store_dwordx4 v[24:25], v[0:3], off sc1
	s_nop 1
	v_cvt_pk_bf16_f32 v0, v9, v11
	v_cvt_pk_bf16_f32 v1, v13, v15
	v_cvt_pk_bf16_f32 v2, v17, v19
	v_cvt_pk_bf16_f32 v3, v21, v23
	v_lshl_add_u64 v[8:9], v[4:5], 0, v[104:105]
	global_store_dwordx4 v[8:9], v[0:3], off sc1
	ds_read2_b32 v[8:9], v113 offset0:48 offset1:56
	ds_read2_b32 v[10:11], v113 offset0:113 offset1:121
	ds_read2_b32 v[12:13], v113 offset0:178 offset1:186
	ds_read2_b32 v[14:15], v113 offset0:243 offset1:251
	ds_read2_b32 v[16:17], v6 offset0:52 offset1:60
	ds_read2_b32 v[18:19], v6 offset0:117 offset1:125
	ds_read2_b32 v[20:21], v6 offset0:182 offset1:190
	ds_read2_b32 v[6:7], v6 offset0:247 offset1:255
	v_lshl_add_u64 v[22:23], v[4:5], 0, v[106:107]
	s_waitcnt lgkmcnt(6)
	v_cvt_pk_bf16_f32 v0, v8, v10
	s_waitcnt lgkmcnt(4)
	v_cvt_pk_bf16_f32 v1, v12, v14
	s_waitcnt lgkmcnt(2)
	v_cvt_pk_bf16_f32 v2, v16, v18
	s_waitcnt lgkmcnt(0)
	v_cvt_pk_bf16_f32 v3, v20, v6
	global_store_dwordx4 v[22:23], v[0:3], off sc1
	v_lshl_add_u64 v[4:5], v[4:5], 0, v[108:109]
	s_nop 0
	v_cvt_pk_bf16_f32 v0, v9, v11
	v_cvt_pk_bf16_f32 v1, v13, v15
	v_cvt_pk_bf16_f32 v2, v17, v19
	v_cvt_pk_bf16_f32 v3, v21, v7
	global_store_dwordx4 v[4:5], v[0:3], off sc1
	s_waitcnt lgkmcnt(0)
	s_cbranch_scc1 .LBB0_231

.LBB0_234:
	s_ashr_i32 s2, s6, 31
	s_lshr_b32 s2, s2, 23
	s_add_i32 s2, s6, s2
	s_ashr_i32 s18, s2, 9
	s_and_b32 s2, s2, 0xfe00
	s_sub_i32 s2, s6, s2
	s_sext_i32_i16 s3, s2
	s_bfe_u32 s3, s3, 0x5001a
	s_add_i32 s3, s2, s3
	s_sext_i32_i16 s4, s3
	s_and_b32 s3, s3, 0xffe0
	s_sub_i32 s2, s2, s3
	s_sext_i32_i16 s3, s2
	s_lshl_b32 s2, s4, 1
	s_ashr_i32 s19, s18, 31
	s_andn2_b32 s2, s2, 63
	s_lshl_b32 s4, s3, 6
	s_lshl_b64 s[18:19], s[18:19], 23
	s_add_u32 s5, s7, s18
	s_addc_u32 s15, s14, s19
	s_ashr_i32 s3, s2, 31
	s_lshl_b64 s[18:19], s[2:3], 13
	s_add_u32 s16, s5, s18
	s_addc_u32 s15, s15, s19
	s_ashr_i32 s5, s4, 31
	s_lshl_b64 s[18:19], s[4:5], 2
	s_add_u32 s18, s16, s18
	s_addc_u32 s19, s15, s19
	v_lshl_add_u64 v[0:1], s[18:19], 0, v[96:97]
	v_lshl_add_u64 v[2:3], v[0:1], 0, v[60:61]
	flat_load_dwordx4 v[116:119], v[2:3] nt
	v_lshl_add_u64 v[2:3], v[0:1], 0, v[62:63]
	flat_load_dwordx4 v[56:59], v[2:3] nt
	v_lshl_add_u64 v[2:3], v[0:1], 0, v[64:65]
	flat_load_dwordx4 v[52:55], v[2:3] nt
	v_lshl_add_u64 v[2:3], v[0:1], 0, v[66:67]
	flat_load_dwordx4 v[48:51], v[2:3] nt
	v_lshl_add_u64 v[2:3], v[0:1], 0, v[68:69]
	flat_load_dwordx4 v[44:47], v[2:3] nt
	v_lshl_add_u64 v[2:3], v[0:1], 0, v[70:71]
	flat_load_dwordx4 v[40:43], v[2:3] nt
	v_lshl_add_u64 v[2:3], v[0:1], 0, v[72:73]
	flat_load_dwordx4 v[36:39], v[2:3] nt
	v_lshl_add_u64 v[2:3], v[0:1], 0, v[74:75]
	flat_load_dwordx4 v[32:35], v[2:3] nt
	v_lshl_add_u64 v[2:3], v[0:1], 0, v[76:77]
	flat_load_dwordx4 v[28:31], v[2:3] nt
	v_lshl_add_u64 v[2:3], v[0:1], 0, v[78:79]
	flat_load_dwordx4 v[24:27], v[2:3] nt
	v_lshl_add_u64 v[2:3], v[0:1], 0, v[80:81]
	flat_load_dwordx4 v[20:23], v[2:3] nt
	v_lshl_add_u64 v[2:3], v[0:1], 0, v[82:83]
	flat_load_dwordx4 v[16:19], v[2:3] nt
	v_lshl_add_u64 v[2:3], v[0:1], 0, v[84:85]
	flat_load_dwordx4 v[12:15], v[2:3] nt
	v_lshl_add_u64 v[2:3], v[0:1], 0, v[86:87]
	flat_load_dwordx4 v[8:11], v[2:3] nt
	v_lshl_add_u64 v[2:3], v[0:1], 0, v[88:89]
	flat_load_dwordx4 v[4:7], v[2:3] nt
	v_lshl_add_u64 v[0:1], v[0:1], 0, v[90:91]
	flat_load_dwordx4 v[0:3], v[0:1] nt
	v_add_u32_e32 v111, 0x410, v114
	s_lshl_b64 s[4:5], s[4:5], 11
	s_add_u32 s4, s20, s4
	s_addc_u32 s5, s21, s5
	s_lshl_b64 s[2:3], s[2:3], 1
	s_add_u32 s2, s4, s2
	s_addc_u32 s3, s5, s3
	s_add_i32 s6, s6, s80
	s_cmpk_lt_i32 s6, 0x200
	s_waitcnt vmcnt(0) lgkmcnt(0)
	ds_write2_b32 v114, v116, v117 offset1:1
	ds_write2_b32 v114, v118, v119 offset0:2 offset1:3
	ds_write2_b32 v111, v56, v57 offset1:1
	v_add_u32_e32 v56, 0x418, v114
	ds_write2_b32 v56, v58, v59 offset1:1
	v_add_u32_e32 v56, 0x820, v114
	ds_write2_b32 v56, v52, v53 offset1:1
	v_add_u32_e32 v52, 0x828, v114
	ds_write2_b32 v52, v54, v55 offset1:1
	v_add_u32_e32 v52, 0xc30, v114
	ds_write2_b32 v52, v48, v49 offset1:1
	v_add_u32_e32 v48, 0xc38, v114
	ds_write2_b32 v48, v50, v51 offset1:1
	v_add_u32_e32 v48, 0x1040, v114
	ds_write2_b32 v48, v44, v45 offset1:1
	v_add_u32_e32 v44, 0x1048, v114
	ds_write2_b32 v44, v46, v47 offset1:1
	v_add_u32_e32 v44, 0x1450, v114
	ds_write2_b32 v44, v40, v41 offset1:1
	v_add_u32_e32 v40, 0x1458, v114
	ds_write2_b32 v40, v42, v43 offset1:1
	v_add_u32_e32 v40, 0x1860, v114
	ds_write2_b32 v40, v36, v37 offset1:1
	v_add_u32_e32 v36, 0x1868, v114
	ds_write2_b32 v36, v38, v39 offset1:1
	v_add_u32_e32 v36, 0x1c70, v114
	ds_write2_b32 v36, v32, v33 offset1:1
	v_add_u32_e32 v32, 0x1c78, v114
	ds_write2_b32 v32, v34, v35 offset1:1
	v_add_u32_e32 v32, 0x2080, v114
	ds_write2_b32 v32, v28, v29 offset1:1
	v_add_u32_e32 v28, 0x2088, v114
	ds_write2_b32 v28, v30, v31 offset1:1
	v_add_u32_e32 v28, 0x2490, v114
	ds_write2_b32 v28, v24, v25 offset1:1
	v_add_u32_e32 v24, 0x2498, v114
	ds_write2_b32 v24, v26, v27 offset1:1
	v_add_u32_e32 v24, 0x28a0, v114
	ds_write2_b32 v24, v20, v21 offset1:1
	v_add_u32_e32 v20, 0x28a8, v114
	ds_write2_b32 v20, v22, v23 offset1:1
	v_add_u32_e32 v20, 0x2cb0, v114
	ds_write2_b32 v20, v16, v17 offset1:1
	v_add_u32_e32 v16, 0x2cb8, v114
	ds_write2_b32 v16, v18, v19 offset1:1
	v_add_u32_e32 v16, 0x30c0, v114
	ds_write2_b32 v16, v12, v13 offset1:1
	v_add_u32_e32 v12, 0x30c8, v114
	ds_write2_b32 v12, v14, v15 offset1:1
	v_add_u32_e32 v12, 0x34d0, v114
	ds_write2_b32 v12, v8, v9 offset1:1
	v_add_u32_e32 v8, 0x34d8, v114
	ds_write2_b32 v8, v10, v11 offset1:1
	v_add_u32_e32 v8, 0x38e0, v114
	ds_write2_b32 v8, v4, v5 offset1:1
	v_add_u32_e32 v4, 0x38e8, v114
	ds_write2_b32 v4, v6, v7 offset1:1
	v_add_u32_e32 v4, 0x3cf0, v114
	ds_write2_b32 v4, v0, v1 offset1:1
	v_add_u32_e32 v0, 0x3cf8, v114
	ds_write2_b32 v0, v2, v3 offset1:1
	s_waitcnt lgkmcnt(0)
	ds_read2_b32 v[6:7], v113 offset0:65 offset1:73
	ds_read2_b32 v[8:9], v113 offset1:8
	ds_read2_b32 v[10:11], v113 offset0:130 offset1:138
	ds_read2_b32 v[12:13], v113 offset0:195 offset1:203
	v_mov_b32_e32 v111, v97
	v_lshl_add_u64 v[4:5], s[2:3], 0, v[110:111]
	v_lshl_add_u64 v[22:23], v[4:5], 0, v[92:93]
	s_waitcnt lgkmcnt(2)
	v_cvt_pk_bf16_f32 v0, v8, v6
	v_add_u32_e32 v6, 0x400, v113
	ds_read2_b32 v[14:15], v6 offset0:4 offset1:12
	ds_read2_b32 v[16:17], v6 offset0:69 offset1:77
	ds_read2_b32 v[18:19], v6 offset0:134 offset1:142
	ds_read2_b32 v[20:21], v6 offset0:199 offset1:207
	s_waitcnt lgkmcnt(4)
	v_cvt_pk_bf16_f32 v1, v10, v12
	v_lshl_add_u64 v[24:25], v[4:5], 0, v[98:99]
	s_waitcnt lgkmcnt(2)
	v_cvt_pk_bf16_f32 v2, v14, v16
	s_waitcnt lgkmcnt(0)
	v_cvt_pk_bf16_f32 v3, v18, v20
	global_store_dwordx4 v[22:23], v[0:3], off sc1
	s_nop 1
	v_cvt_pk_bf16_f32 v0, v9, v7
	v_cvt_pk_bf16_f32 v1, v11, v13
	v_cvt_pk_bf16_f32 v2, v15, v17
	v_cvt_pk_bf16_f32 v3, v19, v21
	v_lshl_add_u64 v[8:9], v[4:5], 0, v[94:95]
	global_store_dwordx4 v[8:9], v[0:3], off sc1
	ds_read2_b32 v[8:9], v113 offset0:81 offset1:89
	ds_read2_b32 v[10:11], v113 offset0:16 offset1:24
	ds_read2_b32 v[12:13], v113 offset0:146 offset1:154
	ds_read2_b32 v[14:15], v113 offset0:211 offset1:219
	ds_read2_b32 v[16:17], v6 offset0:20 offset1:28
	ds_read2_b32 v[18:19], v6 offset0:85 offset1:93
	ds_read2_b32 v[20:21], v6 offset0:150 offset1:158
	ds_read2_b32 v[22:23], v6 offset0:215 offset1:223
	s_waitcnt lgkmcnt(6)
	v_cvt_pk_bf16_f32 v0, v10, v8
	s_waitcnt lgkmcnt(4)
	v_cvt_pk_bf16_f32 v1, v12, v14
	s_waitcnt lgkmcnt(2)
	v_cvt_pk_bf16_f32 v2, v16, v18
	s_waitcnt lgkmcnt(0)
	v_cvt_pk_bf16_f32 v3, v20, v22
	global_store_dwordx4 v[24:25], v[0:3], off sc1
	v_lshl_add_u64 v[24:25], v[4:5], 0, v[102:103]
	s_nop 0
	v_cvt_pk_bf16_f32 v0, v11, v9
	v_cvt_pk_bf16_f32 v1, v13, v15
	v_cvt_pk_bf16_f32 v2, v17, v19
	v_cvt_pk_bf16_f32 v3, v21, v23
	v_lshl_add_u64 v[8:9], v[4:5], 0, v[100:101]
	global_store_dwordx4 v[8:9], v[0:3], off sc1
	ds_read2_b32 v[8:9], v113 offset0:32 offset1:40
	ds_read2_b32 v[10:11], v113 offset0:97 offset1:105
	ds_read2_b32 v[12:13], v113 offset0:162 offset1:170
	ds_read2_b32 v[14:15], v113 offset0:227 offset1:235
	ds_read2_b32 v[16:17], v6 offset0:36 offset1:44
	ds_read2_b32 v[18:19], v6 offset0:101 offset1:109
	ds_read2_b32 v[20:21], v6 offset0:166 offset1:174
	ds_read2_b32 v[22:23], v6 offset0:231 offset1:239
	s_waitcnt lgkmcnt(6)
	v_cvt_pk_bf16_f32 v0, v8, v10
	s_waitcnt lgkmcnt(4)
	v_cvt_pk_bf16_f32 v1, v12, v14
	s_waitcnt lgkmcnt(2)
	v_cvt_pk_bf16_f32 v2, v16, v18
	s_waitcnt lgkmcnt(0)
	v_cvt_pk_bf16_f32 v3, v20, v22
	global_store_dwordx4 v[24:25], v[0:3], off sc1
	s_nop 1
	v_cvt_pk_bf16_f32 v0, v9, v11
	v_cvt_pk_bf16_f32 v1, v13, v15
	v_cvt_pk_bf16_f32 v2, v17, v19
	v_cvt_pk_bf16_f32 v3, v21, v23
	v_lshl_add_u64 v[8:9], v[4:5], 0, v[104:105]
	global_store_dwordx4 v[8:9], v[0:3], off sc1
	ds_read2_b32 v[8:9], v113 offset0:48 offset1:56
	ds_read2_b32 v[10:11], v113 offset0:113 offset1:121
	ds_read2_b32 v[12:13], v113 offset0:178 offset1:186
	ds_read2_b32 v[14:15], v113 offset0:243 offset1:251
	ds_read2_b32 v[16:17], v6 offset0:52 offset1:60
	ds_read2_b32 v[18:19], v6 offset0:117 offset1:125
	ds_read2_b32 v[20:21], v6 offset0:182 offset1:190
	ds_read2_b32 v[6:7], v6 offset0:247 offset1:255
	v_lshl_add_u64 v[22:23], v[4:5], 0, v[106:107]
	s_waitcnt lgkmcnt(6)
	v_cvt_pk_bf16_f32 v0, v8, v10
	s_waitcnt lgkmcnt(4)
	v_cvt_pk_bf16_f32 v1, v12, v14
	s_waitcnt lgkmcnt(2)
	v_cvt_pk_bf16_f32 v2, v16, v18
	s_waitcnt lgkmcnt(0)
	v_cvt_pk_bf16_f32 v3, v20, v6
	global_store_dwordx4 v[22:23], v[0:3], off sc1
	v_lshl_add_u64 v[4:5], v[4:5], 0, v[108:109]
	s_nop 0
	v_cvt_pk_bf16_f32 v0, v9, v11
	v_cvt_pk_bf16_f32 v1, v13, v15
	v_cvt_pk_bf16_f32 v2, v17, v19
	v_cvt_pk_bf16_f32 v3, v21, v7
	global_store_dwordx4 v[4:5], v[0:3], off sc1
	s_waitcnt lgkmcnt(0)
	s_cbranch_scc1 .LBB0_234

.LBB0_237:
	s_ashr_i32 s2, s6, 31
	s_lshr_b32 s2, s2, 23
	s_add_i32 s2, s6, s2
	s_ashr_i32 s18, s2, 9
	s_and_b32 s2, s2, 0xfe00
	s_sub_i32 s2, s6, s2
	s_sext_i32_i16 s3, s2
	s_bfe_u32 s3, s3, 0x5001a
	s_add_i32 s3, s2, s3
	s_sext_i32_i16 s4, s3
	s_and_b32 s3, s3, 0xffe0
	s_sub_i32 s2, s2, s3
	s_sext_i32_i16 s3, s2
	s_lshl_b32 s2, s4, 1
	s_ashr_i32 s19, s18, 31
	s_andn2_b32 s2, s2, 63
	s_lshl_b32 s4, s3, 6
	s_lshl_b64 s[18:19], s[18:19], 23
	s_add_u32 s5, s7, s18
	s_addc_u32 s15, s14, s19
	s_ashr_i32 s3, s2, 31
	s_lshl_b64 s[18:19], s[2:3], 13
	s_add_u32 s16, s5, s18
	s_addc_u32 s15, s15, s19
	s_ashr_i32 s5, s4, 31
	s_lshl_b64 s[18:19], s[4:5], 2
	s_add_u32 s18, s16, s18
	s_addc_u32 s19, s15, s19
	v_lshl_add_u64 v[0:1], s[18:19], 0, v[96:97]
	v_lshl_add_u64 v[2:3], v[0:1], 0, v[60:61]
	flat_load_dwordx4 v[116:119], v[2:3] nt
	v_lshl_add_u64 v[2:3], v[0:1], 0, v[62:63]
	flat_load_dwordx4 v[56:59], v[2:3] nt
	v_lshl_add_u64 v[2:3], v[0:1], 0, v[64:65]
	flat_load_dwordx4 v[52:55], v[2:3] nt
	v_lshl_add_u64 v[2:3], v[0:1], 0, v[66:67]
	flat_load_dwordx4 v[48:51], v[2:3] nt
	v_lshl_add_u64 v[2:3], v[0:1], 0, v[68:69]
	flat_load_dwordx4 v[44:47], v[2:3] nt
	v_lshl_add_u64 v[2:3], v[0:1], 0, v[70:71]
	flat_load_dwordx4 v[40:43], v[2:3] nt
	v_lshl_add_u64 v[2:3], v[0:1], 0, v[72:73]
	flat_load_dwordx4 v[36:39], v[2:3] nt
	v_lshl_add_u64 v[2:3], v[0:1], 0, v[74:75]
	flat_load_dwordx4 v[32:35], v[2:3] nt
	v_lshl_add_u64 v[2:3], v[0:1], 0, v[76:77]
	flat_load_dwordx4 v[28:31], v[2:3] nt
	v_lshl_add_u64 v[2:3], v[0:1], 0, v[78:79]
	flat_load_dwordx4 v[24:27], v[2:3] nt
	v_lshl_add_u64 v[2:3], v[0:1], 0, v[80:81]
	flat_load_dwordx4 v[20:23], v[2:3] nt
	v_lshl_add_u64 v[2:3], v[0:1], 0, v[82:83]
	flat_load_dwordx4 v[16:19], v[2:3] nt
	v_lshl_add_u64 v[2:3], v[0:1], 0, v[84:85]
	flat_load_dwordx4 v[12:15], v[2:3] nt
	v_lshl_add_u64 v[2:3], v[0:1], 0, v[86:87]
	flat_load_dwordx4 v[8:11], v[2:3] nt
	v_lshl_add_u64 v[2:3], v[0:1], 0, v[88:89]
	flat_load_dwordx4 v[4:7], v[2:3] nt
	v_lshl_add_u64 v[0:1], v[0:1], 0, v[90:91]
	flat_load_dwordx4 v[0:3], v[0:1] nt
	v_add_u32_e32 v111, 0x410, v114
	s_lshl_b64 s[4:5], s[4:5], 11
	s_add_u32 s4, s22, s4
	s_addc_u32 s5, s23, s5
	s_lshl_b64 s[2:3], s[2:3], 1
	s_add_u32 s2, s4, s2
	s_addc_u32 s3, s5, s3
	s_add_i32 s6, s6, s80
	s_cmpk_lt_i32 s6, 0x200
	s_waitcnt vmcnt(0) lgkmcnt(0)
	ds_write2_b32 v114, v116, v117 offset1:1
	ds_write2_b32 v114, v118, v119 offset0:2 offset1:3
	ds_write2_b32 v111, v56, v57 offset1:1
	v_add_u32_e32 v56, 0x418, v114
	ds_write2_b32 v56, v58, v59 offset1:1
	v_add_u32_e32 v56, 0x820, v114
	ds_write2_b32 v56, v52, v53 offset1:1
	v_add_u32_e32 v52, 0x828, v114
	ds_write2_b32 v52, v54, v55 offset1:1
	v_add_u32_e32 v52, 0xc30, v114
	ds_write2_b32 v52, v48, v49 offset1:1
	v_add_u32_e32 v48, 0xc38, v114
	ds_write2_b32 v48, v50, v51 offset1:1
	v_add_u32_e32 v48, 0x1040, v114
	ds_write2_b32 v48, v44, v45 offset1:1
	v_add_u32_e32 v44, 0x1048, v114
	ds_write2_b32 v44, v46, v47 offset1:1
	v_add_u32_e32 v44, 0x1450, v114
	ds_write2_b32 v44, v40, v41 offset1:1
	v_add_u32_e32 v40, 0x1458, v114
	ds_write2_b32 v40, v42, v43 offset1:1
	v_add_u32_e32 v40, 0x1860, v114
	ds_write2_b32 v40, v36, v37 offset1:1
	v_add_u32_e32 v36, 0x1868, v114
	ds_write2_b32 v36, v38, v39 offset1:1
	v_add_u32_e32 v36, 0x1c70, v114
	ds_write2_b32 v36, v32, v33 offset1:1
	v_add_u32_e32 v32, 0x1c78, v114
	ds_write2_b32 v32, v34, v35 offset1:1
	v_add_u32_e32 v32, 0x2080, v114
	ds_write2_b32 v32, v28, v29 offset1:1
	v_add_u32_e32 v28, 0x2088, v114
	ds_write2_b32 v28, v30, v31 offset1:1
	v_add_u32_e32 v28, 0x2490, v114
	ds_write2_b32 v28, v24, v25 offset1:1
	v_add_u32_e32 v24, 0x2498, v114
	ds_write2_b32 v24, v26, v27 offset1:1
	v_add_u32_e32 v24, 0x28a0, v114
	ds_write2_b32 v24, v20, v21 offset1:1
	v_add_u32_e32 v20, 0x28a8, v114
	ds_write2_b32 v20, v22, v23 offset1:1
	v_add_u32_e32 v20, 0x2cb0, v114
	ds_write2_b32 v20, v16, v17 offset1:1
	v_add_u32_e32 v16, 0x2cb8, v114
	ds_write2_b32 v16, v18, v19 offset1:1
	v_add_u32_e32 v16, 0x30c0, v114
	ds_write2_b32 v16, v12, v13 offset1:1
	v_add_u32_e32 v12, 0x30c8, v114
	ds_write2_b32 v12, v14, v15 offset1:1
	v_add_u32_e32 v12, 0x34d0, v114
	ds_write2_b32 v12, v8, v9 offset1:1
	v_add_u32_e32 v8, 0x34d8, v114
	ds_write2_b32 v8, v10, v11 offset1:1
	v_add_u32_e32 v8, 0x38e0, v114
	ds_write2_b32 v8, v4, v5 offset1:1
	v_add_u32_e32 v4, 0x38e8, v114
	ds_write2_b32 v4, v6, v7 offset1:1
	v_add_u32_e32 v4, 0x3cf0, v114
	ds_write2_b32 v4, v0, v1 offset1:1
	v_add_u32_e32 v0, 0x3cf8, v114
	ds_write2_b32 v0, v2, v3 offset1:1
	s_waitcnt lgkmcnt(0)
	ds_read2_b32 v[6:7], v113 offset0:65 offset1:73
	ds_read2_b32 v[8:9], v113 offset1:8
	ds_read2_b32 v[10:11], v113 offset0:130 offset1:138
	ds_read2_b32 v[12:13], v113 offset0:195 offset1:203
	v_mov_b32_e32 v111, v97
	v_lshl_add_u64 v[4:5], s[2:3], 0, v[110:111]
	v_lshl_add_u64 v[22:23], v[4:5], 0, v[92:93]
	s_waitcnt lgkmcnt(2)
	v_cvt_pk_bf16_f32 v0, v8, v6
	v_add_u32_e32 v6, 0x400, v113
	ds_read2_b32 v[14:15], v6 offset0:4 offset1:12
	ds_read2_b32 v[16:17], v6 offset0:69 offset1:77
	ds_read2_b32 v[18:19], v6 offset0:134 offset1:142
	ds_read2_b32 v[20:21], v6 offset0:199 offset1:207
	s_waitcnt lgkmcnt(4)
	v_cvt_pk_bf16_f32 v1, v10, v12
	v_lshl_add_u64 v[24:25], v[4:5], 0, v[98:99]
	s_waitcnt lgkmcnt(2)
	v_cvt_pk_bf16_f32 v2, v14, v16
	s_waitcnt lgkmcnt(0)
	v_cvt_pk_bf16_f32 v3, v18, v20
	global_store_dwordx4 v[22:23], v[0:3], off sc1
	s_nop 1
	v_cvt_pk_bf16_f32 v0, v9, v7
	v_cvt_pk_bf16_f32 v1, v11, v13
	v_cvt_pk_bf16_f32 v2, v15, v17
	v_cvt_pk_bf16_f32 v3, v19, v21
	v_lshl_add_u64 v[8:9], v[4:5], 0, v[94:95]
	global_store_dwordx4 v[8:9], v[0:3], off sc1
	ds_read2_b32 v[8:9], v113 offset0:81 offset1:89
	ds_read2_b32 v[10:11], v113 offset0:16 offset1:24
	ds_read2_b32 v[12:13], v113 offset0:146 offset1:154
	ds_read2_b32 v[14:15], v113 offset0:211 offset1:219
	ds_read2_b32 v[16:17], v6 offset0:20 offset1:28
	ds_read2_b32 v[18:19], v6 offset0:85 offset1:93
	ds_read2_b32 v[20:21], v6 offset0:150 offset1:158
	ds_read2_b32 v[22:23], v6 offset0:215 offset1:223
	s_waitcnt lgkmcnt(6)
	v_cvt_pk_bf16_f32 v0, v10, v8
	s_waitcnt lgkmcnt(4)
	v_cvt_pk_bf16_f32 v1, v12, v14
	s_waitcnt lgkmcnt(2)
	v_cvt_pk_bf16_f32 v2, v16, v18
	s_waitcnt lgkmcnt(0)
	v_cvt_pk_bf16_f32 v3, v20, v22
	global_store_dwordx4 v[24:25], v[0:3], off sc1
	v_lshl_add_u64 v[24:25], v[4:5], 0, v[102:103]
	s_nop 0
	v_cvt_pk_bf16_f32 v0, v11, v9
	v_cvt_pk_bf16_f32 v1, v13, v15
	v_cvt_pk_bf16_f32 v2, v17, v19
	v_cvt_pk_bf16_f32 v3, v21, v23
	v_lshl_add_u64 v[8:9], v[4:5], 0, v[100:101]
	global_store_dwordx4 v[8:9], v[0:3], off sc1
	ds_read2_b32 v[8:9], v113 offset0:32 offset1:40
	ds_read2_b32 v[10:11], v113 offset0:97 offset1:105
	ds_read2_b32 v[12:13], v113 offset0:162 offset1:170
	ds_read2_b32 v[14:15], v113 offset0:227 offset1:235
	ds_read2_b32 v[16:17], v6 offset0:36 offset1:44
	ds_read2_b32 v[18:19], v6 offset0:101 offset1:109
	ds_read2_b32 v[20:21], v6 offset0:166 offset1:174
	ds_read2_b32 v[22:23], v6 offset0:231 offset1:239
	s_waitcnt lgkmcnt(6)
	v_cvt_pk_bf16_f32 v0, v8, v10
	s_waitcnt lgkmcnt(4)
	v_cvt_pk_bf16_f32 v1, v12, v14
	s_waitcnt lgkmcnt(2)
	v_cvt_pk_bf16_f32 v2, v16, v18
	s_waitcnt lgkmcnt(0)
	v_cvt_pk_bf16_f32 v3, v20, v22
	global_store_dwordx4 v[24:25], v[0:3], off sc1
	s_nop 1
	v_cvt_pk_bf16_f32 v0, v9, v11
	v_cvt_pk_bf16_f32 v1, v13, v15
	v_cvt_pk_bf16_f32 v2, v17, v19
	v_cvt_pk_bf16_f32 v3, v21, v23
	v_lshl_add_u64 v[8:9], v[4:5], 0, v[104:105]
	global_store_dwordx4 v[8:9], v[0:3], off sc1
	ds_read2_b32 v[8:9], v113 offset0:48 offset1:56
	ds_read2_b32 v[10:11], v113 offset0:113 offset1:121
	ds_read2_b32 v[12:13], v113 offset0:178 offset1:186
	ds_read2_b32 v[14:15], v113 offset0:243 offset1:251
	ds_read2_b32 v[16:17], v6 offset0:52 offset1:60
	ds_read2_b32 v[18:19], v6 offset0:117 offset1:125
	ds_read2_b32 v[20:21], v6 offset0:182 offset1:190
	ds_read2_b32 v[6:7], v6 offset0:247 offset1:255
	v_lshl_add_u64 v[22:23], v[4:5], 0, v[106:107]
	s_waitcnt lgkmcnt(6)
	v_cvt_pk_bf16_f32 v0, v8, v10
	s_waitcnt lgkmcnt(4)
	v_cvt_pk_bf16_f32 v1, v12, v14
	s_waitcnt lgkmcnt(2)
	v_cvt_pk_bf16_f32 v2, v16, v18
	s_waitcnt lgkmcnt(0)
	v_cvt_pk_bf16_f32 v3, v20, v6
	global_store_dwordx4 v[22:23], v[0:3], off sc1
	v_lshl_add_u64 v[4:5], v[4:5], 0, v[108:109]
	s_nop 0
	v_cvt_pk_bf16_f32 v0, v9, v11
	v_cvt_pk_bf16_f32 v1, v13, v15
	v_cvt_pk_bf16_f32 v2, v17, v19
	v_cvt_pk_bf16_f32 v3, v21, v7
	global_store_dwordx4 v[4:5], v[0:3], off sc1
	s_waitcnt lgkmcnt(0)
	s_cbranch_scc1 .LBB0_237
	s_mov_b64 s[4:5], 0x800

.LBB0_241:
	s_ashr_i32 s2, s6, 31
	s_lshr_b32 s2, s2, 23
	s_add_i32 s2, s6, s2
	s_ashr_i32 s18, s2, 9
	s_and_b32 s2, s2, 0xfe00
	s_sub_i32 s2, s6, s2
	s_sext_i32_i16 s3, s2
	s_bfe_u32 s3, s3, 0x5001a
	s_add_i32 s3, s2, s3
	s_sext_i32_i16 s4, s3
	s_and_b32 s3, s3, 0xffe0
	s_sub_i32 s2, s2, s3
	s_sext_i32_i16 s3, s2
	s_lshl_b32 s2, s4, 1
	s_ashr_i32 s19, s18, 31
	s_andn2_b32 s2, s2, 63
	s_lshl_b32 s4, s3, 6
	s_lshl_b64 s[18:19], s[18:19], 23
	s_add_u32 s5, s7, s18
	s_addc_u32 s15, s14, s19
	s_ashr_i32 s3, s2, 31
	s_lshl_b64 s[18:19], s[2:3], 13
	s_add_u32 s16, s5, s18
	s_addc_u32 s15, s15, s19
	s_ashr_i32 s5, s4, 31
	s_lshl_b64 s[18:19], s[4:5], 2
	s_add_u32 s18, s16, s18
	s_addc_u32 s19, s15, s19
	v_lshl_add_u64 v[0:1], s[18:19], 0, v[96:97]
	v_lshl_add_u64 v[2:3], v[0:1], 0, v[60:61]
	flat_load_dwordx4 v[116:119], v[2:3] nt
	v_lshl_add_u64 v[2:3], v[0:1], 0, v[62:63]
	flat_load_dwordx4 v[56:59], v[2:3] nt
	v_lshl_add_u64 v[2:3], v[0:1], 0, v[64:65]
	flat_load_dwordx4 v[52:55], v[2:3] nt
	v_lshl_add_u64 v[2:3], v[0:1], 0, v[66:67]
	flat_load_dwordx4 v[48:51], v[2:3] nt
	v_lshl_add_u64 v[2:3], v[0:1], 0, v[68:69]
	flat_load_dwordx4 v[44:47], v[2:3] nt
	v_lshl_add_u64 v[2:3], v[0:1], 0, v[70:71]
	flat_load_dwordx4 v[40:43], v[2:3] nt
	v_lshl_add_u64 v[2:3], v[0:1], 0, v[72:73]
	flat_load_dwordx4 v[36:39], v[2:3] nt
	v_lshl_add_u64 v[2:3], v[0:1], 0, v[74:75]
	flat_load_dwordx4 v[32:35], v[2:3] nt
	v_lshl_add_u64 v[2:3], v[0:1], 0, v[76:77]
	flat_load_dwordx4 v[28:31], v[2:3] nt
	v_lshl_add_u64 v[2:3], v[0:1], 0, v[78:79]
	flat_load_dwordx4 v[24:27], v[2:3] nt
	v_lshl_add_u64 v[2:3], v[0:1], 0, v[80:81]
	flat_load_dwordx4 v[20:23], v[2:3] nt
	v_lshl_add_u64 v[2:3], v[0:1], 0, v[82:83]
	flat_load_dwordx4 v[16:19], v[2:3] nt
	v_lshl_add_u64 v[2:3], v[0:1], 0, v[84:85]
	flat_load_dwordx4 v[12:15], v[2:3] nt
	v_lshl_add_u64 v[2:3], v[0:1], 0, v[86:87]
	flat_load_dwordx4 v[8:11], v[2:3] nt
	v_lshl_add_u64 v[2:3], v[0:1], 0, v[88:89]
	flat_load_dwordx4 v[4:7], v[2:3] nt
	v_lshl_add_u64 v[0:1], v[0:1], 0, v[90:91]
	flat_load_dwordx4 v[0:3], v[0:1] nt
	v_add_u32_e32 v111, 0x410, v114
	s_lshl_b64 s[4:5], s[4:5], 11
	s_add_u32 s4, s24, s4
	s_addc_u32 s5, s25, s5
	s_lshl_b64 s[2:3], s[2:3], 1
	s_add_u32 s2, s4, s2
	s_addc_u32 s3, s5, s3
	s_add_i32 s6, s6, s80
	s_cmpk_lt_i32 s6, 0x200
	s_waitcnt vmcnt(0) lgkmcnt(0)
	ds_write2_b32 v114, v116, v117 offset1:1
	ds_write2_b32 v114, v118, v119 offset0:2 offset1:3
	ds_write2_b32 v111, v56, v57 offset1:1
	v_add_u32_e32 v56, 0x418, v114
	ds_write2_b32 v56, v58, v59 offset1:1
	v_add_u32_e32 v56, 0x820, v114
	ds_write2_b32 v56, v52, v53 offset1:1
	v_add_u32_e32 v52, 0x828, v114
	ds_write2_b32 v52, v54, v55 offset1:1
	v_add_u32_e32 v52, 0xc30, v114
	ds_write2_b32 v52, v48, v49 offset1:1
	v_add_u32_e32 v48, 0xc38, v114
	ds_write2_b32 v48, v50, v51 offset1:1
	v_add_u32_e32 v48, 0x1040, v114
	ds_write2_b32 v48, v44, v45 offset1:1
	v_add_u32_e32 v44, 0x1048, v114
	ds_write2_b32 v44, v46, v47 offset1:1
	v_add_u32_e32 v44, 0x1450, v114
	ds_write2_b32 v44, v40, v41 offset1:1
	v_add_u32_e32 v40, 0x1458, v114
	ds_write2_b32 v40, v42, v43 offset1:1
	v_add_u32_e32 v40, 0x1860, v114
	ds_write2_b32 v40, v36, v37 offset1:1
	v_add_u32_e32 v36, 0x1868, v114
	ds_write2_b32 v36, v38, v39 offset1:1
	v_add_u32_e32 v36, 0x1c70, v114
	ds_write2_b32 v36, v32, v33 offset1:1
	v_add_u32_e32 v32, 0x1c78, v114
	ds_write2_b32 v32, v34, v35 offset1:1
	v_add_u32_e32 v32, 0x2080, v114
	ds_write2_b32 v32, v28, v29 offset1:1
	v_add_u32_e32 v28, 0x2088, v114
	ds_write2_b32 v28, v30, v31 offset1:1
	v_add_u32_e32 v28, 0x2490, v114
	ds_write2_b32 v28, v24, v25 offset1:1
	v_add_u32_e32 v24, 0x2498, v114
	ds_write2_b32 v24, v26, v27 offset1:1
	v_add_u32_e32 v24, 0x28a0, v114
	ds_write2_b32 v24, v20, v21 offset1:1
	v_add_u32_e32 v20, 0x28a8, v114
	ds_write2_b32 v20, v22, v23 offset1:1
	v_add_u32_e32 v20, 0x2cb0, v114
	ds_write2_b32 v20, v16, v17 offset1:1
	v_add_u32_e32 v16, 0x2cb8, v114
	ds_write2_b32 v16, v18, v19 offset1:1
	v_add_u32_e32 v16, 0x30c0, v114
	ds_write2_b32 v16, v12, v13 offset1:1
	v_add_u32_e32 v12, 0x30c8, v114
	ds_write2_b32 v12, v14, v15 offset1:1
	v_add_u32_e32 v12, 0x34d0, v114
	ds_write2_b32 v12, v8, v9 offset1:1
	v_add_u32_e32 v8, 0x34d8, v114
	ds_write2_b32 v8, v10, v11 offset1:1
	v_add_u32_e32 v8, 0x38e0, v114
	ds_write2_b32 v8, v4, v5 offset1:1
	v_add_u32_e32 v4, 0x38e8, v114
	ds_write2_b32 v4, v6, v7 offset1:1
	v_add_u32_e32 v4, 0x3cf0, v114
	ds_write2_b32 v4, v0, v1 offset1:1
	v_add_u32_e32 v0, 0x3cf8, v114
	ds_write2_b32 v0, v2, v3 offset1:1
	s_waitcnt lgkmcnt(0)
	ds_read2_b32 v[6:7], v113 offset0:65 offset1:73
	ds_read2_b32 v[8:9], v113 offset1:8
	ds_read2_b32 v[10:11], v113 offset0:130 offset1:138
	ds_read2_b32 v[12:13], v113 offset0:195 offset1:203
	v_mov_b32_e32 v111, v97
	v_lshl_add_u64 v[4:5], s[2:3], 0, v[110:111]
	v_lshl_add_u64 v[22:23], v[4:5], 0, v[92:93]
	s_waitcnt lgkmcnt(2)
	v_cvt_pk_bf16_f32 v0, v8, v6
	v_add_u32_e32 v6, 0x400, v113
	ds_read2_b32 v[14:15], v6 offset0:4 offset1:12
	ds_read2_b32 v[16:17], v6 offset0:69 offset1:77
	ds_read2_b32 v[18:19], v6 offset0:134 offset1:142
	ds_read2_b32 v[20:21], v6 offset0:199 offset1:207
	s_waitcnt lgkmcnt(4)
	v_cvt_pk_bf16_f32 v1, v10, v12
	v_lshl_add_u64 v[24:25], v[4:5], 0, v[98:99]
	s_waitcnt lgkmcnt(2)
	v_cvt_pk_bf16_f32 v2, v14, v16
	s_waitcnt lgkmcnt(0)
	v_cvt_pk_bf16_f32 v3, v18, v20
	global_store_dwordx4 v[22:23], v[0:3], off sc1
	s_nop 1
	v_cvt_pk_bf16_f32 v0, v9, v7
	v_cvt_pk_bf16_f32 v1, v11, v13
	v_cvt_pk_bf16_f32 v2, v15, v17
	v_cvt_pk_bf16_f32 v3, v19, v21
	v_lshl_add_u64 v[8:9], v[4:5], 0, v[94:95]
	global_store_dwordx4 v[8:9], v[0:3], off sc1
	ds_read2_b32 v[8:9], v113 offset0:81 offset1:89
	ds_read2_b32 v[10:11], v113 offset0:16 offset1:24
	ds_read2_b32 v[12:13], v113 offset0:146 offset1:154
	ds_read2_b32 v[14:15], v113 offset0:211 offset1:219
	ds_read2_b32 v[16:17], v6 offset0:20 offset1:28
	ds_read2_b32 v[18:19], v6 offset0:85 offset1:93
	ds_read2_b32 v[20:21], v6 offset0:150 offset1:158
	ds_read2_b32 v[22:23], v6 offset0:215 offset1:223
	s_waitcnt lgkmcnt(6)
	v_cvt_pk_bf16_f32 v0, v10, v8
	s_waitcnt lgkmcnt(4)
	v_cvt_pk_bf16_f32 v1, v12, v14
	s_waitcnt lgkmcnt(2)
	v_cvt_pk_bf16_f32 v2, v16, v18
	s_waitcnt lgkmcnt(0)
	v_cvt_pk_bf16_f32 v3, v20, v22
	global_store_dwordx4 v[24:25], v[0:3], off sc1
	v_lshl_add_u64 v[24:25], v[4:5], 0, v[102:103]
	s_nop 0
	v_cvt_pk_bf16_f32 v0, v11, v9
	v_cvt_pk_bf16_f32 v1, v13, v15
	v_cvt_pk_bf16_f32 v2, v17, v19
	v_cvt_pk_bf16_f32 v3, v21, v23
	v_lshl_add_u64 v[8:9], v[4:5], 0, v[100:101]
	global_store_dwordx4 v[8:9], v[0:3], off sc1
	ds_read2_b32 v[8:9], v113 offset0:32 offset1:40
	ds_read2_b32 v[10:11], v113 offset0:97 offset1:105
	ds_read2_b32 v[12:13], v113 offset0:162 offset1:170
	ds_read2_b32 v[14:15], v113 offset0:227 offset1:235
	ds_read2_b32 v[16:17], v6 offset0:36 offset1:44
	ds_read2_b32 v[18:19], v6 offset0:101 offset1:109
	ds_read2_b32 v[20:21], v6 offset0:166 offset1:174
	ds_read2_b32 v[22:23], v6 offset0:231 offset1:239
	s_waitcnt lgkmcnt(6)
	v_cvt_pk_bf16_f32 v0, v8, v10
	s_waitcnt lgkmcnt(4)
	v_cvt_pk_bf16_f32 v1, v12, v14
	s_waitcnt lgkmcnt(2)
	v_cvt_pk_bf16_f32 v2, v16, v18
	s_waitcnt lgkmcnt(0)
	v_cvt_pk_bf16_f32 v3, v20, v22
	global_store_dwordx4 v[24:25], v[0:3], off sc1
	s_nop 1
	v_cvt_pk_bf16_f32 v0, v9, v11
	v_cvt_pk_bf16_f32 v1, v13, v15
	v_cvt_pk_bf16_f32 v2, v17, v19
	v_cvt_pk_bf16_f32 v3, v21, v23
	v_lshl_add_u64 v[8:9], v[4:5], 0, v[104:105]
	global_store_dwordx4 v[8:9], v[0:3], off sc1
	ds_read2_b32 v[8:9], v113 offset0:48 offset1:56
	ds_read2_b32 v[10:11], v113 offset0:113 offset1:121
	ds_read2_b32 v[12:13], v113 offset0:178 offset1:186
	ds_read2_b32 v[14:15], v113 offset0:243 offset1:251
	ds_read2_b32 v[16:17], v6 offset0:52 offset1:60
	ds_read2_b32 v[18:19], v6 offset0:117 offset1:125
	ds_read2_b32 v[20:21], v6 offset0:182 offset1:190
	ds_read2_b32 v[6:7], v6 offset0:247 offset1:255
	v_lshl_add_u64 v[22:23], v[4:5], 0, v[106:107]
	s_waitcnt lgkmcnt(6)
	v_cvt_pk_bf16_f32 v0, v8, v10
	s_waitcnt lgkmcnt(4)
	v_cvt_pk_bf16_f32 v1, v12, v14
	s_waitcnt lgkmcnt(2)
	v_cvt_pk_bf16_f32 v2, v16, v18
	s_waitcnt lgkmcnt(0)
	v_cvt_pk_bf16_f32 v3, v20, v6
	global_store_dwordx4 v[22:23], v[0:3], off sc1
	v_lshl_add_u64 v[4:5], v[4:5], 0, v[108:109]
	s_nop 0
	v_cvt_pk_bf16_f32 v0, v9, v11
	v_cvt_pk_bf16_f32 v1, v13, v15
	v_cvt_pk_bf16_f32 v2, v17, v19
	v_cvt_pk_bf16_f32 v3, v21, v7
	global_store_dwordx4 v[4:5], v[0:3], off sc1
	s_waitcnt lgkmcnt(0)
	s_cbranch_scc1 .LBB0_241
	s_mov_b64 s[4:5], 0x800

.LBB0_245:
	s_ashr_i32 s2, s6, 31
	s_lshr_b32 s2, s2, 22
	s_add_i32 s2, s6, s2
	s_ashr_i32 s18, s2, 10
	s_and_b32 s2, s2, 0xfc00
	s_sub_i32 s2, s6, s2
	s_sext_i32_i16 s3, s2
	s_bfe_u32 s3, s3, 0x5001a
	s_add_i32 s3, s2, s3
	s_sext_i32_i16 s4, s3
	s_and_b32 s3, s3, 0xffe0
	s_sub_i32 s2, s2, s3
	s_sext_i32_i16 s3, s2
	s_lshl_b32 s2, s4, 1
	s_ashr_i32 s19, s18, 31
	s_andn2_b32 s2, s2, 63
	s_lshl_b32 s4, s3, 6
	s_lshl_b64 s[18:19], s[18:19], 24
	s_add_u32 s5, s7, s18
	s_addc_u32 s15, s14, s19
	s_ashr_i32 s3, s2, 31
	s_lshl_b64 s[18:19], s[2:3], 13
	s_add_u32 s16, s5, s18
	s_addc_u32 s15, s15, s19
	s_ashr_i32 s5, s4, 31
	s_lshl_b64 s[18:19], s[4:5], 2
	s_add_u32 s18, s16, s18
	s_addc_u32 s19, s15, s19
	v_lshl_add_u64 v[0:1], s[18:19], 0, v[96:97]
	v_lshl_add_u64 v[2:3], v[0:1], 0, v[60:61]
	flat_load_dwordx4 v[116:119], v[2:3] nt
	v_lshl_add_u64 v[2:3], v[0:1], 0, v[62:63]
	flat_load_dwordx4 v[56:59], v[2:3] nt
	v_lshl_add_u64 v[2:3], v[0:1], 0, v[64:65]
	flat_load_dwordx4 v[52:55], v[2:3] nt
	v_lshl_add_u64 v[2:3], v[0:1], 0, v[66:67]
	flat_load_dwordx4 v[48:51], v[2:3] nt
	v_lshl_add_u64 v[2:3], v[0:1], 0, v[68:69]
	flat_load_dwordx4 v[44:47], v[2:3] nt
	v_lshl_add_u64 v[2:3], v[0:1], 0, v[70:71]
	flat_load_dwordx4 v[40:43], v[2:3] nt
	v_lshl_add_u64 v[2:3], v[0:1], 0, v[72:73]
	flat_load_dwordx4 v[36:39], v[2:3] nt
	v_lshl_add_u64 v[2:3], v[0:1], 0, v[74:75]
	flat_load_dwordx4 v[32:35], v[2:3] nt
	v_lshl_add_u64 v[2:3], v[0:1], 0, v[76:77]
	flat_load_dwordx4 v[28:31], v[2:3] nt
	v_lshl_add_u64 v[2:3], v[0:1], 0, v[78:79]
	flat_load_dwordx4 v[24:27], v[2:3] nt
	v_lshl_add_u64 v[2:3], v[0:1], 0, v[80:81]
	flat_load_dwordx4 v[20:23], v[2:3] nt
	v_lshl_add_u64 v[2:3], v[0:1], 0, v[82:83]
	flat_load_dwordx4 v[16:19], v[2:3] nt
	v_lshl_add_u64 v[2:3], v[0:1], 0, v[84:85]
	flat_load_dwordx4 v[12:15], v[2:3] nt
	v_lshl_add_u64 v[2:3], v[0:1], 0, v[86:87]
	flat_load_dwordx4 v[8:11], v[2:3] nt
	v_lshl_add_u64 v[2:3], v[0:1], 0, v[88:89]
	flat_load_dwordx4 v[4:7], v[2:3] nt
	v_lshl_add_u64 v[0:1], v[0:1], 0, v[90:91]
	flat_load_dwordx4 v[0:3], v[0:1] nt
	v_add_u32_e32 v111, 0x410, v114
	s_lshl_b64 s[4:5], s[4:5], 12
	s_add_u32 s4, s26, s4
	s_addc_u32 s5, s27, s5
	s_lshl_b64 s[2:3], s[2:3], 1
	s_add_u32 s2, s4, s2
	s_addc_u32 s3, s5, s3
	s_add_i32 s6, s6, s80
	s_cmpk_lt_i32 s6, 0x400
	s_waitcnt vmcnt(0) lgkmcnt(0)
	ds_write2_b32 v114, v116, v117 offset1:1
	ds_write2_b32 v114, v118, v119 offset0:2 offset1:3
	ds_write2_b32 v111, v56, v57 offset1:1
	v_add_u32_e32 v56, 0x418, v114
	ds_write2_b32 v56, v58, v59 offset1:1
	v_add_u32_e32 v56, 0x820, v114
	ds_write2_b32 v56, v52, v53 offset1:1
	v_add_u32_e32 v52, 0x828, v114
	ds_write2_b32 v52, v54, v55 offset1:1
	v_add_u32_e32 v52, 0xc30, v114
	ds_write2_b32 v52, v48, v49 offset1:1
	v_add_u32_e32 v48, 0xc38, v114
	ds_write2_b32 v48, v50, v51 offset1:1
	v_add_u32_e32 v48, 0x1040, v114
	ds_write2_b32 v48, v44, v45 offset1:1
	v_add_u32_e32 v44, 0x1048, v114
	ds_write2_b32 v44, v46, v47 offset1:1
	v_add_u32_e32 v44, 0x1450, v114
	ds_write2_b32 v44, v40, v41 offset1:1
	v_add_u32_e32 v40, 0x1458, v114
	ds_write2_b32 v40, v42, v43 offset1:1
	v_add_u32_e32 v40, 0x1860, v114
	ds_write2_b32 v40, v36, v37 offset1:1
	v_add_u32_e32 v36, 0x1868, v114
	ds_write2_b32 v36, v38, v39 offset1:1
	v_add_u32_e32 v36, 0x1c70, v114
	ds_write2_b32 v36, v32, v33 offset1:1
	v_add_u32_e32 v32, 0x1c78, v114
	ds_write2_b32 v32, v34, v35 offset1:1
	v_add_u32_e32 v32, 0x2080, v114
	ds_write2_b32 v32, v28, v29 offset1:1
	v_add_u32_e32 v28, 0x2088, v114
	ds_write2_b32 v28, v30, v31 offset1:1
	v_add_u32_e32 v28, 0x2490, v114
	ds_write2_b32 v28, v24, v25 offset1:1
	v_add_u32_e32 v24, 0x2498, v114
	ds_write2_b32 v24, v26, v27 offset1:1
	v_add_u32_e32 v24, 0x28a0, v114
	ds_write2_b32 v24, v20, v21 offset1:1
	v_add_u32_e32 v20, 0x28a8, v114
	ds_write2_b32 v20, v22, v23 offset1:1
	v_add_u32_e32 v20, 0x2cb0, v114
	ds_write2_b32 v20, v16, v17 offset1:1
	v_add_u32_e32 v16, 0x2cb8, v114
	ds_write2_b32 v16, v18, v19 offset1:1
	v_add_u32_e32 v16, 0x30c0, v114
	ds_write2_b32 v16, v12, v13 offset1:1
	v_add_u32_e32 v12, 0x30c8, v114
	ds_write2_b32 v12, v14, v15 offset1:1
	v_add_u32_e32 v12, 0x34d0, v114
	ds_write2_b32 v12, v8, v9 offset1:1
	v_add_u32_e32 v8, 0x34d8, v114
	ds_write2_b32 v8, v10, v11 offset1:1
	v_add_u32_e32 v8, 0x38e0, v114
	ds_write2_b32 v8, v4, v5 offset1:1
	v_add_u32_e32 v4, 0x38e8, v114
	ds_write2_b32 v4, v6, v7 offset1:1
	v_add_u32_e32 v4, 0x3cf0, v114
	ds_write2_b32 v4, v0, v1 offset1:1
	v_add_u32_e32 v0, 0x3cf8, v114
	ds_write2_b32 v0, v2, v3 offset1:1
	s_waitcnt lgkmcnt(0)
	ds_read2_b32 v[6:7], v113 offset0:65 offset1:73
	ds_read2_b32 v[8:9], v113 offset1:8
	ds_read2_b32 v[10:11], v113 offset0:130 offset1:138
	ds_read2_b32 v[12:13], v113 offset0:195 offset1:203
	v_mov_b32_e32 v111, v97
	v_lshl_add_u64 v[4:5], s[2:3], 0, v[110:111]
	v_lshl_add_u64 v[22:23], v[4:5], 0, v[92:93]
	s_waitcnt lgkmcnt(2)
	v_cvt_pk_bf16_f32 v0, v8, v6
	v_add_u32_e32 v6, 0x400, v113
	ds_read2_b32 v[14:15], v6 offset0:4 offset1:12
	ds_read2_b32 v[16:17], v6 offset0:69 offset1:77
	ds_read2_b32 v[18:19], v6 offset0:134 offset1:142
	ds_read2_b32 v[20:21], v6 offset0:199 offset1:207
	s_waitcnt lgkmcnt(4)
	v_cvt_pk_bf16_f32 v1, v10, v12
	v_lshl_add_u64 v[24:25], v[4:5], 0, v[98:99]
	s_waitcnt lgkmcnt(2)
	v_cvt_pk_bf16_f32 v2, v14, v16
	s_waitcnt lgkmcnt(0)
	v_cvt_pk_bf16_f32 v3, v18, v20
	global_store_dwordx4 v[22:23], v[0:3], off sc1
	s_nop 1
	v_cvt_pk_bf16_f32 v0, v9, v7
	v_cvt_pk_bf16_f32 v1, v11, v13
	v_cvt_pk_bf16_f32 v2, v15, v17
	v_cvt_pk_bf16_f32 v3, v19, v21
	v_lshl_add_u64 v[8:9], v[4:5], 0, v[94:95]
	global_store_dwordx4 v[8:9], v[0:3], off sc1
	ds_read2_b32 v[8:9], v113 offset0:81 offset1:89
	ds_read2_b32 v[10:11], v113 offset0:16 offset1:24
	ds_read2_b32 v[12:13], v113 offset0:146 offset1:154
	ds_read2_b32 v[14:15], v113 offset0:211 offset1:219
	ds_read2_b32 v[16:17], v6 offset0:20 offset1:28
	ds_read2_b32 v[18:19], v6 offset0:85 offset1:93
	ds_read2_b32 v[20:21], v6 offset0:150 offset1:158
	ds_read2_b32 v[22:23], v6 offset0:215 offset1:223
	s_waitcnt lgkmcnt(6)
	v_cvt_pk_bf16_f32 v0, v10, v8
	s_waitcnt lgkmcnt(4)
	v_cvt_pk_bf16_f32 v1, v12, v14
	s_waitcnt lgkmcnt(2)
	v_cvt_pk_bf16_f32 v2, v16, v18
	s_waitcnt lgkmcnt(0)
	v_cvt_pk_bf16_f32 v3, v20, v22
	global_store_dwordx4 v[24:25], v[0:3], off sc1
	v_lshl_add_u64 v[24:25], v[4:5], 0, v[102:103]
	s_nop 0
	v_cvt_pk_bf16_f32 v0, v11, v9
	v_cvt_pk_bf16_f32 v1, v13, v15
	v_cvt_pk_bf16_f32 v2, v17, v19
	v_cvt_pk_bf16_f32 v3, v21, v23
	v_lshl_add_u64 v[8:9], v[4:5], 0, v[100:101]
	global_store_dwordx4 v[8:9], v[0:3], off sc1
	ds_read2_b32 v[8:9], v113 offset0:32 offset1:40
	ds_read2_b32 v[10:11], v113 offset0:97 offset1:105
	ds_read2_b32 v[12:13], v113 offset0:162 offset1:170
	ds_read2_b32 v[14:15], v113 offset0:227 offset1:235
	ds_read2_b32 v[16:17], v6 offset0:36 offset1:44
	ds_read2_b32 v[18:19], v6 offset0:101 offset1:109
	ds_read2_b32 v[20:21], v6 offset0:166 offset1:174
	ds_read2_b32 v[22:23], v6 offset0:231 offset1:239
	s_waitcnt lgkmcnt(6)
	v_cvt_pk_bf16_f32 v0, v8, v10
	s_waitcnt lgkmcnt(4)
	v_cvt_pk_bf16_f32 v1, v12, v14
	s_waitcnt lgkmcnt(2)
	v_cvt_pk_bf16_f32 v2, v16, v18
	s_waitcnt lgkmcnt(0)
	v_cvt_pk_bf16_f32 v3, v20, v22
	global_store_dwordx4 v[24:25], v[0:3], off sc1
	s_nop 1
	v_cvt_pk_bf16_f32 v0, v9, v11
	v_cvt_pk_bf16_f32 v1, v13, v15
	v_cvt_pk_bf16_f32 v2, v17, v19
	v_cvt_pk_bf16_f32 v3, v21, v23
	v_lshl_add_u64 v[8:9], v[4:5], 0, v[104:105]
	global_store_dwordx4 v[8:9], v[0:3], off sc1
	ds_read2_b32 v[8:9], v113 offset0:48 offset1:56
	ds_read2_b32 v[10:11], v113 offset0:113 offset1:121
	ds_read2_b32 v[12:13], v113 offset0:178 offset1:186
	ds_read2_b32 v[14:15], v113 offset0:243 offset1:251
	ds_read2_b32 v[16:17], v6 offset0:52 offset1:60
	ds_read2_b32 v[18:19], v6 offset0:117 offset1:125
	ds_read2_b32 v[20:21], v6 offset0:182 offset1:190
	ds_read2_b32 v[6:7], v6 offset0:247 offset1:255
	v_lshl_add_u64 v[22:23], v[4:5], 0, v[106:107]
	s_waitcnt lgkmcnt(6)
	v_cvt_pk_bf16_f32 v0, v8, v10
	s_waitcnt lgkmcnt(4)
	v_cvt_pk_bf16_f32 v1, v12, v14
	s_waitcnt lgkmcnt(2)
	v_cvt_pk_bf16_f32 v2, v16, v18
	s_waitcnt lgkmcnt(0)
	v_cvt_pk_bf16_f32 v3, v20, v6
	global_store_dwordx4 v[22:23], v[0:3], off sc1
	v_lshl_add_u64 v[4:5], v[4:5], 0, v[108:109]
	s_nop 0
	v_cvt_pk_bf16_f32 v0, v9, v11
	v_cvt_pk_bf16_f32 v1, v13, v15
	v_cvt_pk_bf16_f32 v2, v17, v19
	v_cvt_pk_bf16_f32 v3, v21, v7
	global_store_dwordx4 v[4:5], v[0:3], off sc1
	s_waitcnt lgkmcnt(0)
	s_cbranch_scc1 .LBB0_245
	s_mov_b64 s[4:5], 0x800

.LBB0_249:
	s_ashr_i32 s2, s14, 31
	s_lshr_b32 s2, s2, 28
	s_add_i32 s3, s14, s2
	s_ashr_i32 s2, s3, 4
	s_and_b32 s3, s3, 0xfff0
	s_sub_i32 s3, s14, s3
	s_bfe_i32 s4, s3, 0x80000
	s_bfe_u32 s4, s4, 0x2000d
	s_add_i32 s4, s3, s4
	s_bfe_i32 s5, s4, 0x80000
	s_and_b32 s4, s4, 0xfc
	s_sub_i32 s3, s3, s4
	s_sext_i32_i16 s5, s5
	s_sext_i32_i8 s3, s3
	s_lshl_b32 s4, s5, 4
	s_lshl_b32 s6, s3, 6
	s_ashr_i32 s3, s2, 31
	s_andn2_b32 s4, s4, 63
	s_lshl_b64 s[18:19], s[2:3], 18
	s_add_u32 s7, s15, s18
	s_addc_u32 s20, s16, s19
	s_ashr_i32 s5, s4, 31
	s_lshl_b64 s[18:19], s[4:5], 10
	s_add_u32 s21, s7, s18
	s_addc_u32 s20, s20, s19
	s_ashr_i32 s7, s6, 31
	s_lshl_b64 s[18:19], s[6:7], 2
	s_add_u32 s18, s21, s18
	s_addc_u32 s19, s20, s19
	v_lshl_add_u64 v[0:1], s[18:19], 0, v[96:97]
	v_lshl_add_u64 v[2:3], v[0:1], 0, v[60:61]
	flat_load_dwordx4 v[116:119], v[2:3] nt
	v_lshl_add_u64 v[2:3], v[0:1], 0, v[62:63]
	flat_load_dwordx4 v[56:59], v[2:3] nt
	v_lshl_add_u64 v[2:3], v[0:1], 0, v[64:65]
	flat_load_dwordx4 v[52:55], v[2:3] nt
	v_lshl_add_u64 v[2:3], v[0:1], 0, v[66:67]
	flat_load_dwordx4 v[48:51], v[2:3] nt
	v_lshl_add_u64 v[2:3], v[0:1], 0, v[68:69]
	flat_load_dwordx4 v[44:47], v[2:3] nt
	v_lshl_add_u64 v[2:3], v[0:1], 0, v[70:71]
	flat_load_dwordx4 v[40:43], v[2:3] nt
	v_lshl_add_u64 v[2:3], v[0:1], 0, v[72:73]
	flat_load_dwordx4 v[36:39], v[2:3] nt
	v_lshl_add_u64 v[2:3], v[0:1], 0, v[74:75]
	flat_load_dwordx4 v[32:35], v[2:3] nt
	v_lshl_add_u64 v[2:3], v[0:1], 0, v[76:77]
	flat_load_dwordx4 v[28:31], v[2:3] nt
	v_lshl_add_u64 v[2:3], v[0:1], 0, v[78:79]
	flat_load_dwordx4 v[24:27], v[2:3] nt
	v_lshl_add_u64 v[2:3], v[0:1], 0, v[80:81]
	flat_load_dwordx4 v[20:23], v[2:3] nt
	v_lshl_add_u64 v[2:3], v[0:1], 0, v[82:83]
	flat_load_dwordx4 v[16:19], v[2:3] nt
	v_lshl_add_u64 v[2:3], v[0:1], 0, v[84:85]
	flat_load_dwordx4 v[12:15], v[2:3] nt
	v_lshl_add_u64 v[2:3], v[0:1], 0, v[86:87]
	flat_load_dwordx4 v[8:11], v[2:3] nt
	v_lshl_add_u64 v[2:3], v[0:1], 0, v[88:89]
	flat_load_dwordx4 v[4:7], v[2:3] nt
	v_lshl_add_u64 v[0:1], v[0:1], 0, v[90:91]
	flat_load_dwordx4 v[0:3], v[0:1] nt
	v_add_u32_e32 v111, 0x410, v114
	s_lshl_b64 s[2:3], s[2:3], 17
	s_add_u32 s18, s28, s2
	s_addc_u32 s19, s29, s3
	s_lshl_b64 s[2:3], s[6:7], 9
	s_add_u32 s6, s18, s2
	s_addc_u32 s7, s19, s3
	s_lshl_b64 s[2:3], s[4:5], 1
	s_add_u32 s2, s6, s2
	s_addc_u32 s3, s7, s3
	s_add_i32 s14, s14, s80
	s_cmp_lt_i32 s14, 64
	s_waitcnt vmcnt(0) lgkmcnt(0)
	ds_write2_b32 v114, v116, v117 offset1:1
	ds_write2_b32 v114, v118, v119 offset0:2 offset1:3
	ds_write2_b32 v111, v56, v57 offset1:1
	v_add_u32_e32 v56, 0x418, v114
	ds_write2_b32 v56, v58, v59 offset1:1
	v_add_u32_e32 v56, 0x820, v114
	ds_write2_b32 v56, v52, v53 offset1:1
	v_add_u32_e32 v52, 0x828, v114
	ds_write2_b32 v52, v54, v55 offset1:1
	v_add_u32_e32 v52, 0xc30, v114
	ds_write2_b32 v52, v48, v49 offset1:1
	v_add_u32_e32 v48, 0xc38, v114
	ds_write2_b32 v48, v50, v51 offset1:1
	v_add_u32_e32 v48, 0x1040, v114
	ds_write2_b32 v48, v44, v45 offset1:1
	v_add_u32_e32 v44, 0x1048, v114
	ds_write2_b32 v44, v46, v47 offset1:1
	v_add_u32_e32 v44, 0x1450, v114
	ds_write2_b32 v44, v40, v41 offset1:1
	v_add_u32_e32 v40, 0x1458, v114
	ds_write2_b32 v40, v42, v43 offset1:1
	v_add_u32_e32 v40, 0x1860, v114
	ds_write2_b32 v40, v36, v37 offset1:1
	v_add_u32_e32 v36, 0x1868, v114
	ds_write2_b32 v36, v38, v39 offset1:1
	v_add_u32_e32 v36, 0x1c70, v114
	ds_write2_b32 v36, v32, v33 offset1:1
	v_add_u32_e32 v32, 0x1c78, v114
	ds_write2_b32 v32, v34, v35 offset1:1
	v_add_u32_e32 v32, 0x2080, v114
	ds_write2_b32 v32, v28, v29 offset1:1
	v_add_u32_e32 v28, 0x2088, v114
	ds_write2_b32 v28, v30, v31 offset1:1
	v_add_u32_e32 v28, 0x2490, v114
	ds_write2_b32 v28, v24, v25 offset1:1
	v_add_u32_e32 v24, 0x2498, v114
	ds_write2_b32 v24, v26, v27 offset1:1
	v_add_u32_e32 v24, 0x28a0, v114
	ds_write2_b32 v24, v20, v21 offset1:1
	v_add_u32_e32 v20, 0x28a8, v114
	ds_write2_b32 v20, v22, v23 offset1:1
	v_add_u32_e32 v20, 0x2cb0, v114
	ds_write2_b32 v20, v16, v17 offset1:1
	v_add_u32_e32 v16, 0x2cb8, v114
	ds_write2_b32 v16, v18, v19 offset1:1
	v_add_u32_e32 v16, 0x30c0, v114
	ds_write2_b32 v16, v12, v13 offset1:1
	v_add_u32_e32 v12, 0x30c8, v114
	ds_write2_b32 v12, v14, v15 offset1:1
	v_add_u32_e32 v12, 0x34d0, v114
	ds_write2_b32 v12, v8, v9 offset1:1
	v_add_u32_e32 v8, 0x34d8, v114
	ds_write2_b32 v8, v10, v11 offset1:1
	v_add_u32_e32 v8, 0x38e0, v114
	ds_write2_b32 v8, v4, v5 offset1:1
	v_add_u32_e32 v4, 0x38e8, v114
	ds_write2_b32 v4, v6, v7 offset1:1
	v_add_u32_e32 v4, 0x3cf0, v114
	ds_write2_b32 v4, v0, v1 offset1:1
	v_add_u32_e32 v0, 0x3cf8, v114
	ds_write2_b32 v0, v2, v3 offset1:1
	s_waitcnt lgkmcnt(0)
	ds_read2_b32 v[6:7], v113 offset0:65 offset1:73
	ds_read2_b32 v[8:9], v113 offset1:8
	ds_read2_b32 v[10:11], v113 offset0:130 offset1:138
	ds_read2_b32 v[12:13], v113 offset0:195 offset1:203
	v_mov_b32_e32 v111, v97
	v_lshl_add_u64 v[4:5], s[2:3], 0, v[110:111]
	v_lshl_add_u64 v[22:23], v[4:5], 0, v[92:93]
	s_waitcnt lgkmcnt(2)
	v_cvt_pk_bf16_f32 v0, v8, v6
	v_add_u32_e32 v6, 0x400, v113
	ds_read2_b32 v[14:15], v6 offset0:4 offset1:12
	ds_read2_b32 v[16:17], v6 offset0:69 offset1:77
	ds_read2_b32 v[18:19], v6 offset0:134 offset1:142
	ds_read2_b32 v[20:21], v6 offset0:199 offset1:207
	s_waitcnt lgkmcnt(4)
	v_cvt_pk_bf16_f32 v1, v10, v12
	v_lshl_add_u64 v[24:25], v[4:5], 0, v[98:99]
	s_waitcnt lgkmcnt(2)
	v_cvt_pk_bf16_f32 v2, v14, v16
	s_waitcnt lgkmcnt(0)
	v_cvt_pk_bf16_f32 v3, v18, v20
	global_store_dwordx4 v[22:23], v[0:3], off sc1
	s_nop 1
	v_cvt_pk_bf16_f32 v0, v9, v7
	v_cvt_pk_bf16_f32 v1, v11, v13
	v_cvt_pk_bf16_f32 v2, v15, v17
	v_cvt_pk_bf16_f32 v3, v19, v21
	v_lshl_add_u64 v[8:9], v[4:5], 0, v[94:95]
	global_store_dwordx4 v[8:9], v[0:3], off sc1
	ds_read2_b32 v[8:9], v113 offset0:81 offset1:89
	ds_read2_b32 v[10:11], v113 offset0:16 offset1:24
	ds_read2_b32 v[12:13], v113 offset0:146 offset1:154
	ds_read2_b32 v[14:15], v113 offset0:211 offset1:219
	ds_read2_b32 v[16:17], v6 offset0:20 offset1:28
	ds_read2_b32 v[18:19], v6 offset0:85 offset1:93
	ds_read2_b32 v[20:21], v6 offset0:150 offset1:158
	ds_read2_b32 v[22:23], v6 offset0:215 offset1:223
	s_waitcnt lgkmcnt(6)
	v_cvt_pk_bf16_f32 v0, v10, v8
	s_waitcnt lgkmcnt(4)
	v_cvt_pk_bf16_f32 v1, v12, v14
	s_waitcnt lgkmcnt(2)
	v_cvt_pk_bf16_f32 v2, v16, v18
	s_waitcnt lgkmcnt(0)
	v_cvt_pk_bf16_f32 v3, v20, v22
	global_store_dwordx4 v[24:25], v[0:3], off sc1
	v_lshl_add_u64 v[24:25], v[4:5], 0, v[102:103]
	s_nop 0
	v_cvt_pk_bf16_f32 v0, v11, v9
	v_cvt_pk_bf16_f32 v1, v13, v15
	v_cvt_pk_bf16_f32 v2, v17, v19
	v_cvt_pk_bf16_f32 v3, v21, v23
	v_lshl_add_u64 v[8:9], v[4:5], 0, v[100:101]
	global_store_dwordx4 v[8:9], v[0:3], off sc1
	ds_read2_b32 v[8:9], v113 offset0:97 offset1:105
	ds_read2_b32 v[10:11], v113 offset0:32 offset1:40
	ds_read2_b32 v[12:13], v113 offset0:162 offset1:170
	ds_read2_b32 v[14:15], v113 offset0:227 offset1:235
	ds_read2_b32 v[16:17], v6 offset0:36 offset1:44
	ds_read2_b32 v[18:19], v6 offset0:101 offset1:109
	ds_read2_b32 v[20:21], v6 offset0:166 offset1:174
	ds_read2_b32 v[22:23], v6 offset0:231 offset1:239
	s_waitcnt lgkmcnt(6)
	v_cvt_pk_bf16_f32 v0, v10, v8
	s_waitcnt lgkmcnt(4)
	v_cvt_pk_bf16_f32 v1, v12, v14
	s_waitcnt lgkmcnt(2)
	v_cvt_pk_bf16_f32 v2, v16, v18
	s_waitcnt lgkmcnt(0)
	v_cvt_pk_bf16_f32 v3, v20, v22
	global_store_dwordx4 v[24:25], v[0:3], off sc1
	s_nop 1
	v_cvt_pk_bf16_f32 v0, v11, v9
	v_cvt_pk_bf16_f32 v1, v13, v15
	v_cvt_pk_bf16_f32 v2, v17, v19
	v_cvt_pk_bf16_f32 v3, v21, v23
	v_lshl_add_u64 v[8:9], v[4:5], 0, v[104:105]
	global_store_dwordx4 v[8:9], v[0:3], off sc1
	ds_read2_b32 v[8:9], v113 offset0:48 offset1:56
	ds_read2_b32 v[10:11], v113 offset0:113 offset1:121
	ds_read2_b32 v[12:13], v113 offset0:178 offset1:186
	ds_read2_b32 v[14:15], v113 offset0:243 offset1:251
	ds_read2_b32 v[16:17], v6 offset0:52 offset1:60
	ds_read2_b32 v[18:19], v6 offset0:117 offset1:125
	ds_read2_b32 v[20:21], v6 offset0:182 offset1:190
	ds_read2_b32 v[6:7], v6 offset0:247 offset1:255
	v_lshl_add_u64 v[22:23], v[4:5], 0, v[106:107]
	s_waitcnt lgkmcnt(6)
	v_cvt_pk_bf16_f32 v0, v8, v10
	s_waitcnt lgkmcnt(4)
	v_cvt_pk_bf16_f32 v1, v12, v14
	s_waitcnt lgkmcnt(2)
	v_cvt_pk_bf16_f32 v2, v16, v18
	s_waitcnt lgkmcnt(0)
	v_cvt_pk_bf16_f32 v3, v20, v6
	global_store_dwordx4 v[22:23], v[0:3], off sc1
	v_lshl_add_u64 v[4:5], v[4:5], 0, v[108:109]
	s_nop 0
	v_cvt_pk_bf16_f32 v0, v9, v11
	v_cvt_pk_bf16_f32 v1, v13, v15
	v_cvt_pk_bf16_f32 v2, v17, v19
	v_cvt_pk_bf16_f32 v3, v21, v7
	global_store_dwordx4 v[4:5], v[0:3], off sc1
	s_waitcnt lgkmcnt(0)
	s_cbranch_scc1 .LBB0_249
	s_mov_b64 s[4:5], 0x800

.LBB0_253:
	s_ashr_i32 s2, s6, 31
	s_lshr_b32 s2, s2, 28
	s_add_i32 s2, s6, s2
	s_ashr_i32 s4, s2, 4
	s_lshl_b32 s2, s4, 10
	s_ashr_i32 s5, s4, 31
	s_sub_i32 s2, s15, s2
	s_lshl_b64 s[18:19], s[4:5], 18
	s_add_u32 s20, s7, s18
	s_addc_u32 s21, s14, s19
	s_ashr_i32 s3, s2, 31
	s_lshl_b64 s[18:19], s[2:3], 2
	s_add_u32 s18, s20, s18
	s_addc_u32 s19, s21, s19
	v_lshl_add_u64 v[0:1], s[18:19], 0, v[96:97]
	v_lshl_add_u64 v[2:3], v[0:1], 0, v[52:53]
	flat_load_dwordx4 v[106:109], v[2:3] nt
	v_lshl_add_u64 v[2:3], v[0:1], 0, v[54:55]
	flat_load_dwordx4 v[114:117], v[2:3] nt
	v_lshl_add_u64 v[2:3], v[0:1], 0, v[56:57]
	flat_load_dwordx4 v[118:121], v[2:3] nt
	v_lshl_add_u64 v[2:3], v[0:1], 0, v[58:59]
	flat_load_dwordx4 v[48:51], v[2:3] nt
	v_lshl_add_u64 v[2:3], v[0:1], 0, v[60:61]
	flat_load_dwordx4 v[44:47], v[2:3] nt
	v_lshl_add_u64 v[2:3], v[0:1], 0, v[62:63]
	flat_load_dwordx4 v[40:43], v[2:3] nt
	v_lshl_add_u64 v[2:3], v[0:1], 0, v[64:65]
	flat_load_dwordx4 v[36:39], v[2:3] nt
	v_lshl_add_u64 v[2:3], v[0:1], 0, v[66:67]
	flat_load_dwordx4 v[32:35], v[2:3] nt
	v_lshl_add_u64 v[2:3], v[0:1], 0, v[68:69]
	flat_load_dwordx4 v[28:31], v[2:3] nt
	v_lshl_add_u64 v[2:3], v[0:1], 0, v[70:71]
	flat_load_dwordx4 v[24:27], v[2:3] nt
	v_lshl_add_u64 v[2:3], v[0:1], 0, v[72:73]
	flat_load_dwordx4 v[20:23], v[2:3] nt
	v_lshl_add_u64 v[2:3], v[0:1], 0, v[74:75]
	flat_load_dwordx4 v[16:19], v[2:3] nt
	v_lshl_add_u64 v[2:3], v[0:1], 0, v[76:77]
	flat_load_dwordx4 v[12:15], v[2:3] nt
	v_lshl_add_u64 v[2:3], v[0:1], 0, v[78:79]
	flat_load_dwordx4 v[8:11], v[2:3] nt
	v_lshl_add_u64 v[2:3], v[0:1], 0, v[80:81]
	flat_load_dwordx4 v[4:7], v[2:3] nt
	v_lshl_add_u64 v[0:1], v[0:1], 0, v[82:83]
	flat_load_dwordx4 v[0:3], v[0:1] nt
	v_add_u32_e32 v103, 0x410, v105
	s_lshl_b64 s[4:5], s[4:5], 17
	s_add_u32 s4, s30, s4
	s_addc_u32 s5, s31, s5
	s_lshl_b64 s[2:3], s[2:3], 7
	s_add_u32 s2, s4, s2
	s_addc_u32 s3, s5, s3
	s_add_i32 s6, s6, s80
	s_add_i32 s15, s15, s16
	s_cmp_lt_i32 s6, 32
	s_waitcnt vmcnt(0) lgkmcnt(0)
	ds_write2_b32 v105, v106, v107 offset1:1
	ds_write2_b32 v105, v108, v109 offset0:2 offset1:3
	ds_write2_b32 v103, v114, v115 offset1:1
	v_add_u32_e32 v103, 0x418, v105
	ds_write2_b32 v103, v116, v117 offset1:1
	v_add_u32_e32 v103, 0x820, v105
	ds_write2_b32 v103, v118, v119 offset1:1
	v_add_u32_e32 v103, 0x828, v105
	ds_write2_b32 v103, v120, v121 offset1:1
	v_add_u32_e32 v103, 0xc30, v105
	ds_write2_b32 v103, v48, v49 offset1:1
	v_add_u32_e32 v48, 0xc38, v105
	ds_write2_b32 v48, v50, v51 offset1:1
	v_add_u32_e32 v48, 0x1040, v105
	ds_write2_b32 v48, v44, v45 offset1:1
	v_add_u32_e32 v44, 0x1048, v105
	ds_write2_b32 v44, v46, v47 offset1:1
	v_add_u32_e32 v44, 0x1450, v105
	ds_write2_b32 v44, v40, v41 offset1:1
	v_add_u32_e32 v40, 0x1458, v105
	ds_write2_b32 v40, v42, v43 offset1:1
	v_add_u32_e32 v40, 0x1860, v105
	ds_write2_b32 v40, v36, v37 offset1:1
	v_add_u32_e32 v36, 0x1868, v105
	ds_write2_b32 v36, v38, v39 offset1:1
	v_add_u32_e32 v36, 0x1c70, v105
	ds_write2_b32 v36, v32, v33 offset1:1
	v_add_u32_e32 v32, 0x1c78, v105
	ds_write2_b32 v32, v34, v35 offset1:1
	v_add_u32_e32 v32, 0x2080, v105
	ds_write2_b32 v32, v28, v29 offset1:1
	v_add_u32_e32 v28, 0x2088, v105
	ds_write2_b32 v28, v30, v31 offset1:1
	v_add_u32_e32 v28, 0x2490, v105
	ds_write2_b32 v28, v24, v25 offset1:1
	v_add_u32_e32 v24, 0x2498, v105
	ds_write2_b32 v24, v26, v27 offset1:1
	v_add_u32_e32 v24, 0x28a0, v105
	ds_write2_b32 v24, v20, v21 offset1:1
	v_add_u32_e32 v20, 0x28a8, v105
	ds_write2_b32 v20, v22, v23 offset1:1
	v_add_u32_e32 v20, 0x2cb0, v105
	ds_write2_b32 v20, v16, v17 offset1:1
	v_add_u32_e32 v16, 0x2cb8, v105
	ds_write2_b32 v16, v18, v19 offset1:1
	v_add_u32_e32 v16, 0x30c0, v105
	ds_write2_b32 v16, v12, v13 offset1:1
	v_add_u32_e32 v12, 0x30c8, v105
	ds_write2_b32 v12, v14, v15 offset1:1
	v_add_u32_e32 v12, 0x34d0, v105
	ds_write2_b32 v12, v8, v9 offset1:1
	v_add_u32_e32 v8, 0x34d8, v105
	ds_write2_b32 v8, v10, v11 offset1:1
	v_add_u32_e32 v8, 0x38e0, v105
	ds_write2_b32 v8, v4, v5 offset1:1
	v_add_u32_e32 v4, 0x38e8, v105
	ds_write2_b32 v4, v6, v7 offset1:1
	v_add_u32_e32 v4, 0x3cf0, v105
	ds_write2_b32 v4, v0, v1 offset1:1
	v_add_u32_e32 v0, 0x3cf8, v105
	ds_write2_b32 v0, v2, v3 offset1:1
	s_waitcnt lgkmcnt(0)
	v_add_u32_e32 v24, 0x400, v104
	ds_read2_b32 v[6:7], v104 offset0:65 offset1:73
	ds_read2_b32 v[8:9], v104 offset1:8
	ds_read2_b32 v[10:11], v104 offset0:130 offset1:138
	ds_read2_b32 v[12:13], v104 offset0:195 offset1:203
	ds_read2_b32 v[14:15], v24 offset0:4 offset1:12
	ds_read2_b32 v[16:17], v24 offset0:69 offset1:77
	ds_read2_b32 v[18:19], v24 offset0:134 offset1:142
	ds_read2_b32 v[20:21], v24 offset0:199 offset1:207
	v_mov_b32_e32 v103, v97
	v_lshl_add_u64 v[4:5], s[2:3], 0, v[102:103]
	s_waitcnt lgkmcnt(6)
	v_cvt_pk_bf16_f32 v0, v8, v6
	s_waitcnt lgkmcnt(4)
	v_cvt_pk_bf16_f32 v1, v10, v12
	s_waitcnt lgkmcnt(2)
	v_cvt_pk_bf16_f32 v2, v14, v16
	s_waitcnt lgkmcnt(0)
	v_cvt_pk_bf16_f32 v3, v18, v20
	v_lshl_add_u64 v[22:23], v[4:5], 0, v[84:85]
	global_store_dwordx4 v[22:23], v[0:3], off sc1
	v_lshl_add_u64 v[22:23], v[4:5], 0, v[88:89]
	s_nop 0
	v_cvt_pk_bf16_f32 v0, v9, v7
	v_cvt_pk_bf16_f32 v1, v11, v13
	v_cvt_pk_bf16_f32 v2, v15, v17
	v_cvt_pk_bf16_f32 v3, v19, v21
	v_lshl_add_u64 v[6:7], v[4:5], 0, v[86:87]
	global_store_dwordx4 v[6:7], v[0:3], off sc1
	ds_read2_b32 v[6:7], v104 offset0:81 offset1:89
	ds_read2_b32 v[8:9], v104 offset0:16 offset1:24
	ds_read2_b32 v[10:11], v104 offset0:146 offset1:154
	ds_read2_b32 v[12:13], v104 offset0:211 offset1:219
	ds_read2_b32 v[14:15], v24 offset0:20 offset1:28
	ds_read2_b32 v[16:17], v24 offset0:85 offset1:93
	ds_read2_b32 v[18:19], v24 offset0:150 offset1:158
	ds_read2_b32 v[20:21], v24 offset0:215 offset1:223
	s_waitcnt lgkmcnt(6)
	v_cvt_pk_bf16_f32 v0, v8, v6
	s_waitcnt lgkmcnt(4)
	v_cvt_pk_bf16_f32 v1, v10, v12
	s_waitcnt lgkmcnt(2)
	v_cvt_pk_bf16_f32 v2, v14, v16
	s_waitcnt lgkmcnt(0)
	v_cvt_pk_bf16_f32 v3, v18, v20
	global_store_dwordx4 v[22:23], v[0:3], off sc1
	v_lshl_add_u64 v[22:23], v[4:5], 0, v[92:93]
	s_nop 0
	v_cvt_pk_bf16_f32 v0, v9, v7
	v_cvt_pk_bf16_f32 v1, v11, v13
	v_cvt_pk_bf16_f32 v2, v15, v17
	v_cvt_pk_bf16_f32 v3, v19, v21
	v_lshl_add_u64 v[6:7], v[4:5], 0, v[90:91]
	global_store_dwordx4 v[6:7], v[0:3], off sc1
	ds_read2_b32 v[6:7], v104 offset0:32 offset1:40
	ds_read2_b32 v[8:9], v104 offset0:97 offset1:105
	ds_read2_b32 v[10:11], v104 offset0:162 offset1:170
	ds_read2_b32 v[12:13], v104 offset0:227 offset1:235
	ds_read2_b32 v[14:15], v24 offset0:36 offset1:44
	ds_read2_b32 v[16:17], v24 offset0:101 offset1:109
	ds_read2_b32 v[18:19], v24 offset0:166 offset1:174
	ds_read2_b32 v[20:21], v24 offset0:231 offset1:239
	s_waitcnt lgkmcnt(6)
	v_cvt_pk_bf16_f32 v0, v6, v8
	s_waitcnt lgkmcnt(4)
	v_cvt_pk_bf16_f32 v1, v10, v12
	s_waitcnt lgkmcnt(2)
	v_cvt_pk_bf16_f32 v2, v14, v16
	s_waitcnt lgkmcnt(0)
	v_cvt_pk_bf16_f32 v3, v18, v20
	global_store_dwordx4 v[22:23], v[0:3], off sc1
	v_lshl_add_u64 v[22:23], v[4:5], 0, v[98:99]
	s_nop 0
	v_cvt_pk_bf16_f32 v0, v7, v9
	v_cvt_pk_bf16_f32 v1, v11, v13
	v_cvt_pk_bf16_f32 v2, v15, v17
	v_cvt_pk_bf16_f32 v3, v19, v21
	v_lshl_add_u64 v[6:7], v[4:5], 0, v[94:95]
	global_store_dwordx4 v[6:7], v[0:3], off sc1
	ds_read2_b32 v[6:7], v104 offset0:48 offset1:56
	ds_read2_b32 v[8:9], v104 offset0:113 offset1:121
	ds_read2_b32 v[10:11], v104 offset0:178 offset1:186
	ds_read2_b32 v[12:13], v104 offset0:243 offset1:251
	ds_read2_b32 v[14:15], v24 offset0:52 offset1:60
	ds_read2_b32 v[16:17], v24 offset0:117 offset1:125
	ds_read2_b32 v[18:19], v24 offset0:182 offset1:190
	ds_read2_b32 v[20:21], v24 offset0:247 offset1:255
	v_lshl_add_u64 v[4:5], v[4:5], 0, v[100:101]
	s_waitcnt lgkmcnt(6)
	v_cvt_pk_bf16_f32 v0, v6, v8
	s_waitcnt lgkmcnt(4)
	v_cvt_pk_bf16_f32 v1, v10, v12
	s_waitcnt lgkmcnt(2)
	v_cvt_pk_bf16_f32 v2, v14, v16
	s_waitcnt lgkmcnt(0)
	v_cvt_pk_bf16_f32 v3, v18, v20
	global_store_dwordx4 v[22:23], v[0:3], off sc1
	s_nop 1
	v_cvt_pk_bf16_f32 v0, v7, v9
	v_cvt_pk_bf16_f32 v1, v11, v13
	v_cvt_pk_bf16_f32 v2, v15, v17
	v_cvt_pk_bf16_f32 v3, v19, v21
	global_store_dwordx4 v[4:5], v[0:3], off sc1
	s_waitcnt lgkmcnt(0)
	s_cbranch_scc1 .LBB0_253

.LBB0_256:
	s_ashr_i32 s2, s6, 31
	s_lshr_b32 s2, s2, 28
	s_add_i32 s2, s6, s2
	s_ashr_i32 s4, s2, 4
	s_lshl_b32 s2, s4, 10
	s_ashr_i32 s5, s4, 31
	s_sub_i32 s2, s15, s2
	s_lshl_b64 s[18:19], s[4:5], 18
	s_add_u32 s20, s7, s18
	s_addc_u32 s21, s14, s19
	s_ashr_i32 s3, s2, 31
	s_lshl_b64 s[18:19], s[2:3], 2
	s_add_u32 s18, s20, s18
	s_addc_u32 s19, s21, s19
	v_lshl_add_u64 v[0:1], s[18:19], 0, v[96:97]
	v_lshl_add_u64 v[2:3], v[0:1], 0, v[52:53]
	flat_load_dwordx4 v[106:109], v[2:3] nt
	v_lshl_add_u64 v[2:3], v[0:1], 0, v[54:55]
	flat_load_dwordx4 v[114:117], v[2:3] nt
	v_lshl_add_u64 v[2:3], v[0:1], 0, v[56:57]
	flat_load_dwordx4 v[118:121], v[2:3] nt
	v_lshl_add_u64 v[2:3], v[0:1], 0, v[58:59]
	flat_load_dwordx4 v[48:51], v[2:3] nt
	v_lshl_add_u64 v[2:3], v[0:1], 0, v[60:61]
	flat_load_dwordx4 v[44:47], v[2:3] nt
	v_lshl_add_u64 v[2:3], v[0:1], 0, v[62:63]
	flat_load_dwordx4 v[40:43], v[2:3] nt
	v_lshl_add_u64 v[2:3], v[0:1], 0, v[64:65]
	flat_load_dwordx4 v[36:39], v[2:3] nt
	v_lshl_add_u64 v[2:3], v[0:1], 0, v[66:67]
	flat_load_dwordx4 v[32:35], v[2:3] nt
	v_lshl_add_u64 v[2:3], v[0:1], 0, v[68:69]
	flat_load_dwordx4 v[28:31], v[2:3] nt
	v_lshl_add_u64 v[2:3], v[0:1], 0, v[70:71]
	flat_load_dwordx4 v[24:27], v[2:3] nt
	v_lshl_add_u64 v[2:3], v[0:1], 0, v[72:73]
	flat_load_dwordx4 v[20:23], v[2:3] nt
	v_lshl_add_u64 v[2:3], v[0:1], 0, v[74:75]
	flat_load_dwordx4 v[16:19], v[2:3] nt
	v_lshl_add_u64 v[2:3], v[0:1], 0, v[76:77]
	flat_load_dwordx4 v[12:15], v[2:3] nt
	v_lshl_add_u64 v[2:3], v[0:1], 0, v[78:79]
	flat_load_dwordx4 v[8:11], v[2:3] nt
	v_lshl_add_u64 v[2:3], v[0:1], 0, v[80:81]
	flat_load_dwordx4 v[4:7], v[2:3] nt
	v_lshl_add_u64 v[0:1], v[0:1], 0, v[82:83]
	flat_load_dwordx4 v[0:3], v[0:1] nt
	v_add_u32_e32 v103, 0x410, v105
	s_lshl_b64 s[4:5], s[4:5], 17
	s_add_u32 s4, s35, s4
	s_addc_u32 s5, s38, s5
	s_lshl_b64 s[2:3], s[2:3], 7
	s_add_u32 s2, s4, s2
	s_addc_u32 s3, s5, s3
	s_add_i32 s6, s6, s80
	s_add_i32 s15, s15, s16
	s_cmp_lt_i32 s6, 32
	s_waitcnt vmcnt(0) lgkmcnt(0)
	ds_write2_b32 v105, v106, v107 offset1:1
	ds_write2_b32 v105, v108, v109 offset0:2 offset1:3
	ds_write2_b32 v103, v114, v115 offset1:1
	v_add_u32_e32 v103, 0x418, v105
	ds_write2_b32 v103, v116, v117 offset1:1
	v_add_u32_e32 v103, 0x820, v105
	ds_write2_b32 v103, v118, v119 offset1:1
	v_add_u32_e32 v103, 0x828, v105
	ds_write2_b32 v103, v120, v121 offset1:1
	v_add_u32_e32 v103, 0xc30, v105
	ds_write2_b32 v103, v48, v49 offset1:1
	v_add_u32_e32 v48, 0xc38, v105
	ds_write2_b32 v48, v50, v51 offset1:1
	v_add_u32_e32 v48, 0x1040, v105
	ds_write2_b32 v48, v44, v45 offset1:1
	v_add_u32_e32 v44, 0x1048, v105
	ds_write2_b32 v44, v46, v47 offset1:1
	v_add_u32_e32 v44, 0x1450, v105
	ds_write2_b32 v44, v40, v41 offset1:1
	v_add_u32_e32 v40, 0x1458, v105
	ds_write2_b32 v40, v42, v43 offset1:1
	v_add_u32_e32 v40, 0x1860, v105
	ds_write2_b32 v40, v36, v37 offset1:1
	v_add_u32_e32 v36, 0x1868, v105
	ds_write2_b32 v36, v38, v39 offset1:1
	v_add_u32_e32 v36, 0x1c70, v105
	ds_write2_b32 v36, v32, v33 offset1:1
	v_add_u32_e32 v32, 0x1c78, v105
	ds_write2_b32 v32, v34, v35 offset1:1
	v_add_u32_e32 v32, 0x2080, v105
	ds_write2_b32 v32, v28, v29 offset1:1
	v_add_u32_e32 v28, 0x2088, v105
	ds_write2_b32 v28, v30, v31 offset1:1
	v_add_u32_e32 v28, 0x2490, v105
	ds_write2_b32 v28, v24, v25 offset1:1
	v_add_u32_e32 v24, 0x2498, v105
	ds_write2_b32 v24, v26, v27 offset1:1
	v_add_u32_e32 v24, 0x28a0, v105
	ds_write2_b32 v24, v20, v21 offset1:1
	v_add_u32_e32 v20, 0x28a8, v105
	ds_write2_b32 v20, v22, v23 offset1:1
	v_add_u32_e32 v20, 0x2cb0, v105
	ds_write2_b32 v20, v16, v17 offset1:1
	v_add_u32_e32 v16, 0x2cb8, v105
	ds_write2_b32 v16, v18, v19 offset1:1
	v_add_u32_e32 v16, 0x30c0, v105
	ds_write2_b32 v16, v12, v13 offset1:1
	v_add_u32_e32 v12, 0x30c8, v105
	ds_write2_b32 v12, v14, v15 offset1:1
	v_add_u32_e32 v12, 0x34d0, v105
	ds_write2_b32 v12, v8, v9 offset1:1
	v_add_u32_e32 v8, 0x34d8, v105
	ds_write2_b32 v8, v10, v11 offset1:1
	v_add_u32_e32 v8, 0x38e0, v105
	ds_write2_b32 v8, v4, v5 offset1:1
	v_add_u32_e32 v4, 0x38e8, v105
	ds_write2_b32 v4, v6, v7 offset1:1
	v_add_u32_e32 v4, 0x3cf0, v105
	ds_write2_b32 v4, v0, v1 offset1:1
	v_add_u32_e32 v0, 0x3cf8, v105
	ds_write2_b32 v0, v2, v3 offset1:1
	s_waitcnt lgkmcnt(0)
	v_add_u32_e32 v24, 0x400, v104
	ds_read2_b32 v[6:7], v104 offset0:65 offset1:73
	ds_read2_b32 v[8:9], v104 offset1:8
	ds_read2_b32 v[10:11], v104 offset0:130 offset1:138
	ds_read2_b32 v[12:13], v104 offset0:195 offset1:203
	ds_read2_b32 v[14:15], v24 offset0:4 offset1:12
	ds_read2_b32 v[16:17], v24 offset0:69 offset1:77
	ds_read2_b32 v[18:19], v24 offset0:134 offset1:142
	ds_read2_b32 v[20:21], v24 offset0:199 offset1:207
	v_mov_b32_e32 v103, v97
	v_lshl_add_u64 v[4:5], s[2:3], 0, v[102:103]
	s_waitcnt lgkmcnt(6)
	v_cvt_pk_bf16_f32 v0, v8, v6
	s_waitcnt lgkmcnt(4)
	v_cvt_pk_bf16_f32 v1, v10, v12
	s_waitcnt lgkmcnt(2)
	v_cvt_pk_bf16_f32 v2, v14, v16
	s_waitcnt lgkmcnt(0)
	v_cvt_pk_bf16_f32 v3, v18, v20
	v_lshl_add_u64 v[22:23], v[4:5], 0, v[84:85]
	global_store_dwordx4 v[22:23], v[0:3], off sc1
	v_lshl_add_u64 v[22:23], v[4:5], 0, v[88:89]
	s_nop 0
	v_cvt_pk_bf16_f32 v0, v9, v7
	v_cvt_pk_bf16_f32 v1, v11, v13
	v_cvt_pk_bf16_f32 v2, v15, v17
	v_cvt_pk_bf16_f32 v3, v19, v21
	v_lshl_add_u64 v[6:7], v[4:5], 0, v[86:87]
	global_store_dwordx4 v[6:7], v[0:3], off sc1
	ds_read2_b32 v[6:7], v104 offset0:81 offset1:89
	ds_read2_b32 v[8:9], v104 offset0:16 offset1:24
	ds_read2_b32 v[10:11], v104 offset0:146 offset1:154
	ds_read2_b32 v[12:13], v104 offset0:211 offset1:219
	ds_read2_b32 v[14:15], v24 offset0:20 offset1:28
	ds_read2_b32 v[16:17], v24 offset0:85 offset1:93
	ds_read2_b32 v[18:19], v24 offset0:150 offset1:158
	ds_read2_b32 v[20:21], v24 offset0:215 offset1:223
	s_waitcnt lgkmcnt(6)
	v_cvt_pk_bf16_f32 v0, v8, v6
	s_waitcnt lgkmcnt(4)
	v_cvt_pk_bf16_f32 v1, v10, v12
	s_waitcnt lgkmcnt(2)
	v_cvt_pk_bf16_f32 v2, v14, v16
	s_waitcnt lgkmcnt(0)
	v_cvt_pk_bf16_f32 v3, v18, v20
	global_store_dwordx4 v[22:23], v[0:3], off sc1
	v_lshl_add_u64 v[22:23], v[4:5], 0, v[92:93]
	s_nop 0
	v_cvt_pk_bf16_f32 v0, v9, v7
	v_cvt_pk_bf16_f32 v1, v11, v13
	v_cvt_pk_bf16_f32 v2, v15, v17
	v_cvt_pk_bf16_f32 v3, v19, v21
	v_lshl_add_u64 v[6:7], v[4:5], 0, v[90:91]
	global_store_dwordx4 v[6:7], v[0:3], off sc1
	ds_read2_b32 v[6:7], v104 offset0:32 offset1:40
	ds_read2_b32 v[8:9], v104 offset0:97 offset1:105
	ds_read2_b32 v[10:11], v104 offset0:162 offset1:170
	ds_read2_b32 v[12:13], v104 offset0:227 offset1:235
	ds_read2_b32 v[14:15], v24 offset0:36 offset1:44
	ds_read2_b32 v[16:17], v24 offset0:101 offset1:109
	ds_read2_b32 v[18:19], v24 offset0:166 offset1:174
	ds_read2_b32 v[20:21], v24 offset0:231 offset1:239
	s_waitcnt lgkmcnt(6)
	v_cvt_pk_bf16_f32 v0, v6, v8
	s_waitcnt lgkmcnt(4)
	v_cvt_pk_bf16_f32 v1, v10, v12
	s_waitcnt lgkmcnt(2)
	v_cvt_pk_bf16_f32 v2, v14, v16
	s_waitcnt lgkmcnt(0)
	v_cvt_pk_bf16_f32 v3, v18, v20
	global_store_dwordx4 v[22:23], v[0:3], off sc1
	v_lshl_add_u64 v[22:23], v[4:5], 0, v[98:99]
	s_nop 0
	v_cvt_pk_bf16_f32 v0, v7, v9
	v_cvt_pk_bf16_f32 v1, v11, v13
	v_cvt_pk_bf16_f32 v2, v15, v17
	v_cvt_pk_bf16_f32 v3, v19, v21
	v_lshl_add_u64 v[6:7], v[4:5], 0, v[94:95]
	global_store_dwordx4 v[6:7], v[0:3], off sc1
	ds_read2_b32 v[6:7], v104 offset0:48 offset1:56
	ds_read2_b32 v[8:9], v104 offset0:113 offset1:121
	ds_read2_b32 v[10:11], v104 offset0:178 offset1:186
	ds_read2_b32 v[12:13], v104 offset0:243 offset1:251
	ds_read2_b32 v[14:15], v24 offset0:52 offset1:60
	ds_read2_b32 v[16:17], v24 offset0:117 offset1:125
	ds_read2_b32 v[18:19], v24 offset0:182 offset1:190
	ds_read2_b32 v[20:21], v24 offset0:247 offset1:255
	v_lshl_add_u64 v[4:5], v[4:5], 0, v[100:101]
	s_waitcnt lgkmcnt(6)
	v_cvt_pk_bf16_f32 v0, v6, v8
	s_waitcnt lgkmcnt(4)
	v_cvt_pk_bf16_f32 v1, v10, v12
	s_waitcnt lgkmcnt(2)
	v_cvt_pk_bf16_f32 v2, v14, v16
	s_waitcnt lgkmcnt(0)
	v_cvt_pk_bf16_f32 v3, v18, v20
	global_store_dwordx4 v[22:23], v[0:3], off sc1
	s_nop 1
	v_cvt_pk_bf16_f32 v0, v7, v9
	v_cvt_pk_bf16_f32 v1, v11, v13
	v_cvt_pk_bf16_f32 v2, v15, v17
	v_cvt_pk_bf16_f32 v3, v19, v21
	global_store_dwordx4 v[4:5], v[0:3], off sc1
	s_waitcnt lgkmcnt(0)
	s_cbranch_scc1 .LBB0_256

.LBB0_259:
	s_mul_hi_i32 s2, s12, 0x66666667
	s_lshr_b32 s3, s2, 31
	s_ashr_i32 s2, s2, 5
	s_add_i32 s3, s2, s3
	s_mul_i32 s2, s3, 0xffffffb0
	s_add_i32 s2, s12, s2
	s_bfe_i32 s4, s2, 0x80000
	s_bfe_u32 s4, s4, 0x4000b
	s_add_i32 s4, s2, s4
	s_bfe_i32 s5, s4, 0x80000
	s_and_b32 s4, s4, 0xf0
	s_sext_i32_i16 s5, s5
	s_sub_i32 s2, s2, s4
	s_sext_i32_i8 s13, s2
	s_lshl_b32 s2, s5, 2
	s_andn2_b32 s2, s2, 63
	s_lshl_b32 s4, s13, 6
	s_mul_hi_i32 s5, s3, 0x140000
	s_mul_i32 s3, s3, 0x140000
	s_add_u32 s16, s6, s3
	s_addc_u32 s5, s7, s5
	s_ashr_i32 s3, s2, 31
	s_lshl_b64 s[14:15], s[2:3], 12
	s_add_u32 s16, s16, s14
	s_addc_u32 s18, s5, s15
	s_ashr_i32 s5, s4, 31
	s_lshl_b64 s[14:15], s[4:5], 2
	s_add_u32 s14, s16, s14
	s_addc_u32 s15, s18, s15
	v_lshl_add_u64 v[0:1], s[14:15], 0, v[96:97]
	v_lshl_add_u64 v[2:3], v[0:1], 0, v[60:61]
	flat_load_dwordx4 v[114:117], v[2:3] nt
	v_lshl_add_u64 v[2:3], v[0:1], 0, v[62:63]
	flat_load_dwordx4 v[56:59], v[2:3] nt
	v_lshl_add_u64 v[2:3], v[0:1], 0, v[64:65]
	flat_load_dwordx4 v[52:55], v[2:3] nt
	v_lshl_add_u64 v[2:3], v[0:1], 0, v[66:67]
	flat_load_dwordx4 v[48:51], v[2:3] nt
	v_lshl_add_u64 v[2:3], v[0:1], 0, v[68:69]
	flat_load_dwordx4 v[44:47], v[2:3] nt
	v_lshl_add_u64 v[2:3], v[0:1], 0, v[70:71]
	flat_load_dwordx4 v[40:43], v[2:3] nt
	v_lshl_add_u64 v[2:3], v[0:1], 0, v[72:73]
	flat_load_dwordx4 v[36:39], v[2:3] nt
	v_lshl_add_u64 v[2:3], v[0:1], 0, v[74:75]
	flat_load_dwordx4 v[32:35], v[2:3] nt
	v_lshl_add_u64 v[2:3], v[0:1], 0, v[76:77]
	flat_load_dwordx4 v[28:31], v[2:3] nt
	v_lshl_add_u64 v[2:3], v[0:1], 0, v[78:79]
	flat_load_dwordx4 v[24:27], v[2:3] nt
	v_lshl_add_u64 v[2:3], v[0:1], 0, v[80:81]
	flat_load_dwordx4 v[20:23], v[2:3] nt
	v_lshl_add_u64 v[2:3], v[0:1], 0, v[82:83]
	flat_load_dwordx4 v[16:19], v[2:3] nt
	v_lshl_add_u64 v[2:3], v[0:1], 0, v[84:85]
	flat_load_dwordx4 v[12:15], v[2:3] nt
	v_lshl_add_u64 v[2:3], v[0:1], 0, v[86:87]
	flat_load_dwordx4 v[8:11], v[2:3] nt
	v_lshl_add_u64 v[2:3], v[0:1], 0, v[88:89]
	flat_load_dwordx4 v[4:7], v[2:3] nt
	v_lshl_add_u64 v[0:1], v[0:1], 0, v[90:91]
	flat_load_dwordx4 v[0:3], v[0:1] nt
	v_add_u32_e32 v111, 0x410, v113
	s_mul_i32 s13, s13, 0xa000
	s_mul_hi_i32 s4, s4, 0x280
	s_add_u32 s5, s19, s13
	s_addc_u32 s4, s20, s4
	s_lshl_b64 s[2:3], s[2:3], 1
	s_add_u32 s2, s5, s2
	s_addc_u32 s3, s4, s3
	s_add_i32 s12, s12, s80
	s_cmpk_lt_i32 s12, 0x50
	s_waitcnt vmcnt(0) lgkmcnt(0)
	ds_write2_b32 v113, v114, v115 offset1:1
	ds_write2_b32 v113, v116, v117 offset0:2 offset1:3
	ds_write2_b32 v111, v56, v57 offset1:1
	v_add_u32_e32 v56, 0x418, v113
	ds_write2_b32 v56, v58, v59 offset1:1
	v_add_u32_e32 v56, 0x820, v113
	ds_write2_b32 v56, v52, v53 offset1:1
	v_add_u32_e32 v52, 0x828, v113
	ds_write2_b32 v52, v54, v55 offset1:1
	v_add_u32_e32 v52, 0xc30, v113
	ds_write2_b32 v52, v48, v49 offset1:1
	v_add_u32_e32 v48, 0xc38, v113
	ds_write2_b32 v48, v50, v51 offset1:1
	v_add_u32_e32 v48, 0x1040, v113
	ds_write2_b32 v48, v44, v45 offset1:1
	v_add_u32_e32 v44, 0x1048, v113
	ds_write2_b32 v44, v46, v47 offset1:1
	v_add_u32_e32 v44, 0x1450, v113
	ds_write2_b32 v44, v40, v41 offset1:1
	v_add_u32_e32 v40, 0x1458, v113
	ds_write2_b32 v40, v42, v43 offset1:1
	v_add_u32_e32 v40, 0x1860, v113
	ds_write2_b32 v40, v36, v37 offset1:1
	v_add_u32_e32 v36, 0x1868, v113
	ds_write2_b32 v36, v38, v39 offset1:1
	v_add_u32_e32 v36, 0x1c70, v113
	ds_write2_b32 v36, v32, v33 offset1:1
	v_add_u32_e32 v32, 0x1c78, v113
	ds_write2_b32 v32, v34, v35 offset1:1
	v_add_u32_e32 v32, 0x2080, v113
	ds_write2_b32 v32, v28, v29 offset1:1
	v_add_u32_e32 v28, 0x2088, v113
	ds_write2_b32 v28, v30, v31 offset1:1
	v_add_u32_e32 v28, 0x2490, v113
	ds_write2_b32 v28, v24, v25 offset1:1
	v_add_u32_e32 v24, 0x2498, v113
	ds_write2_b32 v24, v26, v27 offset1:1
	v_add_u32_e32 v24, 0x28a0, v113
	ds_write2_b32 v24, v20, v21 offset1:1
	v_add_u32_e32 v20, 0x28a8, v113
	ds_write2_b32 v20, v22, v23 offset1:1
	v_add_u32_e32 v20, 0x2cb0, v113
	ds_write2_b32 v20, v16, v17 offset1:1
	v_add_u32_e32 v16, 0x2cb8, v113
	ds_write2_b32 v16, v18, v19 offset1:1
	v_add_u32_e32 v16, 0x30c0, v113
	ds_write2_b32 v16, v12, v13 offset1:1
	v_add_u32_e32 v12, 0x30c8, v113
	ds_write2_b32 v12, v14, v15 offset1:1
	v_add_u32_e32 v12, 0x34d0, v113
	ds_write2_b32 v12, v8, v9 offset1:1
	v_add_u32_e32 v8, 0x34d8, v113
	ds_write2_b32 v8, v10, v11 offset1:1
	v_add_u32_e32 v8, 0x38e0, v113
	ds_write2_b32 v8, v4, v5 offset1:1
	v_add_u32_e32 v4, 0x38e8, v113
	ds_write2_b32 v4, v6, v7 offset1:1
	v_add_u32_e32 v4, 0x3cf0, v113
	ds_write2_b32 v4, v0, v1 offset1:1
	v_add_u32_e32 v0, 0x3cf8, v113
	ds_write2_b32 v0, v2, v3 offset1:1
	s_waitcnt lgkmcnt(0)
	ds_read2_b32 v[6:7], v112 offset0:65 offset1:73
	ds_read2_b32 v[8:9], v112 offset1:8
	ds_read2_b32 v[10:11], v112 offset0:130 offset1:138
	ds_read2_b32 v[12:13], v112 offset0:195 offset1:203
	v_mov_b32_e32 v111, v97
	v_lshl_add_u64 v[4:5], s[2:3], 0, v[110:111]
	v_lshl_add_u64 v[22:23], v[4:5], 0, v[92:93]
	s_waitcnt lgkmcnt(2)
	v_cvt_pk_bf16_f32 v0, v8, v6
	v_add_u32_e32 v6, 0x400, v112
	ds_read2_b32 v[14:15], v6 offset0:4 offset1:12
	ds_read2_b32 v[16:17], v6 offset0:69 offset1:77
	ds_read2_b32 v[18:19], v6 offset0:134 offset1:142
	ds_read2_b32 v[20:21], v6 offset0:199 offset1:207
	s_waitcnt lgkmcnt(4)
	v_cvt_pk_bf16_f32 v1, v10, v12
	v_lshl_add_u64 v[24:25], v[4:5], 0, v[98:99]
	s_waitcnt lgkmcnt(2)
	v_cvt_pk_bf16_f32 v2, v14, v16
	s_waitcnt lgkmcnt(0)
	v_cvt_pk_bf16_f32 v3, v18, v20
	global_store_dwordx4 v[22:23], v[0:3], off sc1
	s_nop 1
	v_cvt_pk_bf16_f32 v0, v9, v7
	v_cvt_pk_bf16_f32 v1, v11, v13
	v_cvt_pk_bf16_f32 v2, v15, v17
	v_cvt_pk_bf16_f32 v3, v19, v21
	v_lshl_add_u64 v[8:9], v[4:5], 0, v[94:95]
	global_store_dwordx4 v[8:9], v[0:3], off sc1
	ds_read2_b32 v[8:9], v112 offset0:81 offset1:89
	ds_read2_b32 v[10:11], v112 offset0:16 offset1:24
	ds_read2_b32 v[12:13], v112 offset0:146 offset1:154
	ds_read2_b32 v[14:15], v112 offset0:211 offset1:219
	ds_read2_b32 v[16:17], v6 offset0:20 offset1:28
	ds_read2_b32 v[18:19], v6 offset0:85 offset1:93
	ds_read2_b32 v[20:21], v6 offset0:150 offset1:158
	ds_read2_b32 v[22:23], v6 offset0:215 offset1:223
	s_waitcnt lgkmcnt(6)
	v_cvt_pk_bf16_f32 v0, v10, v8
	s_waitcnt lgkmcnt(4)
	v_cvt_pk_bf16_f32 v1, v12, v14
	s_waitcnt lgkmcnt(2)
	v_cvt_pk_bf16_f32 v2, v16, v18
	s_waitcnt lgkmcnt(0)
	v_cvt_pk_bf16_f32 v3, v20, v22
	global_store_dwordx4 v[24:25], v[0:3], off sc1
	v_lshl_add_u64 v[24:25], v[4:5], 0, v[102:103]
	s_nop 0
	v_cvt_pk_bf16_f32 v0, v11, v9
	v_cvt_pk_bf16_f32 v1, v13, v15
	v_cvt_pk_bf16_f32 v2, v17, v19
	v_cvt_pk_bf16_f32 v3, v21, v23
	v_lshl_add_u64 v[8:9], v[4:5], 0, v[100:101]
	global_store_dwordx4 v[8:9], v[0:3], off sc1
	ds_read2_b32 v[8:9], v112 offset0:97 offset1:105
	ds_read2_b32 v[10:11], v112 offset0:32 offset1:40
	ds_read2_b32 v[12:13], v112 offset0:162 offset1:170
	ds_read2_b32 v[14:15], v112 offset0:227 offset1:235
	ds_read2_b32 v[16:17], v6 offset0:36 offset1:44
	ds_read2_b32 v[18:19], v6 offset0:101 offset1:109
	ds_read2_b32 v[20:21], v6 offset0:166 offset1:174
	ds_read2_b32 v[22:23], v6 offset0:231 offset1:239
	s_waitcnt lgkmcnt(6)
	v_cvt_pk_bf16_f32 v0, v10, v8
	s_waitcnt lgkmcnt(4)
	v_cvt_pk_bf16_f32 v1, v12, v14
	s_waitcnt lgkmcnt(2)
	v_cvt_pk_bf16_f32 v2, v16, v18
	s_waitcnt lgkmcnt(0)
	v_cvt_pk_bf16_f32 v3, v20, v22
	global_store_dwordx4 v[24:25], v[0:3], off sc1
	s_nop 1
	v_cvt_pk_bf16_f32 v0, v11, v9
	v_cvt_pk_bf16_f32 v1, v13, v15
	v_cvt_pk_bf16_f32 v2, v17, v19
	v_cvt_pk_bf16_f32 v3, v21, v23
	v_lshl_add_u64 v[8:9], v[4:5], 0, v[104:105]
	global_store_dwordx4 v[8:9], v[0:3], off sc1
	ds_read2_b32 v[8:9], v112 offset0:48 offset1:56
	ds_read2_b32 v[10:11], v112 offset0:113 offset1:121
	ds_read2_b32 v[12:13], v112 offset0:178 offset1:186
	ds_read2_b32 v[14:15], v112 offset0:243 offset1:251
	ds_read2_b32 v[16:17], v6 offset0:52 offset1:60
	ds_read2_b32 v[18:19], v6 offset0:117 offset1:125
	ds_read2_b32 v[20:21], v6 offset0:182 offset1:190
	ds_read2_b32 v[6:7], v6 offset0:247 offset1:255
	v_lshl_add_u64 v[22:23], v[4:5], 0, v[106:107]
	s_waitcnt lgkmcnt(6)
	v_cvt_pk_bf16_f32 v0, v8, v10
	s_waitcnt lgkmcnt(4)
	v_cvt_pk_bf16_f32 v1, v12, v14
	s_waitcnt lgkmcnt(2)
	v_cvt_pk_bf16_f32 v2, v16, v18
	s_waitcnt lgkmcnt(0)
	v_cvt_pk_bf16_f32 v3, v20, v6
	global_store_dwordx4 v[22:23], v[0:3], off sc1
	v_lshl_add_u64 v[4:5], v[4:5], 0, v[108:109]
	s_nop 0
	v_cvt_pk_bf16_f32 v0, v9, v11
	v_cvt_pk_bf16_f32 v1, v13, v15
	v_cvt_pk_bf16_f32 v2, v17, v19
	v_cvt_pk_bf16_f32 v3, v21, v7
	global_store_dwordx4 v[4:5], v[0:3], off sc1
	s_waitcnt lgkmcnt(0)
	s_cbranch_scc1 .LBB0_259

.LBB0_264:
	s_mul_hi_i32 s2, s6, 0x15390949
	s_lshr_b32 s3, s2, 31
	s_ashr_i32 s2, s2, 9
	s_add_i32 s3, s2, s3
	s_mul_i32 s2, s3, 0xffffe7e0
	s_add_i32 s2, s6, s2
	s_mul_i32 s4, s2, 0xffffa9c9
	s_lshr_b32 s4, s4, 16
	s_add_i32 s4, s4, s2
	s_sext_i32_i16 s5, s4
	s_ashr_i32 s5, s5, 7
	s_bfe_u32 s4, s4, 0x1000f
	s_add_i32 s4, s5, s4
	s_sext_i32_i16 s5, s4
	s_mulk_i32 s4, 0xc1
	s_sub_i32 s2, s2, s4
	s_sext_i32_i16 s15, s2
	s_lshl_b32 s2, s5, 6
	s_lshl_b32 s4, s15, 6
	s_mul_hi_i32 s16, s3, 0x6080000
	s_mul_i32 s3, s3, 0x6080000
	s_add_u32 s18, s7, s3
	s_addc_u32 s16, s14, s16
	s_ashr_i32 s3, s2, 31
	s_mul_i32 s5, s5, 0x304000
	s_mul_hi_i32 s19, s2, 0xc100
	s_add_u32 s20, s18, s5
	s_addc_u32 s16, s16, s19
	s_ashr_i32 s5, s4, 31
	s_lshl_b64 s[18:19], s[4:5], 2
	s_add_u32 s18, s20, s18
	s_addc_u32 s19, s16, s19
	v_lshl_add_u64 v[0:1], s[18:19], 0, v[96:97]
	v_lshl_add_u64 v[2:3], v[0:1], 0, v[60:61]
	flat_load_dwordx4 v[116:119], v[2:3] nt
	v_lshl_add_u64 v[2:3], v[0:1], 0, v[62:63]
	flat_load_dwordx4 v[56:59], v[2:3] nt
	v_lshl_add_u64 v[2:3], v[0:1], 0, v[64:65]
	flat_load_dwordx4 v[52:55], v[2:3] nt
	v_lshl_add_u64 v[2:3], v[0:1], 0, v[66:67]
	flat_load_dwordx4 v[48:51], v[2:3] nt
	v_lshl_add_u64 v[2:3], v[0:1], 0, v[68:69]
	flat_load_dwordx4 v[44:47], v[2:3] nt
	v_lshl_add_u64 v[2:3], v[0:1], 0, v[70:71]
	flat_load_dwordx4 v[40:43], v[2:3] nt
	v_lshl_add_u64 v[2:3], v[0:1], 0, v[72:73]
	flat_load_dwordx4 v[36:39], v[2:3] nt
	v_lshl_add_u64 v[2:3], v[0:1], 0, v[74:75]
	flat_load_dwordx4 v[32:35], v[2:3] nt
	v_lshl_add_u64 v[2:3], v[0:1], 0, v[76:77]
	flat_load_dwordx4 v[28:31], v[2:3] nt
	v_lshl_add_u64 v[2:3], v[0:1], 0, v[78:79]
	flat_load_dwordx4 v[24:27], v[2:3] nt
	v_lshl_add_u64 v[2:3], v[0:1], 0, v[80:81]
	flat_load_dwordx4 v[20:23], v[2:3] nt
	v_lshl_add_u64 v[2:3], v[0:1], 0, v[82:83]
	flat_load_dwordx4 v[16:19], v[2:3] nt
	v_lshl_add_u64 v[2:3], v[0:1], 0, v[84:85]
	flat_load_dwordx4 v[12:15], v[2:3] nt
	v_lshl_add_u64 v[2:3], v[0:1], 0, v[86:87]
	flat_load_dwordx4 v[8:11], v[2:3] nt
	v_lshl_add_u64 v[2:3], v[0:1], 0, v[88:89]
	flat_load_dwordx4 v[4:7], v[2:3] nt
	v_lshl_add_u64 v[0:1], v[0:1], 0, v[90:91]
	flat_load_dwordx4 v[0:3], v[0:1] nt
	v_add_u32_e32 v111, 0x410, v114
	s_add_i32 s5, s4, 0xc0
	s_cmpk_lt_i32 s15, 0x61
	s_cselect_b32 s4, s4, s5
	s_ashr_i32 s5, s4, 31
	s_lshl_b64 s[4:5], s[4:5], 12
	s_add_u32 s4, s21, s4
	s_addc_u32 s5, s22, s5
	s_lshl_b64 s[2:3], s[2:3], 1
	s_add_u32 s2, s4, s2
	s_addc_u32 s3, s5, s3
	s_add_i32 s6, s6, s39
	s_cmpk_lt_i32 s6, 0x1820
	s_waitcnt vmcnt(0) lgkmcnt(0)
	ds_write2_b32 v114, v116, v117 offset1:1
	ds_write2_b32 v114, v118, v119 offset0:2 offset1:3
	ds_write2_b32 v111, v56, v57 offset1:1
	v_add_u32_e32 v56, 0x418, v114
	ds_write2_b32 v56, v58, v59 offset1:1
	v_add_u32_e32 v56, 0x820, v114
	ds_write2_b32 v56, v52, v53 offset1:1
	v_add_u32_e32 v52, 0x828, v114
	ds_write2_b32 v52, v54, v55 offset1:1
	v_add_u32_e32 v52, 0xc30, v114
	ds_write2_b32 v52, v48, v49 offset1:1
	v_add_u32_e32 v48, 0xc38, v114
	ds_write2_b32 v48, v50, v51 offset1:1
	v_add_u32_e32 v48, 0x1040, v114
	ds_write2_b32 v48, v44, v45 offset1:1
	v_add_u32_e32 v44, 0x1048, v114
	ds_write2_b32 v44, v46, v47 offset1:1
	v_add_u32_e32 v44, 0x1450, v114
	ds_write2_b32 v44, v40, v41 offset1:1
	v_add_u32_e32 v40, 0x1458, v114
	ds_write2_b32 v40, v42, v43 offset1:1
	v_add_u32_e32 v40, 0x1860, v114
	ds_write2_b32 v40, v36, v37 offset1:1
	v_add_u32_e32 v36, 0x1868, v114
	ds_write2_b32 v36, v38, v39 offset1:1
	v_add_u32_e32 v36, 0x1c70, v114
	ds_write2_b32 v36, v32, v33 offset1:1
	v_add_u32_e32 v32, 0x1c78, v114
	ds_write2_b32 v32, v34, v35 offset1:1
	v_add_u32_e32 v32, 0x2080, v114
	ds_write2_b32 v32, v28, v29 offset1:1
	v_add_u32_e32 v28, 0x2088, v114
	ds_write2_b32 v28, v30, v31 offset1:1
	v_add_u32_e32 v28, 0x2490, v114
	ds_write2_b32 v28, v24, v25 offset1:1
	v_add_u32_e32 v24, 0x2498, v114
	ds_write2_b32 v24, v26, v27 offset1:1
	v_add_u32_e32 v24, 0x28a0, v114
	ds_write2_b32 v24, v20, v21 offset1:1
	v_add_u32_e32 v20, 0x28a8, v114
	ds_write2_b32 v20, v22, v23 offset1:1
	v_add_u32_e32 v20, 0x2cb0, v114
	ds_write2_b32 v20, v16, v17 offset1:1
	v_add_u32_e32 v16, 0x2cb8, v114
	ds_write2_b32 v16, v18, v19 offset1:1
	v_add_u32_e32 v16, 0x30c0, v114
	ds_write2_b32 v16, v12, v13 offset1:1
	v_add_u32_e32 v12, 0x30c8, v114
	ds_write2_b32 v12, v14, v15 offset1:1
	v_add_u32_e32 v12, 0x34d0, v114
	ds_write2_b32 v12, v8, v9 offset1:1
	v_add_u32_e32 v8, 0x34d8, v114
	ds_write2_b32 v8, v10, v11 offset1:1
	v_add_u32_e32 v8, 0x38e0, v114
	ds_write2_b32 v8, v4, v5 offset1:1
	v_add_u32_e32 v4, 0x38e8, v114
	ds_write2_b32 v4, v6, v7 offset1:1
	v_add_u32_e32 v4, 0x3cf0, v114
	ds_write2_b32 v4, v0, v1 offset1:1
	v_add_u32_e32 v0, 0x3cf8, v114
	ds_write2_b32 v0, v2, v3 offset1:1
	s_waitcnt lgkmcnt(0)
	ds_read2_b32 v[6:7], v113 offset0:65 offset1:73
	ds_read2_b32 v[8:9], v113 offset1:8
	ds_read2_b32 v[10:11], v113 offset0:130 offset1:138
	ds_read2_b32 v[12:13], v113 offset0:195 offset1:203
	v_mov_b32_e32 v111, v97
	v_lshl_add_u64 v[4:5], s[2:3], 0, v[110:111]
	v_lshl_add_u64 v[22:23], v[4:5], 0, v[92:93]
	s_waitcnt lgkmcnt(2)
	v_cvt_pk_bf16_f32 v0, v8, v6
	v_add_u32_e32 v6, 0x400, v113
	ds_read2_b32 v[14:15], v6 offset0:4 offset1:12
	ds_read2_b32 v[16:17], v6 offset0:69 offset1:77
	ds_read2_b32 v[18:19], v6 offset0:134 offset1:142
	ds_read2_b32 v[20:21], v6 offset0:199 offset1:207
	s_waitcnt lgkmcnt(4)
	v_cvt_pk_bf16_f32 v1, v10, v12
	v_lshl_add_u64 v[24:25], v[4:5], 0, v[98:99]
	s_waitcnt lgkmcnt(2)
	v_cvt_pk_bf16_f32 v2, v14, v16
	s_waitcnt lgkmcnt(0)
	v_cvt_pk_bf16_f32 v3, v18, v20
	global_store_dwordx4 v[22:23], v[0:3], off sc1
	s_nop 1
	v_cvt_pk_bf16_f32 v0, v9, v7
	v_cvt_pk_bf16_f32 v1, v11, v13
	v_cvt_pk_bf16_f32 v2, v15, v17
	v_cvt_pk_bf16_f32 v3, v19, v21
	v_lshl_add_u64 v[8:9], v[4:5], 0, v[94:95]
	global_store_dwordx4 v[8:9], v[0:3], off sc1
	ds_read2_b32 v[8:9], v113 offset0:81 offset1:89
	ds_read2_b32 v[10:11], v113 offset0:16 offset1:24
	ds_read2_b32 v[12:13], v113 offset0:146 offset1:154
	ds_read2_b32 v[14:15], v113 offset0:211 offset1:219
	ds_read2_b32 v[16:17], v6 offset0:20 offset1:28
	ds_read2_b32 v[18:19], v6 offset0:85 offset1:93
	ds_read2_b32 v[20:21], v6 offset0:150 offset1:158
	ds_read2_b32 v[22:23], v6 offset0:215 offset1:223
	s_waitcnt lgkmcnt(6)
	v_cvt_pk_bf16_f32 v0, v10, v8
	s_waitcnt lgkmcnt(4)
	v_cvt_pk_bf16_f32 v1, v12, v14
	s_waitcnt lgkmcnt(2)
	v_cvt_pk_bf16_f32 v2, v16, v18
	s_waitcnt lgkmcnt(0)
	v_cvt_pk_bf16_f32 v3, v20, v22
	global_store_dwordx4 v[24:25], v[0:3], off sc1
	v_lshl_add_u64 v[24:25], v[4:5], 0, v[102:103]
	s_nop 0
	v_cvt_pk_bf16_f32 v0, v11, v9
	v_cvt_pk_bf16_f32 v1, v13, v15
	v_cvt_pk_bf16_f32 v2, v17, v19
	v_cvt_pk_bf16_f32 v3, v21, v23
	v_lshl_add_u64 v[8:9], v[4:5], 0, v[100:101]
	global_store_dwordx4 v[8:9], v[0:3], off sc1
	ds_read2_b32 v[8:9], v113 offset0:32 offset1:40
	ds_read2_b32 v[10:11], v113 offset0:97 offset1:105
	ds_read2_b32 v[12:13], v113 offset0:162 offset1:170
	ds_read2_b32 v[14:15], v113 offset0:227 offset1:235
	ds_read2_b32 v[16:17], v6 offset0:36 offset1:44
	ds_read2_b32 v[18:19], v6 offset0:101 offset1:109
	ds_read2_b32 v[20:21], v6 offset0:166 offset1:174
	ds_read2_b32 v[22:23], v6 offset0:231 offset1:239
	s_waitcnt lgkmcnt(6)
	v_cvt_pk_bf16_f32 v0, v8, v10
	s_waitcnt lgkmcnt(4)
	v_cvt_pk_bf16_f32 v1, v12, v14
	s_waitcnt lgkmcnt(2)
	v_cvt_pk_bf16_f32 v2, v16, v18
	s_waitcnt lgkmcnt(0)
	v_cvt_pk_bf16_f32 v3, v20, v22
	global_store_dwordx4 v[24:25], v[0:3], off sc1
	s_nop 1
	v_cvt_pk_bf16_f32 v0, v9, v11
	v_cvt_pk_bf16_f32 v1, v13, v15
	v_cvt_pk_bf16_f32 v2, v17, v19
	v_cvt_pk_bf16_f32 v3, v21, v23
	v_lshl_add_u64 v[8:9], v[4:5], 0, v[104:105]
	global_store_dwordx4 v[8:9], v[0:3], off sc1
	ds_read2_b32 v[8:9], v113 offset0:48 offset1:56
	ds_read2_b32 v[10:11], v113 offset0:113 offset1:121
	ds_read2_b32 v[12:13], v113 offset0:178 offset1:186
	ds_read2_b32 v[14:15], v113 offset0:243 offset1:251
	ds_read2_b32 v[16:17], v6 offset0:52 offset1:60
	ds_read2_b32 v[18:19], v6 offset0:117 offset1:125
	ds_read2_b32 v[20:21], v6 offset0:182 offset1:190
	ds_read2_b32 v[6:7], v6 offset0:247 offset1:255
	v_lshl_add_u64 v[22:23], v[4:5], 0, v[106:107]
	s_waitcnt lgkmcnt(6)
	v_cvt_pk_bf16_f32 v0, v8, v10
	s_waitcnt lgkmcnt(4)
	v_cvt_pk_bf16_f32 v1, v12, v14
	s_waitcnt lgkmcnt(2)
	v_cvt_pk_bf16_f32 v2, v16, v18
	s_waitcnt lgkmcnt(0)
	v_cvt_pk_bf16_f32 v3, v20, v6
	global_store_dwordx4 v[22:23], v[0:3], off sc1
	v_lshl_add_u64 v[4:5], v[4:5], 0, v[108:109]
	s_nop 0
	v_cvt_pk_bf16_f32 v0, v9, v11
	v_cvt_pk_bf16_f32 v1, v13, v15
	v_cvt_pk_bf16_f32 v2, v17, v19
	v_cvt_pk_bf16_f32 v3, v21, v7
	global_store_dwordx4 v[4:5], v[0:3], off sc1
	s_waitcnt lgkmcnt(0)
	s_cbranch_scc1 .LBB0_264

.LBB0_267:
	s_ashr_i32 s2, s6, 31
	s_lshr_b32 s2, s2, 23
	s_add_i32 s2, s6, s2
	s_ashr_i32 s18, s2, 9
	s_and_b32 s2, s2, 0xfe00
	s_sub_i32 s2, s6, s2
	s_sext_i32_i16 s3, s2
	s_bfe_u32 s3, s3, 0x5001a
	s_add_i32 s3, s2, s3
	s_sext_i32_i16 s4, s3
	s_and_b32 s3, s3, 0xffe0
	s_sub_i32 s2, s2, s3
	s_sext_i32_i16 s3, s2
	s_lshl_b32 s2, s4, 1
	s_ashr_i32 s19, s18, 31
	s_andn2_b32 s2, s2, 63
	s_lshl_b32 s4, s3, 6
	s_lshl_b64 s[18:19], s[18:19], 23
	s_add_u32 s5, s7, s18
	s_addc_u32 s15, s14, s19
	s_ashr_i32 s3, s2, 31
	s_lshl_b64 s[18:19], s[2:3], 13
	s_add_u32 s16, s5, s18
	s_addc_u32 s15, s15, s19
	s_ashr_i32 s5, s4, 31
	s_lshl_b64 s[18:19], s[4:5], 2
	s_add_u32 s18, s16, s18
	s_addc_u32 s19, s15, s19
	v_lshl_add_u64 v[0:1], s[18:19], 0, v[96:97]
	v_lshl_add_u64 v[2:3], v[0:1], 0, v[60:61]
	flat_load_dwordx4 v[116:119], v[2:3] nt
	v_lshl_add_u64 v[2:3], v[0:1], 0, v[62:63]
	flat_load_dwordx4 v[56:59], v[2:3] nt
	v_lshl_add_u64 v[2:3], v[0:1], 0, v[64:65]
	flat_load_dwordx4 v[52:55], v[2:3] nt
	v_lshl_add_u64 v[2:3], v[0:1], 0, v[66:67]
	flat_load_dwordx4 v[48:51], v[2:3] nt
	v_lshl_add_u64 v[2:3], v[0:1], 0, v[68:69]
	flat_load_dwordx4 v[44:47], v[2:3] nt
	v_lshl_add_u64 v[2:3], v[0:1], 0, v[70:71]
	flat_load_dwordx4 v[40:43], v[2:3] nt
	v_lshl_add_u64 v[2:3], v[0:1], 0, v[72:73]
	flat_load_dwordx4 v[36:39], v[2:3] nt
	v_lshl_add_u64 v[2:3], v[0:1], 0, v[74:75]
	flat_load_dwordx4 v[32:35], v[2:3] nt
	v_lshl_add_u64 v[2:3], v[0:1], 0, v[76:77]
	flat_load_dwordx4 v[28:31], v[2:3] nt
	v_lshl_add_u64 v[2:3], v[0:1], 0, v[78:79]
	flat_load_dwordx4 v[24:27], v[2:3] nt
	v_lshl_add_u64 v[2:3], v[0:1], 0, v[80:81]
	flat_load_dwordx4 v[20:23], v[2:3] nt
	v_lshl_add_u64 v[2:3], v[0:1], 0, v[82:83]
	flat_load_dwordx4 v[16:19], v[2:3] nt
	v_lshl_add_u64 v[2:3], v[0:1], 0, v[84:85]
	flat_load_dwordx4 v[12:15], v[2:3] nt
	v_lshl_add_u64 v[2:3], v[0:1], 0, v[86:87]
	flat_load_dwordx4 v[8:11], v[2:3] nt
	v_lshl_add_u64 v[2:3], v[0:1], 0, v[88:89]
	flat_load_dwordx4 v[4:7], v[2:3] nt
	v_lshl_add_u64 v[0:1], v[0:1], 0, v[90:91]
	flat_load_dwordx4 v[0:3], v[0:1] nt
	v_add_u32_e32 v111, 0x410, v114
	s_lshl_b64 s[4:5], s[4:5], 11
	s_add_u32 s4, s20, s4
	s_addc_u32 s5, s21, s5
	s_lshl_b64 s[2:3], s[2:3], 1
	s_add_u32 s2, s4, s2
	s_addc_u32 s3, s5, s3
	s_add_i32 s6, s6, s39
	s_cmpk_lt_i32 s6, 0x200
	s_waitcnt vmcnt(0) lgkmcnt(0)
	ds_write2_b32 v114, v116, v117 offset1:1
	ds_write2_b32 v114, v118, v119 offset0:2 offset1:3
	ds_write2_b32 v111, v56, v57 offset1:1
	v_add_u32_e32 v56, 0x418, v114
	ds_write2_b32 v56, v58, v59 offset1:1
	v_add_u32_e32 v56, 0x820, v114
	ds_write2_b32 v56, v52, v53 offset1:1
	v_add_u32_e32 v52, 0x828, v114
	ds_write2_b32 v52, v54, v55 offset1:1
	v_add_u32_e32 v52, 0xc30, v114
	ds_write2_b32 v52, v48, v49 offset1:1
	v_add_u32_e32 v48, 0xc38, v114
	ds_write2_b32 v48, v50, v51 offset1:1
	v_add_u32_e32 v48, 0x1040, v114
	ds_write2_b32 v48, v44, v45 offset1:1
	v_add_u32_e32 v44, 0x1048, v114
	ds_write2_b32 v44, v46, v47 offset1:1
	v_add_u32_e32 v44, 0x1450, v114
	ds_write2_b32 v44, v40, v41 offset1:1
	v_add_u32_e32 v40, 0x1458, v114
	ds_write2_b32 v40, v42, v43 offset1:1
	v_add_u32_e32 v40, 0x1860, v114
	ds_write2_b32 v40, v36, v37 offset1:1
	v_add_u32_e32 v36, 0x1868, v114
	ds_write2_b32 v36, v38, v39 offset1:1
	v_add_u32_e32 v36, 0x1c70, v114
	ds_write2_b32 v36, v32, v33 offset1:1
	v_add_u32_e32 v32, 0x1c78, v114
	ds_write2_b32 v32, v34, v35 offset1:1
	v_add_u32_e32 v32, 0x2080, v114
	ds_write2_b32 v32, v28, v29 offset1:1
	v_add_u32_e32 v28, 0x2088, v114
	ds_write2_b32 v28, v30, v31 offset1:1
	v_add_u32_e32 v28, 0x2490, v114
	ds_write2_b32 v28, v24, v25 offset1:1
	v_add_u32_e32 v24, 0x2498, v114
	ds_write2_b32 v24, v26, v27 offset1:1
	v_add_u32_e32 v24, 0x28a0, v114
	ds_write2_b32 v24, v20, v21 offset1:1
	v_add_u32_e32 v20, 0x28a8, v114
	ds_write2_b32 v20, v22, v23 offset1:1
	v_add_u32_e32 v20, 0x2cb0, v114
	ds_write2_b32 v20, v16, v17 offset1:1
	v_add_u32_e32 v16, 0x2cb8, v114
	ds_write2_b32 v16, v18, v19 offset1:1
	v_add_u32_e32 v16, 0x30c0, v114
	ds_write2_b32 v16, v12, v13 offset1:1
	v_add_u32_e32 v12, 0x30c8, v114
	ds_write2_b32 v12, v14, v15 offset1:1
	v_add_u32_e32 v12, 0x34d0, v114
	ds_write2_b32 v12, v8, v9 offset1:1
	v_add_u32_e32 v8, 0x34d8, v114
	ds_write2_b32 v8, v10, v11 offset1:1
	v_add_u32_e32 v8, 0x38e0, v114
	ds_write2_b32 v8, v4, v5 offset1:1
	v_add_u32_e32 v4, 0x38e8, v114
	ds_write2_b32 v4, v6, v7 offset1:1
	v_add_u32_e32 v4, 0x3cf0, v114
	ds_write2_b32 v4, v0, v1 offset1:1
	v_add_u32_e32 v0, 0x3cf8, v114
	ds_write2_b32 v0, v2, v3 offset1:1
	s_waitcnt lgkmcnt(0)
	ds_read2_b32 v[6:7], v113 offset0:65 offset1:73
	ds_read2_b32 v[8:9], v113 offset1:8
	ds_read2_b32 v[10:11], v113 offset0:130 offset1:138
	ds_read2_b32 v[12:13], v113 offset0:195 offset1:203
	v_mov_b32_e32 v111, v97
	v_lshl_add_u64 v[4:5], s[2:3], 0, v[110:111]
	v_lshl_add_u64 v[22:23], v[4:5], 0, v[92:93]
	s_waitcnt lgkmcnt(2)
	v_cvt_pk_bf16_f32 v0, v8, v6
	v_add_u32_e32 v6, 0x400, v113
	ds_read2_b32 v[14:15], v6 offset0:4 offset1:12
	ds_read2_b32 v[16:17], v6 offset0:69 offset1:77
	ds_read2_b32 v[18:19], v6 offset0:134 offset1:142
	ds_read2_b32 v[20:21], v6 offset0:199 offset1:207
	s_waitcnt lgkmcnt(4)
	v_cvt_pk_bf16_f32 v1, v10, v12
	v_lshl_add_u64 v[24:25], v[4:5], 0, v[98:99]
	s_waitcnt lgkmcnt(2)
	v_cvt_pk_bf16_f32 v2, v14, v16
	s_waitcnt lgkmcnt(0)
	v_cvt_pk_bf16_f32 v3, v18, v20
	global_store_dwordx4 v[22:23], v[0:3], off sc1
	s_nop 1
	v_cvt_pk_bf16_f32 v0, v9, v7
	v_cvt_pk_bf16_f32 v1, v11, v13
	v_cvt_pk_bf16_f32 v2, v15, v17
	v_cvt_pk_bf16_f32 v3, v19, v21
	v_lshl_add_u64 v[8:9], v[4:5], 0, v[94:95]
	global_store_dwordx4 v[8:9], v[0:3], off sc1
	ds_read2_b32 v[8:9], v113 offset0:81 offset1:89
	ds_read2_b32 v[10:11], v113 offset0:16 offset1:24
	ds_read2_b32 v[12:13], v113 offset0:146 offset1:154
	ds_read2_b32 v[14:15], v113 offset0:211 offset1:219
	ds_read2_b32 v[16:17], v6 offset0:20 offset1:28
	ds_read2_b32 v[18:19], v6 offset0:85 offset1:93
	ds_read2_b32 v[20:21], v6 offset0:150 offset1:158
	ds_read2_b32 v[22:23], v6 offset0:215 offset1:223
	s_waitcnt lgkmcnt(6)
	v_cvt_pk_bf16_f32 v0, v10, v8
	s_waitcnt lgkmcnt(4)
	v_cvt_pk_bf16_f32 v1, v12, v14
	s_waitcnt lgkmcnt(2)
	v_cvt_pk_bf16_f32 v2, v16, v18
	s_waitcnt lgkmcnt(0)
	v_cvt_pk_bf16_f32 v3, v20, v22
	global_store_dwordx4 v[24:25], v[0:3], off sc1
	v_lshl_add_u64 v[24:25], v[4:5], 0, v[102:103]
	s_nop 0
	v_cvt_pk_bf16_f32 v0, v11, v9
	v_cvt_pk_bf16_f32 v1, v13, v15
	v_cvt_pk_bf16_f32 v2, v17, v19
	v_cvt_pk_bf16_f32 v3, v21, v23
	v_lshl_add_u64 v[8:9], v[4:5], 0, v[100:101]
	global_store_dwordx4 v[8:9], v[0:3], off sc1
	ds_read2_b32 v[8:9], v113 offset0:32 offset1:40
	ds_read2_b32 v[10:11], v113 offset0:97 offset1:105
	ds_read2_b32 v[12:13], v113 offset0:162 offset1:170
	ds_read2_b32 v[14:15], v113 offset0:227 offset1:235
	ds_read2_b32 v[16:17], v6 offset0:36 offset1:44
	ds_read2_b32 v[18:19], v6 offset0:101 offset1:109
	ds_read2_b32 v[20:21], v6 offset0:166 offset1:174
	ds_read2_b32 v[22:23], v6 offset0:231 offset1:239
	s_waitcnt lgkmcnt(6)
	v_cvt_pk_bf16_f32 v0, v8, v10
	s_waitcnt lgkmcnt(4)
	v_cvt_pk_bf16_f32 v1, v12, v14
	s_waitcnt lgkmcnt(2)
	v_cvt_pk_bf16_f32 v2, v16, v18
	s_waitcnt lgkmcnt(0)
	v_cvt_pk_bf16_f32 v3, v20, v22
	global_store_dwordx4 v[24:25], v[0:3], off sc1
	s_nop 1
	v_cvt_pk_bf16_f32 v0, v9, v11
	v_cvt_pk_bf16_f32 v1, v13, v15
	v_cvt_pk_bf16_f32 v2, v17, v19
	v_cvt_pk_bf16_f32 v3, v21, v23
	v_lshl_add_u64 v[8:9], v[4:5], 0, v[104:105]
	global_store_dwordx4 v[8:9], v[0:3], off sc1
	ds_read2_b32 v[8:9], v113 offset0:48 offset1:56
	ds_read2_b32 v[10:11], v113 offset0:113 offset1:121
	ds_read2_b32 v[12:13], v113 offset0:178 offset1:186
	ds_read2_b32 v[14:15], v113 offset0:243 offset1:251
	ds_read2_b32 v[16:17], v6 offset0:52 offset1:60
	ds_read2_b32 v[18:19], v6 offset0:117 offset1:125
	ds_read2_b32 v[20:21], v6 offset0:182 offset1:190
	ds_read2_b32 v[6:7], v6 offset0:247 offset1:255
	v_lshl_add_u64 v[22:23], v[4:5], 0, v[106:107]
	s_waitcnt lgkmcnt(6)
	v_cvt_pk_bf16_f32 v0, v8, v10
	s_waitcnt lgkmcnt(4)
	v_cvt_pk_bf16_f32 v1, v12, v14
	s_waitcnt lgkmcnt(2)
	v_cvt_pk_bf16_f32 v2, v16, v18
	s_waitcnt lgkmcnt(0)
	v_cvt_pk_bf16_f32 v3, v20, v6
	global_store_dwordx4 v[22:23], v[0:3], off sc1
	v_lshl_add_u64 v[4:5], v[4:5], 0, v[108:109]
	s_nop 0
	v_cvt_pk_bf16_f32 v0, v9, v11
	v_cvt_pk_bf16_f32 v1, v13, v15
	v_cvt_pk_bf16_f32 v2, v17, v19
	v_cvt_pk_bf16_f32 v3, v21, v7
	global_store_dwordx4 v[4:5], v[0:3], off sc1
	s_waitcnt lgkmcnt(0)
	s_cbranch_scc1 .LBB0_267

.LBB0_270:
	s_ashr_i32 s2, s6, 31
	s_lshr_b32 s2, s2, 23
	s_add_i32 s2, s6, s2
	s_ashr_i32 s18, s2, 9
	s_and_b32 s2, s2, 0xfe00
	s_sub_i32 s2, s6, s2
	s_sext_i32_i16 s3, s2
	s_bfe_u32 s3, s3, 0x5001a
	s_add_i32 s3, s2, s3
	s_sext_i32_i16 s4, s3
	s_and_b32 s3, s3, 0xffe0
	s_sub_i32 s2, s2, s3
	s_sext_i32_i16 s3, s2
	s_lshl_b32 s2, s4, 1
	s_ashr_i32 s19, s18, 31
	s_andn2_b32 s2, s2, 63
	s_lshl_b32 s4, s3, 6
	s_lshl_b64 s[18:19], s[18:19], 23
	s_add_u32 s5, s7, s18
	s_addc_u32 s15, s14, s19
	s_ashr_i32 s3, s2, 31
	s_lshl_b64 s[18:19], s[2:3], 13
	s_add_u32 s16, s5, s18
	s_addc_u32 s15, s15, s19
	s_ashr_i32 s5, s4, 31
	s_lshl_b64 s[18:19], s[4:5], 2
	s_add_u32 s18, s16, s18
	s_addc_u32 s19, s15, s19
	v_lshl_add_u64 v[0:1], s[18:19], 0, v[96:97]
	v_lshl_add_u64 v[2:3], v[0:1], 0, v[60:61]
	flat_load_dwordx4 v[116:119], v[2:3] nt
	v_lshl_add_u64 v[2:3], v[0:1], 0, v[62:63]
	flat_load_dwordx4 v[56:59], v[2:3] nt
	v_lshl_add_u64 v[2:3], v[0:1], 0, v[64:65]
	flat_load_dwordx4 v[52:55], v[2:3] nt
	v_lshl_add_u64 v[2:3], v[0:1], 0, v[66:67]
	flat_load_dwordx4 v[48:51], v[2:3] nt
	v_lshl_add_u64 v[2:3], v[0:1], 0, v[68:69]
	flat_load_dwordx4 v[44:47], v[2:3] nt
	v_lshl_add_u64 v[2:3], v[0:1], 0, v[70:71]
	flat_load_dwordx4 v[40:43], v[2:3] nt
	v_lshl_add_u64 v[2:3], v[0:1], 0, v[72:73]
	flat_load_dwordx4 v[36:39], v[2:3] nt
	v_lshl_add_u64 v[2:3], v[0:1], 0, v[74:75]
	flat_load_dwordx4 v[32:35], v[2:3] nt
	v_lshl_add_u64 v[2:3], v[0:1], 0, v[76:77]
	flat_load_dwordx4 v[28:31], v[2:3] nt
	v_lshl_add_u64 v[2:3], v[0:1], 0, v[78:79]
	flat_load_dwordx4 v[24:27], v[2:3] nt
	v_lshl_add_u64 v[2:3], v[0:1], 0, v[80:81]
	flat_load_dwordx4 v[20:23], v[2:3] nt
	v_lshl_add_u64 v[2:3], v[0:1], 0, v[82:83]
	flat_load_dwordx4 v[16:19], v[2:3] nt
	v_lshl_add_u64 v[2:3], v[0:1], 0, v[84:85]
	flat_load_dwordx4 v[12:15], v[2:3] nt
	v_lshl_add_u64 v[2:3], v[0:1], 0, v[86:87]
	flat_load_dwordx4 v[8:11], v[2:3] nt
	v_lshl_add_u64 v[2:3], v[0:1], 0, v[88:89]
	flat_load_dwordx4 v[4:7], v[2:3] nt
	v_lshl_add_u64 v[0:1], v[0:1], 0, v[90:91]
	flat_load_dwordx4 v[0:3], v[0:1] nt
	v_add_u32_e32 v111, 0x410, v114
	s_lshl_b64 s[4:5], s[4:5], 11
	s_add_u32 s4, s22, s4
	s_addc_u32 s5, s23, s5
	s_lshl_b64 s[2:3], s[2:3], 1
	s_add_u32 s2, s4, s2
	s_addc_u32 s3, s5, s3
	s_add_i32 s6, s6, s39
	s_cmpk_lt_i32 s6, 0x200
	s_waitcnt vmcnt(0) lgkmcnt(0)
	ds_write2_b32 v114, v116, v117 offset1:1
	ds_write2_b32 v114, v118, v119 offset0:2 offset1:3
	ds_write2_b32 v111, v56, v57 offset1:1
	v_add_u32_e32 v56, 0x418, v114
	ds_write2_b32 v56, v58, v59 offset1:1
	v_add_u32_e32 v56, 0x820, v114
	ds_write2_b32 v56, v52, v53 offset1:1
	v_add_u32_e32 v52, 0x828, v114
	ds_write2_b32 v52, v54, v55 offset1:1
	v_add_u32_e32 v52, 0xc30, v114
	ds_write2_b32 v52, v48, v49 offset1:1
	v_add_u32_e32 v48, 0xc38, v114
	ds_write2_b32 v48, v50, v51 offset1:1
	v_add_u32_e32 v48, 0x1040, v114
	ds_write2_b32 v48, v44, v45 offset1:1
	v_add_u32_e32 v44, 0x1048, v114
	ds_write2_b32 v44, v46, v47 offset1:1
	v_add_u32_e32 v44, 0x1450, v114
	ds_write2_b32 v44, v40, v41 offset1:1
	v_add_u32_e32 v40, 0x1458, v114
	ds_write2_b32 v40, v42, v43 offset1:1
	v_add_u32_e32 v40, 0x1860, v114
	ds_write2_b32 v40, v36, v37 offset1:1
	v_add_u32_e32 v36, 0x1868, v114
	ds_write2_b32 v36, v38, v39 offset1:1
	v_add_u32_e32 v36, 0x1c70, v114
	ds_write2_b32 v36, v32, v33 offset1:1
	v_add_u32_e32 v32, 0x1c78, v114
	ds_write2_b32 v32, v34, v35 offset1:1
	v_add_u32_e32 v32, 0x2080, v114
	ds_write2_b32 v32, v28, v29 offset1:1
	v_add_u32_e32 v28, 0x2088, v114
	ds_write2_b32 v28, v30, v31 offset1:1
	v_add_u32_e32 v28, 0x2490, v114
	ds_write2_b32 v28, v24, v25 offset1:1
	v_add_u32_e32 v24, 0x2498, v114
	ds_write2_b32 v24, v26, v27 offset1:1
	v_add_u32_e32 v24, 0x28a0, v114
	ds_write2_b32 v24, v20, v21 offset1:1
	v_add_u32_e32 v20, 0x28a8, v114
	ds_write2_b32 v20, v22, v23 offset1:1
	v_add_u32_e32 v20, 0x2cb0, v114
	ds_write2_b32 v20, v16, v17 offset1:1
	v_add_u32_e32 v16, 0x2cb8, v114
	ds_write2_b32 v16, v18, v19 offset1:1
	v_add_u32_e32 v16, 0x30c0, v114
	ds_write2_b32 v16, v12, v13 offset1:1
	v_add_u32_e32 v12, 0x30c8, v114
	ds_write2_b32 v12, v14, v15 offset1:1
	v_add_u32_e32 v12, 0x34d0, v114
	ds_write2_b32 v12, v8, v9 offset1:1
	v_add_u32_e32 v8, 0x34d8, v114
	ds_write2_b32 v8, v10, v11 offset1:1
	v_add_u32_e32 v8, 0x38e0, v114
	ds_write2_b32 v8, v4, v5 offset1:1
	v_add_u32_e32 v4, 0x38e8, v114
	ds_write2_b32 v4, v6, v7 offset1:1
	v_add_u32_e32 v4, 0x3cf0, v114
	ds_write2_b32 v4, v0, v1 offset1:1
	v_add_u32_e32 v0, 0x3cf8, v114
	ds_write2_b32 v0, v2, v3 offset1:1
	s_waitcnt lgkmcnt(0)
	ds_read2_b32 v[6:7], v113 offset0:65 offset1:73
	ds_read2_b32 v[8:9], v113 offset1:8
	ds_read2_b32 v[10:11], v113 offset0:130 offset1:138
	ds_read2_b32 v[12:13], v113 offset0:195 offset1:203
	v_mov_b32_e32 v111, v97
	v_lshl_add_u64 v[4:5], s[2:3], 0, v[110:111]
	v_lshl_add_u64 v[22:23], v[4:5], 0, v[92:93]
	s_waitcnt lgkmcnt(2)
	v_cvt_pk_bf16_f32 v0, v8, v6
	v_add_u32_e32 v6, 0x400, v113
	ds_read2_b32 v[14:15], v6 offset0:4 offset1:12
	ds_read2_b32 v[16:17], v6 offset0:69 offset1:77
	ds_read2_b32 v[18:19], v6 offset0:134 offset1:142
	ds_read2_b32 v[20:21], v6 offset0:199 offset1:207
	s_waitcnt lgkmcnt(4)
	v_cvt_pk_bf16_f32 v1, v10, v12
	v_lshl_add_u64 v[24:25], v[4:5], 0, v[98:99]
	s_waitcnt lgkmcnt(2)
	v_cvt_pk_bf16_f32 v2, v14, v16
	s_waitcnt lgkmcnt(0)
	v_cvt_pk_bf16_f32 v3, v18, v20
	global_store_dwordx4 v[22:23], v[0:3], off sc1
	s_nop 1
	v_cvt_pk_bf16_f32 v0, v9, v7
	v_cvt_pk_bf16_f32 v1, v11, v13
	v_cvt_pk_bf16_f32 v2, v15, v17
	v_cvt_pk_bf16_f32 v3, v19, v21
	v_lshl_add_u64 v[8:9], v[4:5], 0, v[94:95]
	global_store_dwordx4 v[8:9], v[0:3], off sc1
	ds_read2_b32 v[8:9], v113 offset0:81 offset1:89
	ds_read2_b32 v[10:11], v113 offset0:16 offset1:24
	ds_read2_b32 v[12:13], v113 offset0:146 offset1:154
	ds_read2_b32 v[14:15], v113 offset0:211 offset1:219
	ds_read2_b32 v[16:17], v6 offset0:20 offset1:28
	ds_read2_b32 v[18:19], v6 offset0:85 offset1:93
	ds_read2_b32 v[20:21], v6 offset0:150 offset1:158
	ds_read2_b32 v[22:23], v6 offset0:215 offset1:223
	s_waitcnt lgkmcnt(6)
	v_cvt_pk_bf16_f32 v0, v10, v8
	s_waitcnt lgkmcnt(4)
	v_cvt_pk_bf16_f32 v1, v12, v14
	s_waitcnt lgkmcnt(2)
	v_cvt_pk_bf16_f32 v2, v16, v18
	s_waitcnt lgkmcnt(0)
	v_cvt_pk_bf16_f32 v3, v20, v22
	global_store_dwordx4 v[24:25], v[0:3], off sc1
	v_lshl_add_u64 v[24:25], v[4:5], 0, v[102:103]
	s_nop 0
	v_cvt_pk_bf16_f32 v0, v11, v9
	v_cvt_pk_bf16_f32 v1, v13, v15
	v_cvt_pk_bf16_f32 v2, v17, v19
	v_cvt_pk_bf16_f32 v3, v21, v23
	v_lshl_add_u64 v[8:9], v[4:5], 0, v[100:101]
	global_store_dwordx4 v[8:9], v[0:3], off sc1
	ds_read2_b32 v[8:9], v113 offset0:32 offset1:40
	ds_read2_b32 v[10:11], v113 offset0:97 offset1:105
	ds_read2_b32 v[12:13], v113 offset0:162 offset1:170
	ds_read2_b32 v[14:15], v113 offset0:227 offset1:235
	ds_read2_b32 v[16:17], v6 offset0:36 offset1:44
	ds_read2_b32 v[18:19], v6 offset0:101 offset1:109
	ds_read2_b32 v[20:21], v6 offset0:166 offset1:174
	ds_read2_b32 v[22:23], v6 offset0:231 offset1:239
	s_waitcnt lgkmcnt(6)
	v_cvt_pk_bf16_f32 v0, v8, v10
	s_waitcnt lgkmcnt(4)
	v_cvt_pk_bf16_f32 v1, v12, v14
	s_waitcnt lgkmcnt(2)
	v_cvt_pk_bf16_f32 v2, v16, v18
	s_waitcnt lgkmcnt(0)
	v_cvt_pk_bf16_f32 v3, v20, v22
	global_store_dwordx4 v[24:25], v[0:3], off sc1
	s_nop 1
	v_cvt_pk_bf16_f32 v0, v9, v11
	v_cvt_pk_bf16_f32 v1, v13, v15
	v_cvt_pk_bf16_f32 v2, v17, v19
	v_cvt_pk_bf16_f32 v3, v21, v23
	v_lshl_add_u64 v[8:9], v[4:5], 0, v[104:105]
	global_store_dwordx4 v[8:9], v[0:3], off sc1
	ds_read2_b32 v[8:9], v113 offset0:48 offset1:56
	ds_read2_b32 v[10:11], v113 offset0:113 offset1:121
	ds_read2_b32 v[12:13], v113 offset0:178 offset1:186
	ds_read2_b32 v[14:15], v113 offset0:243 offset1:251
	ds_read2_b32 v[16:17], v6 offset0:52 offset1:60
	ds_read2_b32 v[18:19], v6 offset0:117 offset1:125
	ds_read2_b32 v[20:21], v6 offset0:182 offset1:190
	ds_read2_b32 v[6:7], v6 offset0:247 offset1:255
	v_lshl_add_u64 v[22:23], v[4:5], 0, v[106:107]
	s_waitcnt lgkmcnt(6)
	v_cvt_pk_bf16_f32 v0, v8, v10
	s_waitcnt lgkmcnt(4)
	v_cvt_pk_bf16_f32 v1, v12, v14
	s_waitcnt lgkmcnt(2)
	v_cvt_pk_bf16_f32 v2, v16, v18
	s_waitcnt lgkmcnt(0)
	v_cvt_pk_bf16_f32 v3, v20, v6
	global_store_dwordx4 v[22:23], v[0:3], off sc1
	v_lshl_add_u64 v[4:5], v[4:5], 0, v[108:109]
	s_nop 0
	v_cvt_pk_bf16_f32 v0, v9, v11
	v_cvt_pk_bf16_f32 v1, v13, v15
	v_cvt_pk_bf16_f32 v2, v17, v19
	v_cvt_pk_bf16_f32 v3, v21, v7
	global_store_dwordx4 v[4:5], v[0:3], off sc1
	s_waitcnt lgkmcnt(0)
	s_cbranch_scc1 .LBB0_270

.LBB0_273:
	s_ashr_i32 s2, s6, 31
	s_lshr_b32 s2, s2, 23
	s_add_i32 s2, s6, s2
	s_ashr_i32 s18, s2, 9
	s_and_b32 s2, s2, 0xfe00
	s_sub_i32 s2, s6, s2
	s_sext_i32_i16 s3, s2
	s_bfe_u32 s3, s3, 0x5001a
	s_add_i32 s3, s2, s3
	s_sext_i32_i16 s4, s3
	s_and_b32 s3, s3, 0xffe0
	s_sub_i32 s2, s2, s3
	s_sext_i32_i16 s3, s2
	s_lshl_b32 s2, s4, 1
	s_ashr_i32 s19, s18, 31
	s_andn2_b32 s2, s2, 63
	s_lshl_b32 s4, s3, 6
	s_lshl_b64 s[18:19], s[18:19], 23
	s_add_u32 s5, s7, s18
	s_addc_u32 s15, s14, s19
	s_ashr_i32 s3, s2, 31
	s_lshl_b64 s[18:19], s[2:3], 13
	s_add_u32 s16, s5, s18
	s_addc_u32 s15, s15, s19
	s_ashr_i32 s5, s4, 31
	s_lshl_b64 s[18:19], s[4:5], 2
	s_add_u32 s18, s16, s18
	s_addc_u32 s19, s15, s19
	v_lshl_add_u64 v[0:1], s[18:19], 0, v[96:97]
	v_lshl_add_u64 v[2:3], v[0:1], 0, v[60:61]
	flat_load_dwordx4 v[116:119], v[2:3] nt
	v_lshl_add_u64 v[2:3], v[0:1], 0, v[62:63]
	flat_load_dwordx4 v[56:59], v[2:3] nt
	v_lshl_add_u64 v[2:3], v[0:1], 0, v[64:65]
	flat_load_dwordx4 v[52:55], v[2:3] nt
	v_lshl_add_u64 v[2:3], v[0:1], 0, v[66:67]
	flat_load_dwordx4 v[48:51], v[2:3] nt
	v_lshl_add_u64 v[2:3], v[0:1], 0, v[68:69]
	flat_load_dwordx4 v[44:47], v[2:3] nt
	v_lshl_add_u64 v[2:3], v[0:1], 0, v[70:71]
	flat_load_dwordx4 v[40:43], v[2:3] nt
	v_lshl_add_u64 v[2:3], v[0:1], 0, v[72:73]
	flat_load_dwordx4 v[36:39], v[2:3] nt
	v_lshl_add_u64 v[2:3], v[0:1], 0, v[74:75]
	flat_load_dwordx4 v[32:35], v[2:3] nt
	v_lshl_add_u64 v[2:3], v[0:1], 0, v[76:77]
	flat_load_dwordx4 v[28:31], v[2:3] nt
	v_lshl_add_u64 v[2:3], v[0:1], 0, v[78:79]
	flat_load_dwordx4 v[24:27], v[2:3] nt
	v_lshl_add_u64 v[2:3], v[0:1], 0, v[80:81]
	flat_load_dwordx4 v[20:23], v[2:3] nt
	v_lshl_add_u64 v[2:3], v[0:1], 0, v[82:83]
	flat_load_dwordx4 v[16:19], v[2:3] nt
	v_lshl_add_u64 v[2:3], v[0:1], 0, v[84:85]
	flat_load_dwordx4 v[12:15], v[2:3] nt
	v_lshl_add_u64 v[2:3], v[0:1], 0, v[86:87]
	flat_load_dwordx4 v[8:11], v[2:3] nt
	v_lshl_add_u64 v[2:3], v[0:1], 0, v[88:89]
	flat_load_dwordx4 v[4:7], v[2:3] nt
	v_lshl_add_u64 v[0:1], v[0:1], 0, v[90:91]
	flat_load_dwordx4 v[0:3], v[0:1] nt
	v_add_u32_e32 v111, 0x410, v114
	s_lshl_b64 s[4:5], s[4:5], 11
	s_add_u32 s4, s24, s4
	s_addc_u32 s5, s25, s5
	s_lshl_b64 s[2:3], s[2:3], 1
	s_add_u32 s2, s4, s2
	s_addc_u32 s3, s5, s3
	s_add_i32 s6, s6, s39
	s_cmpk_lt_i32 s6, 0x200
	s_waitcnt vmcnt(0) lgkmcnt(0)
	ds_write2_b32 v114, v116, v117 offset1:1
	ds_write2_b32 v114, v118, v119 offset0:2 offset1:3
	ds_write2_b32 v111, v56, v57 offset1:1
	v_add_u32_e32 v56, 0x418, v114
	ds_write2_b32 v56, v58, v59 offset1:1
	v_add_u32_e32 v56, 0x820, v114
	ds_write2_b32 v56, v52, v53 offset1:1
	v_add_u32_e32 v52, 0x828, v114
	ds_write2_b32 v52, v54, v55 offset1:1
	v_add_u32_e32 v52, 0xc30, v114
	ds_write2_b32 v52, v48, v49 offset1:1
	v_add_u32_e32 v48, 0xc38, v114
	ds_write2_b32 v48, v50, v51 offset1:1
	v_add_u32_e32 v48, 0x1040, v114
	ds_write2_b32 v48, v44, v45 offset1:1
	v_add_u32_e32 v44, 0x1048, v114
	ds_write2_b32 v44, v46, v47 offset1:1
	v_add_u32_e32 v44, 0x1450, v114
	ds_write2_b32 v44, v40, v41 offset1:1
	v_add_u32_e32 v40, 0x1458, v114
	ds_write2_b32 v40, v42, v43 offset1:1
	v_add_u32_e32 v40, 0x1860, v114
	ds_write2_b32 v40, v36, v37 offset1:1
	v_add_u32_e32 v36, 0x1868, v114
	ds_write2_b32 v36, v38, v39 offset1:1
	v_add_u32_e32 v36, 0x1c70, v114
	ds_write2_b32 v36, v32, v33 offset1:1
	v_add_u32_e32 v32, 0x1c78, v114
	ds_write2_b32 v32, v34, v35 offset1:1
	v_add_u32_e32 v32, 0x2080, v114
	ds_write2_b32 v32, v28, v29 offset1:1
	v_add_u32_e32 v28, 0x2088, v114
	ds_write2_b32 v28, v30, v31 offset1:1
	v_add_u32_e32 v28, 0x2490, v114
	ds_write2_b32 v28, v24, v25 offset1:1
	v_add_u32_e32 v24, 0x2498, v114
	ds_write2_b32 v24, v26, v27 offset1:1
	v_add_u32_e32 v24, 0x28a0, v114
	ds_write2_b32 v24, v20, v21 offset1:1
	v_add_u32_e32 v20, 0x28a8, v114
	ds_write2_b32 v20, v22, v23 offset1:1
	v_add_u32_e32 v20, 0x2cb0, v114
	ds_write2_b32 v20, v16, v17 offset1:1
	v_add_u32_e32 v16, 0x2cb8, v114
	ds_write2_b32 v16, v18, v19 offset1:1
	v_add_u32_e32 v16, 0x30c0, v114
	ds_write2_b32 v16, v12, v13 offset1:1
	v_add_u32_e32 v12, 0x30c8, v114
	ds_write2_b32 v12, v14, v15 offset1:1
	v_add_u32_e32 v12, 0x34d0, v114
	ds_write2_b32 v12, v8, v9 offset1:1
	v_add_u32_e32 v8, 0x34d8, v114
	ds_write2_b32 v8, v10, v11 offset1:1
	v_add_u32_e32 v8, 0x38e0, v114
	ds_write2_b32 v8, v4, v5 offset1:1
	v_add_u32_e32 v4, 0x38e8, v114
	ds_write2_b32 v4, v6, v7 offset1:1
	v_add_u32_e32 v4, 0x3cf0, v114
	ds_write2_b32 v4, v0, v1 offset1:1
	v_add_u32_e32 v0, 0x3cf8, v114
	ds_write2_b32 v0, v2, v3 offset1:1
	s_waitcnt lgkmcnt(0)
	ds_read2_b32 v[6:7], v113 offset0:65 offset1:73
	ds_read2_b32 v[8:9], v113 offset1:8
	ds_read2_b32 v[10:11], v113 offset0:130 offset1:138
	ds_read2_b32 v[12:13], v113 offset0:195 offset1:203
	v_mov_b32_e32 v111, v97
	v_lshl_add_u64 v[4:5], s[2:3], 0, v[110:111]
	v_lshl_add_u64 v[22:23], v[4:5], 0, v[92:93]
	s_waitcnt lgkmcnt(2)
	v_cvt_pk_bf16_f32 v0, v8, v6
	v_add_u32_e32 v6, 0x400, v113
	ds_read2_b32 v[14:15], v6 offset0:4 offset1:12
	ds_read2_b32 v[16:17], v6 offset0:69 offset1:77
	ds_read2_b32 v[18:19], v6 offset0:134 offset1:142
	ds_read2_b32 v[20:21], v6 offset0:199 offset1:207
	s_waitcnt lgkmcnt(4)
	v_cvt_pk_bf16_f32 v1, v10, v12
	v_lshl_add_u64 v[24:25], v[4:5], 0, v[98:99]
	s_waitcnt lgkmcnt(2)
	v_cvt_pk_bf16_f32 v2, v14, v16
	s_waitcnt lgkmcnt(0)
	v_cvt_pk_bf16_f32 v3, v18, v20
	global_store_dwordx4 v[22:23], v[0:3], off sc1
	s_nop 1
	v_cvt_pk_bf16_f32 v0, v9, v7
	v_cvt_pk_bf16_f32 v1, v11, v13
	v_cvt_pk_bf16_f32 v2, v15, v17
	v_cvt_pk_bf16_f32 v3, v19, v21
	v_lshl_add_u64 v[8:9], v[4:5], 0, v[94:95]
	global_store_dwordx4 v[8:9], v[0:3], off sc1
	ds_read2_b32 v[8:9], v113 offset0:81 offset1:89
	ds_read2_b32 v[10:11], v113 offset0:16 offset1:24
	ds_read2_b32 v[12:13], v113 offset0:146 offset1:154
	ds_read2_b32 v[14:15], v113 offset0:211 offset1:219
	ds_read2_b32 v[16:17], v6 offset0:20 offset1:28
	ds_read2_b32 v[18:19], v6 offset0:85 offset1:93
	ds_read2_b32 v[20:21], v6 offset0:150 offset1:158
	ds_read2_b32 v[22:23], v6 offset0:215 offset1:223
	s_waitcnt lgkmcnt(6)
	v_cvt_pk_bf16_f32 v0, v10, v8
	s_waitcnt lgkmcnt(4)
	v_cvt_pk_bf16_f32 v1, v12, v14
	s_waitcnt lgkmcnt(2)
	v_cvt_pk_bf16_f32 v2, v16, v18
	s_waitcnt lgkmcnt(0)
	v_cvt_pk_bf16_f32 v3, v20, v22
	global_store_dwordx4 v[24:25], v[0:3], off sc1
	v_lshl_add_u64 v[24:25], v[4:5], 0, v[102:103]
	s_nop 0
	v_cvt_pk_bf16_f32 v0, v11, v9
	v_cvt_pk_bf16_f32 v1, v13, v15
	v_cvt_pk_bf16_f32 v2, v17, v19
	v_cvt_pk_bf16_f32 v3, v21, v23
	v_lshl_add_u64 v[8:9], v[4:5], 0, v[100:101]
	global_store_dwordx4 v[8:9], v[0:3], off sc1
	ds_read2_b32 v[8:9], v113 offset0:32 offset1:40
	ds_read2_b32 v[10:11], v113 offset0:97 offset1:105
	ds_read2_b32 v[12:13], v113 offset0:162 offset1:170
	ds_read2_b32 v[14:15], v113 offset0:227 offset1:235
	ds_read2_b32 v[16:17], v6 offset0:36 offset1:44
	ds_read2_b32 v[18:19], v6 offset0:101 offset1:109
	ds_read2_b32 v[20:21], v6 offset0:166 offset1:174
	ds_read2_b32 v[22:23], v6 offset0:231 offset1:239
	s_waitcnt lgkmcnt(6)
	v_cvt_pk_bf16_f32 v0, v8, v10
	s_waitcnt lgkmcnt(4)
	v_cvt_pk_bf16_f32 v1, v12, v14
	s_waitcnt lgkmcnt(2)
	v_cvt_pk_bf16_f32 v2, v16, v18
	s_waitcnt lgkmcnt(0)
	v_cvt_pk_bf16_f32 v3, v20, v22
	global_store_dwordx4 v[24:25], v[0:3], off sc1
	s_nop 1
	v_cvt_pk_bf16_f32 v0, v9, v11
	v_cvt_pk_bf16_f32 v1, v13, v15
	v_cvt_pk_bf16_f32 v2, v17, v19
	v_cvt_pk_bf16_f32 v3, v21, v23
	v_lshl_add_u64 v[8:9], v[4:5], 0, v[104:105]
	global_store_dwordx4 v[8:9], v[0:3], off sc1
	ds_read2_b32 v[8:9], v113 offset0:48 offset1:56
	ds_read2_b32 v[10:11], v113 offset0:113 offset1:121
	ds_read2_b32 v[12:13], v113 offset0:178 offset1:186
	ds_read2_b32 v[14:15], v113 offset0:243 offset1:251
	ds_read2_b32 v[16:17], v6 offset0:52 offset1:60
	ds_read2_b32 v[18:19], v6 offset0:117 offset1:125
	ds_read2_b32 v[20:21], v6 offset0:182 offset1:190
	ds_read2_b32 v[6:7], v6 offset0:247 offset1:255
	v_lshl_add_u64 v[22:23], v[4:5], 0, v[106:107]
	s_waitcnt lgkmcnt(6)
	v_cvt_pk_bf16_f32 v0, v8, v10
	s_waitcnt lgkmcnt(4)
	v_cvt_pk_bf16_f32 v1, v12, v14
	s_waitcnt lgkmcnt(2)
	v_cvt_pk_bf16_f32 v2, v16, v18
	s_waitcnt lgkmcnt(0)
	v_cvt_pk_bf16_f32 v3, v20, v6
	global_store_dwordx4 v[22:23], v[0:3], off sc1
	v_lshl_add_u64 v[4:5], v[4:5], 0, v[108:109]
	s_nop 0
	v_cvt_pk_bf16_f32 v0, v9, v11
	v_cvt_pk_bf16_f32 v1, v13, v15
	v_cvt_pk_bf16_f32 v2, v17, v19
	v_cvt_pk_bf16_f32 v3, v21, v7
	global_store_dwordx4 v[4:5], v[0:3], off sc1
	s_waitcnt lgkmcnt(0)
	s_cbranch_scc1 .LBB0_273

.LBB0_276:
	s_ashr_i32 s2, s6, 31
	s_lshr_b32 s2, s2, 22
	s_add_i32 s2, s6, s2
	s_ashr_i32 s18, s2, 10
	s_and_b32 s2, s2, 0xfc00
	s_sub_i32 s2, s6, s2
	s_sext_i32_i16 s3, s2
	s_bfe_u32 s3, s3, 0x5001a
	s_add_i32 s3, s2, s3
	s_sext_i32_i16 s4, s3
	s_and_b32 s3, s3, 0xffe0
	s_sub_i32 s2, s2, s3
	s_sext_i32_i16 s3, s2
	s_lshl_b32 s2, s4, 1
	s_ashr_i32 s19, s18, 31
	s_andn2_b32 s2, s2, 63
	s_lshl_b32 s4, s3, 6
	s_lshl_b64 s[18:19], s[18:19], 24
	s_add_u32 s5, s7, s18
	s_addc_u32 s15, s14, s19
	s_ashr_i32 s3, s2, 31
	s_lshl_b64 s[18:19], s[2:3], 13
	s_add_u32 s16, s5, s18
	s_addc_u32 s15, s15, s19
	s_ashr_i32 s5, s4, 31
	s_lshl_b64 s[18:19], s[4:5], 2
	s_add_u32 s18, s16, s18
	s_addc_u32 s19, s15, s19
	v_lshl_add_u64 v[0:1], s[18:19], 0, v[96:97]
	v_lshl_add_u64 v[2:3], v[0:1], 0, v[60:61]
	flat_load_dwordx4 v[116:119], v[2:3] nt
	v_lshl_add_u64 v[2:3], v[0:1], 0, v[62:63]
	flat_load_dwordx4 v[56:59], v[2:3] nt
	v_lshl_add_u64 v[2:3], v[0:1], 0, v[64:65]
	flat_load_dwordx4 v[52:55], v[2:3] nt
	v_lshl_add_u64 v[2:3], v[0:1], 0, v[66:67]
	flat_load_dwordx4 v[48:51], v[2:3] nt
	v_lshl_add_u64 v[2:3], v[0:1], 0, v[68:69]
	flat_load_dwordx4 v[44:47], v[2:3] nt
	v_lshl_add_u64 v[2:3], v[0:1], 0, v[70:71]
	flat_load_dwordx4 v[40:43], v[2:3] nt
	v_lshl_add_u64 v[2:3], v[0:1], 0, v[72:73]
	flat_load_dwordx4 v[36:39], v[2:3] nt
	v_lshl_add_u64 v[2:3], v[0:1], 0, v[74:75]
	flat_load_dwordx4 v[32:35], v[2:3] nt
	v_lshl_add_u64 v[2:3], v[0:1], 0, v[76:77]
	flat_load_dwordx4 v[28:31], v[2:3] nt
	v_lshl_add_u64 v[2:3], v[0:1], 0, v[78:79]
	flat_load_dwordx4 v[24:27], v[2:3] nt
	v_lshl_add_u64 v[2:3], v[0:1], 0, v[80:81]
	flat_load_dwordx4 v[20:23], v[2:3] nt
	v_lshl_add_u64 v[2:3], v[0:1], 0, v[82:83]
	flat_load_dwordx4 v[16:19], v[2:3] nt
	v_lshl_add_u64 v[2:3], v[0:1], 0, v[84:85]
	flat_load_dwordx4 v[12:15], v[2:3] nt
	v_lshl_add_u64 v[2:3], v[0:1], 0, v[86:87]
	flat_load_dwordx4 v[8:11], v[2:3] nt
	v_lshl_add_u64 v[2:3], v[0:1], 0, v[88:89]
	flat_load_dwordx4 v[4:7], v[2:3] nt
	v_lshl_add_u64 v[0:1], v[0:1], 0, v[90:91]
	flat_load_dwordx4 v[0:3], v[0:1] nt
	v_add_u32_e32 v111, 0x410, v114
	s_lshl_b64 s[4:5], s[4:5], 12
	s_add_u32 s4, s26, s4
	s_addc_u32 s5, s27, s5
	s_lshl_b64 s[2:3], s[2:3], 1
	s_add_u32 s2, s4, s2
	s_addc_u32 s3, s5, s3
	s_add_i32 s6, s6, s39
	s_cmpk_lt_i32 s6, 0x400
	s_waitcnt vmcnt(0) lgkmcnt(0)
	ds_write2_b32 v114, v116, v117 offset1:1
	ds_write2_b32 v114, v118, v119 offset0:2 offset1:3
	ds_write2_b32 v111, v56, v57 offset1:1
	v_add_u32_e32 v56, 0x418, v114
	ds_write2_b32 v56, v58, v59 offset1:1
	v_add_u32_e32 v56, 0x820, v114
	ds_write2_b32 v56, v52, v53 offset1:1
	v_add_u32_e32 v52, 0x828, v114
	ds_write2_b32 v52, v54, v55 offset1:1
	v_add_u32_e32 v52, 0xc30, v114
	ds_write2_b32 v52, v48, v49 offset1:1
	v_add_u32_e32 v48, 0xc38, v114
	ds_write2_b32 v48, v50, v51 offset1:1
	v_add_u32_e32 v48, 0x1040, v114
	ds_write2_b32 v48, v44, v45 offset1:1
	v_add_u32_e32 v44, 0x1048, v114
	ds_write2_b32 v44, v46, v47 offset1:1
	v_add_u32_e32 v44, 0x1450, v114
	ds_write2_b32 v44, v40, v41 offset1:1
	v_add_u32_e32 v40, 0x1458, v114
	ds_write2_b32 v40, v42, v43 offset1:1
	v_add_u32_e32 v40, 0x1860, v114
	ds_write2_b32 v40, v36, v37 offset1:1
	v_add_u32_e32 v36, 0x1868, v114
	ds_write2_b32 v36, v38, v39 offset1:1
	v_add_u32_e32 v36, 0x1c70, v114
	ds_write2_b32 v36, v32, v33 offset1:1
	v_add_u32_e32 v32, 0x1c78, v114
	ds_write2_b32 v32, v34, v35 offset1:1
	v_add_u32_e32 v32, 0x2080, v114
	ds_write2_b32 v32, v28, v29 offset1:1
	v_add_u32_e32 v28, 0x2088, v114
	ds_write2_b32 v28, v30, v31 offset1:1
	v_add_u32_e32 v28, 0x2490, v114
	ds_write2_b32 v28, v24, v25 offset1:1
	v_add_u32_e32 v24, 0x2498, v114
	ds_write2_b32 v24, v26, v27 offset1:1
	v_add_u32_e32 v24, 0x28a0, v114
	ds_write2_b32 v24, v20, v21 offset1:1
	v_add_u32_e32 v20, 0x28a8, v114
	ds_write2_b32 v20, v22, v23 offset1:1
	v_add_u32_e32 v20, 0x2cb0, v114
	ds_write2_b32 v20, v16, v17 offset1:1
	v_add_u32_e32 v16, 0x2cb8, v114
	ds_write2_b32 v16, v18, v19 offset1:1
	v_add_u32_e32 v16, 0x30c0, v114
	ds_write2_b32 v16, v12, v13 offset1:1
	v_add_u32_e32 v12, 0x30c8, v114
	ds_write2_b32 v12, v14, v15 offset1:1
	v_add_u32_e32 v12, 0x34d0, v114
	ds_write2_b32 v12, v8, v9 offset1:1
	v_add_u32_e32 v8, 0x34d8, v114
	ds_write2_b32 v8, v10, v11 offset1:1
	v_add_u32_e32 v8, 0x38e0, v114
	ds_write2_b32 v8, v4, v5 offset1:1
	v_add_u32_e32 v4, 0x38e8, v114
	ds_write2_b32 v4, v6, v7 offset1:1
	v_add_u32_e32 v4, 0x3cf0, v114
	ds_write2_b32 v4, v0, v1 offset1:1
	v_add_u32_e32 v0, 0x3cf8, v114
	ds_write2_b32 v0, v2, v3 offset1:1
	s_waitcnt lgkmcnt(0)
	ds_read2_b32 v[6:7], v113 offset0:65 offset1:73
	ds_read2_b32 v[8:9], v113 offset1:8
	ds_read2_b32 v[10:11], v113 offset0:130 offset1:138
	ds_read2_b32 v[12:13], v113 offset0:195 offset1:203
	v_mov_b32_e32 v111, v97
	v_lshl_add_u64 v[4:5], s[2:3], 0, v[110:111]
	v_lshl_add_u64 v[22:23], v[4:5], 0, v[92:93]
	s_waitcnt lgkmcnt(2)
	v_cvt_pk_bf16_f32 v0, v8, v6
	v_add_u32_e32 v6, 0x400, v113
	ds_read2_b32 v[14:15], v6 offset0:4 offset1:12
	ds_read2_b32 v[16:17], v6 offset0:69 offset1:77
	ds_read2_b32 v[18:19], v6 offset0:134 offset1:142
	ds_read2_b32 v[20:21], v6 offset0:199 offset1:207
	s_waitcnt lgkmcnt(4)
	v_cvt_pk_bf16_f32 v1, v10, v12
	v_lshl_add_u64 v[24:25], v[4:5], 0, v[98:99]
	s_waitcnt lgkmcnt(2)
	v_cvt_pk_bf16_f32 v2, v14, v16
	s_waitcnt lgkmcnt(0)
	v_cvt_pk_bf16_f32 v3, v18, v20
	global_store_dwordx4 v[22:23], v[0:3], off sc1
	s_nop 1
	v_cvt_pk_bf16_f32 v0, v9, v7
	v_cvt_pk_bf16_f32 v1, v11, v13
	v_cvt_pk_bf16_f32 v2, v15, v17
	v_cvt_pk_bf16_f32 v3, v19, v21
	v_lshl_add_u64 v[8:9], v[4:5], 0, v[94:95]
	global_store_dwordx4 v[8:9], v[0:3], off sc1
	ds_read2_b32 v[8:9], v113 offset0:81 offset1:89
	ds_read2_b32 v[10:11], v113 offset0:16 offset1:24
	ds_read2_b32 v[12:13], v113 offset0:146 offset1:154
	ds_read2_b32 v[14:15], v113 offset0:211 offset1:219
	ds_read2_b32 v[16:17], v6 offset0:20 offset1:28
	ds_read2_b32 v[18:19], v6 offset0:85 offset1:93
	ds_read2_b32 v[20:21], v6 offset0:150 offset1:158
	ds_read2_b32 v[22:23], v6 offset0:215 offset1:223
	s_waitcnt lgkmcnt(6)
	v_cvt_pk_bf16_f32 v0, v10, v8
	s_waitcnt lgkmcnt(4)
	v_cvt_pk_bf16_f32 v1, v12, v14
	s_waitcnt lgkmcnt(2)
	v_cvt_pk_bf16_f32 v2, v16, v18
	s_waitcnt lgkmcnt(0)
	v_cvt_pk_bf16_f32 v3, v20, v22
	global_store_dwordx4 v[24:25], v[0:3], off sc1
	v_lshl_add_u64 v[24:25], v[4:5], 0, v[102:103]
	s_nop 0
	v_cvt_pk_bf16_f32 v0, v11, v9
	v_cvt_pk_bf16_f32 v1, v13, v15
	v_cvt_pk_bf16_f32 v2, v17, v19
	v_cvt_pk_bf16_f32 v3, v21, v23
	v_lshl_add_u64 v[8:9], v[4:5], 0, v[100:101]
	global_store_dwordx4 v[8:9], v[0:3], off sc1
	ds_read2_b32 v[8:9], v113 offset0:32 offset1:40
	ds_read2_b32 v[10:11], v113 offset0:97 offset1:105
	ds_read2_b32 v[12:13], v113 offset0:162 offset1:170
	ds_read2_b32 v[14:15], v113 offset0:227 offset1:235
	ds_read2_b32 v[16:17], v6 offset0:36 offset1:44
	ds_read2_b32 v[18:19], v6 offset0:101 offset1:109
	ds_read2_b32 v[20:21], v6 offset0:166 offset1:174
	ds_read2_b32 v[22:23], v6 offset0:231 offset1:239
	s_waitcnt lgkmcnt(6)
	v_cvt_pk_bf16_f32 v0, v8, v10
	s_waitcnt lgkmcnt(4)
	v_cvt_pk_bf16_f32 v1, v12, v14
	s_waitcnt lgkmcnt(2)
	v_cvt_pk_bf16_f32 v2, v16, v18
	s_waitcnt lgkmcnt(0)
	v_cvt_pk_bf16_f32 v3, v20, v22
	global_store_dwordx4 v[24:25], v[0:3], off sc1
	s_nop 1
	v_cvt_pk_bf16_f32 v0, v9, v11
	v_cvt_pk_bf16_f32 v1, v13, v15
	v_cvt_pk_bf16_f32 v2, v17, v19
	v_cvt_pk_bf16_f32 v3, v21, v23
	v_lshl_add_u64 v[8:9], v[4:5], 0, v[104:105]
	global_store_dwordx4 v[8:9], v[0:3], off sc1
	ds_read2_b32 v[8:9], v113 offset0:48 offset1:56
	ds_read2_b32 v[10:11], v113 offset0:113 offset1:121
	ds_read2_b32 v[12:13], v113 offset0:178 offset1:186
	ds_read2_b32 v[14:15], v113 offset0:243 offset1:251
	ds_read2_b32 v[16:17], v6 offset0:52 offset1:60
	ds_read2_b32 v[18:19], v6 offset0:117 offset1:125
	ds_read2_b32 v[20:21], v6 offset0:182 offset1:190
	ds_read2_b32 v[6:7], v6 offset0:247 offset1:255
	v_lshl_add_u64 v[22:23], v[4:5], 0, v[106:107]
	s_waitcnt lgkmcnt(6)
	v_cvt_pk_bf16_f32 v0, v8, v10
	s_waitcnt lgkmcnt(4)
	v_cvt_pk_bf16_f32 v1, v12, v14
	s_waitcnt lgkmcnt(2)
	v_cvt_pk_bf16_f32 v2, v16, v18
	s_waitcnt lgkmcnt(0)
	v_cvt_pk_bf16_f32 v3, v20, v6
	global_store_dwordx4 v[22:23], v[0:3], off sc1
	v_lshl_add_u64 v[4:5], v[4:5], 0, v[108:109]
	s_nop 0
	v_cvt_pk_bf16_f32 v0, v9, v11
	v_cvt_pk_bf16_f32 v1, v13, v15
	v_cvt_pk_bf16_f32 v2, v17, v19
	v_cvt_pk_bf16_f32 v3, v21, v7
	global_store_dwordx4 v[4:5], v[0:3], off sc1
	s_waitcnt lgkmcnt(0)
	s_cbranch_scc1 .LBB0_276

.LBB0_279:
	s_ashr_i32 s2, s14, 31
	s_lshr_b32 s2, s2, 28
	s_add_i32 s3, s14, s2
	s_ashr_i32 s2, s3, 4
	s_and_b32 s3, s3, 0xfff0
	s_sub_i32 s3, s14, s3
	s_bfe_i32 s4, s3, 0x80000
	s_bfe_u32 s4, s4, 0x2000d
	s_add_i32 s4, s3, s4
	s_bfe_i32 s5, s4, 0x80000
	s_and_b32 s4, s4, 0xfc
	s_sub_i32 s3, s3, s4
	s_sext_i32_i16 s5, s5
	s_sext_i32_i8 s3, s3
	s_lshl_b32 s4, s5, 4
	s_lshl_b32 s6, s3, 6
	s_ashr_i32 s3, s2, 31
	s_andn2_b32 s4, s4, 63
	s_lshl_b64 s[18:19], s[2:3], 18
	s_add_u32 s7, s15, s18
	s_addc_u32 s20, s16, s19
	s_ashr_i32 s5, s4, 31
	s_lshl_b64 s[18:19], s[4:5], 10
	s_add_u32 s21, s7, s18
	s_addc_u32 s20, s20, s19
	s_ashr_i32 s7, s6, 31
	s_lshl_b64 s[18:19], s[6:7], 2
	s_add_u32 s18, s21, s18
	s_addc_u32 s19, s20, s19
	v_lshl_add_u64 v[0:1], s[18:19], 0, v[96:97]
	v_lshl_add_u64 v[2:3], v[0:1], 0, v[60:61]
	flat_load_dwordx4 v[116:119], v[2:3] nt
	v_lshl_add_u64 v[2:3], v[0:1], 0, v[62:63]
	flat_load_dwordx4 v[56:59], v[2:3] nt
	v_lshl_add_u64 v[2:3], v[0:1], 0, v[64:65]
	flat_load_dwordx4 v[52:55], v[2:3] nt
	v_lshl_add_u64 v[2:3], v[0:1], 0, v[66:67]
	flat_load_dwordx4 v[48:51], v[2:3] nt
	v_lshl_add_u64 v[2:3], v[0:1], 0, v[68:69]
	flat_load_dwordx4 v[44:47], v[2:3] nt
	v_lshl_add_u64 v[2:3], v[0:1], 0, v[70:71]
	flat_load_dwordx4 v[40:43], v[2:3] nt
	v_lshl_add_u64 v[2:3], v[0:1], 0, v[72:73]
	flat_load_dwordx4 v[36:39], v[2:3] nt
	v_lshl_add_u64 v[2:3], v[0:1], 0, v[74:75]
	flat_load_dwordx4 v[32:35], v[2:3] nt
	v_lshl_add_u64 v[2:3], v[0:1], 0, v[76:77]
	flat_load_dwordx4 v[28:31], v[2:3] nt
	v_lshl_add_u64 v[2:3], v[0:1], 0, v[78:79]
	flat_load_dwordx4 v[24:27], v[2:3] nt
	v_lshl_add_u64 v[2:3], v[0:1], 0, v[80:81]
	flat_load_dwordx4 v[20:23], v[2:3] nt
	v_lshl_add_u64 v[2:3], v[0:1], 0, v[82:83]
	flat_load_dwordx4 v[16:19], v[2:3] nt
	v_lshl_add_u64 v[2:3], v[0:1], 0, v[84:85]
	flat_load_dwordx4 v[12:15], v[2:3] nt
	v_lshl_add_u64 v[2:3], v[0:1], 0, v[86:87]
	flat_load_dwordx4 v[8:11], v[2:3] nt
	v_lshl_add_u64 v[2:3], v[0:1], 0, v[88:89]
	flat_load_dwordx4 v[4:7], v[2:3] nt
	v_lshl_add_u64 v[0:1], v[0:1], 0, v[90:91]
	flat_load_dwordx4 v[0:3], v[0:1] nt
	v_add_u32_e32 v111, 0x410, v114
	s_lshl_b64 s[2:3], s[2:3], 17
	s_add_u32 s18, s28, s2
	s_addc_u32 s19, s29, s3
	s_lshl_b64 s[2:3], s[6:7], 9
	s_add_u32 s6, s18, s2
	s_addc_u32 s7, s19, s3
	s_lshl_b64 s[2:3], s[4:5], 1
	s_add_u32 s2, s6, s2
	s_addc_u32 s3, s7, s3
	s_add_i32 s14, s14, s39
	s_cmp_lt_i32 s14, 64
	s_waitcnt vmcnt(0) lgkmcnt(0)
	ds_write2_b32 v114, v116, v117 offset1:1
	ds_write2_b32 v114, v118, v119 offset0:2 offset1:3
	ds_write2_b32 v111, v56, v57 offset1:1
	v_add_u32_e32 v56, 0x418, v114
	ds_write2_b32 v56, v58, v59 offset1:1
	v_add_u32_e32 v56, 0x820, v114
	ds_write2_b32 v56, v52, v53 offset1:1
	v_add_u32_e32 v52, 0x828, v114
	ds_write2_b32 v52, v54, v55 offset1:1
	v_add_u32_e32 v52, 0xc30, v114
	ds_write2_b32 v52, v48, v49 offset1:1
	v_add_u32_e32 v48, 0xc38, v114
	ds_write2_b32 v48, v50, v51 offset1:1
	v_add_u32_e32 v48, 0x1040, v114
	ds_write2_b32 v48, v44, v45 offset1:1
	v_add_u32_e32 v44, 0x1048, v114
	ds_write2_b32 v44, v46, v47 offset1:1
	v_add_u32_e32 v44, 0x1450, v114
	ds_write2_b32 v44, v40, v41 offset1:1
	v_add_u32_e32 v40, 0x1458, v114
	ds_write2_b32 v40, v42, v43 offset1:1
	v_add_u32_e32 v40, 0x1860, v114
	ds_write2_b32 v40, v36, v37 offset1:1
	v_add_u32_e32 v36, 0x1868, v114
	ds_write2_b32 v36, v38, v39 offset1:1
	v_add_u32_e32 v36, 0x1c70, v114
	ds_write2_b32 v36, v32, v33 offset1:1
	v_add_u32_e32 v32, 0x1c78, v114
	ds_write2_b32 v32, v34, v35 offset1:1
	v_add_u32_e32 v32, 0x2080, v114
	ds_write2_b32 v32, v28, v29 offset1:1
	v_add_u32_e32 v28, 0x2088, v114
	ds_write2_b32 v28, v30, v31 offset1:1
	v_add_u32_e32 v28, 0x2490, v114
	ds_write2_b32 v28, v24, v25 offset1:1
	v_add_u32_e32 v24, 0x2498, v114
	ds_write2_b32 v24, v26, v27 offset1:1
	v_add_u32_e32 v24, 0x28a0, v114
	ds_write2_b32 v24, v20, v21 offset1:1
	v_add_u32_e32 v20, 0x28a8, v114
	ds_write2_b32 v20, v22, v23 offset1:1
	v_add_u32_e32 v20, 0x2cb0, v114
	ds_write2_b32 v20, v16, v17 offset1:1
	v_add_u32_e32 v16, 0x2cb8, v114
	ds_write2_b32 v16, v18, v19 offset1:1
	v_add_u32_e32 v16, 0x30c0, v114
	ds_write2_b32 v16, v12, v13 offset1:1
	v_add_u32_e32 v12, 0x30c8, v114
	ds_write2_b32 v12, v14, v15 offset1:1
	v_add_u32_e32 v12, 0x34d0, v114
	ds_write2_b32 v12, v8, v9 offset1:1
	v_add_u32_e32 v8, 0x34d8, v114
	ds_write2_b32 v8, v10, v11 offset1:1
	v_add_u32_e32 v8, 0x38e0, v114
	ds_write2_b32 v8, v4, v5 offset1:1
	v_add_u32_e32 v4, 0x38e8, v114
	ds_write2_b32 v4, v6, v7 offset1:1
	v_add_u32_e32 v4, 0x3cf0, v114
	ds_write2_b32 v4, v0, v1 offset1:1
	v_add_u32_e32 v0, 0x3cf8, v114
	ds_write2_b32 v0, v2, v3 offset1:1
	s_waitcnt lgkmcnt(0)
	ds_read2_b32 v[6:7], v113 offset0:65 offset1:73
	ds_read2_b32 v[8:9], v113 offset1:8
	ds_read2_b32 v[10:11], v113 offset0:130 offset1:138
	ds_read2_b32 v[12:13], v113 offset0:195 offset1:203
	v_mov_b32_e32 v111, v97
	v_lshl_add_u64 v[4:5], s[2:3], 0, v[110:111]
	v_lshl_add_u64 v[22:23], v[4:5], 0, v[92:93]
	s_waitcnt lgkmcnt(2)
	v_cvt_pk_bf16_f32 v0, v8, v6
	v_add_u32_e32 v6, 0x400, v113
	ds_read2_b32 v[14:15], v6 offset0:4 offset1:12
	ds_read2_b32 v[16:17], v6 offset0:69 offset1:77
	ds_read2_b32 v[18:19], v6 offset0:134 offset1:142
	ds_read2_b32 v[20:21], v6 offset0:199 offset1:207
	s_waitcnt lgkmcnt(4)
	v_cvt_pk_bf16_f32 v1, v10, v12
	v_lshl_add_u64 v[24:25], v[4:5], 0, v[98:99]
	s_waitcnt lgkmcnt(2)
	v_cvt_pk_bf16_f32 v2, v14, v16
	s_waitcnt lgkmcnt(0)
	v_cvt_pk_bf16_f32 v3, v18, v20
	global_store_dwordx4 v[22:23], v[0:3], off sc1
	s_nop 1
	v_cvt_pk_bf16_f32 v0, v9, v7
	v_cvt_pk_bf16_f32 v1, v11, v13
	v_cvt_pk_bf16_f32 v2, v15, v17
	v_cvt_pk_bf16_f32 v3, v19, v21
	v_lshl_add_u64 v[8:9], v[4:5], 0, v[94:95]
	global_store_dwordx4 v[8:9], v[0:3], off sc1
	ds_read2_b32 v[8:9], v113 offset0:81 offset1:89
	ds_read2_b32 v[10:11], v113 offset0:16 offset1:24
	ds_read2_b32 v[12:13], v113 offset0:146 offset1:154
	ds_read2_b32 v[14:15], v113 offset0:211 offset1:219
	ds_read2_b32 v[16:17], v6 offset0:20 offset1:28
	ds_read2_b32 v[18:19], v6 offset0:85 offset1:93
	ds_read2_b32 v[20:21], v6 offset0:150 offset1:158
	ds_read2_b32 v[22:23], v6 offset0:215 offset1:223
	s_waitcnt lgkmcnt(6)
	v_cvt_pk_bf16_f32 v0, v10, v8
	s_waitcnt lgkmcnt(4)
	v_cvt_pk_bf16_f32 v1, v12, v14
	s_waitcnt lgkmcnt(2)
	v_cvt_pk_bf16_f32 v2, v16, v18
	s_waitcnt lgkmcnt(0)
	v_cvt_pk_bf16_f32 v3, v20, v22
	global_store_dwordx4 v[24:25], v[0:3], off sc1
	v_lshl_add_u64 v[24:25], v[4:5], 0, v[102:103]
	s_nop 0
	v_cvt_pk_bf16_f32 v0, v11, v9
	v_cvt_pk_bf16_f32 v1, v13, v15
	v_cvt_pk_bf16_f32 v2, v17, v19
	v_cvt_pk_bf16_f32 v3, v21, v23
	v_lshl_add_u64 v[8:9], v[4:5], 0, v[100:101]
	global_store_dwordx4 v[8:9], v[0:3], off sc1
	ds_read2_b32 v[8:9], v113 offset0:97 offset1:105
	ds_read2_b32 v[10:11], v113 offset0:32 offset1:40
	ds_read2_b32 v[12:13], v113 offset0:162 offset1:170
	ds_read2_b32 v[14:15], v113 offset0:227 offset1:235
	ds_read2_b32 v[16:17], v6 offset0:36 offset1:44
	ds_read2_b32 v[18:19], v6 offset0:101 offset1:109
	ds_read2_b32 v[20:21], v6 offset0:166 offset1:174
	ds_read2_b32 v[22:23], v6 offset0:231 offset1:239
	s_waitcnt lgkmcnt(6)
	v_cvt_pk_bf16_f32 v0, v10, v8
	s_waitcnt lgkmcnt(4)
	v_cvt_pk_bf16_f32 v1, v12, v14
	s_waitcnt lgkmcnt(2)
	v_cvt_pk_bf16_f32 v2, v16, v18
	s_waitcnt lgkmcnt(0)
	v_cvt_pk_bf16_f32 v3, v20, v22
	global_store_dwordx4 v[24:25], v[0:3], off sc1
	s_nop 1
	v_cvt_pk_bf16_f32 v0, v11, v9
	v_cvt_pk_bf16_f32 v1, v13, v15
	v_cvt_pk_bf16_f32 v2, v17, v19
	v_cvt_pk_bf16_f32 v3, v21, v23
	v_lshl_add_u64 v[8:9], v[4:5], 0, v[104:105]
	global_store_dwordx4 v[8:9], v[0:3], off sc1
	ds_read2_b32 v[8:9], v113 offset0:48 offset1:56
	ds_read2_b32 v[10:11], v113 offset0:113 offset1:121
	ds_read2_b32 v[12:13], v113 offset0:178 offset1:186
	ds_read2_b32 v[14:15], v113 offset0:243 offset1:251
	ds_read2_b32 v[16:17], v6 offset0:52 offset1:60
	ds_read2_b32 v[18:19], v6 offset0:117 offset1:125
	ds_read2_b32 v[20:21], v6 offset0:182 offset1:190
	ds_read2_b32 v[6:7], v6 offset0:247 offset1:255
	v_lshl_add_u64 v[22:23], v[4:5], 0, v[106:107]
	s_waitcnt lgkmcnt(6)
	v_cvt_pk_bf16_f32 v0, v8, v10
	s_waitcnt lgkmcnt(4)
	v_cvt_pk_bf16_f32 v1, v12, v14
	s_waitcnt lgkmcnt(2)
	v_cvt_pk_bf16_f32 v2, v16, v18
	s_waitcnt lgkmcnt(0)
	v_cvt_pk_bf16_f32 v3, v20, v6
	global_store_dwordx4 v[22:23], v[0:3], off sc1
	v_lshl_add_u64 v[4:5], v[4:5], 0, v[108:109]
	s_nop 0
	v_cvt_pk_bf16_f32 v0, v9, v11
	v_cvt_pk_bf16_f32 v1, v13, v15
	v_cvt_pk_bf16_f32 v2, v17, v19
	v_cvt_pk_bf16_f32 v3, v21, v7
	global_store_dwordx4 v[4:5], v[0:3], off sc1
	s_waitcnt lgkmcnt(0)
	s_cbranch_scc1 .LBB0_279

.LBB0_282:
	s_ashr_i32 s2, s6, 31
	s_lshr_b32 s2, s2, 28
	s_add_i32 s2, s6, s2
	s_ashr_i32 s4, s2, 4
	s_lshl_b32 s2, s4, 10
	s_ashr_i32 s5, s4, 31
	s_sub_i32 s2, s15, s2
	s_lshl_b64 s[18:19], s[4:5], 18
	s_add_u32 s20, s7, s18
	s_addc_u32 s21, s14, s19
	s_ashr_i32 s3, s2, 31
	s_lshl_b64 s[18:19], s[2:3], 2
	s_add_u32 s18, s20, s18
	s_addc_u32 s19, s21, s19
	v_lshl_add_u64 v[0:1], s[18:19], 0, v[96:97]
	v_lshl_add_u64 v[2:3], v[0:1], 0, v[52:53]
	flat_load_dwordx4 v[106:109], v[2:3] nt
	v_lshl_add_u64 v[2:3], v[0:1], 0, v[54:55]
	flat_load_dwordx4 v[114:117], v[2:3] nt
	v_lshl_add_u64 v[2:3], v[0:1], 0, v[56:57]
	flat_load_dwordx4 v[118:121], v[2:3] nt
	v_lshl_add_u64 v[2:3], v[0:1], 0, v[58:59]
	flat_load_dwordx4 v[48:51], v[2:3] nt
	v_lshl_add_u64 v[2:3], v[0:1], 0, v[60:61]
	flat_load_dwordx4 v[44:47], v[2:3] nt
	v_lshl_add_u64 v[2:3], v[0:1], 0, v[62:63]
	flat_load_dwordx4 v[40:43], v[2:3] nt
	v_lshl_add_u64 v[2:3], v[0:1], 0, v[64:65]
	flat_load_dwordx4 v[36:39], v[2:3] nt
	v_lshl_add_u64 v[2:3], v[0:1], 0, v[66:67]
	flat_load_dwordx4 v[32:35], v[2:3] nt
	v_lshl_add_u64 v[2:3], v[0:1], 0, v[68:69]
	flat_load_dwordx4 v[28:31], v[2:3] nt
	v_lshl_add_u64 v[2:3], v[0:1], 0, v[70:71]
	flat_load_dwordx4 v[24:27], v[2:3] nt
	v_lshl_add_u64 v[2:3], v[0:1], 0, v[72:73]
	flat_load_dwordx4 v[20:23], v[2:3] nt
	v_lshl_add_u64 v[2:3], v[0:1], 0, v[74:75]
	flat_load_dwordx4 v[16:19], v[2:3] nt
	v_lshl_add_u64 v[2:3], v[0:1], 0, v[76:77]
	flat_load_dwordx4 v[12:15], v[2:3] nt
	v_lshl_add_u64 v[2:3], v[0:1], 0, v[78:79]
	flat_load_dwordx4 v[8:11], v[2:3] nt
	v_lshl_add_u64 v[2:3], v[0:1], 0, v[80:81]
	flat_load_dwordx4 v[4:7], v[2:3] nt
	v_lshl_add_u64 v[0:1], v[0:1], 0, v[82:83]
	flat_load_dwordx4 v[0:3], v[0:1] nt
	v_add_u32_e32 v103, 0x410, v105
	s_lshl_b64 s[4:5], s[4:5], 17
	s_add_u32 s4, s30, s4
	s_addc_u32 s5, s31, s5
	s_lshl_b64 s[2:3], s[2:3], 7
	s_add_u32 s2, s4, s2
	s_addc_u32 s3, s5, s3
	s_add_i32 s6, s6, s39
	s_add_i32 s15, s15, s16
	s_cmp_lt_i32 s6, 32
	s_waitcnt vmcnt(0) lgkmcnt(0)
	ds_write2_b32 v105, v106, v107 offset1:1
	ds_write2_b32 v105, v108, v109 offset0:2 offset1:3
	ds_write2_b32 v103, v114, v115 offset1:1
	v_add_u32_e32 v103, 0x418, v105
	ds_write2_b32 v103, v116, v117 offset1:1
	v_add_u32_e32 v103, 0x820, v105
	ds_write2_b32 v103, v118, v119 offset1:1
	v_add_u32_e32 v103, 0x828, v105
	ds_write2_b32 v103, v120, v121 offset1:1
	v_add_u32_e32 v103, 0xc30, v105
	ds_write2_b32 v103, v48, v49 offset1:1
	v_add_u32_e32 v48, 0xc38, v105
	ds_write2_b32 v48, v50, v51 offset1:1
	v_add_u32_e32 v48, 0x1040, v105
	ds_write2_b32 v48, v44, v45 offset1:1
	v_add_u32_e32 v44, 0x1048, v105
	ds_write2_b32 v44, v46, v47 offset1:1
	v_add_u32_e32 v44, 0x1450, v105
	ds_write2_b32 v44, v40, v41 offset1:1
	v_add_u32_e32 v40, 0x1458, v105
	ds_write2_b32 v40, v42, v43 offset1:1
	v_add_u32_e32 v40, 0x1860, v105
	ds_write2_b32 v40, v36, v37 offset1:1
	v_add_u32_e32 v36, 0x1868, v105
	ds_write2_b32 v36, v38, v39 offset1:1
	v_add_u32_e32 v36, 0x1c70, v105
	ds_write2_b32 v36, v32, v33 offset1:1
	v_add_u32_e32 v32, 0x1c78, v105
	ds_write2_b32 v32, v34, v35 offset1:1
	v_add_u32_e32 v32, 0x2080, v105
	ds_write2_b32 v32, v28, v29 offset1:1
	v_add_u32_e32 v28, 0x2088, v105
	ds_write2_b32 v28, v30, v31 offset1:1
	v_add_u32_e32 v28, 0x2490, v105
	ds_write2_b32 v28, v24, v25 offset1:1
	v_add_u32_e32 v24, 0x2498, v105
	ds_write2_b32 v24, v26, v27 offset1:1
	v_add_u32_e32 v24, 0x28a0, v105
	ds_write2_b32 v24, v20, v21 offset1:1
	v_add_u32_e32 v20, 0x28a8, v105
	ds_write2_b32 v20, v22, v23 offset1:1
	v_add_u32_e32 v20, 0x2cb0, v105
	ds_write2_b32 v20, v16, v17 offset1:1
	v_add_u32_e32 v16, 0x2cb8, v105
	ds_write2_b32 v16, v18, v19 offset1:1
	v_add_u32_e32 v16, 0x30c0, v105
	ds_write2_b32 v16, v12, v13 offset1:1
	v_add_u32_e32 v12, 0x30c8, v105
	ds_write2_b32 v12, v14, v15 offset1:1
	v_add_u32_e32 v12, 0x34d0, v105
	ds_write2_b32 v12, v8, v9 offset1:1
	v_add_u32_e32 v8, 0x34d8, v105
	ds_write2_b32 v8, v10, v11 offset1:1
	v_add_u32_e32 v8, 0x38e0, v105
	ds_write2_b32 v8, v4, v5 offset1:1
	v_add_u32_e32 v4, 0x38e8, v105
	ds_write2_b32 v4, v6, v7 offset1:1
	v_add_u32_e32 v4, 0x3cf0, v105
	ds_write2_b32 v4, v0, v1 offset1:1
	v_add_u32_e32 v0, 0x3cf8, v105
	ds_write2_b32 v0, v2, v3 offset1:1
	s_waitcnt lgkmcnt(0)
	v_add_u32_e32 v24, 0x400, v104
	ds_read2_b32 v[6:7], v104 offset0:65 offset1:73
	ds_read2_b32 v[8:9], v104 offset1:8
	ds_read2_b32 v[10:11], v104 offset0:130 offset1:138
	ds_read2_b32 v[12:13], v104 offset0:195 offset1:203
	ds_read2_b32 v[14:15], v24 offset0:4 offset1:12
	ds_read2_b32 v[16:17], v24 offset0:69 offset1:77
	ds_read2_b32 v[18:19], v24 offset0:134 offset1:142
	ds_read2_b32 v[20:21], v24 offset0:199 offset1:207
	v_mov_b32_e32 v103, v97
	v_lshl_add_u64 v[4:5], s[2:3], 0, v[102:103]
	s_waitcnt lgkmcnt(6)
	v_cvt_pk_bf16_f32 v0, v8, v6
	s_waitcnt lgkmcnt(4)
	v_cvt_pk_bf16_f32 v1, v10, v12
	s_waitcnt lgkmcnt(2)
	v_cvt_pk_bf16_f32 v2, v14, v16
	s_waitcnt lgkmcnt(0)
	v_cvt_pk_bf16_f32 v3, v18, v20
	v_lshl_add_u64 v[22:23], v[4:5], 0, v[84:85]
	global_store_dwordx4 v[22:23], v[0:3], off sc1
	v_lshl_add_u64 v[22:23], v[4:5], 0, v[88:89]
	s_nop 0
	v_cvt_pk_bf16_f32 v0, v9, v7
	v_cvt_pk_bf16_f32 v1, v11, v13
	v_cvt_pk_bf16_f32 v2, v15, v17
	v_cvt_pk_bf16_f32 v3, v19, v21
	v_lshl_add_u64 v[6:7], v[4:5], 0, v[86:87]
	global_store_dwordx4 v[6:7], v[0:3], off sc1
	ds_read2_b32 v[6:7], v104 offset0:81 offset1:89
	ds_read2_b32 v[8:9], v104 offset0:16 offset1:24
	ds_read2_b32 v[10:11], v104 offset0:146 offset1:154
	ds_read2_b32 v[12:13], v104 offset0:211 offset1:219
	ds_read2_b32 v[14:15], v24 offset0:20 offset1:28
	ds_read2_b32 v[16:17], v24 offset0:85 offset1:93
	ds_read2_b32 v[18:19], v24 offset0:150 offset1:158
	ds_read2_b32 v[20:21], v24 offset0:215 offset1:223
	s_waitcnt lgkmcnt(6)
	v_cvt_pk_bf16_f32 v0, v8, v6
	s_waitcnt lgkmcnt(4)
	v_cvt_pk_bf16_f32 v1, v10, v12
	s_waitcnt lgkmcnt(2)
	v_cvt_pk_bf16_f32 v2, v14, v16
	s_waitcnt lgkmcnt(0)
	v_cvt_pk_bf16_f32 v3, v18, v20
	global_store_dwordx4 v[22:23], v[0:3], off sc1
	v_lshl_add_u64 v[22:23], v[4:5], 0, v[92:93]
	s_nop 0
	v_cvt_pk_bf16_f32 v0, v9, v7
	v_cvt_pk_bf16_f32 v1, v11, v13
	v_cvt_pk_bf16_f32 v2, v15, v17
	v_cvt_pk_bf16_f32 v3, v19, v21
	v_lshl_add_u64 v[6:7], v[4:5], 0, v[90:91]
	global_store_dwordx4 v[6:7], v[0:3], off sc1
	ds_read2_b32 v[6:7], v104 offset0:32 offset1:40
	ds_read2_b32 v[8:9], v104 offset0:97 offset1:105
	ds_read2_b32 v[10:11], v104 offset0:162 offset1:170
	ds_read2_b32 v[12:13], v104 offset0:227 offset1:235
	ds_read2_b32 v[14:15], v24 offset0:36 offset1:44
	ds_read2_b32 v[16:17], v24 offset0:101 offset1:109
	ds_read2_b32 v[18:19], v24 offset0:166 offset1:174
	ds_read2_b32 v[20:21], v24 offset0:231 offset1:239
	s_waitcnt lgkmcnt(6)
	v_cvt_pk_bf16_f32 v0, v6, v8
	s_waitcnt lgkmcnt(4)
	v_cvt_pk_bf16_f32 v1, v10, v12
	s_waitcnt lgkmcnt(2)
	v_cvt_pk_bf16_f32 v2, v14, v16
	s_waitcnt lgkmcnt(0)
	v_cvt_pk_bf16_f32 v3, v18, v20
	global_store_dwordx4 v[22:23], v[0:3], off sc1
	v_lshl_add_u64 v[22:23], v[4:5], 0, v[98:99]
	s_nop 0
	v_cvt_pk_bf16_f32 v0, v7, v9
	v_cvt_pk_bf16_f32 v1, v11, v13
	v_cvt_pk_bf16_f32 v2, v15, v17
	v_cvt_pk_bf16_f32 v3, v19, v21
	v_lshl_add_u64 v[6:7], v[4:5], 0, v[94:95]
	global_store_dwordx4 v[6:7], v[0:3], off sc1
	ds_read2_b32 v[6:7], v104 offset0:48 offset1:56
	ds_read2_b32 v[8:9], v104 offset0:113 offset1:121
	ds_read2_b32 v[10:11], v104 offset0:178 offset1:186
	ds_read2_b32 v[12:13], v104 offset0:243 offset1:251
	ds_read2_b32 v[14:15], v24 offset0:52 offset1:60
	ds_read2_b32 v[16:17], v24 offset0:117 offset1:125
	ds_read2_b32 v[18:19], v24 offset0:182 offset1:190
	ds_read2_b32 v[20:21], v24 offset0:247 offset1:255
	v_lshl_add_u64 v[4:5], v[4:5], 0, v[100:101]
	s_waitcnt lgkmcnt(6)
	v_cvt_pk_bf16_f32 v0, v6, v8
	s_waitcnt lgkmcnt(4)
	v_cvt_pk_bf16_f32 v1, v10, v12
	s_waitcnt lgkmcnt(2)
	v_cvt_pk_bf16_f32 v2, v14, v16
	s_waitcnt lgkmcnt(0)
	v_cvt_pk_bf16_f32 v3, v18, v20
	global_store_dwordx4 v[22:23], v[0:3], off sc1
	s_nop 1
	v_cvt_pk_bf16_f32 v0, v7, v9
	v_cvt_pk_bf16_f32 v1, v11, v13
	v_cvt_pk_bf16_f32 v2, v15, v17
	v_cvt_pk_bf16_f32 v3, v19, v21
	global_store_dwordx4 v[4:5], v[0:3], off sc1
	s_waitcnt lgkmcnt(0)
	s_cbranch_scc1 .LBB0_282

.LBB0_285:
	s_ashr_i32 s2, s6, 31
	s_lshr_b32 s2, s2, 28
	s_add_i32 s2, s6, s2
	s_ashr_i32 s4, s2, 4
	s_lshl_b32 s2, s4, 10
	s_ashr_i32 s5, s4, 31
	s_sub_i32 s2, s15, s2
	s_lshl_b64 s[18:19], s[4:5], 18
	s_add_u32 s20, s7, s18
	s_addc_u32 s21, s14, s19
	s_ashr_i32 s3, s2, 31
	s_lshl_b64 s[18:19], s[2:3], 2
	s_add_u32 s18, s20, s18
	s_addc_u32 s19, s21, s19
	v_lshl_add_u64 v[0:1], s[18:19], 0, v[96:97]
	v_lshl_add_u64 v[2:3], v[0:1], 0, v[52:53]
	flat_load_dwordx4 v[106:109], v[2:3] nt
	v_lshl_add_u64 v[2:3], v[0:1], 0, v[54:55]
	flat_load_dwordx4 v[114:117], v[2:3] nt
	v_lshl_add_u64 v[2:3], v[0:1], 0, v[56:57]
	flat_load_dwordx4 v[118:121], v[2:3] nt
	v_lshl_add_u64 v[2:3], v[0:1], 0, v[58:59]
	flat_load_dwordx4 v[48:51], v[2:3] nt
	v_lshl_add_u64 v[2:3], v[0:1], 0, v[60:61]
	flat_load_dwordx4 v[44:47], v[2:3] nt
	v_lshl_add_u64 v[2:3], v[0:1], 0, v[62:63]
	flat_load_dwordx4 v[40:43], v[2:3] nt
	v_lshl_add_u64 v[2:3], v[0:1], 0, v[64:65]
	flat_load_dwordx4 v[36:39], v[2:3] nt
	v_lshl_add_u64 v[2:3], v[0:1], 0, v[66:67]
	flat_load_dwordx4 v[32:35], v[2:3] nt
	v_lshl_add_u64 v[2:3], v[0:1], 0, v[68:69]
	flat_load_dwordx4 v[28:31], v[2:3] nt
	v_lshl_add_u64 v[2:3], v[0:1], 0, v[70:71]
	flat_load_dwordx4 v[24:27], v[2:3] nt
	v_lshl_add_u64 v[2:3], v[0:1], 0, v[72:73]
	flat_load_dwordx4 v[20:23], v[2:3] nt
	v_lshl_add_u64 v[2:3], v[0:1], 0, v[74:75]
	flat_load_dwordx4 v[16:19], v[2:3] nt
	v_lshl_add_u64 v[2:3], v[0:1], 0, v[76:77]
	flat_load_dwordx4 v[12:15], v[2:3] nt
	v_lshl_add_u64 v[2:3], v[0:1], 0, v[78:79]
	flat_load_dwordx4 v[8:11], v[2:3] nt
	v_lshl_add_u64 v[2:3], v[0:1], 0, v[80:81]
	flat_load_dwordx4 v[4:7], v[2:3] nt
	v_lshl_add_u64 v[0:1], v[0:1], 0, v[82:83]
	flat_load_dwordx4 v[0:3], v[0:1] nt
	v_add_u32_e32 v103, 0x410, v105
	s_lshl_b64 s[4:5], s[4:5], 17
	s_add_u32 s4, s35, s4
	s_addc_u32 s5, s38, s5
	s_lshl_b64 s[2:3], s[2:3], 7
	s_add_u32 s2, s4, s2
	s_addc_u32 s3, s5, s3
	s_add_i32 s6, s6, s39
	s_add_i32 s15, s15, s16
	s_cmp_lt_i32 s6, 32
	s_waitcnt vmcnt(0) lgkmcnt(0)
	ds_write2_b32 v105, v106, v107 offset1:1
	ds_write2_b32 v105, v108, v109 offset0:2 offset1:3
	ds_write2_b32 v103, v114, v115 offset1:1
	v_add_u32_e32 v103, 0x418, v105
	ds_write2_b32 v103, v116, v117 offset1:1
	v_add_u32_e32 v103, 0x820, v105
	ds_write2_b32 v103, v118, v119 offset1:1
	v_add_u32_e32 v103, 0x828, v105
	ds_write2_b32 v103, v120, v121 offset1:1
	v_add_u32_e32 v103, 0xc30, v105
	ds_write2_b32 v103, v48, v49 offset1:1
	v_add_u32_e32 v48, 0xc38, v105
	ds_write2_b32 v48, v50, v51 offset1:1
	v_add_u32_e32 v48, 0x1040, v105
	ds_write2_b32 v48, v44, v45 offset1:1
	v_add_u32_e32 v44, 0x1048, v105
	ds_write2_b32 v44, v46, v47 offset1:1
	v_add_u32_e32 v44, 0x1450, v105
	ds_write2_b32 v44, v40, v41 offset1:1
	v_add_u32_e32 v40, 0x1458, v105
	ds_write2_b32 v40, v42, v43 offset1:1
	v_add_u32_e32 v40, 0x1860, v105
	ds_write2_b32 v40, v36, v37 offset1:1
	v_add_u32_e32 v36, 0x1868, v105
	ds_write2_b32 v36, v38, v39 offset1:1
	v_add_u32_e32 v36, 0x1c70, v105
	ds_write2_b32 v36, v32, v33 offset1:1
	v_add_u32_e32 v32, 0x1c78, v105
	ds_write2_b32 v32, v34, v35 offset1:1
	v_add_u32_e32 v32, 0x2080, v105
	ds_write2_b32 v32, v28, v29 offset1:1
	v_add_u32_e32 v28, 0x2088, v105
	ds_write2_b32 v28, v30, v31 offset1:1
	v_add_u32_e32 v28, 0x2490, v105
	ds_write2_b32 v28, v24, v25 offset1:1
	v_add_u32_e32 v24, 0x2498, v105
	ds_write2_b32 v24, v26, v27 offset1:1
	v_add_u32_e32 v24, 0x28a0, v105
	ds_write2_b32 v24, v20, v21 offset1:1
	v_add_u32_e32 v20, 0x28a8, v105
	ds_write2_b32 v20, v22, v23 offset1:1
	v_add_u32_e32 v20, 0x2cb0, v105
	ds_write2_b32 v20, v16, v17 offset1:1
	v_add_u32_e32 v16, 0x2cb8, v105
	ds_write2_b32 v16, v18, v19 offset1:1
	v_add_u32_e32 v16, 0x30c0, v105
	ds_write2_b32 v16, v12, v13 offset1:1
	v_add_u32_e32 v12, 0x30c8, v105
	ds_write2_b32 v12, v14, v15 offset1:1
	v_add_u32_e32 v12, 0x34d0, v105
	ds_write2_b32 v12, v8, v9 offset1:1
	v_add_u32_e32 v8, 0x34d8, v105
	ds_write2_b32 v8, v10, v11 offset1:1
	v_add_u32_e32 v8, 0x38e0, v105
	ds_write2_b32 v8, v4, v5 offset1:1
	v_add_u32_e32 v4, 0x38e8, v105
	ds_write2_b32 v4, v6, v7 offset1:1
	v_add_u32_e32 v4, 0x3cf0, v105
	ds_write2_b32 v4, v0, v1 offset1:1
	v_add_u32_e32 v0, 0x3cf8, v105
	ds_write2_b32 v0, v2, v3 offset1:1
	s_waitcnt lgkmcnt(0)
	v_add_u32_e32 v24, 0x400, v104
	ds_read2_b32 v[6:7], v104 offset0:65 offset1:73
	ds_read2_b32 v[8:9], v104 offset1:8
	ds_read2_b32 v[10:11], v104 offset0:130 offset1:138
	ds_read2_b32 v[12:13], v104 offset0:195 offset1:203
	ds_read2_b32 v[14:15], v24 offset0:4 offset1:12
	ds_read2_b32 v[16:17], v24 offset0:69 offset1:77
	ds_read2_b32 v[18:19], v24 offset0:134 offset1:142
	ds_read2_b32 v[20:21], v24 offset0:199 offset1:207
	v_mov_b32_e32 v103, v97
	v_lshl_add_u64 v[4:5], s[2:3], 0, v[102:103]
	s_waitcnt lgkmcnt(6)
	v_cvt_pk_bf16_f32 v0, v8, v6
	s_waitcnt lgkmcnt(4)
	v_cvt_pk_bf16_f32 v1, v10, v12
	s_waitcnt lgkmcnt(2)
	v_cvt_pk_bf16_f32 v2, v14, v16
	s_waitcnt lgkmcnt(0)
	v_cvt_pk_bf16_f32 v3, v18, v20
	v_lshl_add_u64 v[22:23], v[4:5], 0, v[84:85]
	global_store_dwordx4 v[22:23], v[0:3], off sc1
	v_lshl_add_u64 v[22:23], v[4:5], 0, v[88:89]
	s_nop 0
	v_cvt_pk_bf16_f32 v0, v9, v7
	v_cvt_pk_bf16_f32 v1, v11, v13
	v_cvt_pk_bf16_f32 v2, v15, v17
	v_cvt_pk_bf16_f32 v3, v19, v21
	v_lshl_add_u64 v[6:7], v[4:5], 0, v[86:87]
	global_store_dwordx4 v[6:7], v[0:3], off sc1
	ds_read2_b32 v[6:7], v104 offset0:81 offset1:89
	ds_read2_b32 v[8:9], v104 offset0:16 offset1:24
	ds_read2_b32 v[10:11], v104 offset0:146 offset1:154
	ds_read2_b32 v[12:13], v104 offset0:211 offset1:219
	ds_read2_b32 v[14:15], v24 offset0:20 offset1:28
	ds_read2_b32 v[16:17], v24 offset0:85 offset1:93
	ds_read2_b32 v[18:19], v24 offset0:150 offset1:158
	ds_read2_b32 v[20:21], v24 offset0:215 offset1:223
	s_waitcnt lgkmcnt(6)
	v_cvt_pk_bf16_f32 v0, v8, v6
	s_waitcnt lgkmcnt(4)
	v_cvt_pk_bf16_f32 v1, v10, v12
	s_waitcnt lgkmcnt(2)
	v_cvt_pk_bf16_f32 v2, v14, v16
	s_waitcnt lgkmcnt(0)
	v_cvt_pk_bf16_f32 v3, v18, v20
	global_store_dwordx4 v[22:23], v[0:3], off sc1
	v_lshl_add_u64 v[22:23], v[4:5], 0, v[92:93]
	s_nop 0
	v_cvt_pk_bf16_f32 v0, v9, v7
	v_cvt_pk_bf16_f32 v1, v11, v13
	v_cvt_pk_bf16_f32 v2, v15, v17
	v_cvt_pk_bf16_f32 v3, v19, v21
	v_lshl_add_u64 v[6:7], v[4:5], 0, v[90:91]
	global_store_dwordx4 v[6:7], v[0:3], off sc1
	ds_read2_b32 v[6:7], v104 offset0:32 offset1:40
	ds_read2_b32 v[8:9], v104 offset0:97 offset1:105
	ds_read2_b32 v[10:11], v104 offset0:162 offset1:170
	ds_read2_b32 v[12:13], v104 offset0:227 offset1:235
	ds_read2_b32 v[14:15], v24 offset0:36 offset1:44
	ds_read2_b32 v[16:17], v24 offset0:101 offset1:109
	ds_read2_b32 v[18:19], v24 offset0:166 offset1:174
	ds_read2_b32 v[20:21], v24 offset0:231 offset1:239
	s_waitcnt lgkmcnt(6)
	v_cvt_pk_bf16_f32 v0, v6, v8
	s_waitcnt lgkmcnt(4)
	v_cvt_pk_bf16_f32 v1, v10, v12
	s_waitcnt lgkmcnt(2)
	v_cvt_pk_bf16_f32 v2, v14, v16
	s_waitcnt lgkmcnt(0)
	v_cvt_pk_bf16_f32 v3, v18, v20
	global_store_dwordx4 v[22:23], v[0:3], off sc1
	v_lshl_add_u64 v[22:23], v[4:5], 0, v[98:99]
	s_nop 0
	v_cvt_pk_bf16_f32 v0, v7, v9
	v_cvt_pk_bf16_f32 v1, v11, v13
	v_cvt_pk_bf16_f32 v2, v15, v17
	v_cvt_pk_bf16_f32 v3, v19, v21
	v_lshl_add_u64 v[6:7], v[4:5], 0, v[94:95]
	global_store_dwordx4 v[6:7], v[0:3], off sc1
	ds_read2_b32 v[6:7], v104 offset0:48 offset1:56
	ds_read2_b32 v[8:9], v104 offset0:113 offset1:121
	ds_read2_b32 v[10:11], v104 offset0:178 offset1:186
	ds_read2_b32 v[12:13], v104 offset0:243 offset1:251
	ds_read2_b32 v[14:15], v24 offset0:52 offset1:60
	ds_read2_b32 v[16:17], v24 offset0:117 offset1:125
	ds_read2_b32 v[18:19], v24 offset0:182 offset1:190
	ds_read2_b32 v[20:21], v24 offset0:247 offset1:255
	v_lshl_add_u64 v[4:5], v[4:5], 0, v[100:101]
	s_waitcnt lgkmcnt(6)
	v_cvt_pk_bf16_f32 v0, v6, v8
	s_waitcnt lgkmcnt(4)
	v_cvt_pk_bf16_f32 v1, v10, v12
	s_waitcnt lgkmcnt(2)
	v_cvt_pk_bf16_f32 v2, v14, v16
	s_waitcnt lgkmcnt(0)
	v_cvt_pk_bf16_f32 v3, v18, v20
	global_store_dwordx4 v[22:23], v[0:3], off sc1
	s_nop 1
	v_cvt_pk_bf16_f32 v0, v7, v9
	v_cvt_pk_bf16_f32 v1, v11, v13
	v_cvt_pk_bf16_f32 v2, v15, v17
	v_cvt_pk_bf16_f32 v3, v19, v21
	global_store_dwordx4 v[4:5], v[0:3], off sc1
	s_waitcnt lgkmcnt(0)
	s_cbranch_scc1 .LBB0_285

.LBB0_288:
	s_mul_hi_i32 s2, s12, 0x66666667
	s_lshr_b32 s3, s2, 31
	s_ashr_i32 s2, s2, 5
	s_add_i32 s3, s2, s3
	s_mul_i32 s2, s3, 0xffffffb0
	s_add_i32 s2, s12, s2
	s_bfe_i32 s4, s2, 0x80000
	s_bfe_u32 s4, s4, 0x4000b
	s_add_i32 s4, s2, s4
	s_bfe_i32 s5, s4, 0x80000
	s_and_b32 s4, s4, 0xf0
	s_sext_i32_i16 s5, s5
	s_sub_i32 s2, s2, s4
	s_sext_i32_i8 s13, s2
	s_lshl_b32 s2, s5, 2
	s_andn2_b32 s2, s2, 63
	s_lshl_b32 s4, s13, 6
	s_mul_hi_i32 s5, s3, 0x140000
	s_mul_i32 s3, s3, 0x140000
	s_add_u32 s16, s6, s3
	s_addc_u32 s5, s7, s5
	s_ashr_i32 s3, s2, 31
	s_lshl_b64 s[14:15], s[2:3], 12
	s_add_u32 s16, s16, s14
	s_addc_u32 s18, s5, s15
	s_ashr_i32 s5, s4, 31
	s_lshl_b64 s[14:15], s[4:5], 2
	s_add_u32 s14, s16, s14
	s_addc_u32 s15, s18, s15
	v_lshl_add_u64 v[0:1], s[14:15], 0, v[96:97]
	v_lshl_add_u64 v[2:3], v[0:1], 0, v[60:61]
	flat_load_dwordx4 v[114:117], v[2:3] nt
	v_lshl_add_u64 v[2:3], v[0:1], 0, v[62:63]
	flat_load_dwordx4 v[56:59], v[2:3] nt
	v_lshl_add_u64 v[2:3], v[0:1], 0, v[64:65]
	flat_load_dwordx4 v[52:55], v[2:3] nt
	v_lshl_add_u64 v[2:3], v[0:1], 0, v[66:67]
	flat_load_dwordx4 v[48:51], v[2:3] nt
	v_lshl_add_u64 v[2:3], v[0:1], 0, v[68:69]
	flat_load_dwordx4 v[44:47], v[2:3] nt
	v_lshl_add_u64 v[2:3], v[0:1], 0, v[70:71]
	flat_load_dwordx4 v[40:43], v[2:3] nt
	v_lshl_add_u64 v[2:3], v[0:1], 0, v[72:73]
	flat_load_dwordx4 v[36:39], v[2:3] nt
	v_lshl_add_u64 v[2:3], v[0:1], 0, v[74:75]
	flat_load_dwordx4 v[32:35], v[2:3] nt
	v_lshl_add_u64 v[2:3], v[0:1], 0, v[76:77]
	flat_load_dwordx4 v[28:31], v[2:3] nt
	v_lshl_add_u64 v[2:3], v[0:1], 0, v[78:79]
	flat_load_dwordx4 v[24:27], v[2:3] nt
	v_lshl_add_u64 v[2:3], v[0:1], 0, v[80:81]
	flat_load_dwordx4 v[20:23], v[2:3] nt
	v_lshl_add_u64 v[2:3], v[0:1], 0, v[82:83]
	flat_load_dwordx4 v[16:19], v[2:3] nt
	v_lshl_add_u64 v[2:3], v[0:1], 0, v[84:85]
	flat_load_dwordx4 v[12:15], v[2:3] nt
	v_lshl_add_u64 v[2:3], v[0:1], 0, v[86:87]
	flat_load_dwordx4 v[8:11], v[2:3] nt
	v_lshl_add_u64 v[2:3], v[0:1], 0, v[88:89]
	flat_load_dwordx4 v[4:7], v[2:3] nt
	v_lshl_add_u64 v[0:1], v[0:1], 0, v[90:91]
	flat_load_dwordx4 v[0:3], v[0:1] nt
	v_add_u32_e32 v111, 0x410, v113
	s_mul_i32 s13, s13, 0xa000
	s_mul_hi_i32 s4, s4, 0x280
	s_add_u32 s5, s19, s13
	s_addc_u32 s4, s20, s4
	s_lshl_b64 s[2:3], s[2:3], 1
	s_add_u32 s2, s5, s2
	s_addc_u32 s3, s4, s3
	s_add_i32 s12, s12, s21
	s_cmpk_gt_i32 s12, 0x4f
	s_waitcnt vmcnt(0) lgkmcnt(0)
	ds_write2_b32 v113, v114, v115 offset1:1
	ds_write2_b32 v113, v116, v117 offset0:2 offset1:3
	ds_write2_b32 v111, v56, v57 offset1:1
	v_add_u32_e32 v56, 0x418, v113
	ds_write2_b32 v56, v58, v59 offset1:1
	v_add_u32_e32 v56, 0x820, v113
	ds_write2_b32 v56, v52, v53 offset1:1
	v_add_u32_e32 v52, 0x828, v113
	ds_write2_b32 v52, v54, v55 offset1:1
	v_add_u32_e32 v52, 0xc30, v113
	ds_write2_b32 v52, v48, v49 offset1:1
	v_add_u32_e32 v48, 0xc38, v113
	ds_write2_b32 v48, v50, v51 offset1:1
	v_add_u32_e32 v48, 0x1040, v113
	ds_write2_b32 v48, v44, v45 offset1:1
	v_add_u32_e32 v44, 0x1048, v113
	ds_write2_b32 v44, v46, v47 offset1:1
	v_add_u32_e32 v44, 0x1450, v113
	ds_write2_b32 v44, v40, v41 offset1:1
	v_add_u32_e32 v40, 0x1458, v113
	ds_write2_b32 v40, v42, v43 offset1:1
	v_add_u32_e32 v40, 0x1860, v113
	ds_write2_b32 v40, v36, v37 offset1:1
	v_add_u32_e32 v36, 0x1868, v113
	ds_write2_b32 v36, v38, v39 offset1:1
	v_add_u32_e32 v36, 0x1c70, v113
	ds_write2_b32 v36, v32, v33 offset1:1
	v_add_u32_e32 v32, 0x1c78, v113
	ds_write2_b32 v32, v34, v35 offset1:1
	v_add_u32_e32 v32, 0x2080, v113
	ds_write2_b32 v32, v28, v29 offset1:1
	v_add_u32_e32 v28, 0x2088, v113
	ds_write2_b32 v28, v30, v31 offset1:1
	v_add_u32_e32 v28, 0x2490, v113
	ds_write2_b32 v28, v24, v25 offset1:1
	v_add_u32_e32 v24, 0x2498, v113
	ds_write2_b32 v24, v26, v27 offset1:1
	v_add_u32_e32 v24, 0x28a0, v113
	ds_write2_b32 v24, v20, v21 offset1:1
	v_add_u32_e32 v20, 0x28a8, v113
	ds_write2_b32 v20, v22, v23 offset1:1
	v_add_u32_e32 v20, 0x2cb0, v113
	ds_write2_b32 v20, v16, v17 offset1:1
	v_add_u32_e32 v16, 0x2cb8, v113
	ds_write2_b32 v16, v18, v19 offset1:1
	v_add_u32_e32 v16, 0x30c0, v113
	ds_write2_b32 v16, v12, v13 offset1:1
	v_add_u32_e32 v12, 0x30c8, v113
	ds_write2_b32 v12, v14, v15 offset1:1
	v_add_u32_e32 v12, 0x34d0, v113
	ds_write2_b32 v12, v8, v9 offset1:1
	v_add_u32_e32 v8, 0x34d8, v113
	ds_write2_b32 v8, v10, v11 offset1:1
	v_add_u32_e32 v8, 0x38e0, v113
	ds_write2_b32 v8, v4, v5 offset1:1
	v_add_u32_e32 v4, 0x38e8, v113
	ds_write2_b32 v4, v6, v7 offset1:1
	v_add_u32_e32 v4, 0x3cf0, v113
	ds_write2_b32 v4, v0, v1 offset1:1
	v_add_u32_e32 v0, 0x3cf8, v113
	ds_write2_b32 v0, v2, v3 offset1:1
	s_waitcnt lgkmcnt(0)
	ds_read2_b32 v[6:7], v112 offset0:65 offset1:73
	ds_read2_b32 v[8:9], v112 offset1:8
	ds_read2_b32 v[10:11], v112 offset0:130 offset1:138
	ds_read2_b32 v[12:13], v112 offset0:195 offset1:203
	v_mov_b32_e32 v111, v97
	v_lshl_add_u64 v[4:5], s[2:3], 0, v[110:111]
	v_lshl_add_u64 v[22:23], v[4:5], 0, v[92:93]
	s_waitcnt lgkmcnt(2)
	v_cvt_pk_bf16_f32 v0, v8, v6
	v_add_u32_e32 v6, 0x400, v112
	ds_read2_b32 v[14:15], v6 offset0:4 offset1:12
	ds_read2_b32 v[16:17], v6 offset0:69 offset1:77
	ds_read2_b32 v[18:19], v6 offset0:134 offset1:142
	ds_read2_b32 v[20:21], v6 offset0:199 offset1:207
	s_waitcnt lgkmcnt(4)
	v_cvt_pk_bf16_f32 v1, v10, v12
	v_lshl_add_u64 v[24:25], v[4:5], 0, v[98:99]
	s_waitcnt lgkmcnt(2)
	v_cvt_pk_bf16_f32 v2, v14, v16
	s_waitcnt lgkmcnt(0)
	v_cvt_pk_bf16_f32 v3, v18, v20
	global_store_dwordx4 v[22:23], v[0:3], off sc1
	s_nop 1
	v_cvt_pk_bf16_f32 v0, v9, v7
	v_cvt_pk_bf16_f32 v1, v11, v13
	v_cvt_pk_bf16_f32 v2, v15, v17
	v_cvt_pk_bf16_f32 v3, v19, v21
	v_lshl_add_u64 v[8:9], v[4:5], 0, v[94:95]
	global_store_dwordx4 v[8:9], v[0:3], off sc1
	ds_read2_b32 v[8:9], v112 offset0:81 offset1:89
	ds_read2_b32 v[10:11], v112 offset0:16 offset1:24
	ds_read2_b32 v[12:13], v112 offset0:146 offset1:154
	ds_read2_b32 v[14:15], v112 offset0:211 offset1:219
	ds_read2_b32 v[16:17], v6 offset0:20 offset1:28
	ds_read2_b32 v[18:19], v6 offset0:85 offset1:93
	ds_read2_b32 v[20:21], v6 offset0:150 offset1:158
	ds_read2_b32 v[22:23], v6 offset0:215 offset1:223
	s_waitcnt lgkmcnt(6)
	v_cvt_pk_bf16_f32 v0, v10, v8
	s_waitcnt lgkmcnt(4)
	v_cvt_pk_bf16_f32 v1, v12, v14
	s_waitcnt lgkmcnt(2)
	v_cvt_pk_bf16_f32 v2, v16, v18
	s_waitcnt lgkmcnt(0)
	v_cvt_pk_bf16_f32 v3, v20, v22
	global_store_dwordx4 v[24:25], v[0:3], off sc1
	v_lshl_add_u64 v[24:25], v[4:5], 0, v[102:103]
	s_nop 0
	v_cvt_pk_bf16_f32 v0, v11, v9
	v_cvt_pk_bf16_f32 v1, v13, v15
	v_cvt_pk_bf16_f32 v2, v17, v19
	v_cvt_pk_bf16_f32 v3, v21, v23
	v_lshl_add_u64 v[8:9], v[4:5], 0, v[100:101]
	global_store_dwordx4 v[8:9], v[0:3], off sc1
	ds_read2_b32 v[8:9], v112 offset0:97 offset1:105
	ds_read2_b32 v[10:11], v112 offset0:32 offset1:40
	ds_read2_b32 v[12:13], v112 offset0:162 offset1:170
	ds_read2_b32 v[14:15], v112 offset0:227 offset1:235
	ds_read2_b32 v[16:17], v6 offset0:36 offset1:44
	ds_read2_b32 v[18:19], v6 offset0:101 offset1:109
	ds_read2_b32 v[20:21], v6 offset0:166 offset1:174
	ds_read2_b32 v[22:23], v6 offset0:231 offset1:239
	s_waitcnt lgkmcnt(6)
	v_cvt_pk_bf16_f32 v0, v10, v8
	s_waitcnt lgkmcnt(4)
	v_cvt_pk_bf16_f32 v1, v12, v14
	s_waitcnt lgkmcnt(2)
	v_cvt_pk_bf16_f32 v2, v16, v18
	s_waitcnt lgkmcnt(0)
	v_cvt_pk_bf16_f32 v3, v20, v22
	global_store_dwordx4 v[24:25], v[0:3], off sc1
	s_nop 1
	v_cvt_pk_bf16_f32 v0, v11, v9
	v_cvt_pk_bf16_f32 v1, v13, v15
	v_cvt_pk_bf16_f32 v2, v17, v19
	v_cvt_pk_bf16_f32 v3, v21, v23
	v_lshl_add_u64 v[8:9], v[4:5], 0, v[104:105]
	global_store_dwordx4 v[8:9], v[0:3], off sc1
	ds_read2_b32 v[8:9], v112 offset0:48 offset1:56
	ds_read2_b32 v[10:11], v112 offset0:113 offset1:121
	ds_read2_b32 v[12:13], v112 offset0:178 offset1:186
	ds_read2_b32 v[14:15], v112 offset0:243 offset1:251
	ds_read2_b32 v[16:17], v6 offset0:52 offset1:60
	ds_read2_b32 v[18:19], v6 offset0:117 offset1:125
	ds_read2_b32 v[20:21], v6 offset0:182 offset1:190
	ds_read2_b32 v[6:7], v6 offset0:247 offset1:255
	v_lshl_add_u64 v[22:23], v[4:5], 0, v[106:107]
	s_waitcnt lgkmcnt(6)
	v_cvt_pk_bf16_f32 v0, v8, v10
	s_waitcnt lgkmcnt(4)
	v_cvt_pk_bf16_f32 v1, v12, v14
	s_waitcnt lgkmcnt(2)
	v_cvt_pk_bf16_f32 v2, v16, v18
	s_waitcnt lgkmcnt(0)
	v_cvt_pk_bf16_f32 v3, v20, v6
	global_store_dwordx4 v[22:23], v[0:3], off sc1
	v_lshl_add_u64 v[4:5], v[4:5], 0, v[108:109]
	s_nop 0
	v_cvt_pk_bf16_f32 v0, v9, v11
	v_cvt_pk_bf16_f32 v1, v13, v15
	v_cvt_pk_bf16_f32 v2, v17, v19
	v_cvt_pk_bf16_f32 v3, v21, v7
	global_store_dwordx4 v[4:5], v[0:3], off sc1
	s_waitcnt lgkmcnt(0)
	s_cbranch_scc0 .LBB0_288

.LBB0_294:
	s_ashr_i32 s2, s14, 31
	s_lshr_b32 s2, s2, 23
	s_add_i32 s2, s14, s2
	s_ashr_i32 s4, s2, 9
	s_and_b32 s2, s2, 0xfe00
	s_sub_i32 s2, s14, s2
	s_sext_i32_i16 s3, s2
	s_bfe_u32 s3, s3, 0x4001b
	s_add_i32 s3, s2, s3
	s_sext_i32_i16 s5, s3
	s_and_b32 s3, s3, 0xfff0
	s_sub_i32 s2, s2, s3
	s_sext_i32_i16 s18, s2
	s_lshl_b32 s2, s5, 2
	s_ashr_i32 s5, s4, 31
	s_andn2_b32 s2, s2, 63
	s_lshl_b32 s6, s18, 6
	s_lshl_b64 s[4:5], s[4:5], 23
	s_add_u32 s7, s15, s4
	s_addc_u32 s19, s16, s5
	s_ashr_i32 s3, s2, 31
	s_lshl_b64 s[20:21], s[2:3], 12
	s_add_u32 s22, s7, s20
	s_addc_u32 s19, s19, s21
	s_ashr_i32 s7, s6, 31
	s_lshl_b64 s[20:21], s[6:7], 2
	s_add_u32 s20, s22, s20
	s_addc_u32 s21, s19, s21
	v_lshl_add_u64 v[0:1], s[20:21], 0, v[96:97]
	v_lshl_add_u64 v[2:3], v[0:1], 0, v[60:61]
	flat_load_dwordx4 v[116:119], v[2:3] nt
	v_lshl_add_u64 v[2:3], v[0:1], 0, v[62:63]
	flat_load_dwordx4 v[56:59], v[2:3] nt
	v_lshl_add_u64 v[2:3], v[0:1], 0, v[64:65]
	flat_load_dwordx4 v[52:55], v[2:3] nt
	v_lshl_add_u64 v[2:3], v[0:1], 0, v[66:67]
	flat_load_dwordx4 v[48:51], v[2:3] nt
	v_lshl_add_u64 v[2:3], v[0:1], 0, v[68:69]
	flat_load_dwordx4 v[44:47], v[2:3] nt
	v_lshl_add_u64 v[2:3], v[0:1], 0, v[70:71]
	flat_load_dwordx4 v[40:43], v[2:3] nt
	v_lshl_add_u64 v[2:3], v[0:1], 0, v[72:73]
	flat_load_dwordx4 v[36:39], v[2:3] nt
	v_lshl_add_u64 v[2:3], v[0:1], 0, v[74:75]
	flat_load_dwordx4 v[32:35], v[2:3] nt
	v_lshl_add_u64 v[2:3], v[0:1], 0, v[76:77]
	flat_load_dwordx4 v[28:31], v[2:3] nt
	v_lshl_add_u64 v[2:3], v[0:1], 0, v[78:79]
	flat_load_dwordx4 v[24:27], v[2:3] nt
	v_lshl_add_u64 v[2:3], v[0:1], 0, v[80:81]
	flat_load_dwordx4 v[20:23], v[2:3] nt
	v_lshl_add_u64 v[2:3], v[0:1], 0, v[82:83]
	flat_load_dwordx4 v[16:19], v[2:3] nt
	v_lshl_add_u64 v[2:3], v[0:1], 0, v[84:85]
	flat_load_dwordx4 v[12:15], v[2:3] nt
	v_lshl_add_u64 v[2:3], v[0:1], 0, v[86:87]
	flat_load_dwordx4 v[8:11], v[2:3] nt
	v_lshl_add_u64 v[2:3], v[0:1], 0, v[88:89]
	flat_load_dwordx4 v[4:7], v[2:3] nt
	v_lshl_add_u64 v[0:1], v[0:1], 0, v[90:91]
	flat_load_dwordx4 v[0:3], v[0:1] nt
	v_add_u32_e32 v111, 0x410, v114
	s_lshl_b32 s7, s18, 7
	s_and_b32 s6, s6, 64
	s_or_b32 s6, s6, s7
	s_bitset1_b32 s6, 7
	s_ashr_i32 s7, s6, 31
	s_add_u32 s18, s23, s4
	s_addc_u32 s19, s24, s5
	s_lshl_b64 s[4:5], s[6:7], 12
	s_add_u32 s4, s18, s4
	s_addc_u32 s5, s19, s5
	s_lshl_b64 s[2:3], s[2:3], 1
	s_add_u32 s2, s4, s2
	s_addc_u32 s3, s5, s3
	s_add_i32 s14, s14, s80
	s_cmpk_lt_i32 s14, 0x1000
	s_waitcnt vmcnt(0) lgkmcnt(0)
	ds_write2_b32 v114, v116, v117 offset1:1
	ds_write2_b32 v114, v118, v119 offset0:2 offset1:3
	ds_write2_b32 v111, v56, v57 offset1:1
	v_add_u32_e32 v56, 0x418, v114
	ds_write2_b32 v56, v58, v59 offset1:1
	v_add_u32_e32 v56, 0x820, v114
	ds_write2_b32 v56, v52, v53 offset1:1
	v_add_u32_e32 v52, 0x828, v114
	ds_write2_b32 v52, v54, v55 offset1:1
	v_add_u32_e32 v52, 0xc30, v114
	ds_write2_b32 v52, v48, v49 offset1:1
	v_add_u32_e32 v48, 0xc38, v114
	ds_write2_b32 v48, v50, v51 offset1:1
	v_add_u32_e32 v48, 0x1040, v114
	ds_write2_b32 v48, v44, v45 offset1:1
	v_add_u32_e32 v44, 0x1048, v114
	ds_write2_b32 v44, v46, v47 offset1:1
	v_add_u32_e32 v44, 0x1450, v114
	ds_write2_b32 v44, v40, v41 offset1:1
	v_add_u32_e32 v40, 0x1458, v114
	ds_write2_b32 v40, v42, v43 offset1:1
	v_add_u32_e32 v40, 0x1860, v114
	ds_write2_b32 v40, v36, v37 offset1:1
	v_add_u32_e32 v36, 0x1868, v114
	ds_write2_b32 v36, v38, v39 offset1:1
	v_add_u32_e32 v36, 0x1c70, v114
	ds_write2_b32 v36, v32, v33 offset1:1
	v_add_u32_e32 v32, 0x1c78, v114
	ds_write2_b32 v32, v34, v35 offset1:1
	v_add_u32_e32 v32, 0x2080, v114
	ds_write2_b32 v32, v28, v29 offset1:1
	v_add_u32_e32 v28, 0x2088, v114
	ds_write2_b32 v28, v30, v31 offset1:1
	v_add_u32_e32 v28, 0x2490, v114
	ds_write2_b32 v28, v24, v25 offset1:1
	v_add_u32_e32 v24, 0x2498, v114
	ds_write2_b32 v24, v26, v27 offset1:1
	v_add_u32_e32 v24, 0x28a0, v114
	ds_write2_b32 v24, v20, v21 offset1:1
	v_add_u32_e32 v20, 0x28a8, v114
	ds_write2_b32 v20, v22, v23 offset1:1
	v_add_u32_e32 v20, 0x2cb0, v114
	ds_write2_b32 v20, v16, v17 offset1:1
	v_add_u32_e32 v16, 0x2cb8, v114
	ds_write2_b32 v16, v18, v19 offset1:1
	v_add_u32_e32 v16, 0x30c0, v114
	ds_write2_b32 v16, v12, v13 offset1:1
	v_add_u32_e32 v12, 0x30c8, v114
	ds_write2_b32 v12, v14, v15 offset1:1
	v_add_u32_e32 v12, 0x34d0, v114
	ds_write2_b32 v12, v8, v9 offset1:1
	v_add_u32_e32 v8, 0x34d8, v114
	ds_write2_b32 v8, v10, v11 offset1:1
	v_add_u32_e32 v8, 0x38e0, v114
	ds_write2_b32 v8, v4, v5 offset1:1
	v_add_u32_e32 v4, 0x38e8, v114
	ds_write2_b32 v4, v6, v7 offset1:1
	v_add_u32_e32 v4, 0x3cf0, v114
	ds_write2_b32 v4, v0, v1 offset1:1
	v_add_u32_e32 v0, 0x3cf8, v114
	ds_write2_b32 v0, v2, v3 offset1:1
	s_waitcnt lgkmcnt(0)
	ds_read2_b32 v[6:7], v113 offset0:65 offset1:73
	ds_read2_b32 v[8:9], v113 offset1:8
	ds_read2_b32 v[10:11], v113 offset0:130 offset1:138
	ds_read2_b32 v[12:13], v113 offset0:195 offset1:203
	v_mov_b32_e32 v111, v97
	v_lshl_add_u64 v[4:5], s[2:3], 0, v[110:111]
	v_lshl_add_u64 v[22:23], v[4:5], 0, v[92:93]
	s_waitcnt lgkmcnt(2)
	v_cvt_pk_bf16_f32 v0, v8, v6
	v_add_u32_e32 v6, 0x400, v113
	ds_read2_b32 v[14:15], v6 offset0:4 offset1:12
	ds_read2_b32 v[16:17], v6 offset0:69 offset1:77
	ds_read2_b32 v[18:19], v6 offset0:134 offset1:142
	ds_read2_b32 v[20:21], v6 offset0:199 offset1:207
	s_waitcnt lgkmcnt(4)
	v_cvt_pk_bf16_f32 v1, v10, v12
	v_lshl_add_u64 v[24:25], v[4:5], 0, v[98:99]
	s_waitcnt lgkmcnt(2)
	v_cvt_pk_bf16_f32 v2, v14, v16
	s_waitcnt lgkmcnt(0)
	v_cvt_pk_bf16_f32 v3, v18, v20
	global_store_dwordx4 v[22:23], v[0:3], off sc1
	s_nop 1
	v_cvt_pk_bf16_f32 v0, v9, v7
	v_cvt_pk_bf16_f32 v1, v11, v13
	v_cvt_pk_bf16_f32 v2, v15, v17
	v_cvt_pk_bf16_f32 v3, v19, v21
	v_lshl_add_u64 v[8:9], v[4:5], 0, v[94:95]
	global_store_dwordx4 v[8:9], v[0:3], off sc1
	ds_read2_b32 v[8:9], v113 offset0:81 offset1:89
	ds_read2_b32 v[10:11], v113 offset0:16 offset1:24
	ds_read2_b32 v[12:13], v113 offset0:146 offset1:154
	ds_read2_b32 v[14:15], v113 offset0:211 offset1:219
	ds_read2_b32 v[16:17], v6 offset0:20 offset1:28
	ds_read2_b32 v[18:19], v6 offset0:85 offset1:93
	ds_read2_b32 v[20:21], v6 offset0:150 offset1:158
	ds_read2_b32 v[22:23], v6 offset0:215 offset1:223
	s_waitcnt lgkmcnt(6)
	v_cvt_pk_bf16_f32 v0, v10, v8
	s_waitcnt lgkmcnt(4)
	v_cvt_pk_bf16_f32 v1, v12, v14
	s_waitcnt lgkmcnt(2)
	v_cvt_pk_bf16_f32 v2, v16, v18
	s_waitcnt lgkmcnt(0)
	v_cvt_pk_bf16_f32 v3, v20, v22
	global_store_dwordx4 v[24:25], v[0:3], off sc1
	v_lshl_add_u64 v[24:25], v[4:5], 0, v[102:103]
	s_nop 0
	v_cvt_pk_bf16_f32 v0, v11, v9
	v_cvt_pk_bf16_f32 v1, v13, v15
	v_cvt_pk_bf16_f32 v2, v17, v19
	v_cvt_pk_bf16_f32 v3, v21, v23
	v_lshl_add_u64 v[8:9], v[4:5], 0, v[100:101]
	global_store_dwordx4 v[8:9], v[0:3], off sc1
	ds_read2_b32 v[8:9], v113 offset0:32 offset1:40
	ds_read2_b32 v[10:11], v113 offset0:97 offset1:105
	ds_read2_b32 v[12:13], v113 offset0:162 offset1:170
	ds_read2_b32 v[14:15], v113 offset0:227 offset1:235
	ds_read2_b32 v[16:17], v6 offset0:36 offset1:44
	ds_read2_b32 v[18:19], v6 offset0:101 offset1:109
	ds_read2_b32 v[20:21], v6 offset0:166 offset1:174
	ds_read2_b32 v[22:23], v6 offset0:231 offset1:239
	s_waitcnt lgkmcnt(6)
	v_cvt_pk_bf16_f32 v0, v8, v10
	s_waitcnt lgkmcnt(4)
	v_cvt_pk_bf16_f32 v1, v12, v14
	s_waitcnt lgkmcnt(2)
	v_cvt_pk_bf16_f32 v2, v16, v18
	s_waitcnt lgkmcnt(0)
	v_cvt_pk_bf16_f32 v3, v20, v22
	global_store_dwordx4 v[24:25], v[0:3], off sc1
	s_nop 1
	v_cvt_pk_bf16_f32 v0, v9, v11
	v_cvt_pk_bf16_f32 v1, v13, v15
	v_cvt_pk_bf16_f32 v2, v17, v19
	v_cvt_pk_bf16_f32 v3, v21, v23
	v_lshl_add_u64 v[8:9], v[4:5], 0, v[104:105]
	global_store_dwordx4 v[8:9], v[0:3], off sc1
	ds_read2_b32 v[8:9], v113 offset0:48 offset1:56
	ds_read2_b32 v[10:11], v113 offset0:113 offset1:121
	ds_read2_b32 v[12:13], v113 offset0:178 offset1:186
	ds_read2_b32 v[14:15], v113 offset0:243 offset1:251
	ds_read2_b32 v[16:17], v6 offset0:52 offset1:60
	ds_read2_b32 v[18:19], v6 offset0:117 offset1:125
	ds_read2_b32 v[20:21], v6 offset0:182 offset1:190
	ds_read2_b32 v[6:7], v6 offset0:247 offset1:255
	v_lshl_add_u64 v[22:23], v[4:5], 0, v[106:107]
	s_waitcnt lgkmcnt(6)
	v_cvt_pk_bf16_f32 v0, v8, v10
	s_waitcnt lgkmcnt(4)
	v_cvt_pk_bf16_f32 v1, v12, v14
	s_waitcnt lgkmcnt(2)
	v_cvt_pk_bf16_f32 v2, v16, v18
	s_waitcnt lgkmcnt(0)
	v_cvt_pk_bf16_f32 v3, v20, v6
	global_store_dwordx4 v[22:23], v[0:3], off sc1
	v_lshl_add_u64 v[4:5], v[4:5], 0, v[108:109]
	s_nop 0
	v_cvt_pk_bf16_f32 v0, v9, v11
	v_cvt_pk_bf16_f32 v1, v13, v15
	v_cvt_pk_bf16_f32 v2, v17, v19
	v_cvt_pk_bf16_f32 v3, v21, v7
	global_store_dwordx4 v[4:5], v[0:3], off sc1
	s_waitcnt lgkmcnt(0)
	s_cbranch_scc1 .LBB0_294

.LBB0_297:
	s_ashr_i32 s2, s12, 31
	s_lshr_b32 s2, s2, 23
	s_add_i32 s2, s12, s2
	s_ashr_i32 s4, s2, 9
	s_and_b32 s2, s2, 0xfe00
	s_sub_i32 s2, s12, s2
	s_sext_i32_i16 s3, s2
	s_bfe_u32 s3, s3, 0x4001b
	s_add_i32 s3, s2, s3
	s_sext_i32_i16 s5, s3
	s_and_b32 s3, s3, 0xfff0
	s_sub_i32 s2, s2, s3
	s_sext_i32_i16 s13, s2
	s_lshl_b32 s2, s5, 2
	s_ashr_i32 s5, s4, 31
	s_andn2_b32 s2, s2, 63
	s_lshl_b32 s6, s13, 6
	s_lshl_b64 s[4:5], s[4:5], 23
	s_add_u32 s7, s14, s4
	s_addc_u32 s16, s15, s5
	s_ashr_i32 s3, s2, 31
	s_lshl_b64 s[18:19], s[2:3], 12
	s_add_u32 s20, s7, s18
	s_addc_u32 s16, s16, s19
	s_ashr_i32 s7, s6, 31
	s_lshl_b64 s[18:19], s[6:7], 2
	s_add_u32 s18, s20, s18
	s_addc_u32 s19, s16, s19
	v_lshl_add_u64 v[0:1], s[18:19], 0, v[96:97]
	v_lshl_add_u64 v[2:3], v[0:1], 0, v[60:61]
	flat_load_dwordx4 v[114:117], v[2:3] nt
	v_lshl_add_u64 v[2:3], v[0:1], 0, v[62:63]
	flat_load_dwordx4 v[56:59], v[2:3] nt
	v_lshl_add_u64 v[2:3], v[0:1], 0, v[64:65]
	flat_load_dwordx4 v[52:55], v[2:3] nt
	v_lshl_add_u64 v[2:3], v[0:1], 0, v[66:67]
	flat_load_dwordx4 v[48:51], v[2:3] nt
	v_lshl_add_u64 v[2:3], v[0:1], 0, v[68:69]
	flat_load_dwordx4 v[44:47], v[2:3] nt
	v_lshl_add_u64 v[2:3], v[0:1], 0, v[70:71]
	flat_load_dwordx4 v[40:43], v[2:3] nt
	v_lshl_add_u64 v[2:3], v[0:1], 0, v[72:73]
	flat_load_dwordx4 v[36:39], v[2:3] nt
	v_lshl_add_u64 v[2:3], v[0:1], 0, v[74:75]
	flat_load_dwordx4 v[32:35], v[2:3] nt
	v_lshl_add_u64 v[2:3], v[0:1], 0, v[76:77]
	flat_load_dwordx4 v[28:31], v[2:3] nt
	v_lshl_add_u64 v[2:3], v[0:1], 0, v[78:79]
	flat_load_dwordx4 v[24:27], v[2:3] nt
	v_lshl_add_u64 v[2:3], v[0:1], 0, v[80:81]
	flat_load_dwordx4 v[20:23], v[2:3] nt
	v_lshl_add_u64 v[2:3], v[0:1], 0, v[82:83]
	flat_load_dwordx4 v[16:19], v[2:3] nt
	v_lshl_add_u64 v[2:3], v[0:1], 0, v[84:85]
	flat_load_dwordx4 v[12:15], v[2:3] nt
	v_lshl_add_u64 v[2:3], v[0:1], 0, v[86:87]
	flat_load_dwordx4 v[8:11], v[2:3] nt
	v_lshl_add_u64 v[2:3], v[0:1], 0, v[88:89]
	flat_load_dwordx4 v[4:7], v[2:3] nt
	v_lshl_add_u64 v[0:1], v[0:1], 0, v[90:91]
	flat_load_dwordx4 v[0:3], v[0:1] nt
	v_add_u32_e32 v111, 0x410, v113
	s_lshl_b32 s7, s13, 7
	s_and_b32 s6, s6, 64
	s_or_b32 s6, s6, s7
	s_bitset1_b32 s6, 7
	s_ashr_i32 s7, s6, 31
	s_add_u32 s13, s21, s4
	s_addc_u32 s16, s22, s5
	s_lshl_b64 s[4:5], s[6:7], 12
	s_add_u32 s4, s13, s4
	s_addc_u32 s5, s16, s5
	s_lshl_b64 s[2:3], s[2:3], 1
	s_add_u32 s2, s4, s2
	s_addc_u32 s3, s5, s3
	s_add_i32 s12, s12, s80
	s_cmpk_lt_i32 s12, 0x1000
	s_waitcnt vmcnt(0) lgkmcnt(0)
	ds_write2_b32 v113, v114, v115 offset1:1
	ds_write2_b32 v113, v116, v117 offset0:2 offset1:3
	ds_write2_b32 v111, v56, v57 offset1:1
	v_add_u32_e32 v56, 0x418, v113
	ds_write2_b32 v56, v58, v59 offset1:1
	v_add_u32_e32 v56, 0x820, v113
	ds_write2_b32 v56, v52, v53 offset1:1
	v_add_u32_e32 v52, 0x828, v113
	ds_write2_b32 v52, v54, v55 offset1:1
	v_add_u32_e32 v52, 0xc30, v113
	ds_write2_b32 v52, v48, v49 offset1:1
	v_add_u32_e32 v48, 0xc38, v113
	ds_write2_b32 v48, v50, v51 offset1:1
	v_add_u32_e32 v48, 0x1040, v113
	ds_write2_b32 v48, v44, v45 offset1:1
	v_add_u32_e32 v44, 0x1048, v113
	ds_write2_b32 v44, v46, v47 offset1:1
	v_add_u32_e32 v44, 0x1450, v113
	ds_write2_b32 v44, v40, v41 offset1:1
	v_add_u32_e32 v40, 0x1458, v113
	ds_write2_b32 v40, v42, v43 offset1:1
	v_add_u32_e32 v40, 0x1860, v113
	ds_write2_b32 v40, v36, v37 offset1:1
	v_add_u32_e32 v36, 0x1868, v113
	ds_write2_b32 v36, v38, v39 offset1:1
	v_add_u32_e32 v36, 0x1c70, v113
	ds_write2_b32 v36, v32, v33 offset1:1
	v_add_u32_e32 v32, 0x1c78, v113
	ds_write2_b32 v32, v34, v35 offset1:1
	v_add_u32_e32 v32, 0x2080, v113
	ds_write2_b32 v32, v28, v29 offset1:1
	v_add_u32_e32 v28, 0x2088, v113
	ds_write2_b32 v28, v30, v31 offset1:1
	v_add_u32_e32 v28, 0x2490, v113
	ds_write2_b32 v28, v24, v25 offset1:1
	v_add_u32_e32 v24, 0x2498, v113
	ds_write2_b32 v24, v26, v27 offset1:1
	v_add_u32_e32 v24, 0x28a0, v113
	ds_write2_b32 v24, v20, v21 offset1:1
	v_add_u32_e32 v20, 0x28a8, v113
	ds_write2_b32 v20, v22, v23 offset1:1
	v_add_u32_e32 v20, 0x2cb0, v113
	ds_write2_b32 v20, v16, v17 offset1:1
	v_add_u32_e32 v16, 0x2cb8, v113
	ds_write2_b32 v16, v18, v19 offset1:1
	v_add_u32_e32 v16, 0x30c0, v113
	ds_write2_b32 v16, v12, v13 offset1:1
	v_add_u32_e32 v12, 0x30c8, v113
	ds_write2_b32 v12, v14, v15 offset1:1
	v_add_u32_e32 v12, 0x34d0, v113
	ds_write2_b32 v12, v8, v9 offset1:1
	v_add_u32_e32 v8, 0x34d8, v113
	ds_write2_b32 v8, v10, v11 offset1:1
	v_add_u32_e32 v8, 0x38e0, v113
	ds_write2_b32 v8, v4, v5 offset1:1
	v_add_u32_e32 v4, 0x38e8, v113
	ds_write2_b32 v4, v6, v7 offset1:1
	v_add_u32_e32 v4, 0x3cf0, v113
	ds_write2_b32 v4, v0, v1 offset1:1
	v_add_u32_e32 v0, 0x3cf8, v113
	ds_write2_b32 v0, v2, v3 offset1:1
	s_waitcnt lgkmcnt(0)
	ds_read2_b32 v[6:7], v112 offset0:65 offset1:73
	ds_read2_b32 v[8:9], v112 offset1:8
	ds_read2_b32 v[10:11], v112 offset0:130 offset1:138
	ds_read2_b32 v[12:13], v112 offset0:195 offset1:203
	v_mov_b32_e32 v111, v97
	v_lshl_add_u64 v[4:5], s[2:3], 0, v[110:111]
	v_lshl_add_u64 v[22:23], v[4:5], 0, v[92:93]
	s_waitcnt lgkmcnt(2)
	v_cvt_pk_bf16_f32 v0, v8, v6
	v_add_u32_e32 v6, 0x400, v112
	ds_read2_b32 v[14:15], v6 offset0:4 offset1:12
	ds_read2_b32 v[16:17], v6 offset0:69 offset1:77
	ds_read2_b32 v[18:19], v6 offset0:134 offset1:142
	ds_read2_b32 v[20:21], v6 offset0:199 offset1:207
	s_waitcnt lgkmcnt(4)
	v_cvt_pk_bf16_f32 v1, v10, v12
	v_lshl_add_u64 v[24:25], v[4:5], 0, v[98:99]
	s_waitcnt lgkmcnt(2)
	v_cvt_pk_bf16_f32 v2, v14, v16
	s_waitcnt lgkmcnt(0)
	v_cvt_pk_bf16_f32 v3, v18, v20
	global_store_dwordx4 v[22:23], v[0:3], off sc1
	s_nop 1
	v_cvt_pk_bf16_f32 v0, v9, v7
	v_cvt_pk_bf16_f32 v1, v11, v13
	v_cvt_pk_bf16_f32 v2, v15, v17
	v_cvt_pk_bf16_f32 v3, v19, v21
	v_lshl_add_u64 v[8:9], v[4:5], 0, v[94:95]
	global_store_dwordx4 v[8:9], v[0:3], off sc1
	ds_read2_b32 v[8:9], v112 offset0:81 offset1:89
	ds_read2_b32 v[10:11], v112 offset0:16 offset1:24
	ds_read2_b32 v[12:13], v112 offset0:146 offset1:154
	ds_read2_b32 v[14:15], v112 offset0:211 offset1:219
	ds_read2_b32 v[16:17], v6 offset0:20 offset1:28
	ds_read2_b32 v[18:19], v6 offset0:85 offset1:93
	ds_read2_b32 v[20:21], v6 offset0:150 offset1:158
	ds_read2_b32 v[22:23], v6 offset0:215 offset1:223
	s_waitcnt lgkmcnt(6)
	v_cvt_pk_bf16_f32 v0, v10, v8
	s_waitcnt lgkmcnt(4)
	v_cvt_pk_bf16_f32 v1, v12, v14
	s_waitcnt lgkmcnt(2)
	v_cvt_pk_bf16_f32 v2, v16, v18
	s_waitcnt lgkmcnt(0)
	v_cvt_pk_bf16_f32 v3, v20, v22
	global_store_dwordx4 v[24:25], v[0:3], off sc1
	v_lshl_add_u64 v[24:25], v[4:5], 0, v[102:103]
	s_nop 0
	v_cvt_pk_bf16_f32 v0, v11, v9
	v_cvt_pk_bf16_f32 v1, v13, v15
	v_cvt_pk_bf16_f32 v2, v17, v19
	v_cvt_pk_bf16_f32 v3, v21, v23
	v_lshl_add_u64 v[8:9], v[4:5], 0, v[100:101]
	global_store_dwordx4 v[8:9], v[0:3], off sc1
	ds_read2_b32 v[8:9], v112 offset0:32 offset1:40
	ds_read2_b32 v[10:11], v112 offset0:97 offset1:105
	ds_read2_b32 v[12:13], v112 offset0:162 offset1:170
	ds_read2_b32 v[14:15], v112 offset0:227 offset1:235
	ds_read2_b32 v[16:17], v6 offset0:36 offset1:44
	ds_read2_b32 v[18:19], v6 offset0:101 offset1:109
	ds_read2_b32 v[20:21], v6 offset0:166 offset1:174
	ds_read2_b32 v[22:23], v6 offset0:231 offset1:239
	s_waitcnt lgkmcnt(6)
	v_cvt_pk_bf16_f32 v0, v8, v10
	s_waitcnt lgkmcnt(4)
	v_cvt_pk_bf16_f32 v1, v12, v14
	s_waitcnt lgkmcnt(2)
	v_cvt_pk_bf16_f32 v2, v16, v18
	s_waitcnt lgkmcnt(0)
	v_cvt_pk_bf16_f32 v3, v20, v22
	global_store_dwordx4 v[24:25], v[0:3], off sc1
	s_nop 1
	v_cvt_pk_bf16_f32 v0, v9, v11
	v_cvt_pk_bf16_f32 v1, v13, v15
	v_cvt_pk_bf16_f32 v2, v17, v19
	v_cvt_pk_bf16_f32 v3, v21, v23
	v_lshl_add_u64 v[8:9], v[4:5], 0, v[104:105]
	global_store_dwordx4 v[8:9], v[0:3], off sc1
	ds_read2_b32 v[8:9], v112 offset0:48 offset1:56
	ds_read2_b32 v[10:11], v112 offset0:113 offset1:121
	ds_read2_b32 v[12:13], v112 offset0:178 offset1:186
	ds_read2_b32 v[14:15], v112 offset0:243 offset1:251
	ds_read2_b32 v[16:17], v6 offset0:52 offset1:60
	ds_read2_b32 v[18:19], v6 offset0:117 offset1:125
	ds_read2_b32 v[20:21], v6 offset0:182 offset1:190
	ds_read2_b32 v[6:7], v6 offset0:247 offset1:255
	v_lshl_add_u64 v[22:23], v[4:5], 0, v[106:107]
	s_waitcnt lgkmcnt(6)
	v_cvt_pk_bf16_f32 v0, v8, v10
	s_waitcnt lgkmcnt(4)
	v_cvt_pk_bf16_f32 v1, v12, v14
	s_waitcnt lgkmcnt(2)
	v_cvt_pk_bf16_f32 v2, v16, v18
	s_waitcnt lgkmcnt(0)
	v_cvt_pk_bf16_f32 v3, v20, v6
	global_store_dwordx4 v[22:23], v[0:3], off sc1
	v_lshl_add_u64 v[4:5], v[4:5], 0, v[108:109]
	s_nop 0
	v_cvt_pk_bf16_f32 v0, v9, v11
	v_cvt_pk_bf16_f32 v1, v13, v15
	v_cvt_pk_bf16_f32 v2, v17, v19
	v_cvt_pk_bf16_f32 v3, v21, v7
	global_store_dwordx4 v[4:5], v[0:3], off sc1
	s_waitcnt lgkmcnt(0)
	s_cbranch_scc1 .LBB0_297

.LBB0_302:
	s_ashr_i32 s2, s14, 31
	s_lshr_b32 s2, s2, 23
	s_add_i32 s2, s14, s2
	s_ashr_i32 s4, s2, 9
	s_and_b32 s2, s2, 0xfe00
	s_sub_i32 s2, s14, s2
	s_sext_i32_i16 s3, s2
	s_bfe_u32 s3, s3, 0x4001b
	s_add_i32 s3, s2, s3
	s_sext_i32_i16 s5, s3
	s_and_b32 s3, s3, 0xfff0
	s_sub_i32 s2, s2, s3
	s_sext_i32_i16 s18, s2
	s_lshl_b32 s2, s5, 2
	s_ashr_i32 s5, s4, 31
	s_andn2_b32 s2, s2, 63
	s_lshl_b32 s6, s18, 6
	s_lshl_b64 s[4:5], s[4:5], 23
	s_add_u32 s7, s15, s4
	s_addc_u32 s19, s16, s5
	s_ashr_i32 s3, s2, 31
	s_lshl_b64 s[20:21], s[2:3], 12
	s_add_u32 s22, s7, s20
	s_addc_u32 s19, s19, s21
	s_ashr_i32 s7, s6, 31
	s_lshl_b64 s[20:21], s[6:7], 2
	s_add_u32 s20, s22, s20
	s_addc_u32 s21, s19, s21
	v_lshl_add_u64 v[0:1], s[20:21], 0, v[96:97]
	v_lshl_add_u64 v[2:3], v[0:1], 0, v[60:61]
	flat_load_dwordx4 v[116:119], v[2:3] nt
	v_lshl_add_u64 v[2:3], v[0:1], 0, v[62:63]
	flat_load_dwordx4 v[56:59], v[2:3] nt
	v_lshl_add_u64 v[2:3], v[0:1], 0, v[64:65]
	flat_load_dwordx4 v[52:55], v[2:3] nt
	v_lshl_add_u64 v[2:3], v[0:1], 0, v[66:67]
	flat_load_dwordx4 v[48:51], v[2:3] nt
	v_lshl_add_u64 v[2:3], v[0:1], 0, v[68:69]
	flat_load_dwordx4 v[44:47], v[2:3] nt
	v_lshl_add_u64 v[2:3], v[0:1], 0, v[70:71]
	flat_load_dwordx4 v[40:43], v[2:3] nt
	v_lshl_add_u64 v[2:3], v[0:1], 0, v[72:73]
	flat_load_dwordx4 v[36:39], v[2:3] nt
	v_lshl_add_u64 v[2:3], v[0:1], 0, v[74:75]
	flat_load_dwordx4 v[32:35], v[2:3] nt
	v_lshl_add_u64 v[2:3], v[0:1], 0, v[76:77]
	flat_load_dwordx4 v[28:31], v[2:3] nt
	v_lshl_add_u64 v[2:3], v[0:1], 0, v[78:79]
	flat_load_dwordx4 v[24:27], v[2:3] nt
	v_lshl_add_u64 v[2:3], v[0:1], 0, v[80:81]
	flat_load_dwordx4 v[20:23], v[2:3] nt
	v_lshl_add_u64 v[2:3], v[0:1], 0, v[82:83]
	flat_load_dwordx4 v[16:19], v[2:3] nt
	v_lshl_add_u64 v[2:3], v[0:1], 0, v[84:85]
	flat_load_dwordx4 v[12:15], v[2:3] nt
	v_lshl_add_u64 v[2:3], v[0:1], 0, v[86:87]
	flat_load_dwordx4 v[8:11], v[2:3] nt
	v_lshl_add_u64 v[2:3], v[0:1], 0, v[88:89]
	flat_load_dwordx4 v[4:7], v[2:3] nt
	v_lshl_add_u64 v[0:1], v[0:1], 0, v[90:91]
	flat_load_dwordx4 v[0:3], v[0:1] nt
	v_add_u32_e32 v111, 0x410, v114
	s_lshl_b32 s7, s18, 7
	s_and_b32 s6, s6, 64
	s_or_b32 s6, s6, s7
	s_bitset1_b32 s6, 7
	s_ashr_i32 s7, s6, 31
	s_add_u32 s18, s23, s4
	s_addc_u32 s19, s24, s5
	s_lshl_b64 s[4:5], s[6:7], 12
	s_add_u32 s4, s18, s4
	s_addc_u32 s5, s19, s5
	s_lshl_b64 s[2:3], s[2:3], 1
	s_add_u32 s2, s4, s2
	s_addc_u32 s3, s5, s3
	s_add_i32 s14, s14, s25
	s_cmpk_lt_i32 s14, 0x1000
	s_waitcnt vmcnt(0) lgkmcnt(0)
	ds_write2_b32 v114, v116, v117 offset1:1
	ds_write2_b32 v114, v118, v119 offset0:2 offset1:3
	ds_write2_b32 v111, v56, v57 offset1:1
	v_add_u32_e32 v56, 0x418, v114
	ds_write2_b32 v56, v58, v59 offset1:1
	v_add_u32_e32 v56, 0x820, v114
	ds_write2_b32 v56, v52, v53 offset1:1
	v_add_u32_e32 v52, 0x828, v114
	ds_write2_b32 v52, v54, v55 offset1:1
	v_add_u32_e32 v52, 0xc30, v114
	ds_write2_b32 v52, v48, v49 offset1:1
	v_add_u32_e32 v48, 0xc38, v114
	ds_write2_b32 v48, v50, v51 offset1:1
	v_add_u32_e32 v48, 0x1040, v114
	ds_write2_b32 v48, v44, v45 offset1:1
	v_add_u32_e32 v44, 0x1048, v114
	ds_write2_b32 v44, v46, v47 offset1:1
	v_add_u32_e32 v44, 0x1450, v114
	ds_write2_b32 v44, v40, v41 offset1:1
	v_add_u32_e32 v40, 0x1458, v114
	ds_write2_b32 v40, v42, v43 offset1:1
	v_add_u32_e32 v40, 0x1860, v114
	ds_write2_b32 v40, v36, v37 offset1:1
	v_add_u32_e32 v36, 0x1868, v114
	ds_write2_b32 v36, v38, v39 offset1:1
	v_add_u32_e32 v36, 0x1c70, v114
	ds_write2_b32 v36, v32, v33 offset1:1
	v_add_u32_e32 v32, 0x1c78, v114
	ds_write2_b32 v32, v34, v35 offset1:1
	v_add_u32_e32 v32, 0x2080, v114
	ds_write2_b32 v32, v28, v29 offset1:1
	v_add_u32_e32 v28, 0x2088, v114
	ds_write2_b32 v28, v30, v31 offset1:1
	v_add_u32_e32 v28, 0x2490, v114
	ds_write2_b32 v28, v24, v25 offset1:1
	v_add_u32_e32 v24, 0x2498, v114
	ds_write2_b32 v24, v26, v27 offset1:1
	v_add_u32_e32 v24, 0x28a0, v114
	ds_write2_b32 v24, v20, v21 offset1:1
	v_add_u32_e32 v20, 0x28a8, v114
	ds_write2_b32 v20, v22, v23 offset1:1
	v_add_u32_e32 v20, 0x2cb0, v114
	ds_write2_b32 v20, v16, v17 offset1:1
	v_add_u32_e32 v16, 0x2cb8, v114
	ds_write2_b32 v16, v18, v19 offset1:1
	v_add_u32_e32 v16, 0x30c0, v114
	ds_write2_b32 v16, v12, v13 offset1:1
	v_add_u32_e32 v12, 0x30c8, v114
	ds_write2_b32 v12, v14, v15 offset1:1
	v_add_u32_e32 v12, 0x34d0, v114
	ds_write2_b32 v12, v8, v9 offset1:1
	v_add_u32_e32 v8, 0x34d8, v114
	ds_write2_b32 v8, v10, v11 offset1:1
	v_add_u32_e32 v8, 0x38e0, v114
	ds_write2_b32 v8, v4, v5 offset1:1
	v_add_u32_e32 v4, 0x38e8, v114
	ds_write2_b32 v4, v6, v7 offset1:1
	v_add_u32_e32 v4, 0x3cf0, v114
	ds_write2_b32 v4, v0, v1 offset1:1
	v_add_u32_e32 v0, 0x3cf8, v114
	ds_write2_b32 v0, v2, v3 offset1:1
	s_waitcnt lgkmcnt(0)
	ds_read2_b32 v[6:7], v113 offset0:65 offset1:73
	ds_read2_b32 v[8:9], v113 offset1:8
	ds_read2_b32 v[10:11], v113 offset0:130 offset1:138
	ds_read2_b32 v[12:13], v113 offset0:195 offset1:203
	v_mov_b32_e32 v111, v97
	v_lshl_add_u64 v[4:5], s[2:3], 0, v[110:111]
	v_lshl_add_u64 v[22:23], v[4:5], 0, v[92:93]
	s_waitcnt lgkmcnt(2)
	v_cvt_pk_bf16_f32 v0, v8, v6
	v_add_u32_e32 v6, 0x400, v113
	ds_read2_b32 v[14:15], v6 offset0:4 offset1:12
	ds_read2_b32 v[16:17], v6 offset0:69 offset1:77
	ds_read2_b32 v[18:19], v6 offset0:134 offset1:142
	ds_read2_b32 v[20:21], v6 offset0:199 offset1:207
	s_waitcnt lgkmcnt(4)
	v_cvt_pk_bf16_f32 v1, v10, v12
	v_lshl_add_u64 v[24:25], v[4:5], 0, v[98:99]
	s_waitcnt lgkmcnt(2)
	v_cvt_pk_bf16_f32 v2, v14, v16
	s_waitcnt lgkmcnt(0)
	v_cvt_pk_bf16_f32 v3, v18, v20
	global_store_dwordx4 v[22:23], v[0:3], off sc1
	s_nop 1
	v_cvt_pk_bf16_f32 v0, v9, v7
	v_cvt_pk_bf16_f32 v1, v11, v13
	v_cvt_pk_bf16_f32 v2, v15, v17
	v_cvt_pk_bf16_f32 v3, v19, v21
	v_lshl_add_u64 v[8:9], v[4:5], 0, v[94:95]
	global_store_dwordx4 v[8:9], v[0:3], off sc1
	ds_read2_b32 v[8:9], v113 offset0:81 offset1:89
	ds_read2_b32 v[10:11], v113 offset0:16 offset1:24
	ds_read2_b32 v[12:13], v113 offset0:146 offset1:154
	ds_read2_b32 v[14:15], v113 offset0:211 offset1:219
	ds_read2_b32 v[16:17], v6 offset0:20 offset1:28
	ds_read2_b32 v[18:19], v6 offset0:85 offset1:93
	ds_read2_b32 v[20:21], v6 offset0:150 offset1:158
	ds_read2_b32 v[22:23], v6 offset0:215 offset1:223
	s_waitcnt lgkmcnt(6)
	v_cvt_pk_bf16_f32 v0, v10, v8
	s_waitcnt lgkmcnt(4)
	v_cvt_pk_bf16_f32 v1, v12, v14
	s_waitcnt lgkmcnt(2)
	v_cvt_pk_bf16_f32 v2, v16, v18
	s_waitcnt lgkmcnt(0)
	v_cvt_pk_bf16_f32 v3, v20, v22
	global_store_dwordx4 v[24:25], v[0:3], off sc1
	v_lshl_add_u64 v[24:25], v[4:5], 0, v[102:103]
	s_nop 0
	v_cvt_pk_bf16_f32 v0, v11, v9
	v_cvt_pk_bf16_f32 v1, v13, v15
	v_cvt_pk_bf16_f32 v2, v17, v19
	v_cvt_pk_bf16_f32 v3, v21, v23
	v_lshl_add_u64 v[8:9], v[4:5], 0, v[100:101]
	global_store_dwordx4 v[8:9], v[0:3], off sc1
	ds_read2_b32 v[8:9], v113 offset0:32 offset1:40
	ds_read2_b32 v[10:11], v113 offset0:97 offset1:105
	ds_read2_b32 v[12:13], v113 offset0:162 offset1:170
	ds_read2_b32 v[14:15], v113 offset0:227 offset1:235
	ds_read2_b32 v[16:17], v6 offset0:36 offset1:44
	ds_read2_b32 v[18:19], v6 offset0:101 offset1:109
	ds_read2_b32 v[20:21], v6 offset0:166 offset1:174
	ds_read2_b32 v[22:23], v6 offset0:231 offset1:239
	s_waitcnt lgkmcnt(6)
	v_cvt_pk_bf16_f32 v0, v8, v10
	s_waitcnt lgkmcnt(4)
	v_cvt_pk_bf16_f32 v1, v12, v14
	s_waitcnt lgkmcnt(2)
	v_cvt_pk_bf16_f32 v2, v16, v18
	s_waitcnt lgkmcnt(0)
	v_cvt_pk_bf16_f32 v3, v20, v22
	global_store_dwordx4 v[24:25], v[0:3], off sc1
	s_nop 1
	v_cvt_pk_bf16_f32 v0, v9, v11
	v_cvt_pk_bf16_f32 v1, v13, v15
	v_cvt_pk_bf16_f32 v2, v17, v19
	v_cvt_pk_bf16_f32 v3, v21, v23
	v_lshl_add_u64 v[8:9], v[4:5], 0, v[104:105]
	global_store_dwordx4 v[8:9], v[0:3], off sc1
	ds_read2_b32 v[8:9], v113 offset0:48 offset1:56
	ds_read2_b32 v[10:11], v113 offset0:113 offset1:121
	ds_read2_b32 v[12:13], v113 offset0:178 offset1:186
	ds_read2_b32 v[14:15], v113 offset0:243 offset1:251
	ds_read2_b32 v[16:17], v6 offset0:52 offset1:60
	ds_read2_b32 v[18:19], v6 offset0:117 offset1:125
	ds_read2_b32 v[20:21], v6 offset0:182 offset1:190
	ds_read2_b32 v[6:7], v6 offset0:247 offset1:255
	v_lshl_add_u64 v[22:23], v[4:5], 0, v[106:107]
	s_waitcnt lgkmcnt(6)
	v_cvt_pk_bf16_f32 v0, v8, v10
	s_waitcnt lgkmcnt(4)
	v_cvt_pk_bf16_f32 v1, v12, v14
	s_waitcnt lgkmcnt(2)
	v_cvt_pk_bf16_f32 v2, v16, v18
	s_waitcnt lgkmcnt(0)
	v_cvt_pk_bf16_f32 v3, v20, v6
	global_store_dwordx4 v[22:23], v[0:3], off sc1
	v_lshl_add_u64 v[4:5], v[4:5], 0, v[108:109]
	s_nop 0
	v_cvt_pk_bf16_f32 v0, v9, v11
	v_cvt_pk_bf16_f32 v1, v13, v15
	v_cvt_pk_bf16_f32 v2, v17, v19
	v_cvt_pk_bf16_f32 v3, v21, v7
	global_store_dwordx4 v[4:5], v[0:3], off sc1
	s_waitcnt lgkmcnt(0)
	s_cbranch_scc1 .LBB0_302

.LBB0_305:
	s_ashr_i32 s2, s12, 31
	s_lshr_b32 s2, s2, 23
	s_add_i32 s2, s12, s2
	s_ashr_i32 s4, s2, 9
	s_and_b32 s2, s2, 0xfe00
	s_sub_i32 s2, s12, s2
	s_sext_i32_i16 s3, s2
	s_bfe_u32 s3, s3, 0x4001b
	s_add_i32 s3, s2, s3
	s_sext_i32_i16 s5, s3
	s_and_b32 s3, s3, 0xfff0
	s_sub_i32 s2, s2, s3
	s_sext_i32_i16 s13, s2
	s_lshl_b32 s2, s5, 2
	s_ashr_i32 s5, s4, 31
	s_andn2_b32 s2, s2, 63
	s_lshl_b32 s6, s13, 6
	s_lshl_b64 s[4:5], s[4:5], 23
	s_add_u32 s7, s14, s4
	s_addc_u32 s16, s15, s5
	s_ashr_i32 s3, s2, 31
	s_lshl_b64 s[18:19], s[2:3], 12
	s_add_u32 s20, s7, s18
	s_addc_u32 s16, s16, s19
	s_ashr_i32 s7, s6, 31
	s_lshl_b64 s[18:19], s[6:7], 2
	s_add_u32 s18, s20, s18
	s_addc_u32 s19, s16, s19
	v_lshl_add_u64 v[0:1], s[18:19], 0, v[96:97]
	v_lshl_add_u64 v[2:3], v[0:1], 0, v[60:61]
	flat_load_dwordx4 v[114:117], v[2:3] nt
	v_lshl_add_u64 v[2:3], v[0:1], 0, v[62:63]
	flat_load_dwordx4 v[56:59], v[2:3] nt
	v_lshl_add_u64 v[2:3], v[0:1], 0, v[64:65]
	flat_load_dwordx4 v[52:55], v[2:3] nt
	v_lshl_add_u64 v[2:3], v[0:1], 0, v[66:67]
	flat_load_dwordx4 v[48:51], v[2:3] nt
	v_lshl_add_u64 v[2:3], v[0:1], 0, v[68:69]
	flat_load_dwordx4 v[44:47], v[2:3] nt
	v_lshl_add_u64 v[2:3], v[0:1], 0, v[70:71]
	flat_load_dwordx4 v[40:43], v[2:3] nt
	v_lshl_add_u64 v[2:3], v[0:1], 0, v[72:73]
	flat_load_dwordx4 v[36:39], v[2:3] nt
	v_lshl_add_u64 v[2:3], v[0:1], 0, v[74:75]
	flat_load_dwordx4 v[32:35], v[2:3] nt
	v_lshl_add_u64 v[2:3], v[0:1], 0, v[76:77]
	flat_load_dwordx4 v[28:31], v[2:3] nt
	v_lshl_add_u64 v[2:3], v[0:1], 0, v[78:79]
	flat_load_dwordx4 v[24:27], v[2:3] nt
	v_lshl_add_u64 v[2:3], v[0:1], 0, v[80:81]
	flat_load_dwordx4 v[20:23], v[2:3] nt
	v_lshl_add_u64 v[2:3], v[0:1], 0, v[82:83]
	flat_load_dwordx4 v[16:19], v[2:3] nt
	v_lshl_add_u64 v[2:3], v[0:1], 0, v[84:85]
	flat_load_dwordx4 v[12:15], v[2:3] nt
	v_lshl_add_u64 v[2:3], v[0:1], 0, v[86:87]
	flat_load_dwordx4 v[8:11], v[2:3] nt
	v_lshl_add_u64 v[2:3], v[0:1], 0, v[88:89]
	flat_load_dwordx4 v[4:7], v[2:3] nt
	v_lshl_add_u64 v[0:1], v[0:1], 0, v[90:91]
	flat_load_dwordx4 v[0:3], v[0:1] nt
	v_add_u32_e32 v111, 0x410, v113
	s_lshl_b32 s7, s13, 7
	s_and_b32 s6, s6, 64
	s_or_b32 s6, s6, s7
	s_bitset1_b32 s6, 7
	s_ashr_i32 s7, s6, 31
	s_add_u32 s13, s21, s4
	s_addc_u32 s16, s22, s5
	s_lshl_b64 s[4:5], s[6:7], 12
	s_add_u32 s4, s13, s4
	s_addc_u32 s5, s16, s5
	s_lshl_b64 s[2:3], s[2:3], 1
	s_add_u32 s2, s4, s2
	s_addc_u32 s3, s5, s3
	s_add_i32 s12, s12, s23
	s_cmpk_gt_i32 s12, 0xfff
	s_waitcnt vmcnt(0) lgkmcnt(0)
	ds_write2_b32 v113, v114, v115 offset1:1
	ds_write2_b32 v113, v116, v117 offset0:2 offset1:3
	ds_write2_b32 v111, v56, v57 offset1:1
	v_add_u32_e32 v56, 0x418, v113
	ds_write2_b32 v56, v58, v59 offset1:1
	v_add_u32_e32 v56, 0x820, v113
	ds_write2_b32 v56, v52, v53 offset1:1
	v_add_u32_e32 v52, 0x828, v113
	ds_write2_b32 v52, v54, v55 offset1:1
	v_add_u32_e32 v52, 0xc30, v113
	ds_write2_b32 v52, v48, v49 offset1:1
	v_add_u32_e32 v48, 0xc38, v113
	ds_write2_b32 v48, v50, v51 offset1:1
	v_add_u32_e32 v48, 0x1040, v113
	ds_write2_b32 v48, v44, v45 offset1:1
	v_add_u32_e32 v44, 0x1048, v113
	ds_write2_b32 v44, v46, v47 offset1:1
	v_add_u32_e32 v44, 0x1450, v113
	ds_write2_b32 v44, v40, v41 offset1:1
	v_add_u32_e32 v40, 0x1458, v113
	ds_write2_b32 v40, v42, v43 offset1:1
	v_add_u32_e32 v40, 0x1860, v113
	ds_write2_b32 v40, v36, v37 offset1:1
	v_add_u32_e32 v36, 0x1868, v113
	ds_write2_b32 v36, v38, v39 offset1:1
	v_add_u32_e32 v36, 0x1c70, v113
	ds_write2_b32 v36, v32, v33 offset1:1
	v_add_u32_e32 v32, 0x1c78, v113
	ds_write2_b32 v32, v34, v35 offset1:1
	v_add_u32_e32 v32, 0x2080, v113
	ds_write2_b32 v32, v28, v29 offset1:1
	v_add_u32_e32 v28, 0x2088, v113
	ds_write2_b32 v28, v30, v31 offset1:1
	v_add_u32_e32 v28, 0x2490, v113
	ds_write2_b32 v28, v24, v25 offset1:1
	v_add_u32_e32 v24, 0x2498, v113
	ds_write2_b32 v24, v26, v27 offset1:1
	v_add_u32_e32 v24, 0x28a0, v113
	ds_write2_b32 v24, v20, v21 offset1:1
	v_add_u32_e32 v20, 0x28a8, v113
	ds_write2_b32 v20, v22, v23 offset1:1
	v_add_u32_e32 v20, 0x2cb0, v113
	ds_write2_b32 v20, v16, v17 offset1:1
	v_add_u32_e32 v16, 0x2cb8, v113
	ds_write2_b32 v16, v18, v19 offset1:1
	v_add_u32_e32 v16, 0x30c0, v113
	ds_write2_b32 v16, v12, v13 offset1:1
	v_add_u32_e32 v12, 0x30c8, v113
	ds_write2_b32 v12, v14, v15 offset1:1
	v_add_u32_e32 v12, 0x34d0, v113
	ds_write2_b32 v12, v8, v9 offset1:1
	v_add_u32_e32 v8, 0x34d8, v113
	ds_write2_b32 v8, v10, v11 offset1:1
	v_add_u32_e32 v8, 0x38e0, v113
	ds_write2_b32 v8, v4, v5 offset1:1
	v_add_u32_e32 v4, 0x38e8, v113
	ds_write2_b32 v4, v6, v7 offset1:1
	v_add_u32_e32 v4, 0x3cf0, v113
	ds_write2_b32 v4, v0, v1 offset1:1
	v_add_u32_e32 v0, 0x3cf8, v113
	ds_write2_b32 v0, v2, v3 offset1:1
	s_waitcnt lgkmcnt(0)
	ds_read2_b32 v[6:7], v112 offset0:65 offset1:73
	ds_read2_b32 v[8:9], v112 offset1:8
	ds_read2_b32 v[10:11], v112 offset0:130 offset1:138
	ds_read2_b32 v[12:13], v112 offset0:195 offset1:203
	v_mov_b32_e32 v111, v97
	v_lshl_add_u64 v[4:5], s[2:3], 0, v[110:111]
	v_lshl_add_u64 v[22:23], v[4:5], 0, v[92:93]
	s_waitcnt lgkmcnt(2)
	v_cvt_pk_bf16_f32 v0, v8, v6
	v_add_u32_e32 v6, 0x400, v112
	ds_read2_b32 v[14:15], v6 offset0:4 offset1:12
	ds_read2_b32 v[16:17], v6 offset0:69 offset1:77
	ds_read2_b32 v[18:19], v6 offset0:134 offset1:142
	ds_read2_b32 v[20:21], v6 offset0:199 offset1:207
	s_waitcnt lgkmcnt(4)
	v_cvt_pk_bf16_f32 v1, v10, v12
	v_lshl_add_u64 v[24:25], v[4:5], 0, v[98:99]
	s_waitcnt lgkmcnt(2)
	v_cvt_pk_bf16_f32 v2, v14, v16
	s_waitcnt lgkmcnt(0)
	v_cvt_pk_bf16_f32 v3, v18, v20
	global_store_dwordx4 v[22:23], v[0:3], off sc1
	s_nop 1
	v_cvt_pk_bf16_f32 v0, v9, v7
	v_cvt_pk_bf16_f32 v1, v11, v13
	v_cvt_pk_bf16_f32 v2, v15, v17
	v_cvt_pk_bf16_f32 v3, v19, v21
	v_lshl_add_u64 v[8:9], v[4:5], 0, v[94:95]
	global_store_dwordx4 v[8:9], v[0:3], off sc1
	ds_read2_b32 v[8:9], v112 offset0:81 offset1:89
	ds_read2_b32 v[10:11], v112 offset0:16 offset1:24
	ds_read2_b32 v[12:13], v112 offset0:146 offset1:154
	ds_read2_b32 v[14:15], v112 offset0:211 offset1:219
	ds_read2_b32 v[16:17], v6 offset0:20 offset1:28
	ds_read2_b32 v[18:19], v6 offset0:85 offset1:93
	ds_read2_b32 v[20:21], v6 offset0:150 offset1:158
	ds_read2_b32 v[22:23], v6 offset0:215 offset1:223
	s_waitcnt lgkmcnt(6)
	v_cvt_pk_bf16_f32 v0, v10, v8
	s_waitcnt lgkmcnt(4)
	v_cvt_pk_bf16_f32 v1, v12, v14
	s_waitcnt lgkmcnt(2)
	v_cvt_pk_bf16_f32 v2, v16, v18
	s_waitcnt lgkmcnt(0)
	v_cvt_pk_bf16_f32 v3, v20, v22
	global_store_dwordx4 v[24:25], v[0:3], off sc1
	v_lshl_add_u64 v[24:25], v[4:5], 0, v[102:103]
	s_nop 0
	v_cvt_pk_bf16_f32 v0, v11, v9
	v_cvt_pk_bf16_f32 v1, v13, v15
	v_cvt_pk_bf16_f32 v2, v17, v19
	v_cvt_pk_bf16_f32 v3, v21, v23
	v_lshl_add_u64 v[8:9], v[4:5], 0, v[100:101]
	global_store_dwordx4 v[8:9], v[0:3], off sc1
	ds_read2_b32 v[8:9], v112 offset0:32 offset1:40
	ds_read2_b32 v[10:11], v112 offset0:97 offset1:105
	ds_read2_b32 v[12:13], v112 offset0:162 offset1:170
	ds_read2_b32 v[14:15], v112 offset0:227 offset1:235
	ds_read2_b32 v[16:17], v6 offset0:36 offset1:44
	ds_read2_b32 v[18:19], v6 offset0:101 offset1:109
	ds_read2_b32 v[20:21], v6 offset0:166 offset1:174
	ds_read2_b32 v[22:23], v6 offset0:231 offset1:239
	s_waitcnt lgkmcnt(6)
	v_cvt_pk_bf16_f32 v0, v8, v10
	s_waitcnt lgkmcnt(4)
	v_cvt_pk_bf16_f32 v1, v12, v14
	s_waitcnt lgkmcnt(2)
	v_cvt_pk_bf16_f32 v2, v16, v18
	s_waitcnt lgkmcnt(0)
	v_cvt_pk_bf16_f32 v3, v20, v22
	global_store_dwordx4 v[24:25], v[0:3], off sc1
	s_nop 1
	v_cvt_pk_bf16_f32 v0, v9, v11
	v_cvt_pk_bf16_f32 v1, v13, v15
	v_cvt_pk_bf16_f32 v2, v17, v19
	v_cvt_pk_bf16_f32 v3, v21, v23
	v_lshl_add_u64 v[8:9], v[4:5], 0, v[104:105]
	global_store_dwordx4 v[8:9], v[0:3], off sc1
	ds_read2_b32 v[8:9], v112 offset0:48 offset1:56
	ds_read2_b32 v[10:11], v112 offset0:113 offset1:121
	ds_read2_b32 v[12:13], v112 offset0:178 offset1:186
	ds_read2_b32 v[14:15], v112 offset0:243 offset1:251
	ds_read2_b32 v[16:17], v6 offset0:52 offset1:60
	ds_read2_b32 v[18:19], v6 offset0:117 offset1:125
	ds_read2_b32 v[20:21], v6 offset0:182 offset1:190
	ds_read2_b32 v[6:7], v6 offset0:247 offset1:255
	v_lshl_add_u64 v[22:23], v[4:5], 0, v[106:107]
	s_waitcnt lgkmcnt(6)
	v_cvt_pk_bf16_f32 v0, v8, v10
	s_waitcnt lgkmcnt(4)
	v_cvt_pk_bf16_f32 v1, v12, v14
	s_waitcnt lgkmcnt(2)
	v_cvt_pk_bf16_f32 v2, v16, v18
	s_waitcnt lgkmcnt(0)
	v_cvt_pk_bf16_f32 v3, v20, v6
	global_store_dwordx4 v[22:23], v[0:3], off sc1
	v_lshl_add_u64 v[4:5], v[4:5], 0, v[108:109]
	s_nop 0
	v_cvt_pk_bf16_f32 v0, v9, v11
	v_cvt_pk_bf16_f32 v1, v13, v15
	v_cvt_pk_bf16_f32 v2, v17, v19
	v_cvt_pk_bf16_f32 v3, v21, v7
	global_store_dwordx4 v[4:5], v[0:3], off sc1
	s_waitcnt lgkmcnt(0)
	s_cbranch_scc0 .LBB0_305

.LBB0_410:
	ds_read_b128 v[136:139], v123 offset:4096
	ds_read_b128 v[140:143], v123 offset:4112
	s_waitcnt vmcnt(12)
	v_lshlrev_b32_e32 v146, 16, v98
	v_and_b32_e32 v147, 0xffff0000, v98
	v_lshlrev_b32_e32 v148, 16, v110
	v_and_b32_e32 v149, 0xffff0000, v110
	v_lshlrev_b32_e32 v98, 16, v99
	v_and_b32_e32 v99, 0xffff0000, v99
	v_lshlrev_b32_e32 v110, 16, v111
	v_and_b32_e32 v111, 0xffff0000, v111
	v_lshlrev_b32_e32 v144, 16, v92
	v_and_b32_e32 v145, 0xffff0000, v92
	v_lshlrev_b32_e32 v92, 16, v93
	v_and_b32_e32 v93, 0xffff0000, v93
	v_pk_add_f32 v[98:99], v[98:99], v[110:111]
	v_lshlrev_b32_e32 v110, 16, v100
	v_pk_fma_f32 v[98:99], v[98:99], 0.5, v[92:93] op_sel_hi:[1,0,1] neg_lo:[0,0,1] neg_hi:[0,0,1]
	v_and_b32_e32 v111, 0xffff0000, v100
	s_waitcnt lgkmcnt(1)
	v_pk_fma_f32 v[98:99], v[98:99], v[138:139], v[92:93]
	v_lshlrev_b32_e32 v138, 16, v112
	v_and_b32_e32 v139, 0xffff0000, v112
	v_lshlrev_b32_e32 v92, 16, v94
	v_and_b32_e32 v93, 0xffff0000, v94
	v_pk_add_f32 v[110:111], v[110:111], v[138:139]
	v_lshlrev_b32_e32 v94, 16, v101
	v_pk_fma_f32 v[110:111], v[110:111], 0.5, v[92:93] op_sel_hi:[1,0,1] neg_lo:[0,0,1] neg_hi:[0,0,1]
	v_lshlrev_b32_e32 v100, 16, v113
	s_waitcnt lgkmcnt(0)
	v_pk_fma_f32 v[110:111], v[110:111], v[140:141], v[92:93]
	v_lshlrev_b32_e32 v92, 16, v95
	v_and_b32_e32 v93, 0xffff0000, v95
	v_and_b32_e32 v95, 0xffff0000, v101
	v_and_b32_e32 v101, 0xffff0000, v113
	s_add_u32 s4, s78, s14
	v_pk_add_f32 v[146:147], v[146:147], v[148:149]
	v_pk_add_f32 v[94:95], v[94:95], v[100:101]
	s_addc_u32 s5, s79, s15
	v_pk_fma_f32 v[146:147], v[146:147], 0.5, v[144:145] op_sel_hi:[1,0,1] neg_lo:[0,0,1] neg_hi:[0,0,1]
	v_pk_fma_f32 v[94:95], v[94:95], 0.5, v[92:93] op_sel_hi:[1,0,1] neg_lo:[0,0,1] neg_hi:[0,0,1]
	v_lshl_add_u64 v[112:113], v[126:127], 1, s[4:5]
	v_pk_fma_f32 v[136:137], v[146:147], v[136:137], v[144:145]
	v_pk_fma_f32 v[100:101], v[94:95], v[142:143], v[92:93]
	v_cvt_pk_bf16_f32 v93, v98, v99
	v_add_co_u32_e32 v98, vcc, 0x4209c000, v112
	v_cvt_pk_bf16_f32 v92, v136, v137
	v_cvt_pk_bf16_f32 v94, v110, v111
	v_cvt_pk_bf16_f32 v95, v100, v101
	v_addc_co_u32_e32 v99, vcc, 0, v113, vcc
	global_store_dwordx4 v[98:99], v[92:95], off sc1
	s_or_b64 exec, exec, s[2:3]
	s_and_saveexec_b64 s[2:3], s[58:59]
	s_cbranch_execz .LBB0_403
.LBB0_411:
	s_waitcnt vmcnt(12)
	v_lshl_add_u32 v98, v130, 2, 0
	ds_read_b128 v[92:95], v98 offset:4096
	ds_read_b128 v[98:101], v98 offset:4112
	s_waitcnt vmcnt(11)
	v_lshlrev_b32_e32 v112, 16, v80
	v_and_b32_e32 v113, 0xffff0000, v80
	v_lshlrev_b32_e32 v136, 16, v106
	v_and_b32_e32 v137, 0xffff0000, v106
	v_lshlrev_b32_e32 v80, 16, v81
	v_and_b32_e32 v81, 0xffff0000, v81
	v_lshlrev_b32_e32 v106, 16, v107
	v_and_b32_e32 v107, 0xffff0000, v107
	v_lshlrev_b32_e32 v110, 16, v88
	v_and_b32_e32 v111, 0xffff0000, v88
	v_lshlrev_b32_e32 v88, 16, v89
	v_and_b32_e32 v89, 0xffff0000, v89
	v_pk_add_f32 v[80:81], v[80:81], v[106:107]
	v_lshlrev_b32_e32 v106, 16, v108
	v_pk_fma_f32 v[80:81], v[80:81], 0.5, v[88:89] op_sel_hi:[1,0,1] neg_lo:[0,0,1] neg_hi:[0,0,1]
	v_and_b32_e32 v107, 0xffff0000, v108
	s_waitcnt lgkmcnt(1)
	v_pk_fma_f32 v[88:89], v[80:81], v[94:95], v[88:89]
	v_lshlrev_b32_e32 v94, 16, v82
	v_and_b32_e32 v95, 0xffff0000, v82
	v_lshlrev_b32_e32 v80, 16, v90
	v_and_b32_e32 v81, 0xffff0000, v90
	v_pk_add_f32 v[94:95], v[94:95], v[106:107]
	v_lshlrev_b32_e32 v82, 16, v83
	v_pk_fma_f32 v[94:95], v[94:95], 0.5, v[80:81] op_sel_hi:[1,0,1] neg_lo:[0,0,1] neg_hi:[0,0,1]
	v_and_b32_e32 v83, 0xffff0000, v83
	s_waitcnt lgkmcnt(0)
	v_pk_fma_f32 v[94:95], v[94:95], v[98:99], v[80:81]
	v_lshlrev_b32_e32 v80, 16, v91
	v_and_b32_e32 v81, 0xffff0000, v91
	v_lshlrev_b32_e32 v90, 16, v109
	v_and_b32_e32 v91, 0xffff0000, v109
	s_add_u32 s4, s78, s14
	v_pk_add_f32 v[112:113], v[112:113], v[136:137]
	v_pk_add_f32 v[82:83], v[82:83], v[90:91]
	v_ashrrev_i32_e32 v131, 31, v130
	s_addc_u32 s5, s79, s15
	v_pk_fma_f32 v[112:113], v[112:113], 0.5, v[110:111] op_sel_hi:[1,0,1] neg_lo:[0,0,1] neg_hi:[0,0,1]
	v_pk_fma_f32 v[82:83], v[82:83], 0.5, v[80:81] op_sel_hi:[1,0,1] neg_lo:[0,0,1] neg_hi:[0,0,1]
	v_lshl_add_u64 v[98:99], v[130:131], 1, s[4:5]
	v_pk_fma_f32 v[92:93], v[112:113], v[92:93], v[110:111]
	v_pk_fma_f32 v[90:91], v[82:83], v[100:101], v[80:81]
	v_cvt_pk_bf16_f32 v81, v88, v89
	v_add_co_u32_e32 v88, vcc, 0x4209c000, v98
	v_cvt_pk_bf16_f32 v80, v92, v93
	v_cvt_pk_bf16_f32 v82, v94, v95
	v_cvt_pk_bf16_f32 v83, v90, v91
	v_addc_co_u32_e32 v89, vcc, 0, v99, vcc
	global_store_dwordx4 v[88:89], v[80:83], off sc1
	s_or_b64 exec, exec, s[2:3]
	s_and_saveexec_b64 s[4:5], s[56:57]
	s_cbranch_execz .LBB0_404
.LBB0_412:
	s_waitcnt vmcnt(11)
	ds_read_b128 v[80:83], v123 offset:8192
	ds_read_b128 v[88:91], v123 offset:8208
	s_waitcnt vmcnt(10)
	v_lshlrev_b32_e32 v94, 16, v76
	v_and_b32_e32 v95, 0xffff0000, v76
	v_lshlrev_b32_e32 v98, 16, v102
	v_and_b32_e32 v99, 0xffff0000, v102
	v_lshlrev_b32_e32 v92, 16, v84
	v_and_b32_e32 v93, 0xffff0000, v84
	v_pk_add_f32 v[94:95], v[94:95], v[98:99]
	v_lshlrev_b32_e32 v76, 16, v77
	v_pk_fma_f32 v[94:95], v[94:95], 0.5, v[92:93] op_sel_hi:[1,0,1] neg_lo:[0,0,1] neg_hi:[0,0,1]
	v_and_b32_e32 v77, 0xffff0000, v77
	s_waitcnt lgkmcnt(1)
	v_pk_fma_f32 v[92:93], v[94:95], v[80:81], v[92:93]
	v_lshlrev_b32_e32 v80, 16, v85
	v_and_b32_e32 v81, 0xffff0000, v85
	v_lshlrev_b32_e32 v84, 16, v103
	v_and_b32_e32 v85, 0xffff0000, v103
	v_pk_add_f32 v[76:77], v[76:77], v[84:85]
	s_add_u32 s2, s78, s14
	v_pk_fma_f32 v[76:77], v[76:77], 0.5, v[80:81] op_sel_hi:[1,0,1] neg_lo:[0,0,1] neg_hi:[0,0,1]
	s_addc_u32 s3, s79, s15
	v_pk_fma_f32 v[84:85], v[76:77], v[82:83], v[80:81]
	v_lshlrev_b32_e32 v80, 16, v78
	v_and_b32_e32 v81, 0xffff0000, v78
	v_lshlrev_b32_e32 v82, 16, v104
	v_and_b32_e32 v83, 0xffff0000, v104
	v_lshlrev_b32_e32 v76, 16, v86
	v_and_b32_e32 v77, 0xffff0000, v86
	v_pk_add_f32 v[80:81], v[80:81], v[82:83]
	v_lshlrev_b32_e32 v78, 16, v79
	v_pk_fma_f32 v[80:81], v[80:81], 0.5, v[76:77] op_sel_hi:[1,0,1] neg_lo:[0,0,1] neg_hi:[0,0,1]
	v_and_b32_e32 v79, 0xffff0000, v79
	s_waitcnt lgkmcnt(0)
	v_pk_fma_f32 v[88:89], v[80:81], v[88:89], v[76:77]
	v_lshlrev_b32_e32 v80, 16, v105
	v_and_b32_e32 v81, 0xffff0000, v105
	v_lshlrev_b32_e32 v76, 16, v87
	v_and_b32_e32 v77, 0xffff0000, v87
	v_pk_add_f32 v[78:79], v[78:79], v[80:81]
	s_nop 0
	v_pk_fma_f32 v[78:79], v[78:79], 0.5, v[76:77] op_sel_hi:[1,0,1] neg_lo:[0,0,1] neg_hi:[0,0,1]
	s_nop 0
	v_pk_fma_f32 v[86:87], v[78:79], v[90:91], v[76:77]
	v_lshl_add_u64 v[90:91], v[126:127], 1, s[2:3]
	s_mov_b32 s2, 0x4649c000
	v_add_co_u32_e32 v80, vcc, s2, v90
	v_cvt_pk_bf16_f32 v76, v92, v93
	v_cvt_pk_bf16_f32 v77, v84, v85
	v_cvt_pk_bf16_f32 v78, v88, v89
	v_cvt_pk_bf16_f32 v79, v86, v87
	v_addc_co_u32_e32 v81, vcc, 0, v91, vcc
	global_store_dwordx4 v[80:81], v[76:79], off sc1
	ds_read_b128 v[76:79], v123 offset:18688
	ds_read_b128 v[80:83], v123 offset:18704
	v_cmp_lt_i32_e32 vcc, v203, v202
	s_mov_b32 s2, 0xf800000
	s_waitcnt lgkmcnt(1)
	v_pk_mul_f32 v[76:77], v[92:93], v[76:77]
	v_pk_mul_f32 v[78:79], v[84:85], v[78:79]
	v_pk_mul_f32 v[92:93], v[76:77], v[76:77]
	v_pk_mul_f32 v[84:85], v[78:79], v[78:79]
	v_add_f32_e32 v92, v92, v93
	s_waitcnt lgkmcnt(0)
	v_pk_mul_f32 v[80:81], v[88:89], v[80:81]
	v_add_f32_e32 v84, v84, v92
	v_pk_mul_f32 v[88:89], v[80:81], v[80:81]
	v_add_f32_e32 v84, v85, v84
	v_pk_mul_f32 v[82:83], v[86:87], v[82:83]
	v_add_f32_e32 v84, v88, v84
	v_pk_mul_f32 v[86:87], v[82:83], v[82:83]
	v_add_f32_e32 v84, v89, v84
	v_cndmask_b32_e32 v94, v200, v203, vcc
	v_add_f32_e32 v84, v86, v84
	v_lshlrev_b32_e32 v94, 2, v94
	v_add_f32_e32 v84, v87, v84
	ds_bpermute_b32 v85, v94, v84
	v_cmp_lt_i32_e32 vcc, v204, v202
	s_waitcnt lgkmcnt(0)
	v_add_f32_e32 v84, v84, v85
	v_cndmask_b32_e32 v95, v200, v204, vcc
	v_lshlrev_b32_e32 v95, 2, v95
	ds_bpermute_b32 v85, v95, v84
	v_cmp_lt_i32_e32 vcc, v205, v202
	s_waitcnt lgkmcnt(0)
	v_add_f32_e32 v84, v84, v85
	v_cndmask_b32_e32 v98, v200, v205, vcc
	v_lshlrev_b32_e32 v98, 2, v98
	ds_bpermute_b32 v85, v98, v84
	s_waitcnt lgkmcnt(0)
	v_add_f32_e32 v84, v84, v85
	v_cmp_gt_f32_e32 vcc, s2, v84
	v_mul_f32_e32 v85, 0x4f800000, v84
	s_nop 0
	v_cndmask_b32_e32 v84, v84, v85, vcc
	v_sqrt_f32_e32 v85, v84
	s_nop 0
	v_add_u32_e32 v86, -1, v85
	v_fma_f32 v87, -v86, v85, v84
	v_cmp_ge_f32_e64 s[2:3], 0, v87
	v_add_u32_e32 v87, 1, v85
	s_nop 0
	v_cndmask_b32_e64 v86, v85, v86, s[2:3]
	v_fma_f32 v85, -v87, v85, v84
	v_cmp_lt_f32_e64 s[2:3], 0, v85
	s_nop 1
	v_cndmask_b32_e64 v85, v86, v87, s[2:3]
	v_mul_f32_e32 v86, 0x37800000, v85
	v_cndmask_b32_e32 v85, v85, v86, vcc
	v_mov_b32_e32 v86, 0x260
	v_cmp_class_f32_e32 vcc, v84, v86
	s_nop 1
	v_cndmask_b32_e32 v84, v85, v84, vcc
	v_max_f32_e32 v84, 0x2b8cbccc, v84
	v_div_scale_f32 v85, s[2:3], v84, v84, 1.0
	v_rcp_f32_e32 v86, v85
	s_nop 0
	v_fma_f32 v87, -v85, v86, 1.0
	v_fmac_f32_e32 v86, v87, v86
	v_div_scale_f32 v87, vcc, 1.0, v84, 1.0
	v_mul_f32_e32 v88, v87, v86
	v_fma_f32 v89, -v85, v88, v87
	v_fmac_f32_e32 v88, v89, v86
	v_fma_f32 v85, -v85, v88, v87
	v_div_fmas_f32 v85, v85, v86, v88
	v_div_fixup_f32 v84, v85, v84, 1.0
	v_pk_mul_f32 v[76:77], v[76:77], v[84:85] op_sel_hi:[1,0]
	v_pk_mul_f32 v[78:79], v[78:79], v[84:85] op_sel_hi:[1,0]
	v_pk_mul_f32 v[80:81], v[80:81], v[84:85] op_sel_hi:[1,0]
	v_pk_mul_f32 v[82:83], v[82:83], v[84:85] op_sel_hi:[1,0]
	v_cvt_pk_bf16_f32 v76, v76, v77
	v_cvt_pk_bf16_f32 v77, v78, v79
	v_cvt_pk_bf16_f32 v78, v80, v81
	v_add_co_u32_e32 v80, vcc, 0x3fe9c000, v90
	v_cvt_pk_bf16_f32 v79, v82, v83
	s_nop 0
	v_addc_co_u32_e32 v81, vcc, 0, v91, vcc
	global_store_dwordx4 v[80:81], v[76:79], off sc1
	s_or_b64 exec, exec, s[4:5]
	s_and_saveexec_b64 s[4:5], s[54:55]
	s_cbranch_execz .LBB0_405
.LBB0_413:
	s_waitcnt vmcnt(10)
	ds_read_b128 v[76:79], v123 offset:10240
	ds_read_b128 v[80:83], v123 offset:10256
	s_waitcnt vmcnt(9)
	v_lshlrev_b32_e32 v86, 16, v64
	v_and_b32_e32 v87, 0xffff0000, v64
	v_lshlrev_b32_e32 v88, 16, v72
	v_and_b32_e32 v89, 0xffff0000, v72
	v_lshlrev_b32_e32 v64, 16, v65
	v_and_b32_e32 v65, 0xffff0000, v65
	v_lshlrev_b32_e32 v72, 16, v73
	v_and_b32_e32 v73, 0xffff0000, v73
	v_lshlrev_b32_e32 v84, 16, v68
	v_and_b32_e32 v85, 0xffff0000, v68
	v_lshlrev_b32_e32 v68, 16, v69
	v_and_b32_e32 v69, 0xffff0000, v69
	v_pk_add_f32 v[64:65], v[64:65], v[72:73]
	s_add_u32 s2, s78, s14
	v_pk_fma_f32 v[64:65], v[64:65], 0.5, v[68:69] op_sel_hi:[1,0,1] neg_lo:[0,0,1] neg_hi:[0,0,1]
	v_pk_add_f32 v[86:87], v[86:87], v[88:89]
	s_waitcnt lgkmcnt(1)
	v_pk_fma_f32 v[72:73], v[64:65], v[78:79], v[68:69]
	v_lshlrev_b32_e32 v68, 16, v66
	v_and_b32_e32 v69, 0xffff0000, v66
	v_lshlrev_b32_e32 v78, 16, v74
	v_and_b32_e32 v79, 0xffff0000, v74
	v_lshlrev_b32_e32 v64, 16, v70
	v_and_b32_e32 v65, 0xffff0000, v70
	v_pk_add_f32 v[68:69], v[68:69], v[78:79]
	v_lshlrev_b32_e32 v66, 16, v67
	v_pk_fma_f32 v[68:69], v[68:69], 0.5, v[64:65] op_sel_hi:[1,0,1] neg_lo:[0,0,1] neg_hi:[0,0,1]
	v_and_b32_e32 v67, 0xffff0000, v67
	s_waitcnt lgkmcnt(0)
	v_pk_fma_f32 v[78:79], v[68:69], v[80:81], v[64:65]
	v_lshlrev_b32_e32 v68, 16, v75
	v_and_b32_e32 v69, 0xffff0000, v75
	v_lshlrev_b32_e32 v64, 16, v71
	v_and_b32_e32 v65, 0xffff0000, v71
	v_pk_add_f32 v[66:67], v[66:67], v[68:69]
	s_addc_u32 s3, s79, s15
	v_pk_fma_f32 v[86:87], v[86:87], 0.5, v[84:85] op_sel_hi:[1,0,1] neg_lo:[0,0,1] neg_hi:[0,0,1]
	v_pk_fma_f32 v[66:67], v[66:67], 0.5, v[64:65] op_sel_hi:[1,0,1] neg_lo:[0,0,1] neg_hi:[0,0,1]
	v_lshl_add_u64 v[80:81], v[126:127], 1, s[2:3]
	s_mov_b32 s2, 0x4649c000
	v_pk_fma_f32 v[76:77], v[86:87], v[76:77], v[84:85]
	v_pk_fma_f32 v[74:75], v[66:67], v[82:83], v[64:65]
	v_add_co_u32_e32 v68, vcc, s2, v80
	v_cvt_pk_bf16_f32 v64, v76, v77
	v_cvt_pk_bf16_f32 v65, v72, v73
	v_cvt_pk_bf16_f32 v66, v78, v79
	v_cvt_pk_bf16_f32 v67, v74, v75
	v_addc_co_u32_e32 v69, vcc, 0, v81, vcc
	global_store_dwordx4 v[68:69], v[64:67], off offset:1024 sc1
	ds_read_b128 v[64:67], v123 offset:20736
	ds_read_b128 v[68:71], v123 offset:20752
	v_cmp_lt_i32_e32 vcc, v203, v202
	s_mov_b32 s2, 0xf800000
	s_waitcnt lgkmcnt(1)
	v_pk_mul_f32 v[64:65], v[76:77], v[64:65]
	v_pk_mul_f32 v[66:67], v[72:73], v[66:67]
	v_pk_mul_f32 v[76:77], v[64:65], v[64:65]
	v_pk_mul_f32 v[72:73], v[66:67], v[66:67]
	v_add_f32_e32 v76, v76, v77
	s_waitcnt lgkmcnt(0)
	v_pk_mul_f32 v[68:69], v[78:79], v[68:69]
	v_add_f32_e32 v72, v72, v76
	v_pk_mul_f32 v[78:79], v[68:69], v[68:69]
	v_add_f32_e32 v72, v73, v72
	v_pk_mul_f32 v[70:71], v[74:75], v[70:71]
	v_add_f32_e32 v72, v78, v72
	v_pk_mul_f32 v[74:75], v[70:71], v[70:71]
	v_add_f32_e32 v72, v79, v72
	v_cndmask_b32_e32 v82, v200, v203, vcc
	v_add_f32_e32 v72, v74, v72
	v_lshlrev_b32_e32 v82, 2, v82
	v_add_f32_e32 v72, v75, v72
	ds_bpermute_b32 v73, v82, v72
	v_cmp_lt_i32_e32 vcc, v204, v202
	s_waitcnt lgkmcnt(0)
	v_add_f32_e32 v72, v72, v73
	v_cndmask_b32_e32 v83, v200, v204, vcc
	v_lshlrev_b32_e32 v83, 2, v83
	ds_bpermute_b32 v73, v83, v72
	v_cmp_lt_i32_e32 vcc, v205, v202
	s_waitcnt lgkmcnt(0)
	v_add_f32_e32 v72, v72, v73
	v_cndmask_b32_e32 v84, v200, v205, vcc
	v_lshlrev_b32_e32 v84, 2, v84
	ds_bpermute_b32 v73, v84, v72
	s_waitcnt lgkmcnt(0)
	v_add_f32_e32 v72, v72, v73
	v_cmp_gt_f32_e32 vcc, s2, v72
	v_mul_f32_e32 v73, 0x4f800000, v72
	s_nop 0
	v_cndmask_b32_e32 v72, v72, v73, vcc
	v_sqrt_f32_e32 v73, v72
	s_nop 0
	v_add_u32_e32 v74, -1, v73
	v_fma_f32 v75, -v74, v73, v72
	v_cmp_ge_f32_e64 s[2:3], 0, v75
	v_add_u32_e32 v75, 1, v73
	s_nop 0
	v_cndmask_b32_e64 v74, v73, v74, s[2:3]
	v_fma_f32 v73, -v75, v73, v72
	v_cmp_lt_f32_e64 s[2:3], 0, v73
	s_nop 1
	v_cndmask_b32_e64 v73, v74, v75, s[2:3]
	v_mul_f32_e32 v74, 0x37800000, v73
	v_cndmask_b32_e32 v73, v73, v74, vcc
	v_mov_b32_e32 v74, 0x260
	v_cmp_class_f32_e32 vcc, v72, v74
	s_nop 1
	v_cndmask_b32_e32 v72, v73, v72, vcc
	v_max_f32_e32 v72, 0x2b8cbccc, v72
	v_div_scale_f32 v73, s[2:3], v72, v72, 1.0
	v_rcp_f32_e32 v74, v73
	s_nop 0
	v_fma_f32 v75, -v73, v74, 1.0
	v_fmac_f32_e32 v74, v75, v74
	v_div_scale_f32 v75, vcc, 1.0, v72, 1.0
	v_mul_f32_e32 v76, v75, v74
	v_fma_f32 v77, -v73, v76, v75
	v_fmac_f32_e32 v76, v77, v74
	v_fma_f32 v73, -v73, v76, v75
	v_div_fmas_f32 v73, v73, v74, v76
	v_div_fixup_f32 v72, v73, v72, 1.0
	v_pk_mul_f32 v[64:65], v[64:65], v[72:73] op_sel_hi:[1,0]
	v_pk_mul_f32 v[66:67], v[66:67], v[72:73] op_sel_hi:[1,0]
	v_pk_mul_f32 v[68:69], v[68:69], v[72:73] op_sel_hi:[1,0]
	v_pk_mul_f32 v[70:71], v[70:71], v[72:73] op_sel_hi:[1,0]
	v_cvt_pk_bf16_f32 v64, v64, v65
	v_cvt_pk_bf16_f32 v65, v66, v67
	v_cvt_pk_bf16_f32 v66, v68, v69
	v_add_co_u32_e32 v68, vcc, 0x3fe9c000, v80
	v_cvt_pk_bf16_f32 v67, v70, v71
	s_nop 0
	v_addc_co_u32_e32 v69, vcc, 0, v81, vcc
	global_store_dwordx4 v[68:69], v[64:67], off offset:1024 sc1
	s_or_b64 exec, exec, s[4:5]
	s_and_saveexec_b64 s[2:3], s[50:51]
	s_cbranch_execz .LBB0_406
.LBB0_414:
	s_waitcnt vmcnt(9)
	ds_read_b128 v[64:67], v123 offset:12288
	ds_read_b128 v[68:71], v123 offset:12304
	s_waitcnt vmcnt(8)
	v_lshlrev_b32_e32 v74, 16, v36
	v_and_b32_e32 v75, 0xffff0000, v36
	v_lshlrev_b32_e32 v76, 16, v60
	v_and_b32_e32 v77, 0xffff0000, v60
	v_lshlrev_b32_e32 v36, 16, v37
	v_and_b32_e32 v37, 0xffff0000, v37
	v_lshlrev_b32_e32 v60, 16, v61
	v_and_b32_e32 v61, 0xffff0000, v61
	v_lshlrev_b32_e32 v72, 16, v48
	v_and_b32_e32 v73, 0xffff0000, v48
	v_lshlrev_b32_e32 v48, 16, v49
	v_and_b32_e32 v49, 0xffff0000, v49
	v_pk_add_f32 v[36:37], v[36:37], v[60:61]
	v_lshlrev_b32_e32 v60, 16, v38
	v_pk_fma_f32 v[36:37], v[36:37], 0.5, v[48:49] op_sel_hi:[1,0,1] neg_lo:[0,0,1] neg_hi:[0,0,1]
	v_and_b32_e32 v61, 0xffff0000, v38
	s_waitcnt lgkmcnt(1)
	v_pk_fma_f32 v[48:49], v[36:37], v[66:67], v[48:49]
	v_lshlrev_b32_e32 v66, 16, v62
	v_and_b32_e32 v67, 0xffff0000, v62
	v_lshlrev_b32_e32 v36, 16, v50
	v_and_b32_e32 v37, 0xffff0000, v50
	v_pk_add_f32 v[60:61], v[60:61], v[66:67]
	v_lshlrev_b32_e32 v38, 16, v39
	v_pk_fma_f32 v[60:61], v[60:61], 0.5, v[36:37] op_sel_hi:[1,0,1] neg_lo:[0,0,1] neg_hi:[0,0,1]
	v_and_b32_e32 v39, 0xffff0000, v39
	s_waitcnt lgkmcnt(0)
	v_pk_fma_f32 v[60:61], v[60:61], v[68:69], v[36:37]
	v_lshlrev_b32_e32 v36, 16, v51
	v_and_b32_e32 v37, 0xffff0000, v51
	v_lshlrev_b32_e32 v50, 16, v63
	v_and_b32_e32 v51, 0xffff0000, v63
	s_add_u32 s4, s78, s14
	v_pk_add_f32 v[74:75], v[74:75], v[76:77]
	v_pk_add_f32 v[38:39], v[38:39], v[50:51]
	v_ashrrev_i32_e32 v129, 31, v128
	s_addc_u32 s5, s79, s15
	v_pk_fma_f32 v[74:75], v[74:75], 0.5, v[72:73] op_sel_hi:[1,0,1] neg_lo:[0,0,1] neg_hi:[0,0,1]
	v_pk_fma_f32 v[38:39], v[38:39], 0.5, v[36:37] op_sel_hi:[1,0,1] neg_lo:[0,0,1] neg_hi:[0,0,1]
	v_lshl_add_u64 v[62:63], v[128:129], 1, s[4:5]
	v_pk_fma_f32 v[64:65], v[74:75], v[64:65], v[72:73]
	v_pk_fma_f32 v[50:51], v[38:39], v[70:71], v[36:37]
	v_cvt_pk_bf16_f32 v37, v48, v49
	v_add_co_u32_e32 v48, vcc, 0x4429b000, v62
	v_cvt_pk_bf16_f32 v36, v64, v65
	v_cvt_pk_bf16_f32 v38, v60, v61
	v_cvt_pk_bf16_f32 v39, v50, v51
	v_addc_co_u32_e32 v49, vcc, 0, v63, vcc
	global_store_dwordx4 v[48:49], v[36:39], off sc1
	s_or_b64 exec, exec, s[2:3]
	s_and_saveexec_b64 s[2:3], s[48:49]
	s_cbranch_execz .LBB0_407
.LBB0_415:
	s_waitcnt vmcnt(8)
	ds_read_b128 v[36:39], v123 offset:14336
	ds_read_b128 v[48:51], v123 offset:14352
	s_waitcnt vmcnt(7)
	v_lshlrev_b32_e32 v62, 16, v32
	v_and_b32_e32 v63, 0xffff0000, v32
	v_lshlrev_b32_e32 v64, 16, v56
	v_and_b32_e32 v65, 0xffff0000, v56
	v_lshlrev_b32_e32 v32, 16, v33
	v_and_b32_e32 v33, 0xffff0000, v33
	v_lshlrev_b32_e32 v56, 16, v57
	v_and_b32_e32 v57, 0xffff0000, v57
	v_lshlrev_b32_e32 v60, 16, v44
	v_and_b32_e32 v61, 0xffff0000, v44
	v_lshlrev_b32_e32 v44, 16, v45
	v_and_b32_e32 v45, 0xffff0000, v45
	v_pk_add_f32 v[32:33], v[32:33], v[56:57]
	v_lshlrev_b32_e32 v56, 16, v58
	v_pk_fma_f32 v[32:33], v[32:33], 0.5, v[44:45] op_sel_hi:[1,0,1] neg_lo:[0,0,1] neg_hi:[0,0,1]
	v_and_b32_e32 v57, 0xffff0000, v58
	s_waitcnt lgkmcnt(1)
	v_pk_fma_f32 v[38:39], v[32:33], v[38:39], v[44:45]
	v_lshlrev_b32_e32 v44, 16, v34
	v_and_b32_e32 v45, 0xffff0000, v34
	v_lshlrev_b32_e32 v32, 16, v46
	v_and_b32_e32 v33, 0xffff0000, v46
	v_pk_add_f32 v[44:45], v[44:45], v[56:57]
	v_pk_add_f32 v[62:63], v[62:63], v[64:65]
	v_pk_fma_f32 v[44:45], v[44:45], 0.5, v[32:33] op_sel_hi:[1,0,1] neg_lo:[0,0,1] neg_hi:[0,0,1]
	v_lshlrev_b32_e32 v34, 16, v35
	s_waitcnt lgkmcnt(0)
	v_pk_fma_f32 v[44:45], v[44:45], v[48:49], v[32:33]
	v_lshlrev_b32_e32 v32, 16, v47
	v_and_b32_e32 v33, 0xffff0000, v47
	v_and_b32_e32 v35, 0xffff0000, v35
	v_lshlrev_b32_e32 v46, 16, v59
	v_and_b32_e32 v47, 0xffff0000, v59
	s_add_u32 s4, s78, s14
	v_pk_fma_f32 v[62:63], v[62:63], 0.5, v[60:61] op_sel_hi:[1,0,1] neg_lo:[0,0,1] neg_hi:[0,0,1]
	v_pk_add_f32 v[34:35], v[34:35], v[46:47]
	v_ashrrev_i32_e32 v125, 31, v124
	s_addc_u32 s5, s79, s15
	v_pk_fma_f32 v[36:37], v[62:63], v[36:37], v[60:61]
	v_pk_fma_f32 v[34:35], v[34:35], 0.5, v[32:33] op_sel_hi:[1,0,1] neg_lo:[0,0,1] neg_hi:[0,0,1]
	v_lshl_add_u64 v[48:49], v[124:125], 1, s[4:5]
	v_pk_fma_f32 v[46:47], v[34:35], v[50:51], v[32:33]
	v_cvt_pk_bf16_f32 v32, v36, v37
	v_add_co_u32_e32 v36, vcc, 0x4429b000, v48
	v_cvt_pk_bf16_f32 v33, v38, v39
	v_cvt_pk_bf16_f32 v34, v44, v45
	v_cvt_pk_bf16_f32 v35, v46, v47
	v_addc_co_u32_e32 v37, vcc, 0, v49, vcc
	global_store_dwordx4 v[36:37], v[32:35], off sc1
	s_or_b64 exec, exec, s[2:3]
	s_and_saveexec_b64 s[2:3], s[46:47]
	s_cbranch_execz .LBB0_408

.LBB0_422:
	s_or_b64 exec, exec, s[4:5]
	s_add_u32 s4, s78, s22
	v_ashrrev_i32_e32 v123, 31, v122
	s_addc_u32 s5, s79, s13
	v_lshl_add_u64 v[36:37], v[122:123], 1, s[4:5]
	v_cvt_pk_bf16_f32 v32, v32, v33
	v_cvt_pk_bf16_f32 v33, v34, v35
	v_cvt_pk_bf16_f32 v34, v28, v29
	v_add_co_u32_e32 v28, vcc, 0x4869a000, v36
	v_cvt_pk_bf16_f32 v35, v30, v31
	s_nop 0
	v_addc_co_u32_e32 v29, vcc, 0, v37, vcc
	global_store_dwordx4 v[28:29], v[32:35], off offset:2048 sc1
	s_or_b64 exec, exec, s[2:3]
	s_and_saveexec_b64 s[2:3], s[44:45]
	s_cbranch_execz .LBB0_409

.LBB0_429:
	s_or_b64 exec, exec, s[4:5]
	s_add_u32 s4, s78, s22
	v_ashrrev_i32_e32 v121, 31, v120
	s_addc_u32 s5, s79, s13
	v_lshl_add_u64 v[26:27], v[120:121], 1, s[4:5]
	v_cvt_pk_bf16_f32 v24, v16, v17
	v_add_co_u32_e32 v16, vcc, 0x4869a000, v26
	v_cvt_pk_bf16_f32 v22, v28, v29
	v_cvt_pk_bf16_f32 v23, v20, v21
	v_cvt_pk_bf16_f32 v25, v18, v19
	v_addc_co_u32_e32 v17, vcc, 0, v27, vcc
	global_store_dwordx4 v[16:17], v[22:25], off offset:2048 sc1
	s_or_b64 exec, exec, s[2:3]
	v_mov_b32_e32 v16, 0
	s_andn2_b64 vcc, exec, s[38:39]
	s_cbranch_vccnz .LBB0_435

.LBB0_437:
	s_andn2_saveexec_b64 s[2:3], s[20:21]
	v_mul_f32_e32 v17, 0x3f22f983, v16
	v_rndne_f32_e32 v19, v17
	v_cvt_i32_f32_e32 v18, v19
	v_fmamk_f32 v17, v19, 0xbfc90fda, v16
	v_fmac_f32_e32 v17, 0xb3a22168, v19
	v_fmac_f32_e32 v17, 0xa7c234c4, v19
	s_or_b64 exec, exec, s[2:3]
	v_mul_f32_e32 v19, v17, v17
	v_mov_b32_e32 v20, 0x3c0881c4
	v_fmamk_f32 v20, v19, 0xb94c1982, v20
	v_fmaak_f32 v20, v19, v20, 0xbe2aaa9d
	v_mul_f32_e32 v20, v19, v20
	v_fmac_f32_e32 v17, v17, v20
	v_mov_b32_e32 v20, 0xbab64f3b
	v_fmamk_f32 v20, v19, 0x37d75334, v20
	v_fmaak_f32 v20, v19, v20, 0x3d2aabf7
	v_fmaak_f32 v20, v19, v20, 0xbf000004
	v_fma_f32 v19, v19, v20, 1.0
	v_lshlrev_b32_e32 v20, 30, v18
	v_and_b32_e32 v18, 1, v18
	v_cmp_eq_u32_e32 vcc, 0, v18
	s_brev_b32 s2, 1
	s_waitcnt vmcnt(3)
	v_lshlrev_b32_e32 v26, 16, v8
	v_cndmask_b32_e32 v18, v19, v17, vcc
	v_xor_b32_e32 v17, 0x80000000, v17
	v_cndmask_b32_e32 v17, v17, v19, vcc
	v_bitop3_b32 v18, v18, v20, s2 bitop3:0x78
	v_bitop3_b32 v17, v17, v20, s2 bitop3:0x78
	s_mov_b32 s2, 0x7f800000
	v_cmp_lg_f32_e32 vcc, s2, v16
	v_and_b32_e32 v27, 0xffff0000, v8
	v_lshlrev_b32_e32 v22, 16, v12
	v_cndmask_b32_e32 v16, v201, v17, vcc
	v_cndmask_b32_e32 v17, v201, v18, vcc
	v_lshl_add_u32 v18, v133, 2, s16
	v_cmp_lt_i32_e32 vcc, v203, v202
	ds_write2st64_b32 v18, v16, v17 offset1:1
	v_and_b32_e32 v23, 0xffff0000, v12
	v_cndmask_b32_e32 v16, v200, v203, vcc
	v_cmp_lt_i32_e32 vcc, v204, v202
	v_lshlrev_b32_e32 v38, 2, v16
	v_lshlrev_b32_e32 v32, 16, v9
	v_cndmask_b32_e32 v16, v200, v204, vcc
	v_cmp_lt_i32_e32 vcc, v205, v202
	v_lshlrev_b32_e32 v39, 2, v16
	v_and_b32_e32 v33, 0xffff0000, v9
	v_cndmask_b32_e32 v16, v200, v205, vcc
	v_lshlrev_b32_e32 v40, 2, v16
	v_pk_mul_f32 v[16:17], v[26:27], v[26:27]
	v_lshlrev_b32_e32 v30, 16, v13
	v_pk_fma_f32 v[16:17], v[22:23], v[22:23], v[16:17]
	v_and_b32_e32 v31, 0xffff0000, v13
	v_pk_mul_f32 v[8:9], v[32:33], v[32:33]
	v_lshlrev_b32_e32 v34, 16, v14
	v_pk_fma_f32 v[8:9], v[30:31], v[30:31], v[8:9]
	v_and_b32_e32 v35, 0xffff0000, v14
	v_lshlrev_b32_e32 v36, 16, v10
	v_and_b32_e32 v37, 0xffff0000, v10
	v_add_f32_e32 v14, v16, v17
	v_pk_mul_f32 v[12:13], v[36:37], v[36:37]
	v_add_f32_e32 v8, v8, v14
	v_pk_fma_f32 v[12:13], v[34:35], v[34:35], v[12:13]
	v_lshlrev_b32_e32 v28, 16, v11
	v_and_b32_e32 v29, 0xffff0000, v11
	v_add_f32_e32 v8, v9, v8
	v_lshlrev_b32_e32 v24, 16, v15
	v_and_b32_e32 v25, 0xffff0000, v15
	v_pk_mul_f32 v[10:11], v[28:29], v[28:29]
	v_add_f32_e32 v8, v12, v8
	v_pk_fma_f32 v[10:11], v[24:25], v[24:25], v[10:11]
	v_add_f32_e32 v8, v13, v8
	v_add_f32_e32 v8, v10, v8
	v_add_f32_e32 v8, v11, v8
	ds_bpermute_b32 v9, v38, v8
	s_waitcnt lgkmcnt(0)
	s_waitcnt lgkmcnt(0)
	v_add_f32_e32 v8, v8, v9
	ds_bpermute_b32 v9, v39, v8
	s_waitcnt lgkmcnt(0)
	v_add_f32_e32 v16, v8, v9
	ds_bpermute_b32 v17, v40, v16
	v_bfe_u32 v8, v133, 2, 1
	v_lshlrev_b32_e32 v20, 7, v8
	v_lshlrev_b32_e32 v41, 8, v8
	s_and_saveexec_b64 s[2:3], s[42:43]
	s_cbranch_execz .LBB0_441
	s_waitcnt lgkmcnt(0)
	v_add_f32_e32 v16, v16, v17
	v_fmamk_f32 v16, v16, 0x3c000000, v196
	v_cmp_gt_f32_e32 vcc, s35, v16
	v_mul_f32_e32 v17, 0x4b800000, v16
	v_ashrrev_i32_e32 v59, 3, v133
	v_cndmask_b32_e32 v16, v16, v17, vcc
	v_rsq_f32_e32 v16, v16
	v_lshlrev_b32_e32 v18, 2, v135
	v_add3_u32 v21, s16, v20, v18
	ds_read_b128 v[12:15], v21
	ds_read_b128 v[8:11], v21 offset:16
	v_mul_f32_e32 v17, 0x45800000, v16
	v_cndmask_b32_e32 v58, v16, v17, vcc
	v_cmp_gt_i32_e32 vcc, 8, v59
	v_mov_b32_e32 v16, 0x200
	v_pk_mul_f32 v[36:37], v[58:59], v[36:37] op_sel_hi:[0,1]
	v_cndmask_b32_e64 v16, v16, 0, vcc
	v_add_u32_e32 v16, 0, v16
	v_add3_u32 v54, v16, v41, v18
	ds_read_b128 v[42:45], v54 offset:22928
	ds_read_b128 v[46:49], v54 offset:22784
	ds_read_b128 v[50:53], v54 offset:22800
	ds_read_b128 v[16:19], v21 offset:272
	v_pk_mul_f32 v[34:35], v[58:59], v[34:35] op_sel_hi:[0,1]
	s_waitcnt lgkmcnt(3)
	v_pk_mul_f32 v[36:37], v[36:37], v[42:43]
	v_mov_b32_e32 v42, v8
	s_waitcnt lgkmcnt(1)
	v_pk_mul_f32 v[34:35], v[34:35], v[50:51]
	v_mov_b32_e32 v50, v36
	v_mov_b32_e32 v43, v34
	s_waitcnt lgkmcnt(0)
	v_mov_b32_e32 v51, v16
	v_pk_mul_f32 v[42:43], v[42:43], v[50:51]
	v_mov_b32_e32 v50, v37
	v_add_f32_e32 v42, v42, v43
	v_cndmask_b32_e64 v60, v36, v42, s[38:39]
	v_mov_b32_e32 v42, v9
	v_mov_b32_e32 v43, v35
	v_mov_b32_e32 v51, v17
	v_pk_mul_f32 v[42:43], v[42:43], v[50:51]
	v_pk_mul_f32 v[16:17], v[36:37], v[16:17]
	v_add_f32_e32 v42, v42, v43
	v_pk_fma_f32 v[8:9], v[8:9], v[34:35], v[16:17] neg_lo:[0,0,1] neg_hi:[0,0,1]
	v_cndmask_b32_e64 v42, v37, v42, s[38:39]
	v_cndmask_b32_e64 v43, v35, v9, s[38:39]
	v_cndmask_b32_e64 v50, v34, v8, s[38:39]
	ds_read_b128 v[34:37], v54 offset:22912
	ds_read_b128 v[54:57], v21 offset:256
	v_pk_mul_f32 v[8:9], v[58:59], v[32:33] op_sel_hi:[0,1]
	v_pk_mul_f32 v[16:17], v[58:59], v[30:31] op_sel_hi:[0,1]
	v_pk_mul_f32 v[16:17], v[16:17], v[48:49]
	s_waitcnt lgkmcnt(1)
	v_pk_mul_f32 v[8:9], v[8:9], v[36:37]
	v_mov_b32_e32 v31, v16
	v_mov_b32_e32 v30, v8
	v_mov_b32_e32 v32, v14
	s_waitcnt lgkmcnt(0)
	v_mov_b32_e32 v33, v56
	v_pk_mul_f32 v[30:31], v[30:31], v[32:33]
	v_mov_b32_e32 v32, v15
	v_add_f32_e32 v21, v30, v31
	v_mov_b32_e32 v30, v9
	v_mov_b32_e32 v31, v17
	v_mov_b32_e32 v33, v57
	v_pk_mul_f32 v[30:31], v[30:31], v[32:33]
	v_cndmask_b32_e64 v36, v8, v21, s[38:39]
	v_add_f32_e32 v21, v30, v31
	v_cndmask_b32_e64 v30, v9, v21, s[38:39]
	v_pk_mul_f32 v[8:9], v[8:9], v[56:57]
	s_add_u32 s4, s78, s14
	v_pk_fma_f32 v[8:9], v[14:15], v[16:17], v[8:9] neg_lo:[0,0,1] neg_hi:[0,0,1]
	v_pk_mul_f32 v[14:15], v[58:59], v[22:23] op_sel_hi:[0,1]
	v_cndmask_b32_e64 v31, v17, v9, s[38:39]
	v_cndmask_b32_e64 v32, v16, v8, s[38:39]
	v_pk_mul_f32 v[8:9], v[58:59], v[26:27] op_sel_hi:[0,1]
	v_pk_mul_f32 v[8:9], v[8:9], v[34:35]
	v_pk_mul_f32 v[14:15], v[14:15], v[46:47]
	v_mov_b32_e32 v16, v8
	v_mov_b32_e32 v17, v14
	v_mov_b32_e32 v22, v12
	v_mov_b32_e32 v23, v54
	v_pk_mul_f32 v[16:17], v[16:17], v[22:23]
	v_mov_b32_e32 v22, v13
	v_add_f32_e32 v16, v16, v17
	v_cndmask_b32_e64 v26, v8, v16, s[38:39]
	v_mov_b32_e32 v16, v9
	v_mov_b32_e32 v17, v15
	v_mov_b32_e32 v23, v55
	v_pk_mul_f32 v[16:17], v[16:17], v[22:23]
	v_mov_b32_e32 v23, v18
	v_add_f32_e32 v16, v16, v17
	v_cndmask_b32_e64 v27, v9, v16, s[38:39]
	v_pk_mul_f32 v[8:9], v[8:9], v[54:55]
	v_mov_b32_e32 v16, v10
	v_pk_fma_f32 v[8:9], v[12:13], v[14:15], v[8:9] neg_lo:[0,0,1] neg_hi:[0,0,1]
	v_pk_mul_f32 v[12:13], v[58:59], v[28:29] op_sel_hi:[0,1]
	v_cndmask_b32_e64 v33, v15, v9, s[38:39]
	v_cndmask_b32_e64 v34, v14, v8, s[38:39]
	v_pk_mul_f32 v[14:15], v[58:59], v[24:25] op_sel_hi:[0,1]
	v_pk_mul_f32 v[12:13], v[12:13], v[44:45]
	v_pk_mul_f32 v[14:15], v[14:15], v[52:53]
	v_mov_b32_e32 v22, v12
	v_mov_b32_e32 v17, v14
	v_pk_mul_f32 v[16:17], v[16:17], v[22:23]
	v_lshlrev_b32_e32 v8, 7, v59
	v_add_f32_e32 v9, v16, v17
	v_pk_mul_f32 v[16:17], v[12:13], v[18:19]
	v_mov_b32_e32 v18, v13
	v_pk_fma_f32 v[16:17], v[10:11], v[14:15], v[16:17] neg_lo:[0,0,1] neg_hi:[0,0,1]
	v_cndmask_b32_e64 v22, v12, v9, s[38:39]
	v_cndmask_b32_e64 v16, v14, v16, s[38:39]
	v_mov_b32_e32 v14, v11
	v_pk_mul_f32 v[10:11], v[14:15], v[18:19]
	s_addc_u32 s5, s79, s15
	v_add_f32_e32 v9, v10, v11
	v_cndmask_b32_e64 v14, v13, v9, s[38:39]
	v_ashrrev_i32_e32 v9, 31, v8
	v_lshl_add_u64 v[10:11], v[8:9], 1, s[4:5]
	s_mov_b64 s[4:5], 0x2bb9c000
	v_lshl_add_u64 v[10:11], v[10:11], 0, s[4:5]
	s_add_u32 s4, s78, s18
	v_add_u32_e32 v96, 0xfffffc00, v8
	s_addc_u32 s5, s79, s19
	v_lshl_add_u64 v[8:9], v[96:97], 1, s[4:5]
	s_mov_b64 s[4:5], 0x2dd9c000
	v_lshl_add_u64 v[8:9], v[8:9], 0, s[4:5]
	v_cndmask_b32_e32 v9, v9, v11, vcc
	v_cndmask_b32_e32 v8, v8, v10, vcc
	v_mov_b32_e32 v21, v97
	v_cndmask_b32_e64 v17, v15, v17, s[38:39]
	v_lshl_add_u64 v[8:9], v[8:9], 0, v[20:21]
	v_lshlrev_b32_e32 v96, 1, v135
	v_lshl_add_u64 v[12:13], v[8:9], 0, v[96:97]
	v_cvt_pk_bf16_f32 v8, v34, v33
	v_cvt_pk_bf16_f32 v9, v32, v31
	v_cvt_pk_bf16_f32 v10, v50, v43
	v_cvt_pk_bf16_f32 v11, v16, v17
	global_store_dwordx4 v[12:13], v[8:11], off sc1
	s_nop 1
	v_cvt_pk_bf16_f32 v8, v26, v27
	v_cvt_pk_bf16_f32 v9, v36, v30
	v_cvt_pk_bf16_f32 v10, v60, v42
	v_cvt_pk_bf16_f32 v11, v22, v14
	global_store_dwordx4 v[12:13], v[8:11], off offset:64 sc1
.LBB0_441:
	s_or_b64 exec, exec, s[2:3]
	s_waitcnt vmcnt(1)
	v_lshlrev_b32_e32 v16, 16, v0
	s_waitcnt lgkmcnt(0)
	v_and_b32_e32 v17, 0xffff0000, v0
	v_lshlrev_b32_e32 v12, 16, v4
	v_and_b32_e32 v13, 0xffff0000, v4
	v_pk_mul_f32 v[8:9], v[16:17], v[16:17]
	v_lshlrev_b32_e32 v24, 16, v1
	v_and_b32_e32 v25, 0xffff0000, v1
	v_pk_fma_f32 v[8:9], v[12:13], v[12:13], v[8:9]
	v_lshlrev_b32_e32 v22, 16, v5
	v_and_b32_e32 v23, 0xffff0000, v5
	v_pk_mul_f32 v[0:1], v[24:25], v[24:25]
	v_lshlrev_b32_e32 v26, 16, v6
	v_pk_fma_f32 v[0:1], v[22:23], v[22:23], v[0:1]
	v_and_b32_e32 v27, 0xffff0000, v6
	v_lshlrev_b32_e32 v28, 16, v2
	v_and_b32_e32 v29, 0xffff0000, v2
	v_add_f32_e32 v6, v8, v9
	v_pk_mul_f32 v[4:5], v[28:29], v[28:29]
	v_add_f32_e32 v0, v0, v6
	v_pk_fma_f32 v[4:5], v[26:27], v[26:27], v[4:5]
	v_lshlrev_b32_e32 v18, 16, v3
	v_and_b32_e32 v19, 0xffff0000, v3
	v_add_f32_e32 v0, v1, v0
	v_lshlrev_b32_e32 v14, 16, v7
	v_and_b32_e32 v15, 0xffff0000, v7
	v_pk_mul_f32 v[2:3], v[18:19], v[18:19]
	v_add_f32_e32 v0, v4, v0
	v_pk_fma_f32 v[2:3], v[14:15], v[14:15], v[2:3]
	v_add_f32_e32 v0, v5, v0
	v_add_f32_e32 v0, v2, v0
	v_add_f32_e32 v0, v3, v0
	ds_bpermute_b32 v1, v38, v0
	s_waitcnt lgkmcnt(0)
	v_add_f32_e32 v0, v0, v1
	ds_bpermute_b32 v1, v39, v0
	s_waitcnt lgkmcnt(0)
	v_add_f32_e32 v8, v0, v1
	ds_bpermute_b32 v9, v40, v8
	s_and_saveexec_b64 s[2:3], s[40:41]
	s_cbranch_execz .LBB0_367
	s_waitcnt lgkmcnt(0)
	v_add_f32_e32 v8, v8, v9
	v_fmamk_f32 v8, v8, 0x3c000000, v196
	v_cmp_gt_f32_e32 vcc, s35, v8
	v_mul_f32_e32 v9, 0x4b800000, v8
	v_ashrrev_i32_e32 v47, 3, v132
	v_cndmask_b32_e32 v8, v8, v9, vcc
	v_rsq_f32_e32 v8, v8
	v_lshlrev_b32_e32 v10, 2, v134
	v_add3_u32 v21, s16, v20, v10
	ds_read_b128 v[4:7], v21
	ds_read_b128 v[0:3], v21 offset:16
	v_mul_f32_e32 v9, 0x45800000, v8
	v_cndmask_b32_e32 v46, v8, v9, vcc
	v_cmp_gt_i32_e32 vcc, 8, v47
	v_mov_b32_e32 v8, 0x200
	v_pk_mul_f32 v[28:29], v[46:47], v[28:29] op_sel_hi:[0,1]
	v_cndmask_b32_e64 v8, v8, 0, vcc
	v_add_u32_e32 v8, 0, v8
	v_add3_u32 v42, v8, v41, v10
	ds_read_b128 v[30:33], v42 offset:22928
	ds_read_b128 v[34:37], v42 offset:22784
	ds_read_b128 v[38:41], v42 offset:22800
	ds_read_b128 v[8:11], v21 offset:272
	v_pk_mul_f32 v[26:27], v[46:47], v[26:27] op_sel_hi:[0,1]
	s_waitcnt lgkmcnt(3)
	v_pk_mul_f32 v[28:29], v[28:29], v[30:31]
	v_mov_b32_e32 v30, v0
	s_waitcnt lgkmcnt(1)
	v_pk_mul_f32 v[26:27], v[26:27], v[38:39]
	v_mov_b32_e32 v38, v28
	v_mov_b32_e32 v31, v26
	s_waitcnt lgkmcnt(0)
	v_mov_b32_e32 v39, v8
	v_pk_mul_f32 v[30:31], v[30:31], v[38:39]
	v_mov_b32_e32 v38, v29
	v_add_f32_e32 v30, v30, v31
	v_cndmask_b32_e64 v48, v28, v30, s[38:39]
	v_mov_b32_e32 v30, v1
	v_mov_b32_e32 v31, v27
	v_mov_b32_e32 v39, v9
	v_pk_mul_f32 v[30:31], v[30:31], v[38:39]
	v_pk_mul_f32 v[8:9], v[28:29], v[8:9]
	v_add_f32_e32 v30, v30, v31
	v_pk_fma_f32 v[0:1], v[0:1], v[26:27], v[8:9] neg_lo:[0,0,1] neg_hi:[0,0,1]
	v_cndmask_b32_e64 v30, v29, v30, s[38:39]
	v_cndmask_b32_e64 v31, v27, v1, s[38:39]
	v_cndmask_b32_e64 v38, v26, v0, s[38:39]
	ds_read_b128 v[26:29], v42 offset:22912
	ds_read_b128 v[42:45], v21 offset:256
	v_pk_mul_f32 v[0:1], v[46:47], v[24:25] op_sel_hi:[0,1]
	v_pk_mul_f32 v[8:9], v[46:47], v[22:23] op_sel_hi:[0,1]
	v_pk_mul_f32 v[8:9], v[8:9], v[36:37]
	s_waitcnt lgkmcnt(1)
	v_pk_mul_f32 v[0:1], v[0:1], v[28:29]
	v_mov_b32_e32 v23, v8
	v_mov_b32_e32 v22, v0
	v_mov_b32_e32 v24, v6
	s_waitcnt lgkmcnt(0)
	v_mov_b32_e32 v25, v44
	v_pk_mul_f32 v[22:23], v[22:23], v[24:25]
	v_mov_b32_e32 v24, v7
	v_add_f32_e32 v21, v22, v23
	v_mov_b32_e32 v22, v1
	v_mov_b32_e32 v23, v9
	v_mov_b32_e32 v25, v45
	v_pk_mul_f32 v[22:23], v[22:23], v[24:25]
	v_cndmask_b32_e64 v28, v0, v21, s[38:39]
	v_add_f32_e32 v21, v22, v23
	v_cndmask_b32_e64 v22, v1, v21, s[38:39]
	v_pk_mul_f32 v[0:1], v[0:1], v[44:45]
	s_add_u32 s4, s78, s14
	v_pk_fma_f32 v[0:1], v[6:7], v[8:9], v[0:1] neg_lo:[0,0,1] neg_hi:[0,0,1]
	v_pk_mul_f32 v[6:7], v[46:47], v[12:13] op_sel_hi:[0,1]
	v_cndmask_b32_e64 v23, v9, v1, s[38:39]
	v_cndmask_b32_e64 v24, v8, v0, s[38:39]
	v_pk_mul_f32 v[0:1], v[46:47], v[16:17] op_sel_hi:[0,1]
	v_pk_mul_f32 v[0:1], v[0:1], v[26:27]
	v_pk_mul_f32 v[6:7], v[6:7], v[34:35]
	v_mov_b32_e32 v8, v0
	v_mov_b32_e32 v9, v6
	v_mov_b32_e32 v12, v4
	v_mov_b32_e32 v13, v42
	v_pk_mul_f32 v[8:9], v[8:9], v[12:13]
	v_mov_b32_e32 v12, v5
	v_add_f32_e32 v8, v8, v9
	v_cndmask_b32_e64 v16, v0, v8, s[38:39]
	v_mov_b32_e32 v8, v1
	v_mov_b32_e32 v9, v7
	v_mov_b32_e32 v13, v43
	v_pk_mul_f32 v[8:9], v[8:9], v[12:13]
	v_mov_b32_e32 v13, v10
	v_add_f32_e32 v8, v8, v9
	v_cndmask_b32_e64 v17, v1, v8, s[38:39]
	v_pk_mul_f32 v[0:1], v[0:1], v[42:43]
	v_mov_b32_e32 v8, v2
	v_pk_fma_f32 v[0:1], v[4:5], v[6:7], v[0:1] neg_lo:[0,0,1] neg_hi:[0,0,1]
	v_pk_mul_f32 v[4:5], v[46:47], v[18:19] op_sel_hi:[0,1]
	v_cndmask_b32_e64 v25, v7, v1, s[38:39]
	v_cndmask_b32_e64 v26, v6, v0, s[38:39]
	v_pk_mul_f32 v[6:7], v[46:47], v[14:15] op_sel_hi:[0,1]
	v_pk_mul_f32 v[4:5], v[4:5], v[32:33]
	v_pk_mul_f32 v[6:7], v[6:7], v[40:41]
	v_mov_b32_e32 v12, v4
	v_mov_b32_e32 v9, v6
	v_pk_mul_f32 v[8:9], v[8:9], v[12:13]
	v_lshlrev_b32_e32 v0, 7, v47
	v_add_f32_e32 v1, v8, v9
	v_pk_mul_f32 v[8:9], v[4:5], v[10:11]
	v_mov_b32_e32 v10, v5
	v_pk_fma_f32 v[8:9], v[2:3], v[6:7], v[8:9] neg_lo:[0,0,1] neg_hi:[0,0,1]
	v_cndmask_b32_e64 v12, v4, v1, s[38:39]
	v_cndmask_b32_e64 v8, v6, v8, s[38:39]
	v_mov_b32_e32 v6, v3
	v_pk_mul_f32 v[2:3], v[6:7], v[10:11]
	s_addc_u32 s5, s79, s15
	v_add_f32_e32 v1, v2, v3
	v_cndmask_b32_e64 v6, v5, v1, s[38:39]
	v_ashrrev_i32_e32 v1, 31, v0
	v_lshl_add_u64 v[2:3], v[0:1], 1, s[4:5]
	s_mov_b64 s[4:5], 0x2bb9c000
	v_lshl_add_u64 v[2:3], v[2:3], 0, s[4:5]
	s_add_u32 s4, s78, s18
	v_add_u32_e32 v96, 0xfffffc00, v0
	s_addc_u32 s5, s79, s19
	v_lshl_add_u64 v[0:1], v[96:97], 1, s[4:5]
	s_mov_b64 s[4:5], 0x2dd9c000
	v_lshl_add_u64 v[0:1], v[0:1], 0, s[4:5]
	v_cndmask_b32_e32 v1, v1, v3, vcc
	v_cndmask_b32_e32 v0, v0, v2, vcc
	v_mov_b32_e32 v21, v97
	v_cndmask_b32_e64 v9, v7, v9, s[38:39]
	v_lshl_add_u64 v[0:1], v[0:1], 0, v[20:21]
	v_lshlrev_b32_e32 v96, 1, v134
	v_lshl_add_u64 v[4:5], v[0:1], 0, v[96:97]
	v_cvt_pk_bf16_f32 v0, v26, v25
	v_cvt_pk_bf16_f32 v1, v24, v23
	v_cvt_pk_bf16_f32 v2, v38, v31
	v_cvt_pk_bf16_f32 v3, v8, v9
	global_store_dwordx4 v[4:5], v[0:3], off sc1
	s_nop 1
	v_cvt_pk_bf16_f32 v0, v16, v17
	v_cvt_pk_bf16_f32 v1, v28, v22
	v_cvt_pk_bf16_f32 v2, v48, v30
	v_cvt_pk_bf16_f32 v3, v12, v6
	global_store_dwordx4 v[4:5], v[0:3], off offset:64 sc1
	s_branch .LBB0_367

.LBB0_445:
	s_or_b64 exec, exec, s[6:7]
	v_readlane_b32 s6, v253, 16
	v_readlane_b32 s7, v253, 17
	v_cvt_pk_bf16_f32 v0, v0, v1
	v_cvt_pk_bf16_f32 v1, v2, v3
	s_waitcnt lgkmcnt(0)
	v_lshl_add_u64 v[8:9], s[6:7], 0, v[8:9]
	v_readlane_b32 s6, v253, 8
	v_lshl_add_u64 v[8:9], v[66:67], 1, v[8:9]
	v_cvt_pk_bf16_f32 v2, v4, v5
	v_add_u32_e32 v69, s6, v69
	s_mov_b32 s6, 0x21ffff
	v_cmp_lt_i32_e32 vcc, s6, v69
	v_cvt_pk_bf16_f32 v3, v6, v7
	s_or_b64 s[4:5], vcc, s[4:5]
	global_store_dwordx4 v[8:9], v[0:3], off sc1
	s_andn2_b64 exec, exec, s[4:5]
	s_cbranch_execz .LBB0_458

.LBB0_1077:
	s_ashr_i32 s4, s16, 31
	s_lshr_b32 s4, s4, 23
	s_add_i32 s4, s16, s4
	s_ashr_i32 s6, s4, 9
	s_and_b32 s4, s4, 0xfe00
	s_sub_i32 s4, s16, s4
	s_sext_i32_i16 s5, s4
	s_bfe_u32 s5, s5, 0x4001b
	s_add_i32 s5, s4, s5
	s_sext_i32_i16 s7, s5
	s_and_b32 s5, s5, 0xfff0
	s_sub_i32 s4, s4, s5
	s_sext_i32_i16 s18, s4
	s_lshl_b32 s4, s7, 2
	s_ashr_i32 s7, s6, 31
	s_andn2_b32 s4, s4, 63
	s_lshl_b32 s12, s18, 6
	s_lshl_b64 s[6:7], s[6:7], 23
	s_waitcnt lgkmcnt(0)
	s_add_u32 s13, s2, s6
	s_addc_u32 s19, s3, s7
	s_ashr_i32 s5, s4, 31
	s_lshl_b64 s[20:21], s[4:5], 12
	s_add_u32 s22, s13, s20
	s_addc_u32 s19, s19, s21
	s_ashr_i32 s13, s12, 31
	s_lshl_b64 s[20:21], s[12:13], 2
	s_add_u32 s20, s22, s20
	s_addc_u32 s21, s19, s21
	v_lshl_add_u64 v[0:1], s[20:21], 0, v[96:97]
	v_lshl_add_u64 v[2:3], v[0:1], 0, v[60:61]
	flat_load_dwordx4 v[116:119], v[2:3] nt
	v_lshl_add_u64 v[2:3], v[0:1], 0, v[62:63]
	flat_load_dwordx4 v[56:59], v[2:3] nt
	v_lshl_add_u64 v[2:3], v[0:1], 0, v[64:65]
	flat_load_dwordx4 v[52:55], v[2:3] nt
	v_lshl_add_u64 v[2:3], v[0:1], 0, v[66:67]
	flat_load_dwordx4 v[48:51], v[2:3] nt
	v_lshl_add_u64 v[2:3], v[0:1], 0, v[68:69]
	flat_load_dwordx4 v[44:47], v[2:3] nt
	v_lshl_add_u64 v[2:3], v[0:1], 0, v[70:71]
	flat_load_dwordx4 v[40:43], v[2:3] nt
	v_lshl_add_u64 v[2:3], v[0:1], 0, v[72:73]
	flat_load_dwordx4 v[36:39], v[2:3] nt
	v_lshl_add_u64 v[2:3], v[0:1], 0, v[74:75]
	flat_load_dwordx4 v[32:35], v[2:3] nt
	v_lshl_add_u64 v[2:3], v[0:1], 0, v[76:77]
	flat_load_dwordx4 v[28:31], v[2:3] nt
	v_lshl_add_u64 v[2:3], v[0:1], 0, v[78:79]
	flat_load_dwordx4 v[24:27], v[2:3] nt
	v_lshl_add_u64 v[2:3], v[0:1], 0, v[80:81]
	flat_load_dwordx4 v[20:23], v[2:3] nt
	v_lshl_add_u64 v[2:3], v[0:1], 0, v[82:83]
	flat_load_dwordx4 v[16:19], v[2:3] nt
	v_lshl_add_u64 v[2:3], v[0:1], 0, v[84:85]
	flat_load_dwordx4 v[12:15], v[2:3] nt
	v_lshl_add_u64 v[2:3], v[0:1], 0, v[86:87]
	flat_load_dwordx4 v[8:11], v[2:3] nt
	v_lshl_add_u64 v[2:3], v[0:1], 0, v[88:89]
	flat_load_dwordx4 v[4:7], v[2:3] nt
	v_lshl_add_u64 v[0:1], v[0:1], 0, v[90:91]
	flat_load_dwordx4 v[0:3], v[0:1] nt
	v_add_u32_e32 v111, 0x410, v114
	s_lshl_b32 s13, s18, 7
	s_and_b32 s13, s13, 0xffffff00
	s_and_b32 s12, s12, 64
	s_or_b32 s12, s13, s12
	s_ashr_i32 s13, s12, 31
	s_add_u32 s18, s23, s6
	s_addc_u32 s19, s24, s7
	s_lshl_b64 s[6:7], s[12:13], 12
	s_add_u32 s6, s18, s6
	s_addc_u32 s7, s19, s7
	s_lshl_b64 s[4:5], s[4:5], 1
	s_add_u32 s4, s6, s4
	s_addc_u32 s5, s7, s5
	s_add_i32 s16, s16, s80
	s_cmpk_lt_i32 s16, 0x2000
	s_waitcnt vmcnt(0) lgkmcnt(0)
	ds_write2_b32 v114, v116, v117 offset1:1
	ds_write2_b32 v114, v118, v119 offset0:2 offset1:3
	ds_write2_b32 v111, v56, v57 offset1:1
	v_add_u32_e32 v56, 0x418, v114
	ds_write2_b32 v56, v58, v59 offset1:1
	v_add_u32_e32 v56, 0x820, v114
	ds_write2_b32 v56, v52, v53 offset1:1
	v_add_u32_e32 v52, 0x828, v114
	ds_write2_b32 v52, v54, v55 offset1:1
	v_add_u32_e32 v52, 0xc30, v114
	ds_write2_b32 v52, v48, v49 offset1:1
	v_add_u32_e32 v48, 0xc38, v114
	ds_write2_b32 v48, v50, v51 offset1:1
	v_add_u32_e32 v48, 0x1040, v114
	ds_write2_b32 v48, v44, v45 offset1:1
	v_add_u32_e32 v44, 0x1048, v114
	ds_write2_b32 v44, v46, v47 offset1:1
	v_add_u32_e32 v44, 0x1450, v114
	ds_write2_b32 v44, v40, v41 offset1:1
	v_add_u32_e32 v40, 0x1458, v114
	ds_write2_b32 v40, v42, v43 offset1:1
	v_add_u32_e32 v40, 0x1860, v114
	ds_write2_b32 v40, v36, v37 offset1:1
	v_add_u32_e32 v36, 0x1868, v114
	ds_write2_b32 v36, v38, v39 offset1:1
	v_add_u32_e32 v36, 0x1c70, v114
	ds_write2_b32 v36, v32, v33 offset1:1
	v_add_u32_e32 v32, 0x1c78, v114
	ds_write2_b32 v32, v34, v35 offset1:1
	v_add_u32_e32 v32, 0x2080, v114
	ds_write2_b32 v32, v28, v29 offset1:1
	v_add_u32_e32 v28, 0x2088, v114
	ds_write2_b32 v28, v30, v31 offset1:1
	v_add_u32_e32 v28, 0x2490, v114
	ds_write2_b32 v28, v24, v25 offset1:1
	v_add_u32_e32 v24, 0x2498, v114
	ds_write2_b32 v24, v26, v27 offset1:1
	v_add_u32_e32 v24, 0x28a0, v114
	ds_write2_b32 v24, v20, v21 offset1:1
	v_add_u32_e32 v20, 0x28a8, v114
	ds_write2_b32 v20, v22, v23 offset1:1
	v_add_u32_e32 v20, 0x2cb0, v114
	ds_write2_b32 v20, v16, v17 offset1:1
	v_add_u32_e32 v16, 0x2cb8, v114
	ds_write2_b32 v16, v18, v19 offset1:1
	v_add_u32_e32 v16, 0x30c0, v114
	ds_write2_b32 v16, v12, v13 offset1:1
	v_add_u32_e32 v12, 0x30c8, v114
	ds_write2_b32 v12, v14, v15 offset1:1
	v_add_u32_e32 v12, 0x34d0, v114
	ds_write2_b32 v12, v8, v9 offset1:1
	v_add_u32_e32 v8, 0x34d8, v114
	ds_write2_b32 v8, v10, v11 offset1:1
	v_add_u32_e32 v8, 0x38e0, v114
	ds_write2_b32 v8, v4, v5 offset1:1
	v_add_u32_e32 v4, 0x38e8, v114
	ds_write2_b32 v4, v6, v7 offset1:1
	v_add_u32_e32 v4, 0x3cf0, v114
	ds_write2_b32 v4, v0, v1 offset1:1
	v_add_u32_e32 v0, 0x3cf8, v114
	ds_write2_b32 v0, v2, v3 offset1:1
	s_waitcnt lgkmcnt(0)
	ds_read2_b32 v[6:7], v113 offset0:65 offset1:73
	ds_read2_b32 v[8:9], v113 offset1:8
	ds_read2_b32 v[10:11], v113 offset0:130 offset1:138
	ds_read2_b32 v[12:13], v113 offset0:195 offset1:203
	v_mov_b32_e32 v111, v97
	v_lshl_add_u64 v[4:5], s[4:5], 0, v[110:111]
	v_lshl_add_u64 v[22:23], v[4:5], 0, v[92:93]
	s_waitcnt lgkmcnt(2)
	v_cvt_pk_bf16_f32 v0, v8, v6
	v_add_u32_e32 v6, 0x400, v113
	ds_read2_b32 v[14:15], v6 offset0:4 offset1:12
	ds_read2_b32 v[16:17], v6 offset0:69 offset1:77
	ds_read2_b32 v[18:19], v6 offset0:134 offset1:142
	ds_read2_b32 v[20:21], v6 offset0:199 offset1:207
	s_waitcnt lgkmcnt(4)
	v_cvt_pk_bf16_f32 v1, v10, v12
	v_lshl_add_u64 v[24:25], v[4:5], 0, v[98:99]
	s_waitcnt lgkmcnt(2)
	v_cvt_pk_bf16_f32 v2, v14, v16
	s_waitcnt lgkmcnt(0)
	v_cvt_pk_bf16_f32 v3, v18, v20
	global_store_dwordx4 v[22:23], v[0:3], off sc1
	s_nop 1
	v_cvt_pk_bf16_f32 v0, v9, v7
	v_cvt_pk_bf16_f32 v1, v11, v13
	v_cvt_pk_bf16_f32 v2, v15, v17
	v_cvt_pk_bf16_f32 v3, v19, v21
	v_lshl_add_u64 v[8:9], v[4:5], 0, v[94:95]
	global_store_dwordx4 v[8:9], v[0:3], off sc1
	ds_read2_b32 v[8:9], v113 offset0:81 offset1:89
	ds_read2_b32 v[10:11], v113 offset0:16 offset1:24
	ds_read2_b32 v[12:13], v113 offset0:146 offset1:154
	ds_read2_b32 v[14:15], v113 offset0:211 offset1:219
	ds_read2_b32 v[16:17], v6 offset0:20 offset1:28
	ds_read2_b32 v[18:19], v6 offset0:85 offset1:93
	ds_read2_b32 v[20:21], v6 offset0:150 offset1:158
	ds_read2_b32 v[22:23], v6 offset0:215 offset1:223
	s_waitcnt lgkmcnt(6)
	v_cvt_pk_bf16_f32 v0, v10, v8
	s_waitcnt lgkmcnt(4)
	v_cvt_pk_bf16_f32 v1, v12, v14
	s_waitcnt lgkmcnt(2)
	v_cvt_pk_bf16_f32 v2, v16, v18
	s_waitcnt lgkmcnt(0)
	v_cvt_pk_bf16_f32 v3, v20, v22
	global_store_dwordx4 v[24:25], v[0:3], off sc1
	v_lshl_add_u64 v[24:25], v[4:5], 0, v[102:103]
	s_nop 0
	v_cvt_pk_bf16_f32 v0, v11, v9
	v_cvt_pk_bf16_f32 v1, v13, v15
	v_cvt_pk_bf16_f32 v2, v17, v19
	v_cvt_pk_bf16_f32 v3, v21, v23
	v_lshl_add_u64 v[8:9], v[4:5], 0, v[100:101]
	global_store_dwordx4 v[8:9], v[0:3], off sc1
	ds_read2_b32 v[8:9], v113 offset0:32 offset1:40
	ds_read2_b32 v[10:11], v113 offset0:97 offset1:105
	ds_read2_b32 v[12:13], v113 offset0:162 offset1:170
	ds_read2_b32 v[14:15], v113 offset0:227 offset1:235
	ds_read2_b32 v[16:17], v6 offset0:36 offset1:44
	ds_read2_b32 v[18:19], v6 offset0:101 offset1:109
	ds_read2_b32 v[20:21], v6 offset0:166 offset1:174
	ds_read2_b32 v[22:23], v6 offset0:231 offset1:239
	s_waitcnt lgkmcnt(6)
	v_cvt_pk_bf16_f32 v0, v8, v10
	s_waitcnt lgkmcnt(4)
	v_cvt_pk_bf16_f32 v1, v12, v14
	s_waitcnt lgkmcnt(2)
	v_cvt_pk_bf16_f32 v2, v16, v18
	s_waitcnt lgkmcnt(0)
	v_cvt_pk_bf16_f32 v3, v20, v22
	global_store_dwordx4 v[24:25], v[0:3], off sc1
	s_nop 1
	v_cvt_pk_bf16_f32 v0, v9, v11
	v_cvt_pk_bf16_f32 v1, v13, v15
	v_cvt_pk_bf16_f32 v2, v17, v19
	v_cvt_pk_bf16_f32 v3, v21, v23
	v_lshl_add_u64 v[8:9], v[4:5], 0, v[104:105]
	global_store_dwordx4 v[8:9], v[0:3], off sc1
	ds_read2_b32 v[8:9], v113 offset0:48 offset1:56
	ds_read2_b32 v[10:11], v113 offset0:113 offset1:121
	ds_read2_b32 v[12:13], v113 offset0:178 offset1:186
	ds_read2_b32 v[14:15], v113 offset0:243 offset1:251
	ds_read2_b32 v[16:17], v6 offset0:52 offset1:60
	ds_read2_b32 v[18:19], v6 offset0:117 offset1:125
	ds_read2_b32 v[20:21], v6 offset0:182 offset1:190
	ds_read2_b32 v[6:7], v6 offset0:247 offset1:255
	v_lshl_add_u64 v[22:23], v[4:5], 0, v[106:107]
	s_waitcnt lgkmcnt(6)
	v_cvt_pk_bf16_f32 v0, v8, v10
	s_waitcnt lgkmcnt(4)
	v_cvt_pk_bf16_f32 v1, v12, v14
	s_waitcnt lgkmcnt(2)
	v_cvt_pk_bf16_f32 v2, v16, v18
	s_waitcnt lgkmcnt(0)
	v_cvt_pk_bf16_f32 v3, v20, v6
	global_store_dwordx4 v[22:23], v[0:3], off sc1
	v_lshl_add_u64 v[4:5], v[4:5], 0, v[108:109]
	s_nop 0
	v_cvt_pk_bf16_f32 v0, v9, v11
	v_cvt_pk_bf16_f32 v1, v13, v15
	v_cvt_pk_bf16_f32 v2, v17, v19
	v_cvt_pk_bf16_f32 v3, v21, v7
	global_store_dwordx4 v[4:5], v[0:3], off sc1
	s_waitcnt lgkmcnt(0)
	s_cbranch_scc1 .LBB0_1077

.LBB0_1080:
	s_ashr_i32 s4, s14, 31
	s_lshr_b32 s4, s4, 23
	s_add_i32 s4, s14, s4
	s_ashr_i32 s6, s4, 9
	s_and_b32 s4, s4, 0xfe00
	s_sub_i32 s4, s14, s4
	s_sext_i32_i16 s5, s4
	s_bfe_u32 s5, s5, 0x4001b
	s_add_i32 s5, s4, s5
	s_sext_i32_i16 s7, s5
	s_and_b32 s5, s5, 0xfff0
	s_sub_i32 s4, s4, s5
	s_sext_i32_i16 s15, s4
	s_lshl_b32 s4, s7, 2
	s_ashr_i32 s7, s6, 31
	s_andn2_b32 s4, s4, 63
	s_lshl_b32 s12, s15, 6
	s_lshl_b64 s[6:7], s[6:7], 23
	s_waitcnt lgkmcnt(0)
	s_add_u32 s13, s2, s6
	s_addc_u32 s16, s3, s7
	s_ashr_i32 s5, s4, 31
	s_lshl_b64 s[18:19], s[4:5], 12
	s_add_u32 s20, s13, s18
	s_addc_u32 s16, s16, s19
	s_ashr_i32 s13, s12, 31
	s_lshl_b64 s[18:19], s[12:13], 2
	s_add_u32 s18, s20, s18
	s_addc_u32 s19, s16, s19
	v_lshl_add_u64 v[0:1], s[18:19], 0, v[96:97]
	v_lshl_add_u64 v[2:3], v[0:1], 0, v[60:61]
	flat_load_dwordx4 v[114:117], v[2:3] nt
	v_lshl_add_u64 v[2:3], v[0:1], 0, v[62:63]
	flat_load_dwordx4 v[56:59], v[2:3] nt
	v_lshl_add_u64 v[2:3], v[0:1], 0, v[64:65]
	flat_load_dwordx4 v[52:55], v[2:3] nt
	v_lshl_add_u64 v[2:3], v[0:1], 0, v[66:67]
	flat_load_dwordx4 v[48:51], v[2:3] nt
	v_lshl_add_u64 v[2:3], v[0:1], 0, v[68:69]
	flat_load_dwordx4 v[44:47], v[2:3] nt
	v_lshl_add_u64 v[2:3], v[0:1], 0, v[70:71]
	flat_load_dwordx4 v[40:43], v[2:3] nt
	v_lshl_add_u64 v[2:3], v[0:1], 0, v[72:73]
	flat_load_dwordx4 v[36:39], v[2:3] nt
	v_lshl_add_u64 v[2:3], v[0:1], 0, v[74:75]
	flat_load_dwordx4 v[32:35], v[2:3] nt
	v_lshl_add_u64 v[2:3], v[0:1], 0, v[76:77]
	flat_load_dwordx4 v[28:31], v[2:3] nt
	v_lshl_add_u64 v[2:3], v[0:1], 0, v[78:79]
	flat_load_dwordx4 v[24:27], v[2:3] nt
	v_lshl_add_u64 v[2:3], v[0:1], 0, v[80:81]
	flat_load_dwordx4 v[20:23], v[2:3] nt
	v_lshl_add_u64 v[2:3], v[0:1], 0, v[82:83]
	flat_load_dwordx4 v[16:19], v[2:3] nt
	v_lshl_add_u64 v[2:3], v[0:1], 0, v[84:85]
	flat_load_dwordx4 v[12:15], v[2:3] nt
	v_lshl_add_u64 v[2:3], v[0:1], 0, v[86:87]
	flat_load_dwordx4 v[8:11], v[2:3] nt
	v_lshl_add_u64 v[2:3], v[0:1], 0, v[88:89]
	flat_load_dwordx4 v[4:7], v[2:3] nt
	v_lshl_add_u64 v[0:1], v[0:1], 0, v[90:91]
	flat_load_dwordx4 v[0:3], v[0:1] nt
	v_add_u32_e32 v111, 0x410, v113
	s_lshl_b32 s13, s15, 7
	s_and_b32 s12, s12, 64
	s_or_b32 s12, s12, s13
	s_bitset1_b32 s12, 7
	s_ashr_i32 s13, s12, 31
	s_add_u32 s15, s23, s6
	s_addc_u32 s16, s24, s7
	s_lshl_b64 s[6:7], s[12:13], 12
	s_add_u32 s6, s15, s6
	s_addc_u32 s7, s16, s7
	s_lshl_b64 s[4:5], s[4:5], 1
	s_add_u32 s4, s6, s4
	s_addc_u32 s5, s7, s5
	s_add_i32 s14, s14, s80
	s_cmpk_lt_i32 s14, 0x1000
	s_waitcnt vmcnt(0) lgkmcnt(0)
	ds_write2_b32 v113, v114, v115 offset1:1
	ds_write2_b32 v113, v116, v117 offset0:2 offset1:3
	ds_write2_b32 v111, v56, v57 offset1:1
	v_add_u32_e32 v56, 0x418, v113
	ds_write2_b32 v56, v58, v59 offset1:1
	v_add_u32_e32 v56, 0x820, v113
	ds_write2_b32 v56, v52, v53 offset1:1
	v_add_u32_e32 v52, 0x828, v113
	ds_write2_b32 v52, v54, v55 offset1:1
	v_add_u32_e32 v52, 0xc30, v113
	ds_write2_b32 v52, v48, v49 offset1:1
	v_add_u32_e32 v48, 0xc38, v113
	ds_write2_b32 v48, v50, v51 offset1:1
	v_add_u32_e32 v48, 0x1040, v113
	ds_write2_b32 v48, v44, v45 offset1:1
	v_add_u32_e32 v44, 0x1048, v113
	ds_write2_b32 v44, v46, v47 offset1:1
	v_add_u32_e32 v44, 0x1450, v113
	ds_write2_b32 v44, v40, v41 offset1:1
	v_add_u32_e32 v40, 0x1458, v113
	ds_write2_b32 v40, v42, v43 offset1:1
	v_add_u32_e32 v40, 0x1860, v113
	ds_write2_b32 v40, v36, v37 offset1:1
	v_add_u32_e32 v36, 0x1868, v113
	ds_write2_b32 v36, v38, v39 offset1:1
	v_add_u32_e32 v36, 0x1c70, v113
	ds_write2_b32 v36, v32, v33 offset1:1
	v_add_u32_e32 v32, 0x1c78, v113
	ds_write2_b32 v32, v34, v35 offset1:1
	v_add_u32_e32 v32, 0x2080, v113
	ds_write2_b32 v32, v28, v29 offset1:1
	v_add_u32_e32 v28, 0x2088, v113
	ds_write2_b32 v28, v30, v31 offset1:1
	v_add_u32_e32 v28, 0x2490, v113
	ds_write2_b32 v28, v24, v25 offset1:1
	v_add_u32_e32 v24, 0x2498, v113
	ds_write2_b32 v24, v26, v27 offset1:1
	v_add_u32_e32 v24, 0x28a0, v113
	ds_write2_b32 v24, v20, v21 offset1:1
	v_add_u32_e32 v20, 0x28a8, v113
	ds_write2_b32 v20, v22, v23 offset1:1
	v_add_u32_e32 v20, 0x2cb0, v113
	ds_write2_b32 v20, v16, v17 offset1:1
	v_add_u32_e32 v16, 0x2cb8, v113
	ds_write2_b32 v16, v18, v19 offset1:1
	v_add_u32_e32 v16, 0x30c0, v113
	ds_write2_b32 v16, v12, v13 offset1:1
	v_add_u32_e32 v12, 0x30c8, v113
	ds_write2_b32 v12, v14, v15 offset1:1
	v_add_u32_e32 v12, 0x34d0, v113
	ds_write2_b32 v12, v8, v9 offset1:1
	v_add_u32_e32 v8, 0x34d8, v113
	ds_write2_b32 v8, v10, v11 offset1:1
	v_add_u32_e32 v8, 0x38e0, v113
	ds_write2_b32 v8, v4, v5 offset1:1
	v_add_u32_e32 v4, 0x38e8, v113
	ds_write2_b32 v4, v6, v7 offset1:1
	v_add_u32_e32 v4, 0x3cf0, v113
	ds_write2_b32 v4, v0, v1 offset1:1
	v_add_u32_e32 v0, 0x3cf8, v113
	ds_write2_b32 v0, v2, v3 offset1:1
	s_waitcnt lgkmcnt(0)
	ds_read2_b32 v[6:7], v112 offset0:65 offset1:73
	ds_read2_b32 v[8:9], v112 offset1:8
	ds_read2_b32 v[10:11], v112 offset0:130 offset1:138
	ds_read2_b32 v[12:13], v112 offset0:195 offset1:203
	v_mov_b32_e32 v111, v97
	v_lshl_add_u64 v[4:5], s[4:5], 0, v[110:111]
	v_lshl_add_u64 v[22:23], v[4:5], 0, v[92:93]
	s_waitcnt lgkmcnt(2)
	v_cvt_pk_bf16_f32 v0, v8, v6
	v_add_u32_e32 v6, 0x400, v112
	ds_read2_b32 v[14:15], v6 offset0:4 offset1:12
	ds_read2_b32 v[16:17], v6 offset0:69 offset1:77
	ds_read2_b32 v[18:19], v6 offset0:134 offset1:142
	ds_read2_b32 v[20:21], v6 offset0:199 offset1:207
	s_waitcnt lgkmcnt(4)
	v_cvt_pk_bf16_f32 v1, v10, v12
	v_lshl_add_u64 v[24:25], v[4:5], 0, v[98:99]
	s_waitcnt lgkmcnt(2)
	v_cvt_pk_bf16_f32 v2, v14, v16
	s_waitcnt lgkmcnt(0)
	v_cvt_pk_bf16_f32 v3, v18, v20
	global_store_dwordx4 v[22:23], v[0:3], off sc1
	s_nop 1
	v_cvt_pk_bf16_f32 v0, v9, v7
	v_cvt_pk_bf16_f32 v1, v11, v13
	v_cvt_pk_bf16_f32 v2, v15, v17
	v_cvt_pk_bf16_f32 v3, v19, v21
	v_lshl_add_u64 v[8:9], v[4:5], 0, v[94:95]
	global_store_dwordx4 v[8:9], v[0:3], off sc1
	ds_read2_b32 v[8:9], v112 offset0:81 offset1:89
	ds_read2_b32 v[10:11], v112 offset0:16 offset1:24
	ds_read2_b32 v[12:13], v112 offset0:146 offset1:154
	ds_read2_b32 v[14:15], v112 offset0:211 offset1:219
	ds_read2_b32 v[16:17], v6 offset0:20 offset1:28
	ds_read2_b32 v[18:19], v6 offset0:85 offset1:93
	ds_read2_b32 v[20:21], v6 offset0:150 offset1:158
	ds_read2_b32 v[22:23], v6 offset0:215 offset1:223
	s_waitcnt lgkmcnt(6)
	v_cvt_pk_bf16_f32 v0, v10, v8
	s_waitcnt lgkmcnt(4)
	v_cvt_pk_bf16_f32 v1, v12, v14
	s_waitcnt lgkmcnt(2)
	v_cvt_pk_bf16_f32 v2, v16, v18
	s_waitcnt lgkmcnt(0)
	v_cvt_pk_bf16_f32 v3, v20, v22
	global_store_dwordx4 v[24:25], v[0:3], off sc1
	v_lshl_add_u64 v[24:25], v[4:5], 0, v[102:103]
	s_nop 0
	v_cvt_pk_bf16_f32 v0, v11, v9
	v_cvt_pk_bf16_f32 v1, v13, v15
	v_cvt_pk_bf16_f32 v2, v17, v19
	v_cvt_pk_bf16_f32 v3, v21, v23
	v_lshl_add_u64 v[8:9], v[4:5], 0, v[100:101]
	global_store_dwordx4 v[8:9], v[0:3], off sc1
	ds_read2_b32 v[8:9], v112 offset0:32 offset1:40
	ds_read2_b32 v[10:11], v112 offset0:97 offset1:105
	ds_read2_b32 v[12:13], v112 offset0:162 offset1:170
	ds_read2_b32 v[14:15], v112 offset0:227 offset1:235
	ds_read2_b32 v[16:17], v6 offset0:36 offset1:44
	ds_read2_b32 v[18:19], v6 offset0:101 offset1:109
	ds_read2_b32 v[20:21], v6 offset0:166 offset1:174
	ds_read2_b32 v[22:23], v6 offset0:231 offset1:239
	s_waitcnt lgkmcnt(6)
	v_cvt_pk_bf16_f32 v0, v8, v10
	s_waitcnt lgkmcnt(4)
	v_cvt_pk_bf16_f32 v1, v12, v14
	s_waitcnt lgkmcnt(2)
	v_cvt_pk_bf16_f32 v2, v16, v18
	s_waitcnt lgkmcnt(0)
	v_cvt_pk_bf16_f32 v3, v20, v22
	global_store_dwordx4 v[24:25], v[0:3], off sc1
	s_nop 1
	v_cvt_pk_bf16_f32 v0, v9, v11
	v_cvt_pk_bf16_f32 v1, v13, v15
	v_cvt_pk_bf16_f32 v2, v17, v19
	v_cvt_pk_bf16_f32 v3, v21, v23
	v_lshl_add_u64 v[8:9], v[4:5], 0, v[104:105]
	global_store_dwordx4 v[8:9], v[0:3], off sc1
	ds_read2_b32 v[8:9], v112 offset0:48 offset1:56
	ds_read2_b32 v[10:11], v112 offset0:113 offset1:121
	ds_read2_b32 v[12:13], v112 offset0:178 offset1:186
	ds_read2_b32 v[14:15], v112 offset0:243 offset1:251
	ds_read2_b32 v[16:17], v6 offset0:52 offset1:60
	ds_read2_b32 v[18:19], v6 offset0:117 offset1:125
	ds_read2_b32 v[20:21], v6 offset0:182 offset1:190
	ds_read2_b32 v[6:7], v6 offset0:247 offset1:255
	v_lshl_add_u64 v[22:23], v[4:5], 0, v[106:107]
	s_waitcnt lgkmcnt(6)
	v_cvt_pk_bf16_f32 v0, v8, v10
	s_waitcnt lgkmcnt(4)
	v_cvt_pk_bf16_f32 v1, v12, v14
	s_waitcnt lgkmcnt(2)
	v_cvt_pk_bf16_f32 v2, v16, v18
	s_waitcnt lgkmcnt(0)
	v_cvt_pk_bf16_f32 v3, v20, v6
	global_store_dwordx4 v[22:23], v[0:3], off sc1
	v_lshl_add_u64 v[4:5], v[4:5], 0, v[108:109]
	s_nop 0
	v_cvt_pk_bf16_f32 v0, v9, v11
	v_cvt_pk_bf16_f32 v1, v13, v15
	v_cvt_pk_bf16_f32 v2, v17, v19
	v_cvt_pk_bf16_f32 v3, v21, v7
	global_store_dwordx4 v[4:5], v[0:3], off sc1
	s_waitcnt lgkmcnt(0)
	s_cbranch_scc1 .LBB0_1080

.LBB0_1085:
	s_ashr_i32 s4, s16, 31
	s_lshr_b32 s4, s4, 23
	s_add_i32 s4, s16, s4
	s_ashr_i32 s6, s4, 9
	s_and_b32 s4, s4, 0xfe00
	s_sub_i32 s4, s16, s4
	s_sext_i32_i16 s5, s4
	s_bfe_u32 s5, s5, 0x4001b
	s_add_i32 s5, s4, s5
	s_sext_i32_i16 s7, s5
	s_and_b32 s5, s5, 0xfff0
	s_sub_i32 s4, s4, s5
	s_sext_i32_i16 s18, s4
	s_lshl_b32 s4, s7, 2
	s_ashr_i32 s7, s6, 31
	s_andn2_b32 s4, s4, 63
	s_lshl_b32 s12, s18, 6
	s_lshl_b64 s[6:7], s[6:7], 23
	s_waitcnt lgkmcnt(0)
	s_add_u32 s13, s2, s6
	s_addc_u32 s19, s3, s7
	s_ashr_i32 s5, s4, 31
	s_lshl_b64 s[20:21], s[4:5], 12
	s_add_u32 s22, s13, s20
	s_addc_u32 s19, s19, s21
	s_ashr_i32 s13, s12, 31
	s_lshl_b64 s[20:21], s[12:13], 2
	s_add_u32 s20, s22, s20
	s_addc_u32 s21, s19, s21
	v_lshl_add_u64 v[0:1], s[20:21], 0, v[96:97]
	v_lshl_add_u64 v[2:3], v[0:1], 0, v[60:61]
	flat_load_dwordx4 v[116:119], v[2:3] nt
	v_lshl_add_u64 v[2:3], v[0:1], 0, v[62:63]
	flat_load_dwordx4 v[56:59], v[2:3] nt
	v_lshl_add_u64 v[2:3], v[0:1], 0, v[64:65]
	flat_load_dwordx4 v[52:55], v[2:3] nt
	v_lshl_add_u64 v[2:3], v[0:1], 0, v[66:67]
	flat_load_dwordx4 v[48:51], v[2:3] nt
	v_lshl_add_u64 v[2:3], v[0:1], 0, v[68:69]
	flat_load_dwordx4 v[44:47], v[2:3] nt
	v_lshl_add_u64 v[2:3], v[0:1], 0, v[70:71]
	flat_load_dwordx4 v[40:43], v[2:3] nt
	v_lshl_add_u64 v[2:3], v[0:1], 0, v[72:73]
	flat_load_dwordx4 v[36:39], v[2:3] nt
	v_lshl_add_u64 v[2:3], v[0:1], 0, v[74:75]
	flat_load_dwordx4 v[32:35], v[2:3] nt
	v_lshl_add_u64 v[2:3], v[0:1], 0, v[76:77]
	flat_load_dwordx4 v[28:31], v[2:3] nt
	v_lshl_add_u64 v[2:3], v[0:1], 0, v[78:79]
	flat_load_dwordx4 v[24:27], v[2:3] nt
	v_lshl_add_u64 v[2:3], v[0:1], 0, v[80:81]
	flat_load_dwordx4 v[20:23], v[2:3] nt
	v_lshl_add_u64 v[2:3], v[0:1], 0, v[82:83]
	flat_load_dwordx4 v[16:19], v[2:3] nt
	v_lshl_add_u64 v[2:3], v[0:1], 0, v[84:85]
	flat_load_dwordx4 v[12:15], v[2:3] nt
	v_lshl_add_u64 v[2:3], v[0:1], 0, v[86:87]
	flat_load_dwordx4 v[8:11], v[2:3] nt
	v_lshl_add_u64 v[2:3], v[0:1], 0, v[88:89]
	flat_load_dwordx4 v[4:7], v[2:3] nt
	v_lshl_add_u64 v[0:1], v[0:1], 0, v[90:91]
	flat_load_dwordx4 v[0:3], v[0:1] nt
	v_add_u32_e32 v111, 0x410, v114
	s_lshl_b32 s13, s18, 7
	s_and_b32 s13, s13, 0xffffff00
	s_and_b32 s12, s12, 64
	s_or_b32 s12, s13, s12
	s_ashr_i32 s13, s12, 31
	s_add_u32 s18, s23, s6
	s_addc_u32 s19, s24, s7
	s_lshl_b64 s[6:7], s[12:13], 12
	s_add_u32 s6, s18, s6
	s_addc_u32 s7, s19, s7
	s_lshl_b64 s[4:5], s[4:5], 1
	s_add_u32 s4, s6, s4
	s_addc_u32 s5, s7, s5
	s_add_i32 s16, s16, s25
	s_cmpk_lt_i32 s16, 0x2000
	s_waitcnt vmcnt(0) lgkmcnt(0)
	ds_write2_b32 v114, v116, v117 offset1:1
	ds_write2_b32 v114, v118, v119 offset0:2 offset1:3
	ds_write2_b32 v111, v56, v57 offset1:1
	v_add_u32_e32 v56, 0x418, v114
	ds_write2_b32 v56, v58, v59 offset1:1
	v_add_u32_e32 v56, 0x820, v114
	ds_write2_b32 v56, v52, v53 offset1:1
	v_add_u32_e32 v52, 0x828, v114
	ds_write2_b32 v52, v54, v55 offset1:1
	v_add_u32_e32 v52, 0xc30, v114
	ds_write2_b32 v52, v48, v49 offset1:1
	v_add_u32_e32 v48, 0xc38, v114
	ds_write2_b32 v48, v50, v51 offset1:1
	v_add_u32_e32 v48, 0x1040, v114
	ds_write2_b32 v48, v44, v45 offset1:1
	v_add_u32_e32 v44, 0x1048, v114
	ds_write2_b32 v44, v46, v47 offset1:1
	v_add_u32_e32 v44, 0x1450, v114
	ds_write2_b32 v44, v40, v41 offset1:1
	v_add_u32_e32 v40, 0x1458, v114
	ds_write2_b32 v40, v42, v43 offset1:1
	v_add_u32_e32 v40, 0x1860, v114
	ds_write2_b32 v40, v36, v37 offset1:1
	v_add_u32_e32 v36, 0x1868, v114
	ds_write2_b32 v36, v38, v39 offset1:1
	v_add_u32_e32 v36, 0x1c70, v114
	ds_write2_b32 v36, v32, v33 offset1:1
	v_add_u32_e32 v32, 0x1c78, v114
	ds_write2_b32 v32, v34, v35 offset1:1
	v_add_u32_e32 v32, 0x2080, v114
	ds_write2_b32 v32, v28, v29 offset1:1
	v_add_u32_e32 v28, 0x2088, v114
	ds_write2_b32 v28, v30, v31 offset1:1
	v_add_u32_e32 v28, 0x2490, v114
	ds_write2_b32 v28, v24, v25 offset1:1
	v_add_u32_e32 v24, 0x2498, v114
	ds_write2_b32 v24, v26, v27 offset1:1
	v_add_u32_e32 v24, 0x28a0, v114
	ds_write2_b32 v24, v20, v21 offset1:1
	v_add_u32_e32 v20, 0x28a8, v114
	ds_write2_b32 v20, v22, v23 offset1:1
	v_add_u32_e32 v20, 0x2cb0, v114
	ds_write2_b32 v20, v16, v17 offset1:1
	v_add_u32_e32 v16, 0x2cb8, v114
	ds_write2_b32 v16, v18, v19 offset1:1
	v_add_u32_e32 v16, 0x30c0, v114
	ds_write2_b32 v16, v12, v13 offset1:1
	v_add_u32_e32 v12, 0x30c8, v114
	ds_write2_b32 v12, v14, v15 offset1:1
	v_add_u32_e32 v12, 0x34d0, v114
	ds_write2_b32 v12, v8, v9 offset1:1
	v_add_u32_e32 v8, 0x34d8, v114
	ds_write2_b32 v8, v10, v11 offset1:1
	v_add_u32_e32 v8, 0x38e0, v114
	ds_write2_b32 v8, v4, v5 offset1:1
	v_add_u32_e32 v4, 0x38e8, v114
	ds_write2_b32 v4, v6, v7 offset1:1
	v_add_u32_e32 v4, 0x3cf0, v114
	ds_write2_b32 v4, v0, v1 offset1:1
	v_add_u32_e32 v0, 0x3cf8, v114
	ds_write2_b32 v0, v2, v3 offset1:1
	s_waitcnt lgkmcnt(0)
	ds_read2_b32 v[6:7], v113 offset0:65 offset1:73
	ds_read2_b32 v[8:9], v113 offset1:8
	ds_read2_b32 v[10:11], v113 offset0:130 offset1:138
	ds_read2_b32 v[12:13], v113 offset0:195 offset1:203
	v_mov_b32_e32 v111, v97
	v_lshl_add_u64 v[4:5], s[4:5], 0, v[110:111]
	v_lshl_add_u64 v[22:23], v[4:5], 0, v[92:93]
	s_waitcnt lgkmcnt(2)
	v_cvt_pk_bf16_f32 v0, v8, v6
	v_add_u32_e32 v6, 0x400, v113
	ds_read2_b32 v[14:15], v6 offset0:4 offset1:12
	ds_read2_b32 v[16:17], v6 offset0:69 offset1:77
	ds_read2_b32 v[18:19], v6 offset0:134 offset1:142
	ds_read2_b32 v[20:21], v6 offset0:199 offset1:207
	s_waitcnt lgkmcnt(4)
	v_cvt_pk_bf16_f32 v1, v10, v12
	v_lshl_add_u64 v[24:25], v[4:5], 0, v[98:99]
	s_waitcnt lgkmcnt(2)
	v_cvt_pk_bf16_f32 v2, v14, v16
	s_waitcnt lgkmcnt(0)
	v_cvt_pk_bf16_f32 v3, v18, v20
	global_store_dwordx4 v[22:23], v[0:3], off sc1
	s_nop 1
	v_cvt_pk_bf16_f32 v0, v9, v7
	v_cvt_pk_bf16_f32 v1, v11, v13
	v_cvt_pk_bf16_f32 v2, v15, v17
	v_cvt_pk_bf16_f32 v3, v19, v21
	v_lshl_add_u64 v[8:9], v[4:5], 0, v[94:95]
	global_store_dwordx4 v[8:9], v[0:3], off sc1
	ds_read2_b32 v[8:9], v113 offset0:81 offset1:89
	ds_read2_b32 v[10:11], v113 offset0:16 offset1:24
	ds_read2_b32 v[12:13], v113 offset0:146 offset1:154
	ds_read2_b32 v[14:15], v113 offset0:211 offset1:219
	ds_read2_b32 v[16:17], v6 offset0:20 offset1:28
	ds_read2_b32 v[18:19], v6 offset0:85 offset1:93
	ds_read2_b32 v[20:21], v6 offset0:150 offset1:158
	ds_read2_b32 v[22:23], v6 offset0:215 offset1:223
	s_waitcnt lgkmcnt(6)
	v_cvt_pk_bf16_f32 v0, v10, v8
	s_waitcnt lgkmcnt(4)
	v_cvt_pk_bf16_f32 v1, v12, v14
	s_waitcnt lgkmcnt(2)
	v_cvt_pk_bf16_f32 v2, v16, v18
	s_waitcnt lgkmcnt(0)
	v_cvt_pk_bf16_f32 v3, v20, v22
	global_store_dwordx4 v[24:25], v[0:3], off sc1
	v_lshl_add_u64 v[24:25], v[4:5], 0, v[102:103]
	s_nop 0
	v_cvt_pk_bf16_f32 v0, v11, v9
	v_cvt_pk_bf16_f32 v1, v13, v15
	v_cvt_pk_bf16_f32 v2, v17, v19
	v_cvt_pk_bf16_f32 v3, v21, v23
	v_lshl_add_u64 v[8:9], v[4:5], 0, v[100:101]
	global_store_dwordx4 v[8:9], v[0:3], off sc1
	ds_read2_b32 v[8:9], v113 offset0:32 offset1:40
	ds_read2_b32 v[10:11], v113 offset0:97 offset1:105
	ds_read2_b32 v[12:13], v113 offset0:162 offset1:170
	ds_read2_b32 v[14:15], v113 offset0:227 offset1:235
	ds_read2_b32 v[16:17], v6 offset0:36 offset1:44
	ds_read2_b32 v[18:19], v6 offset0:101 offset1:109
	ds_read2_b32 v[20:21], v6 offset0:166 offset1:174
	ds_read2_b32 v[22:23], v6 offset0:231 offset1:239
	s_waitcnt lgkmcnt(6)
	v_cvt_pk_bf16_f32 v0, v8, v10
	s_waitcnt lgkmcnt(4)
	v_cvt_pk_bf16_f32 v1, v12, v14
	s_waitcnt lgkmcnt(2)
	v_cvt_pk_bf16_f32 v2, v16, v18
	s_waitcnt lgkmcnt(0)
	v_cvt_pk_bf16_f32 v3, v20, v22
	global_store_dwordx4 v[24:25], v[0:3], off sc1
	s_nop 1
	v_cvt_pk_bf16_f32 v0, v9, v11
	v_cvt_pk_bf16_f32 v1, v13, v15
	v_cvt_pk_bf16_f32 v2, v17, v19
	v_cvt_pk_bf16_f32 v3, v21, v23
	v_lshl_add_u64 v[8:9], v[4:5], 0, v[104:105]
	global_store_dwordx4 v[8:9], v[0:3], off sc1
	ds_read2_b32 v[8:9], v113 offset0:48 offset1:56
	ds_read2_b32 v[10:11], v113 offset0:113 offset1:121
	ds_read2_b32 v[12:13], v113 offset0:178 offset1:186
	ds_read2_b32 v[14:15], v113 offset0:243 offset1:251
	ds_read2_b32 v[16:17], v6 offset0:52 offset1:60
	ds_read2_b32 v[18:19], v6 offset0:117 offset1:125
	ds_read2_b32 v[20:21], v6 offset0:182 offset1:190
	ds_read2_b32 v[6:7], v6 offset0:247 offset1:255
	v_lshl_add_u64 v[22:23], v[4:5], 0, v[106:107]
	s_waitcnt lgkmcnt(6)
	v_cvt_pk_bf16_f32 v0, v8, v10
	s_waitcnt lgkmcnt(4)
	v_cvt_pk_bf16_f32 v1, v12, v14
	s_waitcnt lgkmcnt(2)
	v_cvt_pk_bf16_f32 v2, v16, v18
	s_waitcnt lgkmcnt(0)
	v_cvt_pk_bf16_f32 v3, v20, v6
	global_store_dwordx4 v[22:23], v[0:3], off sc1
	v_lshl_add_u64 v[4:5], v[4:5], 0, v[108:109]
	s_nop 0
	v_cvt_pk_bf16_f32 v0, v9, v11
	v_cvt_pk_bf16_f32 v1, v13, v15
	v_cvt_pk_bf16_f32 v2, v17, v19
	v_cvt_pk_bf16_f32 v3, v21, v7
	global_store_dwordx4 v[4:5], v[0:3], off sc1
	s_waitcnt lgkmcnt(0)
	s_cbranch_scc1 .LBB0_1085

.LBB0_1088:
	s_ashr_i32 s4, s14, 31
	s_lshr_b32 s4, s4, 23
	s_add_i32 s4, s14, s4
	s_ashr_i32 s6, s4, 9
	s_and_b32 s4, s4, 0xfe00
	s_sub_i32 s4, s14, s4
	s_sext_i32_i16 s5, s4
	s_bfe_u32 s5, s5, 0x4001b
	s_add_i32 s5, s4, s5
	s_sext_i32_i16 s7, s5
	s_and_b32 s5, s5, 0xfff0
	s_sub_i32 s4, s4, s5
	s_sext_i32_i16 s15, s4
	s_lshl_b32 s4, s7, 2
	s_ashr_i32 s7, s6, 31
	s_andn2_b32 s4, s4, 63
	s_lshl_b32 s12, s15, 6
	s_lshl_b64 s[6:7], s[6:7], 23
	s_waitcnt lgkmcnt(0)
	s_add_u32 s13, s2, s6
	s_addc_u32 s16, s3, s7
	s_ashr_i32 s5, s4, 31
	s_lshl_b64 s[18:19], s[4:5], 12
	s_add_u32 s20, s13, s18
	s_addc_u32 s16, s16, s19
	s_ashr_i32 s13, s12, 31
	s_lshl_b64 s[18:19], s[12:13], 2
	s_add_u32 s18, s20, s18
	s_addc_u32 s19, s16, s19
	v_lshl_add_u64 v[0:1], s[18:19], 0, v[96:97]
	v_lshl_add_u64 v[2:3], v[0:1], 0, v[60:61]
	flat_load_dwordx4 v[114:117], v[2:3] nt
	v_lshl_add_u64 v[2:3], v[0:1], 0, v[62:63]
	flat_load_dwordx4 v[56:59], v[2:3] nt
	v_lshl_add_u64 v[2:3], v[0:1], 0, v[64:65]
	flat_load_dwordx4 v[52:55], v[2:3] nt
	v_lshl_add_u64 v[2:3], v[0:1], 0, v[66:67]
	flat_load_dwordx4 v[48:51], v[2:3] nt
	v_lshl_add_u64 v[2:3], v[0:1], 0, v[68:69]
	flat_load_dwordx4 v[44:47], v[2:3] nt
	v_lshl_add_u64 v[2:3], v[0:1], 0, v[70:71]
	flat_load_dwordx4 v[40:43], v[2:3] nt
	v_lshl_add_u64 v[2:3], v[0:1], 0, v[72:73]
	flat_load_dwordx4 v[36:39], v[2:3] nt
	v_lshl_add_u64 v[2:3], v[0:1], 0, v[74:75]
	flat_load_dwordx4 v[32:35], v[2:3] nt
	v_lshl_add_u64 v[2:3], v[0:1], 0, v[76:77]
	flat_load_dwordx4 v[28:31], v[2:3] nt
	v_lshl_add_u64 v[2:3], v[0:1], 0, v[78:79]
	flat_load_dwordx4 v[24:27], v[2:3] nt
	v_lshl_add_u64 v[2:3], v[0:1], 0, v[80:81]
	flat_load_dwordx4 v[20:23], v[2:3] nt
	v_lshl_add_u64 v[2:3], v[0:1], 0, v[82:83]
	flat_load_dwordx4 v[16:19], v[2:3] nt
	v_lshl_add_u64 v[2:3], v[0:1], 0, v[84:85]
	flat_load_dwordx4 v[12:15], v[2:3] nt
	v_lshl_add_u64 v[2:3], v[0:1], 0, v[86:87]
	flat_load_dwordx4 v[8:11], v[2:3] nt
	v_lshl_add_u64 v[2:3], v[0:1], 0, v[88:89]
	flat_load_dwordx4 v[4:7], v[2:3] nt
	v_lshl_add_u64 v[0:1], v[0:1], 0, v[90:91]
	flat_load_dwordx4 v[0:3], v[0:1] nt
	v_add_u32_e32 v111, 0x410, v113
	s_lshl_b32 s13, s15, 7
	s_and_b32 s12, s12, 64
	s_or_b32 s12, s12, s13
	s_bitset1_b32 s12, 7
	s_ashr_i32 s13, s12, 31
	s_add_u32 s15, s21, s6
	s_addc_u32 s16, s22, s7
	s_lshl_b64 s[6:7], s[12:13], 12
	s_add_u32 s6, s15, s6
	s_addc_u32 s7, s16, s7
	s_lshl_b64 s[4:5], s[4:5], 1
	s_add_u32 s4, s6, s4
	s_addc_u32 s5, s7, s5
	s_add_i32 s14, s14, s23
	s_cmpk_gt_i32 s14, 0xfff
	s_waitcnt vmcnt(0) lgkmcnt(0)
	ds_write2_b32 v113, v114, v115 offset1:1
	ds_write2_b32 v113, v116, v117 offset0:2 offset1:3
	ds_write2_b32 v111, v56, v57 offset1:1
	v_add_u32_e32 v56, 0x418, v113
	ds_write2_b32 v56, v58, v59 offset1:1
	v_add_u32_e32 v56, 0x820, v113
	ds_write2_b32 v56, v52, v53 offset1:1
	v_add_u32_e32 v52, 0x828, v113
	ds_write2_b32 v52, v54, v55 offset1:1
	v_add_u32_e32 v52, 0xc30, v113
	ds_write2_b32 v52, v48, v49 offset1:1
	v_add_u32_e32 v48, 0xc38, v113
	ds_write2_b32 v48, v50, v51 offset1:1
	v_add_u32_e32 v48, 0x1040, v113
	ds_write2_b32 v48, v44, v45 offset1:1
	v_add_u32_e32 v44, 0x1048, v113
	ds_write2_b32 v44, v46, v47 offset1:1
	v_add_u32_e32 v44, 0x1450, v113
	ds_write2_b32 v44, v40, v41 offset1:1
	v_add_u32_e32 v40, 0x1458, v113
	ds_write2_b32 v40, v42, v43 offset1:1
	v_add_u32_e32 v40, 0x1860, v113
	ds_write2_b32 v40, v36, v37 offset1:1
	v_add_u32_e32 v36, 0x1868, v113
	ds_write2_b32 v36, v38, v39 offset1:1
	v_add_u32_e32 v36, 0x1c70, v113
	ds_write2_b32 v36, v32, v33 offset1:1
	v_add_u32_e32 v32, 0x1c78, v113
	ds_write2_b32 v32, v34, v35 offset1:1
	v_add_u32_e32 v32, 0x2080, v113
	ds_write2_b32 v32, v28, v29 offset1:1
	v_add_u32_e32 v28, 0x2088, v113
	ds_write2_b32 v28, v30, v31 offset1:1
	v_add_u32_e32 v28, 0x2490, v113
	ds_write2_b32 v28, v24, v25 offset1:1
	v_add_u32_e32 v24, 0x2498, v113
	ds_write2_b32 v24, v26, v27 offset1:1
	v_add_u32_e32 v24, 0x28a0, v113
	ds_write2_b32 v24, v20, v21 offset1:1
	v_add_u32_e32 v20, 0x28a8, v113
	ds_write2_b32 v20, v22, v23 offset1:1
	v_add_u32_e32 v20, 0x2cb0, v113
	ds_write2_b32 v20, v16, v17 offset1:1
	v_add_u32_e32 v16, 0x2cb8, v113
	ds_write2_b32 v16, v18, v19 offset1:1
	v_add_u32_e32 v16, 0x30c0, v113
	ds_write2_b32 v16, v12, v13 offset1:1
	v_add_u32_e32 v12, 0x30c8, v113
	ds_write2_b32 v12, v14, v15 offset1:1
	v_add_u32_e32 v12, 0x34d0, v113
	ds_write2_b32 v12, v8, v9 offset1:1
	v_add_u32_e32 v8, 0x34d8, v113
	ds_write2_b32 v8, v10, v11 offset1:1
	v_add_u32_e32 v8, 0x38e0, v113
	ds_write2_b32 v8, v4, v5 offset1:1
	v_add_u32_e32 v4, 0x38e8, v113
	ds_write2_b32 v4, v6, v7 offset1:1
	v_add_u32_e32 v4, 0x3cf0, v113
	ds_write2_b32 v4, v0, v1 offset1:1
	v_add_u32_e32 v0, 0x3cf8, v113
	ds_write2_b32 v0, v2, v3 offset1:1
	s_waitcnt lgkmcnt(0)
	ds_read2_b32 v[6:7], v112 offset0:65 offset1:73
	ds_read2_b32 v[8:9], v112 offset1:8
	ds_read2_b32 v[10:11], v112 offset0:130 offset1:138
	ds_read2_b32 v[12:13], v112 offset0:195 offset1:203
	v_mov_b32_e32 v111, v97
	v_lshl_add_u64 v[4:5], s[4:5], 0, v[110:111]
	v_lshl_add_u64 v[22:23], v[4:5], 0, v[92:93]
	s_waitcnt lgkmcnt(2)
	v_cvt_pk_bf16_f32 v0, v8, v6
	v_add_u32_e32 v6, 0x400, v112
	ds_read2_b32 v[14:15], v6 offset0:4 offset1:12
	ds_read2_b32 v[16:17], v6 offset0:69 offset1:77
	ds_read2_b32 v[18:19], v6 offset0:134 offset1:142
	ds_read2_b32 v[20:21], v6 offset0:199 offset1:207
	s_waitcnt lgkmcnt(4)
	v_cvt_pk_bf16_f32 v1, v10, v12
	v_lshl_add_u64 v[24:25], v[4:5], 0, v[98:99]
	s_waitcnt lgkmcnt(2)
	v_cvt_pk_bf16_f32 v2, v14, v16
	s_waitcnt lgkmcnt(0)
	v_cvt_pk_bf16_f32 v3, v18, v20
	global_store_dwordx4 v[22:23], v[0:3], off sc1
	s_nop 1
	v_cvt_pk_bf16_f32 v0, v9, v7
	v_cvt_pk_bf16_f32 v1, v11, v13
	v_cvt_pk_bf16_f32 v2, v15, v17
	v_cvt_pk_bf16_f32 v3, v19, v21
	v_lshl_add_u64 v[8:9], v[4:5], 0, v[94:95]
	global_store_dwordx4 v[8:9], v[0:3], off sc1
	ds_read2_b32 v[8:9], v112 offset0:81 offset1:89
	ds_read2_b32 v[10:11], v112 offset0:16 offset1:24
	ds_read2_b32 v[12:13], v112 offset0:146 offset1:154
	ds_read2_b32 v[14:15], v112 offset0:211 offset1:219
	ds_read2_b32 v[16:17], v6 offset0:20 offset1:28
	ds_read2_b32 v[18:19], v6 offset0:85 offset1:93
	ds_read2_b32 v[20:21], v6 offset0:150 offset1:158
	ds_read2_b32 v[22:23], v6 offset0:215 offset1:223
	s_waitcnt lgkmcnt(6)
	v_cvt_pk_bf16_f32 v0, v10, v8
	s_waitcnt lgkmcnt(4)
	v_cvt_pk_bf16_f32 v1, v12, v14
	s_waitcnt lgkmcnt(2)
	v_cvt_pk_bf16_f32 v2, v16, v18
	s_waitcnt lgkmcnt(0)
	v_cvt_pk_bf16_f32 v3, v20, v22
	global_store_dwordx4 v[24:25], v[0:3], off sc1
	v_lshl_add_u64 v[24:25], v[4:5], 0, v[102:103]
	s_nop 0
	v_cvt_pk_bf16_f32 v0, v11, v9
	v_cvt_pk_bf16_f32 v1, v13, v15
	v_cvt_pk_bf16_f32 v2, v17, v19
	v_cvt_pk_bf16_f32 v3, v21, v23
	v_lshl_add_u64 v[8:9], v[4:5], 0, v[100:101]
	global_store_dwordx4 v[8:9], v[0:3], off sc1
	ds_read2_b32 v[8:9], v112 offset0:32 offset1:40
	ds_read2_b32 v[10:11], v112 offset0:97 offset1:105
	ds_read2_b32 v[12:13], v112 offset0:162 offset1:170
	ds_read2_b32 v[14:15], v112 offset0:227 offset1:235
	ds_read2_b32 v[16:17], v6 offset0:36 offset1:44
	ds_read2_b32 v[18:19], v6 offset0:101 offset1:109
	ds_read2_b32 v[20:21], v6 offset0:166 offset1:174
	ds_read2_b32 v[22:23], v6 offset0:231 offset1:239
	s_waitcnt lgkmcnt(6)
	v_cvt_pk_bf16_f32 v0, v8, v10
	s_waitcnt lgkmcnt(4)
	v_cvt_pk_bf16_f32 v1, v12, v14
	s_waitcnt lgkmcnt(2)
	v_cvt_pk_bf16_f32 v2, v16, v18
	s_waitcnt lgkmcnt(0)
	v_cvt_pk_bf16_f32 v3, v20, v22
	global_store_dwordx4 v[24:25], v[0:3], off sc1
	s_nop 1
	v_cvt_pk_bf16_f32 v0, v9, v11
	v_cvt_pk_bf16_f32 v1, v13, v15
	v_cvt_pk_bf16_f32 v2, v17, v19
	v_cvt_pk_bf16_f32 v3, v21, v23
	v_lshl_add_u64 v[8:9], v[4:5], 0, v[104:105]
	global_store_dwordx4 v[8:9], v[0:3], off sc1
	ds_read2_b32 v[8:9], v112 offset0:48 offset1:56
	ds_read2_b32 v[10:11], v112 offset0:113 offset1:121
	ds_read2_b32 v[12:13], v112 offset0:178 offset1:186
	ds_read2_b32 v[14:15], v112 offset0:243 offset1:251
	ds_read2_b32 v[16:17], v6 offset0:52 offset1:60
	ds_read2_b32 v[18:19], v6 offset0:117 offset1:125
	ds_read2_b32 v[20:21], v6 offset0:182 offset1:190
	ds_read2_b32 v[6:7], v6 offset0:247 offset1:255
	v_lshl_add_u64 v[22:23], v[4:5], 0, v[106:107]
	s_waitcnt lgkmcnt(6)
	v_cvt_pk_bf16_f32 v0, v8, v10
	s_waitcnt lgkmcnt(4)
	v_cvt_pk_bf16_f32 v1, v12, v14
	s_waitcnt lgkmcnt(2)
	v_cvt_pk_bf16_f32 v2, v16, v18
	s_waitcnt lgkmcnt(0)
	v_cvt_pk_bf16_f32 v3, v20, v6
	global_store_dwordx4 v[22:23], v[0:3], off sc1
	v_lshl_add_u64 v[4:5], v[4:5], 0, v[108:109]
	s_nop 0
	v_cvt_pk_bf16_f32 v0, v9, v11
	v_cvt_pk_bf16_f32 v1, v13, v15
	v_cvt_pk_bf16_f32 v2, v17, v19
	v_cvt_pk_bf16_f32 v3, v21, v7
	global_store_dwordx4 v[4:5], v[0:3], off sc1
	s_waitcnt lgkmcnt(0)
	s_cbranch_scc0 .LBB0_1088

.LBB0_1164:
	s_ashr_i32 s2, s9, 31
	s_lshr_b32 s2, s2, 23
	s_add_i32 s2, s9, s2
	s_ashr_i32 s4, s2, 9
	s_and_b32 s2, s2, 0xfe00
	s_sub_i32 s2, s9, s2
	s_sext_i32_i16 s3, s2
	s_bfe_u32 s3, s3, 0x4001b
	s_add_i32 s3, s2, s3
	s_sext_i32_i16 s5, s3
	s_and_b32 s3, s3, 0xfff0
	s_sub_i32 s2, s2, s3
	s_sext_i32_i16 s13, s2
	s_lshl_b32 s2, s5, 2
	s_ashr_i32 s5, s4, 31
	s_andn2_b32 s2, s2, 63
	s_lshl_b32 s6, s13, 6
	s_lshl_b64 s[4:5], s[4:5], 23
	s_add_u32 s7, s11, s4
	s_addc_u32 s16, s12, s5
	s_ashr_i32 s3, s2, 31
	s_lshl_b64 s[14:15], s[2:3], 12
	s_add_u32 s18, s7, s14
	s_addc_u32 s16, s16, s15
	s_ashr_i32 s7, s6, 31
	s_lshl_b64 s[14:15], s[6:7], 2
	s_add_u32 s14, s18, s14
	s_addc_u32 s15, s16, s15
	v_lshl_add_u64 v[0:1], s[14:15], 0, v[96:97]
	v_lshl_add_u64 v[2:3], v[0:1], 0, v[60:61]
	flat_load_dwordx4 v[116:119], v[2:3] nt
	v_lshl_add_u64 v[2:3], v[0:1], 0, v[62:63]
	flat_load_dwordx4 v[56:59], v[2:3] nt
	v_lshl_add_u64 v[2:3], v[0:1], 0, v[64:65]
	flat_load_dwordx4 v[52:55], v[2:3] nt
	v_lshl_add_u64 v[2:3], v[0:1], 0, v[66:67]
	flat_load_dwordx4 v[48:51], v[2:3] nt
	v_lshl_add_u64 v[2:3], v[0:1], 0, v[68:69]
	flat_load_dwordx4 v[44:47], v[2:3] nt
	v_lshl_add_u64 v[2:3], v[0:1], 0, v[70:71]
	flat_load_dwordx4 v[40:43], v[2:3] nt
	v_lshl_add_u64 v[2:3], v[0:1], 0, v[72:73]
	flat_load_dwordx4 v[36:39], v[2:3] nt
	v_lshl_add_u64 v[2:3], v[0:1], 0, v[74:75]
	flat_load_dwordx4 v[32:35], v[2:3] nt
	v_lshl_add_u64 v[2:3], v[0:1], 0, v[76:77]
	flat_load_dwordx4 v[28:31], v[2:3] nt
	v_lshl_add_u64 v[2:3], v[0:1], 0, v[78:79]
	flat_load_dwordx4 v[24:27], v[2:3] nt
	v_lshl_add_u64 v[2:3], v[0:1], 0, v[80:81]
	flat_load_dwordx4 v[20:23], v[2:3] nt
	v_lshl_add_u64 v[2:3], v[0:1], 0, v[82:83]
	flat_load_dwordx4 v[16:19], v[2:3] nt
	v_lshl_add_u64 v[2:3], v[0:1], 0, v[84:85]
	flat_load_dwordx4 v[12:15], v[2:3] nt
	v_lshl_add_u64 v[2:3], v[0:1], 0, v[86:87]
	flat_load_dwordx4 v[8:11], v[2:3] nt
	v_lshl_add_u64 v[2:3], v[0:1], 0, v[88:89]
	flat_load_dwordx4 v[4:7], v[2:3] nt
	v_lshl_add_u64 v[0:1], v[0:1], 0, v[90:91]
	flat_load_dwordx4 v[0:3], v[0:1] nt
	v_add_u32_e32 v111, 0x410, v114
	s_lshl_b32 s7, s13, 7
	s_and_b32 s6, s6, 64
	s_or_b32 s6, s6, s7
	s_bitset1_b32 s6, 7
	s_ashr_i32 s7, s6, 31
	s_add_u32 s13, s21, s4
	s_addc_u32 s14, s22, s5
	s_lshl_b64 s[4:5], s[6:7], 12
	s_add_u32 s4, s13, s4
	s_addc_u32 s5, s14, s5
	s_lshl_b64 s[2:3], s[2:3], 1
	s_add_u32 s2, s4, s2
	s_addc_u32 s3, s5, s3
	s_add_i32 s9, s9, s80
	s_cmpk_lt_i32 s9, 0x1000
	s_waitcnt vmcnt(0) lgkmcnt(0)
	ds_write2_b32 v114, v116, v117 offset1:1
	ds_write2_b32 v114, v118, v119 offset0:2 offset1:3
	ds_write2_b32 v111, v56, v57 offset1:1
	v_add_u32_e32 v56, 0x418, v114
	ds_write2_b32 v56, v58, v59 offset1:1
	v_add_u32_e32 v56, 0x820, v114
	ds_write2_b32 v56, v52, v53 offset1:1
	v_add_u32_e32 v52, 0x828, v114
	ds_write2_b32 v52, v54, v55 offset1:1
	v_add_u32_e32 v52, 0xc30, v114
	ds_write2_b32 v52, v48, v49 offset1:1
	v_add_u32_e32 v48, 0xc38, v114
	ds_write2_b32 v48, v50, v51 offset1:1
	v_add_u32_e32 v48, 0x1040, v114
	ds_write2_b32 v48, v44, v45 offset1:1
	v_add_u32_e32 v44, 0x1048, v114
	ds_write2_b32 v44, v46, v47 offset1:1
	v_add_u32_e32 v44, 0x1450, v114
	ds_write2_b32 v44, v40, v41 offset1:1
	v_add_u32_e32 v40, 0x1458, v114
	ds_write2_b32 v40, v42, v43 offset1:1
	v_add_u32_e32 v40, 0x1860, v114
	ds_write2_b32 v40, v36, v37 offset1:1
	v_add_u32_e32 v36, 0x1868, v114
	ds_write2_b32 v36, v38, v39 offset1:1
	v_add_u32_e32 v36, 0x1c70, v114
	ds_write2_b32 v36, v32, v33 offset1:1
	v_add_u32_e32 v32, 0x1c78, v114
	ds_write2_b32 v32, v34, v35 offset1:1
	v_add_u32_e32 v32, 0x2080, v114
	ds_write2_b32 v32, v28, v29 offset1:1
	v_add_u32_e32 v28, 0x2088, v114
	ds_write2_b32 v28, v30, v31 offset1:1
	v_add_u32_e32 v28, 0x2490, v114
	ds_write2_b32 v28, v24, v25 offset1:1
	v_add_u32_e32 v24, 0x2498, v114
	ds_write2_b32 v24, v26, v27 offset1:1
	v_add_u32_e32 v24, 0x28a0, v114
	ds_write2_b32 v24, v20, v21 offset1:1
	v_add_u32_e32 v20, 0x28a8, v114
	ds_write2_b32 v20, v22, v23 offset1:1
	v_add_u32_e32 v20, 0x2cb0, v114
	ds_write2_b32 v20, v16, v17 offset1:1
	v_add_u32_e32 v16, 0x2cb8, v114
	ds_write2_b32 v16, v18, v19 offset1:1
	v_add_u32_e32 v16, 0x30c0, v114
	ds_write2_b32 v16, v12, v13 offset1:1
	v_add_u32_e32 v12, 0x30c8, v114
	ds_write2_b32 v12, v14, v15 offset1:1
	v_add_u32_e32 v12, 0x34d0, v114
	ds_write2_b32 v12, v8, v9 offset1:1
	v_add_u32_e32 v8, 0x34d8, v114
	ds_write2_b32 v8, v10, v11 offset1:1
	v_add_u32_e32 v8, 0x38e0, v114
	ds_write2_b32 v8, v4, v5 offset1:1
	v_add_u32_e32 v4, 0x38e8, v114
	ds_write2_b32 v4, v6, v7 offset1:1
	v_add_u32_e32 v4, 0x3cf0, v114
	ds_write2_b32 v4, v0, v1 offset1:1
	v_add_u32_e32 v0, 0x3cf8, v114
	ds_write2_b32 v0, v2, v3 offset1:1
	s_waitcnt lgkmcnt(0)
	ds_read2_b32 v[6:7], v113 offset0:65 offset1:73
	ds_read2_b32 v[8:9], v113 offset1:8
	ds_read2_b32 v[10:11], v113 offset0:130 offset1:138
	ds_read2_b32 v[12:13], v113 offset0:195 offset1:203
	v_mov_b32_e32 v111, v97
	v_lshl_add_u64 v[4:5], s[2:3], 0, v[110:111]
	v_lshl_add_u64 v[22:23], v[4:5], 0, v[92:93]
	s_waitcnt lgkmcnt(2)
	v_cvt_pk_bf16_f32 v0, v8, v6
	v_add_u32_e32 v6, 0x400, v113
	ds_read2_b32 v[14:15], v6 offset0:4 offset1:12
	ds_read2_b32 v[16:17], v6 offset0:69 offset1:77
	ds_read2_b32 v[18:19], v6 offset0:134 offset1:142
	ds_read2_b32 v[20:21], v6 offset0:199 offset1:207
	s_waitcnt lgkmcnt(4)
	v_cvt_pk_bf16_f32 v1, v10, v12
	v_lshl_add_u64 v[24:25], v[4:5], 0, v[98:99]
	s_waitcnt lgkmcnt(2)
	v_cvt_pk_bf16_f32 v2, v14, v16
	s_waitcnt lgkmcnt(0)
	v_cvt_pk_bf16_f32 v3, v18, v20
	global_store_dwordx4 v[22:23], v[0:3], off sc1
	s_nop 1
	v_cvt_pk_bf16_f32 v0, v9, v7
	v_cvt_pk_bf16_f32 v1, v11, v13
	v_cvt_pk_bf16_f32 v2, v15, v17
	v_cvt_pk_bf16_f32 v3, v19, v21
	v_lshl_add_u64 v[8:9], v[4:5], 0, v[94:95]
	global_store_dwordx4 v[8:9], v[0:3], off sc1
	ds_read2_b32 v[8:9], v113 offset0:81 offset1:89
	ds_read2_b32 v[10:11], v113 offset0:16 offset1:24
	ds_read2_b32 v[12:13], v113 offset0:146 offset1:154
	ds_read2_b32 v[14:15], v113 offset0:211 offset1:219
	ds_read2_b32 v[16:17], v6 offset0:20 offset1:28
	ds_read2_b32 v[18:19], v6 offset0:85 offset1:93
	ds_read2_b32 v[20:21], v6 offset0:150 offset1:158
	ds_read2_b32 v[22:23], v6 offset0:215 offset1:223
	s_waitcnt lgkmcnt(6)
	v_cvt_pk_bf16_f32 v0, v10, v8
	s_waitcnt lgkmcnt(4)
	v_cvt_pk_bf16_f32 v1, v12, v14
	s_waitcnt lgkmcnt(2)
	v_cvt_pk_bf16_f32 v2, v16, v18
	s_waitcnt lgkmcnt(0)
	v_cvt_pk_bf16_f32 v3, v20, v22
	global_store_dwordx4 v[24:25], v[0:3], off sc1
	v_lshl_add_u64 v[24:25], v[4:5], 0, v[102:103]
	s_nop 0
	v_cvt_pk_bf16_f32 v0, v11, v9
	v_cvt_pk_bf16_f32 v1, v13, v15
	v_cvt_pk_bf16_f32 v2, v17, v19
	v_cvt_pk_bf16_f32 v3, v21, v23
	v_lshl_add_u64 v[8:9], v[4:5], 0, v[100:101]
	global_store_dwordx4 v[8:9], v[0:3], off sc1
	ds_read2_b32 v[8:9], v113 offset0:32 offset1:40
	ds_read2_b32 v[10:11], v113 offset0:97 offset1:105
	ds_read2_b32 v[12:13], v113 offset0:162 offset1:170
	ds_read2_b32 v[14:15], v113 offset0:227 offset1:235
	ds_read2_b32 v[16:17], v6 offset0:36 offset1:44
	ds_read2_b32 v[18:19], v6 offset0:101 offset1:109
	ds_read2_b32 v[20:21], v6 offset0:166 offset1:174
	ds_read2_b32 v[22:23], v6 offset0:231 offset1:239
	s_waitcnt lgkmcnt(6)
	v_cvt_pk_bf16_f32 v0, v8, v10
	s_waitcnt lgkmcnt(4)
	v_cvt_pk_bf16_f32 v1, v12, v14
	s_waitcnt lgkmcnt(2)
	v_cvt_pk_bf16_f32 v2, v16, v18
	s_waitcnt lgkmcnt(0)
	v_cvt_pk_bf16_f32 v3, v20, v22
	global_store_dwordx4 v[24:25], v[0:3], off sc1
	s_nop 1
	v_cvt_pk_bf16_f32 v0, v9, v11
	v_cvt_pk_bf16_f32 v1, v13, v15
	v_cvt_pk_bf16_f32 v2, v17, v19
	v_cvt_pk_bf16_f32 v3, v21, v23
	v_lshl_add_u64 v[8:9], v[4:5], 0, v[104:105]
	global_store_dwordx4 v[8:9], v[0:3], off sc1
	ds_read2_b32 v[8:9], v113 offset0:48 offset1:56
	ds_read2_b32 v[10:11], v113 offset0:113 offset1:121
	ds_read2_b32 v[12:13], v113 offset0:178 offset1:186
	ds_read2_b32 v[14:15], v113 offset0:243 offset1:251
	ds_read2_b32 v[16:17], v6 offset0:52 offset1:60
	ds_read2_b32 v[18:19], v6 offset0:117 offset1:125
	ds_read2_b32 v[20:21], v6 offset0:182 offset1:190
	ds_read2_b32 v[6:7], v6 offset0:247 offset1:255
	v_lshl_add_u64 v[22:23], v[4:5], 0, v[106:107]
	s_waitcnt lgkmcnt(6)
	v_cvt_pk_bf16_f32 v0, v8, v10
	s_waitcnt lgkmcnt(4)
	v_cvt_pk_bf16_f32 v1, v12, v14
	s_waitcnt lgkmcnt(2)
	v_cvt_pk_bf16_f32 v2, v16, v18
	s_waitcnt lgkmcnt(0)
	v_cvt_pk_bf16_f32 v3, v20, v6
	global_store_dwordx4 v[22:23], v[0:3], off sc1
	v_lshl_add_u64 v[4:5], v[4:5], 0, v[108:109]
	s_nop 0
	v_cvt_pk_bf16_f32 v0, v9, v11
	v_cvt_pk_bf16_f32 v1, v13, v15
	v_cvt_pk_bf16_f32 v2, v17, v19
	v_cvt_pk_bf16_f32 v3, v21, v7
	global_store_dwordx4 v[4:5], v[0:3], off sc1
	s_waitcnt lgkmcnt(0)
	s_cbranch_scc1 .LBB0_1164

.LBB0_1167:
	s_ashr_i32 s4, s10, 31
	s_lshr_b32 s4, s4, 23
	s_add_i32 s5, s10, s4
	s_ashr_i32 s4, s5, 9
	s_and_b32 s5, s5, 0xfe00
	s_sub_i32 s5, s10, s5
	s_sext_i32_i16 s6, s5
	s_bfe_u32 s6, s6, 0x5001a
	s_add_i32 s6, s5, s6
	s_sext_i32_i16 s7, s6
	s_and_b32 s6, s6, 0xffe0
	s_sub_i32 s5, s5, s6
	s_sext_i32_i16 s5, s5
	s_lshl_b32 s6, s7, 1
	s_lshl_b32 s8, s5, 6
	s_ashr_i32 s5, s4, 31
	s_andn2_b32 s6, s6, 63
	s_lshl_b64 s[12:13], s[4:5], 23
	s_waitcnt lgkmcnt(0)
	s_add_u32 s9, s2, s12
	s_addc_u32 s11, s3, s13
	s_ashr_i32 s7, s6, 31
	s_lshl_b64 s[12:13], s[6:7], 13
	s_add_u32 s14, s9, s12
	s_addc_u32 s11, s11, s13
	s_ashr_i32 s9, s8, 31
	s_lshl_b64 s[12:13], s[8:9], 2
	s_add_u32 s12, s14, s12
	s_addc_u32 s13, s11, s13
	v_lshl_add_u64 v[0:1], s[12:13], 0, v[96:97]
	v_lshl_add_u64 v[2:3], v[0:1], 0, v[60:61]
	flat_load_dwordx4 v[114:117], v[2:3] nt
	v_lshl_add_u64 v[2:3], v[0:1], 0, v[62:63]
	flat_load_dwordx4 v[56:59], v[2:3] nt
	v_lshl_add_u64 v[2:3], v[0:1], 0, v[64:65]
	flat_load_dwordx4 v[52:55], v[2:3] nt
	v_lshl_add_u64 v[2:3], v[0:1], 0, v[66:67]
	flat_load_dwordx4 v[48:51], v[2:3] nt
	v_lshl_add_u64 v[2:3], v[0:1], 0, v[68:69]
	flat_load_dwordx4 v[44:47], v[2:3] nt
	v_lshl_add_u64 v[2:3], v[0:1], 0, v[70:71]
	flat_load_dwordx4 v[40:43], v[2:3] nt
	v_lshl_add_u64 v[2:3], v[0:1], 0, v[72:73]
	flat_load_dwordx4 v[36:39], v[2:3] nt
	v_lshl_add_u64 v[2:3], v[0:1], 0, v[74:75]
	flat_load_dwordx4 v[32:35], v[2:3] nt
	v_lshl_add_u64 v[2:3], v[0:1], 0, v[76:77]
	flat_load_dwordx4 v[28:31], v[2:3] nt
	v_lshl_add_u64 v[2:3], v[0:1], 0, v[78:79]
	flat_load_dwordx4 v[24:27], v[2:3] nt
	v_lshl_add_u64 v[2:3], v[0:1], 0, v[80:81]
	flat_load_dwordx4 v[20:23], v[2:3] nt
	v_lshl_add_u64 v[2:3], v[0:1], 0, v[82:83]
	flat_load_dwordx4 v[16:19], v[2:3] nt
	v_lshl_add_u64 v[2:3], v[0:1], 0, v[84:85]
	flat_load_dwordx4 v[12:15], v[2:3] nt
	v_lshl_add_u64 v[2:3], v[0:1], 0, v[86:87]
	flat_load_dwordx4 v[8:11], v[2:3] nt
	v_lshl_add_u64 v[2:3], v[0:1], 0, v[88:89]
	flat_load_dwordx4 v[4:7], v[2:3] nt
	v_lshl_add_u64 v[0:1], v[0:1], 0, v[90:91]
	flat_load_dwordx4 v[0:3], v[0:1] nt
	v_add_u32_e32 v111, 0x410, v113
	s_lshl_b64 s[4:5], s[4:5], 22
	s_add_u32 s11, s19, s4
	s_addc_u32 s12, s20, s5
	s_lshl_b64 s[4:5], s[8:9], 11
	s_add_u32 s8, s11, s4
	s_addc_u32 s9, s12, s5
	s_lshl_b64 s[4:5], s[6:7], 1
	s_add_u32 s4, s8, s4
	s_addc_u32 s5, s9, s5
	s_add_i32 s10, s10, s80
	s_cmpk_lt_i32 s10, 0x2000
	s_waitcnt vmcnt(0) lgkmcnt(0)
	ds_write2_b32 v113, v114, v115 offset1:1
	ds_write2_b32 v113, v116, v117 offset0:2 offset1:3
	ds_write2_b32 v111, v56, v57 offset1:1
	v_add_u32_e32 v56, 0x418, v113
	ds_write2_b32 v56, v58, v59 offset1:1
	v_add_u32_e32 v56, 0x820, v113
	ds_write2_b32 v56, v52, v53 offset1:1
	v_add_u32_e32 v52, 0x828, v113
	ds_write2_b32 v52, v54, v55 offset1:1
	v_add_u32_e32 v52, 0xc30, v113
	ds_write2_b32 v52, v48, v49 offset1:1
	v_add_u32_e32 v48, 0xc38, v113
	ds_write2_b32 v48, v50, v51 offset1:1
	v_add_u32_e32 v48, 0x1040, v113
	ds_write2_b32 v48, v44, v45 offset1:1
	v_add_u32_e32 v44, 0x1048, v113
	ds_write2_b32 v44, v46, v47 offset1:1
	v_add_u32_e32 v44, 0x1450, v113
	ds_write2_b32 v44, v40, v41 offset1:1
	v_add_u32_e32 v40, 0x1458, v113
	ds_write2_b32 v40, v42, v43 offset1:1
	v_add_u32_e32 v40, 0x1860, v113
	ds_write2_b32 v40, v36, v37 offset1:1
	v_add_u32_e32 v36, 0x1868, v113
	ds_write2_b32 v36, v38, v39 offset1:1
	v_add_u32_e32 v36, 0x1c70, v113
	ds_write2_b32 v36, v32, v33 offset1:1
	v_add_u32_e32 v32, 0x1c78, v113
	ds_write2_b32 v32, v34, v35 offset1:1
	v_add_u32_e32 v32, 0x2080, v113
	ds_write2_b32 v32, v28, v29 offset1:1
	v_add_u32_e32 v28, 0x2088, v113
	ds_write2_b32 v28, v30, v31 offset1:1
	v_add_u32_e32 v28, 0x2490, v113
	ds_write2_b32 v28, v24, v25 offset1:1
	v_add_u32_e32 v24, 0x2498, v113
	ds_write2_b32 v24, v26, v27 offset1:1
	v_add_u32_e32 v24, 0x28a0, v113
	ds_write2_b32 v24, v20, v21 offset1:1
	v_add_u32_e32 v20, 0x28a8, v113
	ds_write2_b32 v20, v22, v23 offset1:1
	v_add_u32_e32 v20, 0x2cb0, v113
	ds_write2_b32 v20, v16, v17 offset1:1
	v_add_u32_e32 v16, 0x2cb8, v113
	ds_write2_b32 v16, v18, v19 offset1:1
	v_add_u32_e32 v16, 0x30c0, v113
	ds_write2_b32 v16, v12, v13 offset1:1
	v_add_u32_e32 v12, 0x30c8, v113
	ds_write2_b32 v12, v14, v15 offset1:1
	v_add_u32_e32 v12, 0x34d0, v113
	ds_write2_b32 v12, v8, v9 offset1:1
	v_add_u32_e32 v8, 0x34d8, v113
	ds_write2_b32 v8, v10, v11 offset1:1
	v_add_u32_e32 v8, 0x38e0, v113
	ds_write2_b32 v8, v4, v5 offset1:1
	v_add_u32_e32 v4, 0x38e8, v113
	ds_write2_b32 v4, v6, v7 offset1:1
	v_add_u32_e32 v4, 0x3cf0, v113
	ds_write2_b32 v4, v0, v1 offset1:1
	v_add_u32_e32 v0, 0x3cf8, v113
	ds_write2_b32 v0, v2, v3 offset1:1
	s_waitcnt lgkmcnt(0)
	ds_read2_b32 v[6:7], v112 offset0:65 offset1:73
	ds_read2_b32 v[8:9], v112 offset1:8
	ds_read2_b32 v[10:11], v112 offset0:130 offset1:138
	ds_read2_b32 v[12:13], v112 offset0:195 offset1:203
	v_mov_b32_e32 v111, v97
	v_lshl_add_u64 v[4:5], s[4:5], 0, v[110:111]
	v_lshl_add_u64 v[22:23], v[4:5], 0, v[92:93]
	s_waitcnt lgkmcnt(2)
	v_cvt_pk_bf16_f32 v0, v8, v6
	v_add_u32_e32 v6, 0x400, v112
	ds_read2_b32 v[14:15], v6 offset0:4 offset1:12
	ds_read2_b32 v[16:17], v6 offset0:69 offset1:77
	ds_read2_b32 v[18:19], v6 offset0:134 offset1:142
	ds_read2_b32 v[20:21], v6 offset0:199 offset1:207
	s_waitcnt lgkmcnt(4)
	v_cvt_pk_bf16_f32 v1, v10, v12
	v_lshl_add_u64 v[24:25], v[4:5], 0, v[98:99]
	s_waitcnt lgkmcnt(2)
	v_cvt_pk_bf16_f32 v2, v14, v16
	s_waitcnt lgkmcnt(0)
	v_cvt_pk_bf16_f32 v3, v18, v20
	global_store_dwordx4 v[22:23], v[0:3], off sc1
	s_nop 1
	v_cvt_pk_bf16_f32 v0, v9, v7
	v_cvt_pk_bf16_f32 v1, v11, v13
	v_cvt_pk_bf16_f32 v2, v15, v17
	v_cvt_pk_bf16_f32 v3, v19, v21
	v_lshl_add_u64 v[8:9], v[4:5], 0, v[94:95]
	global_store_dwordx4 v[8:9], v[0:3], off sc1
	ds_read2_b32 v[8:9], v112 offset0:81 offset1:89
	ds_read2_b32 v[10:11], v112 offset0:16 offset1:24
	ds_read2_b32 v[12:13], v112 offset0:146 offset1:154
	ds_read2_b32 v[14:15], v112 offset0:211 offset1:219
	ds_read2_b32 v[16:17], v6 offset0:20 offset1:28
	ds_read2_b32 v[18:19], v6 offset0:85 offset1:93
	ds_read2_b32 v[20:21], v6 offset0:150 offset1:158
	ds_read2_b32 v[22:23], v6 offset0:215 offset1:223
	s_waitcnt lgkmcnt(6)
	v_cvt_pk_bf16_f32 v0, v10, v8
	s_waitcnt lgkmcnt(4)
	v_cvt_pk_bf16_f32 v1, v12, v14
	s_waitcnt lgkmcnt(2)
	v_cvt_pk_bf16_f32 v2, v16, v18
	s_waitcnt lgkmcnt(0)
	v_cvt_pk_bf16_f32 v3, v20, v22
	global_store_dwordx4 v[24:25], v[0:3], off sc1
	v_lshl_add_u64 v[24:25], v[4:5], 0, v[102:103]
	s_nop 0
	v_cvt_pk_bf16_f32 v0, v11, v9
	v_cvt_pk_bf16_f32 v1, v13, v15
	v_cvt_pk_bf16_f32 v2, v17, v19
	v_cvt_pk_bf16_f32 v3, v21, v23
	v_lshl_add_u64 v[8:9], v[4:5], 0, v[100:101]
	global_store_dwordx4 v[8:9], v[0:3], off sc1
	ds_read2_b32 v[8:9], v112 offset0:32 offset1:40
	ds_read2_b32 v[10:11], v112 offset0:97 offset1:105
	ds_read2_b32 v[12:13], v112 offset0:162 offset1:170
	ds_read2_b32 v[14:15], v112 offset0:227 offset1:235
	ds_read2_b32 v[16:17], v6 offset0:36 offset1:44
	ds_read2_b32 v[18:19], v6 offset0:101 offset1:109
	ds_read2_b32 v[20:21], v6 offset0:166 offset1:174
	ds_read2_b32 v[22:23], v6 offset0:231 offset1:239
	s_waitcnt lgkmcnt(6)
	v_cvt_pk_bf16_f32 v0, v8, v10
	s_waitcnt lgkmcnt(4)
	v_cvt_pk_bf16_f32 v1, v12, v14
	s_waitcnt lgkmcnt(2)
	v_cvt_pk_bf16_f32 v2, v16, v18
	s_waitcnt lgkmcnt(0)
	v_cvt_pk_bf16_f32 v3, v20, v22
	global_store_dwordx4 v[24:25], v[0:3], off sc1
	s_nop 1
	v_cvt_pk_bf16_f32 v0, v9, v11
	v_cvt_pk_bf16_f32 v1, v13, v15
	v_cvt_pk_bf16_f32 v2, v17, v19
	v_cvt_pk_bf16_f32 v3, v21, v23
	v_lshl_add_u64 v[8:9], v[4:5], 0, v[104:105]
	global_store_dwordx4 v[8:9], v[0:3], off sc1
	ds_read2_b32 v[8:9], v112 offset0:48 offset1:56
	ds_read2_b32 v[10:11], v112 offset0:113 offset1:121
	ds_read2_b32 v[12:13], v112 offset0:178 offset1:186
	ds_read2_b32 v[14:15], v112 offset0:243 offset1:251
	ds_read2_b32 v[16:17], v6 offset0:52 offset1:60
	ds_read2_b32 v[18:19], v6 offset0:117 offset1:125
	ds_read2_b32 v[20:21], v6 offset0:182 offset1:190
	ds_read2_b32 v[6:7], v6 offset0:247 offset1:255
	v_lshl_add_u64 v[22:23], v[4:5], 0, v[106:107]
	s_waitcnt lgkmcnt(6)
	v_cvt_pk_bf16_f32 v0, v8, v10
	s_waitcnt lgkmcnt(4)
	v_cvt_pk_bf16_f32 v1, v12, v14
	s_waitcnt lgkmcnt(2)
	v_cvt_pk_bf16_f32 v2, v16, v18
	s_waitcnt lgkmcnt(0)
	v_cvt_pk_bf16_f32 v3, v20, v6
	global_store_dwordx4 v[22:23], v[0:3], off sc1
	v_lshl_add_u64 v[4:5], v[4:5], 0, v[108:109]
	s_nop 0
	v_cvt_pk_bf16_f32 v0, v9, v11
	v_cvt_pk_bf16_f32 v1, v13, v15
	v_cvt_pk_bf16_f32 v2, v17, v19
	v_cvt_pk_bf16_f32 v3, v21, v7
	global_store_dwordx4 v[4:5], v[0:3], off sc1
	s_waitcnt lgkmcnt(0)
	s_cbranch_scc1 .LBB0_1167

.LBB0_1172:
	s_ashr_i32 s2, s9, 31
	s_lshr_b32 s2, s2, 23
	s_add_i32 s2, s9, s2
	s_ashr_i32 s4, s2, 9
	s_and_b32 s2, s2, 0xfe00
	s_sub_i32 s2, s9, s2
	s_sext_i32_i16 s3, s2
	s_bfe_u32 s3, s3, 0x4001b
	s_add_i32 s3, s2, s3
	s_sext_i32_i16 s5, s3
	s_and_b32 s3, s3, 0xfff0
	s_sub_i32 s2, s2, s3
	s_sext_i32_i16 s13, s2
	s_lshl_b32 s2, s5, 2
	s_ashr_i32 s5, s4, 31
	s_andn2_b32 s2, s2, 63
	s_lshl_b32 s6, s13, 6
	s_lshl_b64 s[4:5], s[4:5], 23
	s_add_u32 s7, s11, s4
	s_addc_u32 s16, s12, s5
	s_ashr_i32 s3, s2, 31
	s_lshl_b64 s[14:15], s[2:3], 12
	s_add_u32 s18, s7, s14
	s_addc_u32 s16, s16, s15
	s_ashr_i32 s7, s6, 31
	s_lshl_b64 s[14:15], s[6:7], 2
	s_add_u32 s14, s18, s14
	s_addc_u32 s15, s16, s15
	v_lshl_add_u64 v[0:1], s[14:15], 0, v[96:97]
	v_lshl_add_u64 v[2:3], v[0:1], 0, v[60:61]
	flat_load_dwordx4 v[116:119], v[2:3] nt
	v_lshl_add_u64 v[2:3], v[0:1], 0, v[62:63]
	flat_load_dwordx4 v[56:59], v[2:3] nt
	v_lshl_add_u64 v[2:3], v[0:1], 0, v[64:65]
	flat_load_dwordx4 v[52:55], v[2:3] nt
	v_lshl_add_u64 v[2:3], v[0:1], 0, v[66:67]
	flat_load_dwordx4 v[48:51], v[2:3] nt
	v_lshl_add_u64 v[2:3], v[0:1], 0, v[68:69]
	flat_load_dwordx4 v[44:47], v[2:3] nt
	v_lshl_add_u64 v[2:3], v[0:1], 0, v[70:71]
	flat_load_dwordx4 v[40:43], v[2:3] nt
	v_lshl_add_u64 v[2:3], v[0:1], 0, v[72:73]
	flat_load_dwordx4 v[36:39], v[2:3] nt
	v_lshl_add_u64 v[2:3], v[0:1], 0, v[74:75]
	flat_load_dwordx4 v[32:35], v[2:3] nt
	v_lshl_add_u64 v[2:3], v[0:1], 0, v[76:77]
	flat_load_dwordx4 v[28:31], v[2:3] nt
	v_lshl_add_u64 v[2:3], v[0:1], 0, v[78:79]
	flat_load_dwordx4 v[24:27], v[2:3] nt
	v_lshl_add_u64 v[2:3], v[0:1], 0, v[80:81]
	flat_load_dwordx4 v[20:23], v[2:3] nt
	v_lshl_add_u64 v[2:3], v[0:1], 0, v[82:83]
	flat_load_dwordx4 v[16:19], v[2:3] nt
	v_lshl_add_u64 v[2:3], v[0:1], 0, v[84:85]
	flat_load_dwordx4 v[12:15], v[2:3] nt
	v_lshl_add_u64 v[2:3], v[0:1], 0, v[86:87]
	flat_load_dwordx4 v[8:11], v[2:3] nt
	v_lshl_add_u64 v[2:3], v[0:1], 0, v[88:89]
	flat_load_dwordx4 v[4:7], v[2:3] nt
	v_lshl_add_u64 v[0:1], v[0:1], 0, v[90:91]
	flat_load_dwordx4 v[0:3], v[0:1] nt
	v_add_u32_e32 v111, 0x410, v114
	s_lshl_b32 s7, s13, 7
	s_and_b32 s6, s6, 64
	s_or_b32 s6, s6, s7
	s_bitset1_b32 s6, 7
	s_ashr_i32 s7, s6, 31
	s_add_u32 s13, s21, s4
	s_addc_u32 s14, s22, s5
	s_lshl_b64 s[4:5], s[6:7], 12
	s_add_u32 s4, s13, s4
	s_addc_u32 s5, s14, s5
	s_lshl_b64 s[2:3], s[2:3], 1
	s_add_u32 s2, s4, s2
	s_addc_u32 s3, s5, s3
	s_add_i32 s9, s9, s23
	s_cmpk_lt_i32 s9, 0x1000
	s_waitcnt vmcnt(0) lgkmcnt(0)
	ds_write2_b32 v114, v116, v117 offset1:1
	ds_write2_b32 v114, v118, v119 offset0:2 offset1:3
	ds_write2_b32 v111, v56, v57 offset1:1
	v_add_u32_e32 v56, 0x418, v114
	ds_write2_b32 v56, v58, v59 offset1:1
	v_add_u32_e32 v56, 0x820, v114
	ds_write2_b32 v56, v52, v53 offset1:1
	v_add_u32_e32 v52, 0x828, v114
	ds_write2_b32 v52, v54, v55 offset1:1
	v_add_u32_e32 v52, 0xc30, v114
	ds_write2_b32 v52, v48, v49 offset1:1
	v_add_u32_e32 v48, 0xc38, v114
	ds_write2_b32 v48, v50, v51 offset1:1
	v_add_u32_e32 v48, 0x1040, v114
	ds_write2_b32 v48, v44, v45 offset1:1
	v_add_u32_e32 v44, 0x1048, v114
	ds_write2_b32 v44, v46, v47 offset1:1
	v_add_u32_e32 v44, 0x1450, v114
	ds_write2_b32 v44, v40, v41 offset1:1
	v_add_u32_e32 v40, 0x1458, v114
	ds_write2_b32 v40, v42, v43 offset1:1
	v_add_u32_e32 v40, 0x1860, v114
	ds_write2_b32 v40, v36, v37 offset1:1
	v_add_u32_e32 v36, 0x1868, v114
	ds_write2_b32 v36, v38, v39 offset1:1
	v_add_u32_e32 v36, 0x1c70, v114
	ds_write2_b32 v36, v32, v33 offset1:1
	v_add_u32_e32 v32, 0x1c78, v114
	ds_write2_b32 v32, v34, v35 offset1:1
	v_add_u32_e32 v32, 0x2080, v114
	ds_write2_b32 v32, v28, v29 offset1:1
	v_add_u32_e32 v28, 0x2088, v114
	ds_write2_b32 v28, v30, v31 offset1:1
	v_add_u32_e32 v28, 0x2490, v114
	ds_write2_b32 v28, v24, v25 offset1:1
	v_add_u32_e32 v24, 0x2498, v114
	ds_write2_b32 v24, v26, v27 offset1:1
	v_add_u32_e32 v24, 0x28a0, v114
	ds_write2_b32 v24, v20, v21 offset1:1
	v_add_u32_e32 v20, 0x28a8, v114
	ds_write2_b32 v20, v22, v23 offset1:1
	v_add_u32_e32 v20, 0x2cb0, v114
	ds_write2_b32 v20, v16, v17 offset1:1
	v_add_u32_e32 v16, 0x2cb8, v114
	ds_write2_b32 v16, v18, v19 offset1:1
	v_add_u32_e32 v16, 0x30c0, v114
	ds_write2_b32 v16, v12, v13 offset1:1
	v_add_u32_e32 v12, 0x30c8, v114
	ds_write2_b32 v12, v14, v15 offset1:1
	v_add_u32_e32 v12, 0x34d0, v114
	ds_write2_b32 v12, v8, v9 offset1:1
	v_add_u32_e32 v8, 0x34d8, v114
	ds_write2_b32 v8, v10, v11 offset1:1
	v_add_u32_e32 v8, 0x38e0, v114
	ds_write2_b32 v8, v4, v5 offset1:1
	v_add_u32_e32 v4, 0x38e8, v114
	ds_write2_b32 v4, v6, v7 offset1:1
	v_add_u32_e32 v4, 0x3cf0, v114
	ds_write2_b32 v4, v0, v1 offset1:1
	v_add_u32_e32 v0, 0x3cf8, v114
	ds_write2_b32 v0, v2, v3 offset1:1
	s_waitcnt lgkmcnt(0)
	ds_read2_b32 v[6:7], v113 offset0:65 offset1:73
	ds_read2_b32 v[8:9], v113 offset1:8
	ds_read2_b32 v[10:11], v113 offset0:130 offset1:138
	ds_read2_b32 v[12:13], v113 offset0:195 offset1:203
	v_mov_b32_e32 v111, v97
	v_lshl_add_u64 v[4:5], s[2:3], 0, v[110:111]
	v_lshl_add_u64 v[22:23], v[4:5], 0, v[92:93]
	s_waitcnt lgkmcnt(2)
	v_cvt_pk_bf16_f32 v0, v8, v6
	v_add_u32_e32 v6, 0x400, v113
	ds_read2_b32 v[14:15], v6 offset0:4 offset1:12
	ds_read2_b32 v[16:17], v6 offset0:69 offset1:77
	ds_read2_b32 v[18:19], v6 offset0:134 offset1:142
	ds_read2_b32 v[20:21], v6 offset0:199 offset1:207
	s_waitcnt lgkmcnt(4)
	v_cvt_pk_bf16_f32 v1, v10, v12
	v_lshl_add_u64 v[24:25], v[4:5], 0, v[98:99]
	s_waitcnt lgkmcnt(2)
	v_cvt_pk_bf16_f32 v2, v14, v16
	s_waitcnt lgkmcnt(0)
	v_cvt_pk_bf16_f32 v3, v18, v20
	global_store_dwordx4 v[22:23], v[0:3], off sc1
	s_nop 1
	v_cvt_pk_bf16_f32 v0, v9, v7
	v_cvt_pk_bf16_f32 v1, v11, v13
	v_cvt_pk_bf16_f32 v2, v15, v17
	v_cvt_pk_bf16_f32 v3, v19, v21
	v_lshl_add_u64 v[8:9], v[4:5], 0, v[94:95]
	global_store_dwordx4 v[8:9], v[0:3], off sc1
	ds_read2_b32 v[8:9], v113 offset0:81 offset1:89
	ds_read2_b32 v[10:11], v113 offset0:16 offset1:24
	ds_read2_b32 v[12:13], v113 offset0:146 offset1:154
	ds_read2_b32 v[14:15], v113 offset0:211 offset1:219
	ds_read2_b32 v[16:17], v6 offset0:20 offset1:28
	ds_read2_b32 v[18:19], v6 offset0:85 offset1:93
	ds_read2_b32 v[20:21], v6 offset0:150 offset1:158
	ds_read2_b32 v[22:23], v6 offset0:215 offset1:223
	s_waitcnt lgkmcnt(6)
	v_cvt_pk_bf16_f32 v0, v10, v8
	s_waitcnt lgkmcnt(4)
	v_cvt_pk_bf16_f32 v1, v12, v14
	s_waitcnt lgkmcnt(2)
	v_cvt_pk_bf16_f32 v2, v16, v18
	s_waitcnt lgkmcnt(0)
	v_cvt_pk_bf16_f32 v3, v20, v22
	global_store_dwordx4 v[24:25], v[0:3], off sc1
	v_lshl_add_u64 v[24:25], v[4:5], 0, v[102:103]
	s_nop 0
	v_cvt_pk_bf16_f32 v0, v11, v9
	v_cvt_pk_bf16_f32 v1, v13, v15
	v_cvt_pk_bf16_f32 v2, v17, v19
	v_cvt_pk_bf16_f32 v3, v21, v23
	v_lshl_add_u64 v[8:9], v[4:5], 0, v[100:101]
	global_store_dwordx4 v[8:9], v[0:3], off sc1
	ds_read2_b32 v[8:9], v113 offset0:32 offset1:40
	ds_read2_b32 v[10:11], v113 offset0:97 offset1:105
	ds_read2_b32 v[12:13], v113 offset0:162 offset1:170
	ds_read2_b32 v[14:15], v113 offset0:227 offset1:235
	ds_read2_b32 v[16:17], v6 offset0:36 offset1:44
	ds_read2_b32 v[18:19], v6 offset0:101 offset1:109
	ds_read2_b32 v[20:21], v6 offset0:166 offset1:174
	ds_read2_b32 v[22:23], v6 offset0:231 offset1:239
	s_waitcnt lgkmcnt(6)
	v_cvt_pk_bf16_f32 v0, v8, v10
	s_waitcnt lgkmcnt(4)
	v_cvt_pk_bf16_f32 v1, v12, v14
	s_waitcnt lgkmcnt(2)
	v_cvt_pk_bf16_f32 v2, v16, v18
	s_waitcnt lgkmcnt(0)
	v_cvt_pk_bf16_f32 v3, v20, v22
	global_store_dwordx4 v[24:25], v[0:3], off sc1
	s_nop 1
	v_cvt_pk_bf16_f32 v0, v9, v11
	v_cvt_pk_bf16_f32 v1, v13, v15
	v_cvt_pk_bf16_f32 v2, v17, v19
	v_cvt_pk_bf16_f32 v3, v21, v23
	v_lshl_add_u64 v[8:9], v[4:5], 0, v[104:105]
	global_store_dwordx4 v[8:9], v[0:3], off sc1
	ds_read2_b32 v[8:9], v113 offset0:48 offset1:56
	ds_read2_b32 v[10:11], v113 offset0:113 offset1:121
	ds_read2_b32 v[12:13], v113 offset0:178 offset1:186
	ds_read2_b32 v[14:15], v113 offset0:243 offset1:251
	ds_read2_b32 v[16:17], v6 offset0:52 offset1:60
	ds_read2_b32 v[18:19], v6 offset0:117 offset1:125
	ds_read2_b32 v[20:21], v6 offset0:182 offset1:190
	ds_read2_b32 v[6:7], v6 offset0:247 offset1:255
	v_lshl_add_u64 v[22:23], v[4:5], 0, v[106:107]
	s_waitcnt lgkmcnt(6)
	v_cvt_pk_bf16_f32 v0, v8, v10
	s_waitcnt lgkmcnt(4)
	v_cvt_pk_bf16_f32 v1, v12, v14
	s_waitcnt lgkmcnt(2)
	v_cvt_pk_bf16_f32 v2, v16, v18
	s_waitcnt lgkmcnt(0)
	v_cvt_pk_bf16_f32 v3, v20, v6
	global_store_dwordx4 v[22:23], v[0:3], off sc1
	v_lshl_add_u64 v[4:5], v[4:5], 0, v[108:109]
	s_nop 0
	v_cvt_pk_bf16_f32 v0, v9, v11
	v_cvt_pk_bf16_f32 v1, v13, v15
	v_cvt_pk_bf16_f32 v2, v17, v19
	v_cvt_pk_bf16_f32 v3, v21, v7
	global_store_dwordx4 v[4:5], v[0:3], off sc1
	s_waitcnt lgkmcnt(0)
	s_cbranch_scc1 .LBB0_1172

.LBB0_1175:
	s_ashr_i32 s4, s10, 31
	s_lshr_b32 s4, s4, 23
	s_add_i32 s5, s10, s4
	s_ashr_i32 s4, s5, 9
	s_and_b32 s5, s5, 0xfe00
	s_sub_i32 s5, s10, s5
	s_sext_i32_i16 s6, s5
	s_bfe_u32 s6, s6, 0x5001a
	s_add_i32 s6, s5, s6
	s_sext_i32_i16 s7, s6
	s_and_b32 s6, s6, 0xffe0
	s_sub_i32 s5, s5, s6
	s_sext_i32_i16 s5, s5
	s_lshl_b32 s6, s7, 1
	s_lshl_b32 s8, s5, 6
	s_ashr_i32 s5, s4, 31
	s_andn2_b32 s6, s6, 63
	s_lshl_b64 s[12:13], s[4:5], 23
	s_waitcnt lgkmcnt(0)
	s_add_u32 s9, s2, s12
	s_addc_u32 s11, s3, s13
	s_ashr_i32 s7, s6, 31
	s_lshl_b64 s[12:13], s[6:7], 13
	s_add_u32 s14, s9, s12
	s_addc_u32 s11, s11, s13
	s_ashr_i32 s9, s8, 31
	s_lshl_b64 s[12:13], s[8:9], 2
	s_add_u32 s12, s14, s12
	s_addc_u32 s13, s11, s13
	v_lshl_add_u64 v[0:1], s[12:13], 0, v[96:97]
	v_lshl_add_u64 v[2:3], v[0:1], 0, v[60:61]
	flat_load_dwordx4 v[114:117], v[2:3] nt
	v_lshl_add_u64 v[2:3], v[0:1], 0, v[62:63]
	flat_load_dwordx4 v[56:59], v[2:3] nt
	v_lshl_add_u64 v[2:3], v[0:1], 0, v[64:65]
	flat_load_dwordx4 v[52:55], v[2:3] nt
	v_lshl_add_u64 v[2:3], v[0:1], 0, v[66:67]
	flat_load_dwordx4 v[48:51], v[2:3] nt
	v_lshl_add_u64 v[2:3], v[0:1], 0, v[68:69]
	flat_load_dwordx4 v[44:47], v[2:3] nt
	v_lshl_add_u64 v[2:3], v[0:1], 0, v[70:71]
	flat_load_dwordx4 v[40:43], v[2:3] nt
	v_lshl_add_u64 v[2:3], v[0:1], 0, v[72:73]
	flat_load_dwordx4 v[36:39], v[2:3] nt
	v_lshl_add_u64 v[2:3], v[0:1], 0, v[74:75]
	flat_load_dwordx4 v[32:35], v[2:3] nt
	v_lshl_add_u64 v[2:3], v[0:1], 0, v[76:77]
	flat_load_dwordx4 v[28:31], v[2:3] nt
	v_lshl_add_u64 v[2:3], v[0:1], 0, v[78:79]
	flat_load_dwordx4 v[24:27], v[2:3] nt
	v_lshl_add_u64 v[2:3], v[0:1], 0, v[80:81]
	flat_load_dwordx4 v[20:23], v[2:3] nt
	v_lshl_add_u64 v[2:3], v[0:1], 0, v[82:83]
	flat_load_dwordx4 v[16:19], v[2:3] nt
	v_lshl_add_u64 v[2:3], v[0:1], 0, v[84:85]
	flat_load_dwordx4 v[12:15], v[2:3] nt
	v_lshl_add_u64 v[2:3], v[0:1], 0, v[86:87]
	flat_load_dwordx4 v[8:11], v[2:3] nt
	v_lshl_add_u64 v[2:3], v[0:1], 0, v[88:89]
	flat_load_dwordx4 v[4:7], v[2:3] nt
	v_lshl_add_u64 v[0:1], v[0:1], 0, v[90:91]
	flat_load_dwordx4 v[0:3], v[0:1] nt
	v_add_u32_e32 v111, 0x410, v113
	s_lshl_b64 s[4:5], s[4:5], 22
	s_add_u32 s11, s19, s4
	s_addc_u32 s12, s20, s5
	s_lshl_b64 s[4:5], s[8:9], 11
	s_add_u32 s8, s11, s4
	s_addc_u32 s9, s12, s5
	s_lshl_b64 s[4:5], s[6:7], 1
	s_add_u32 s4, s8, s4
	s_addc_u32 s5, s9, s5
	s_add_i32 s10, s10, s15
	s_cmpk_gt_i32 s10, 0x1fff
	s_waitcnt vmcnt(0) lgkmcnt(0)
	ds_write2_b32 v113, v114, v115 offset1:1
	ds_write2_b32 v113, v116, v117 offset0:2 offset1:3
	ds_write2_b32 v111, v56, v57 offset1:1
	v_add_u32_e32 v56, 0x418, v113
	ds_write2_b32 v56, v58, v59 offset1:1
	v_add_u32_e32 v56, 0x820, v113
	ds_write2_b32 v56, v52, v53 offset1:1
	v_add_u32_e32 v52, 0x828, v113
	ds_write2_b32 v52, v54, v55 offset1:1
	v_add_u32_e32 v52, 0xc30, v113
	ds_write2_b32 v52, v48, v49 offset1:1
	v_add_u32_e32 v48, 0xc38, v113
	ds_write2_b32 v48, v50, v51 offset1:1
	v_add_u32_e32 v48, 0x1040, v113
	ds_write2_b32 v48, v44, v45 offset1:1
	v_add_u32_e32 v44, 0x1048, v113
	ds_write2_b32 v44, v46, v47 offset1:1
	v_add_u32_e32 v44, 0x1450, v113
	ds_write2_b32 v44, v40, v41 offset1:1
	v_add_u32_e32 v40, 0x1458, v113
	ds_write2_b32 v40, v42, v43 offset1:1
	v_add_u32_e32 v40, 0x1860, v113
	ds_write2_b32 v40, v36, v37 offset1:1
	v_add_u32_e32 v36, 0x1868, v113
	ds_write2_b32 v36, v38, v39 offset1:1
	v_add_u32_e32 v36, 0x1c70, v113
	ds_write2_b32 v36, v32, v33 offset1:1
	v_add_u32_e32 v32, 0x1c78, v113
	ds_write2_b32 v32, v34, v35 offset1:1
	v_add_u32_e32 v32, 0x2080, v113
	ds_write2_b32 v32, v28, v29 offset1:1
	v_add_u32_e32 v28, 0x2088, v113
	ds_write2_b32 v28, v30, v31 offset1:1
	v_add_u32_e32 v28, 0x2490, v113
	ds_write2_b32 v28, v24, v25 offset1:1
	v_add_u32_e32 v24, 0x2498, v113
	ds_write2_b32 v24, v26, v27 offset1:1
	v_add_u32_e32 v24, 0x28a0, v113
	ds_write2_b32 v24, v20, v21 offset1:1
	v_add_u32_e32 v20, 0x28a8, v113
	ds_write2_b32 v20, v22, v23 offset1:1
	v_add_u32_e32 v20, 0x2cb0, v113
	ds_write2_b32 v20, v16, v17 offset1:1
	v_add_u32_e32 v16, 0x2cb8, v113
	ds_write2_b32 v16, v18, v19 offset1:1
	v_add_u32_e32 v16, 0x30c0, v113
	ds_write2_b32 v16, v12, v13 offset1:1
	v_add_u32_e32 v12, 0x30c8, v113
	ds_write2_b32 v12, v14, v15 offset1:1
	v_add_u32_e32 v12, 0x34d0, v113
	ds_write2_b32 v12, v8, v9 offset1:1
	v_add_u32_e32 v8, 0x34d8, v113
	ds_write2_b32 v8, v10, v11 offset1:1
	v_add_u32_e32 v8, 0x38e0, v113
	ds_write2_b32 v8, v4, v5 offset1:1
	v_add_u32_e32 v4, 0x38e8, v113
	ds_write2_b32 v4, v6, v7 offset1:1
	v_add_u32_e32 v4, 0x3cf0, v113
	ds_write2_b32 v4, v0, v1 offset1:1
	v_add_u32_e32 v0, 0x3cf8, v113
	ds_write2_b32 v0, v2, v3 offset1:1
	s_waitcnt lgkmcnt(0)
	ds_read2_b32 v[6:7], v112 offset0:65 offset1:73
	ds_read2_b32 v[8:9], v112 offset1:8
	ds_read2_b32 v[10:11], v112 offset0:130 offset1:138
	ds_read2_b32 v[12:13], v112 offset0:195 offset1:203
	v_mov_b32_e32 v111, v97
	v_lshl_add_u64 v[4:5], s[4:5], 0, v[110:111]
	v_lshl_add_u64 v[22:23], v[4:5], 0, v[92:93]
	s_waitcnt lgkmcnt(2)
	v_cvt_pk_bf16_f32 v0, v8, v6
	v_add_u32_e32 v6, 0x400, v112
	ds_read2_b32 v[14:15], v6 offset0:4 offset1:12
	ds_read2_b32 v[16:17], v6 offset0:69 offset1:77
	ds_read2_b32 v[18:19], v6 offset0:134 offset1:142
	ds_read2_b32 v[20:21], v6 offset0:199 offset1:207
	s_waitcnt lgkmcnt(4)
	v_cvt_pk_bf16_f32 v1, v10, v12
	v_lshl_add_u64 v[24:25], v[4:5], 0, v[98:99]
	s_waitcnt lgkmcnt(2)
	v_cvt_pk_bf16_f32 v2, v14, v16
	s_waitcnt lgkmcnt(0)
	v_cvt_pk_bf16_f32 v3, v18, v20
	global_store_dwordx4 v[22:23], v[0:3], off sc1
	s_nop 1
	v_cvt_pk_bf16_f32 v0, v9, v7
	v_cvt_pk_bf16_f32 v1, v11, v13
	v_cvt_pk_bf16_f32 v2, v15, v17
	v_cvt_pk_bf16_f32 v3, v19, v21
	v_lshl_add_u64 v[8:9], v[4:5], 0, v[94:95]
	global_store_dwordx4 v[8:9], v[0:3], off sc1
	ds_read2_b32 v[8:9], v112 offset0:81 offset1:89
	ds_read2_b32 v[10:11], v112 offset0:16 offset1:24
	ds_read2_b32 v[12:13], v112 offset0:146 offset1:154
	ds_read2_b32 v[14:15], v112 offset0:211 offset1:219
	ds_read2_b32 v[16:17], v6 offset0:20 offset1:28
	ds_read2_b32 v[18:19], v6 offset0:85 offset1:93
	ds_read2_b32 v[20:21], v6 offset0:150 offset1:158
	ds_read2_b32 v[22:23], v6 offset0:215 offset1:223
	s_waitcnt lgkmcnt(6)
	v_cvt_pk_bf16_f32 v0, v10, v8
	s_waitcnt lgkmcnt(4)
	v_cvt_pk_bf16_f32 v1, v12, v14
	s_waitcnt lgkmcnt(2)
	v_cvt_pk_bf16_f32 v2, v16, v18
	s_waitcnt lgkmcnt(0)
	v_cvt_pk_bf16_f32 v3, v20, v22
	global_store_dwordx4 v[24:25], v[0:3], off sc1
	v_lshl_add_u64 v[24:25], v[4:5], 0, v[102:103]
	s_nop 0
	v_cvt_pk_bf16_f32 v0, v11, v9
	v_cvt_pk_bf16_f32 v1, v13, v15
	v_cvt_pk_bf16_f32 v2, v17, v19
	v_cvt_pk_bf16_f32 v3, v21, v23
	v_lshl_add_u64 v[8:9], v[4:5], 0, v[100:101]
	global_store_dwordx4 v[8:9], v[0:3], off sc1
	ds_read2_b32 v[8:9], v112 offset0:32 offset1:40
	ds_read2_b32 v[10:11], v112 offset0:97 offset1:105
	ds_read2_b32 v[12:13], v112 offset0:162 offset1:170
	ds_read2_b32 v[14:15], v112 offset0:227 offset1:235
	ds_read2_b32 v[16:17], v6 offset0:36 offset1:44
	ds_read2_b32 v[18:19], v6 offset0:101 offset1:109
	ds_read2_b32 v[20:21], v6 offset0:166 offset1:174
	ds_read2_b32 v[22:23], v6 offset0:231 offset1:239
	s_waitcnt lgkmcnt(6)
	v_cvt_pk_bf16_f32 v0, v8, v10
	s_waitcnt lgkmcnt(4)
	v_cvt_pk_bf16_f32 v1, v12, v14
	s_waitcnt lgkmcnt(2)
	v_cvt_pk_bf16_f32 v2, v16, v18
	s_waitcnt lgkmcnt(0)
	v_cvt_pk_bf16_f32 v3, v20, v22
	global_store_dwordx4 v[24:25], v[0:3], off sc1
	s_nop 1
	v_cvt_pk_bf16_f32 v0, v9, v11
	v_cvt_pk_bf16_f32 v1, v13, v15
	v_cvt_pk_bf16_f32 v2, v17, v19
	v_cvt_pk_bf16_f32 v3, v21, v23
	v_lshl_add_u64 v[8:9], v[4:5], 0, v[104:105]
	global_store_dwordx4 v[8:9], v[0:3], off sc1
	ds_read2_b32 v[8:9], v112 offset0:48 offset1:56
	ds_read2_b32 v[10:11], v112 offset0:113 offset1:121
	ds_read2_b32 v[12:13], v112 offset0:178 offset1:186
	ds_read2_b32 v[14:15], v112 offset0:243 offset1:251
	ds_read2_b32 v[16:17], v6 offset0:52 offset1:60
	ds_read2_b32 v[18:19], v6 offset0:117 offset1:125
	ds_read2_b32 v[20:21], v6 offset0:182 offset1:190
	ds_read2_b32 v[6:7], v6 offset0:247 offset1:255
	v_lshl_add_u64 v[22:23], v[4:5], 0, v[106:107]
	s_waitcnt lgkmcnt(6)
	v_cvt_pk_bf16_f32 v0, v8, v10
	s_waitcnt lgkmcnt(4)
	v_cvt_pk_bf16_f32 v1, v12, v14
	s_waitcnt lgkmcnt(2)
	v_cvt_pk_bf16_f32 v2, v16, v18
	s_waitcnt lgkmcnt(0)
	v_cvt_pk_bf16_f32 v3, v20, v6
	global_store_dwordx4 v[22:23], v[0:3], off sc1
	v_lshl_add_u64 v[4:5], v[4:5], 0, v[108:109]
	s_nop 0
	v_cvt_pk_bf16_f32 v0, v9, v11
	v_cvt_pk_bf16_f32 v1, v13, v15
	v_cvt_pk_bf16_f32 v2, v17, v19
	v_cvt_pk_bf16_f32 v3, v21, v7
	global_store_dwordx4 v[4:5], v[0:3], off sc1
	s_waitcnt lgkmcnt(0)
	s_cbranch_scc0 .LBB0_1175

.LBB0_1536:
	s_ashr_i32 s2, s8, 31
	s_lshr_b32 s2, s2, 23
	s_add_i32 s2, s8, s2
	s_ashr_i32 s4, s2, 9
	s_and_b32 s2, s2, 0xfe00
	s_sub_i32 s2, s8, s2
	s_sext_i32_i16 s3, s2
	s_bfe_u32 s3, s3, 0x4001b
	s_add_i32 s3, s2, s3
	s_sext_i32_i16 s5, s3
	s_and_b32 s3, s3, 0xfff0
	s_sub_i32 s2, s2, s3
	s_sext_i32_i16 s11, s2
	s_lshl_b32 s2, s5, 2
	s_ashr_i32 s5, s4, 31
	s_andn2_b32 s2, s2, 63
	s_lshl_b32 s6, s11, 6
	s_lshl_b64 s[4:5], s[4:5], 23
	s_add_u32 s7, s9, s4
	s_addc_u32 s14, s10, s5
	s_ashr_i32 s3, s2, 31
	s_lshl_b64 s[12:13], s[2:3], 12
	s_add_u32 s15, s7, s12
	s_addc_u32 s14, s14, s13
	s_ashr_i32 s7, s6, 31
	s_lshl_b64 s[12:13], s[6:7], 2
	s_add_u32 s12, s15, s12
	s_addc_u32 s13, s14, s13
	v_lshl_add_u64 v[0:1], s[12:13], 0, v[96:97]
	v_lshl_add_u64 v[2:3], v[0:1], 0, v[60:61]
	flat_load_dwordx4 v[114:117], v[2:3] nt
	v_lshl_add_u64 v[2:3], v[0:1], 0, v[62:63]
	flat_load_dwordx4 v[56:59], v[2:3] nt
	v_lshl_add_u64 v[2:3], v[0:1], 0, v[64:65]
	flat_load_dwordx4 v[52:55], v[2:3] nt
	v_lshl_add_u64 v[2:3], v[0:1], 0, v[66:67]
	flat_load_dwordx4 v[48:51], v[2:3] nt
	v_lshl_add_u64 v[2:3], v[0:1], 0, v[68:69]
	flat_load_dwordx4 v[44:47], v[2:3] nt
	v_lshl_add_u64 v[2:3], v[0:1], 0, v[70:71]
	flat_load_dwordx4 v[40:43], v[2:3] nt
	v_lshl_add_u64 v[2:3], v[0:1], 0, v[72:73]
	flat_load_dwordx4 v[36:39], v[2:3] nt
	v_lshl_add_u64 v[2:3], v[0:1], 0, v[74:75]
	flat_load_dwordx4 v[32:35], v[2:3] nt
	v_lshl_add_u64 v[2:3], v[0:1], 0, v[76:77]
	flat_load_dwordx4 v[28:31], v[2:3] nt
	v_lshl_add_u64 v[2:3], v[0:1], 0, v[78:79]
	flat_load_dwordx4 v[24:27], v[2:3] nt
	v_lshl_add_u64 v[2:3], v[0:1], 0, v[80:81]
	flat_load_dwordx4 v[20:23], v[2:3] nt
	v_lshl_add_u64 v[2:3], v[0:1], 0, v[82:83]
	flat_load_dwordx4 v[16:19], v[2:3] nt
	v_lshl_add_u64 v[2:3], v[0:1], 0, v[84:85]
	flat_load_dwordx4 v[12:15], v[2:3] nt
	v_lshl_add_u64 v[2:3], v[0:1], 0, v[86:87]
	flat_load_dwordx4 v[8:11], v[2:3] nt
	v_lshl_add_u64 v[2:3], v[0:1], 0, v[88:89]
	flat_load_dwordx4 v[4:7], v[2:3] nt
	v_lshl_add_u64 v[0:1], v[0:1], 0, v[90:91]
	flat_load_dwordx4 v[0:3], v[0:1] nt
	v_add_u32_e32 v111, 0x410, v113
	s_lshl_b32 s7, s11, 7
	s_and_b32 s7, s7, 0xffffff00
	s_and_b32 s6, s6, 64
	s_or_b32 s6, s7, s6
	s_ashr_i32 s7, s6, 31
	s_add_u32 s11, s16, s4
	s_addc_u32 s12, s18, s5
	s_lshl_b64 s[4:5], s[6:7], 12
	s_add_u32 s4, s11, s4
	s_addc_u32 s5, s12, s5
	s_lshl_b64 s[2:3], s[2:3], 1
	s_add_u32 s2, s4, s2
	s_addc_u32 s3, s5, s3
	s_add_i32 s8, s8, s80
	s_cmpk_lt_i32 s8, 0x2000
	s_waitcnt vmcnt(0) lgkmcnt(0)
	ds_write2_b32 v113, v114, v115 offset1:1
	ds_write2_b32 v113, v116, v117 offset0:2 offset1:3
	ds_write2_b32 v111, v56, v57 offset1:1
	v_add_u32_e32 v56, 0x418, v113
	ds_write2_b32 v56, v58, v59 offset1:1
	v_add_u32_e32 v56, 0x820, v113
	ds_write2_b32 v56, v52, v53 offset1:1
	v_add_u32_e32 v52, 0x828, v113
	ds_write2_b32 v52, v54, v55 offset1:1
	v_add_u32_e32 v52, 0xc30, v113
	ds_write2_b32 v52, v48, v49 offset1:1
	v_add_u32_e32 v48, 0xc38, v113
	ds_write2_b32 v48, v50, v51 offset1:1
	v_add_u32_e32 v48, 0x1040, v113
	ds_write2_b32 v48, v44, v45 offset1:1
	v_add_u32_e32 v44, 0x1048, v113
	ds_write2_b32 v44, v46, v47 offset1:1
	v_add_u32_e32 v44, 0x1450, v113
	ds_write2_b32 v44, v40, v41 offset1:1
	v_add_u32_e32 v40, 0x1458, v113
	ds_write2_b32 v40, v42, v43 offset1:1
	v_add_u32_e32 v40, 0x1860, v113
	ds_write2_b32 v40, v36, v37 offset1:1
	v_add_u32_e32 v36, 0x1868, v113
	ds_write2_b32 v36, v38, v39 offset1:1
	v_add_u32_e32 v36, 0x1c70, v113
	ds_write2_b32 v36, v32, v33 offset1:1
	v_add_u32_e32 v32, 0x1c78, v113
	ds_write2_b32 v32, v34, v35 offset1:1
	v_add_u32_e32 v32, 0x2080, v113
	ds_write2_b32 v32, v28, v29 offset1:1
	v_add_u32_e32 v28, 0x2088, v113
	ds_write2_b32 v28, v30, v31 offset1:1
	v_add_u32_e32 v28, 0x2490, v113
	ds_write2_b32 v28, v24, v25 offset1:1
	v_add_u32_e32 v24, 0x2498, v113
	ds_write2_b32 v24, v26, v27 offset1:1
	v_add_u32_e32 v24, 0x28a0, v113
	ds_write2_b32 v24, v20, v21 offset1:1
	v_add_u32_e32 v20, 0x28a8, v113
	ds_write2_b32 v20, v22, v23 offset1:1
	v_add_u32_e32 v20, 0x2cb0, v113
	ds_write2_b32 v20, v16, v17 offset1:1
	v_add_u32_e32 v16, 0x2cb8, v113
	ds_write2_b32 v16, v18, v19 offset1:1
	v_add_u32_e32 v16, 0x30c0, v113
	ds_write2_b32 v16, v12, v13 offset1:1
	v_add_u32_e32 v12, 0x30c8, v113
	ds_write2_b32 v12, v14, v15 offset1:1
	v_add_u32_e32 v12, 0x34d0, v113
	ds_write2_b32 v12, v8, v9 offset1:1
	v_add_u32_e32 v8, 0x34d8, v113
	ds_write2_b32 v8, v10, v11 offset1:1
	v_add_u32_e32 v8, 0x38e0, v113
	ds_write2_b32 v8, v4, v5 offset1:1
	v_add_u32_e32 v4, 0x38e8, v113
	ds_write2_b32 v4, v6, v7 offset1:1
	v_add_u32_e32 v4, 0x3cf0, v113
	ds_write2_b32 v4, v0, v1 offset1:1
	v_add_u32_e32 v0, 0x3cf8, v113
	ds_write2_b32 v0, v2, v3 offset1:1
	s_waitcnt lgkmcnt(0)
	ds_read2_b32 v[6:7], v112 offset0:65 offset1:73
	ds_read2_b32 v[8:9], v112 offset1:8
	ds_read2_b32 v[10:11], v112 offset0:130 offset1:138
	ds_read2_b32 v[12:13], v112 offset0:195 offset1:203
	v_mov_b32_e32 v111, v97
	v_lshl_add_u64 v[4:5], s[2:3], 0, v[110:111]
	v_lshl_add_u64 v[22:23], v[4:5], 0, v[92:93]
	s_waitcnt lgkmcnt(2)
	v_cvt_pk_bf16_f32 v0, v8, v6
	v_add_u32_e32 v6, 0x400, v112
	ds_read2_b32 v[14:15], v6 offset0:4 offset1:12
	ds_read2_b32 v[16:17], v6 offset0:69 offset1:77
	ds_read2_b32 v[18:19], v6 offset0:134 offset1:142
	ds_read2_b32 v[20:21], v6 offset0:199 offset1:207
	s_waitcnt lgkmcnt(4)
	v_cvt_pk_bf16_f32 v1, v10, v12
	v_lshl_add_u64 v[24:25], v[4:5], 0, v[98:99]
	s_waitcnt lgkmcnt(2)
	v_cvt_pk_bf16_f32 v2, v14, v16
	s_waitcnt lgkmcnt(0)
	v_cvt_pk_bf16_f32 v3, v18, v20
	global_store_dwordx4 v[22:23], v[0:3], off sc1
	s_nop 1
	v_cvt_pk_bf16_f32 v0, v9, v7
	v_cvt_pk_bf16_f32 v1, v11, v13
	v_cvt_pk_bf16_f32 v2, v15, v17
	v_cvt_pk_bf16_f32 v3, v19, v21
	v_lshl_add_u64 v[8:9], v[4:5], 0, v[94:95]
	global_store_dwordx4 v[8:9], v[0:3], off sc1
	ds_read2_b32 v[8:9], v112 offset0:81 offset1:89
	ds_read2_b32 v[10:11], v112 offset0:16 offset1:24
	ds_read2_b32 v[12:13], v112 offset0:146 offset1:154
	ds_read2_b32 v[14:15], v112 offset0:211 offset1:219
	ds_read2_b32 v[16:17], v6 offset0:20 offset1:28
	ds_read2_b32 v[18:19], v6 offset0:85 offset1:93
	ds_read2_b32 v[20:21], v6 offset0:150 offset1:158
	ds_read2_b32 v[22:23], v6 offset0:215 offset1:223
	s_waitcnt lgkmcnt(6)
	v_cvt_pk_bf16_f32 v0, v10, v8
	s_waitcnt lgkmcnt(4)
	v_cvt_pk_bf16_f32 v1, v12, v14
	s_waitcnt lgkmcnt(2)
	v_cvt_pk_bf16_f32 v2, v16, v18
	s_waitcnt lgkmcnt(0)
	v_cvt_pk_bf16_f32 v3, v20, v22
	global_store_dwordx4 v[24:25], v[0:3], off sc1
	v_lshl_add_u64 v[24:25], v[4:5], 0, v[102:103]
	s_nop 0
	v_cvt_pk_bf16_f32 v0, v11, v9
	v_cvt_pk_bf16_f32 v1, v13, v15
	v_cvt_pk_bf16_f32 v2, v17, v19
	v_cvt_pk_bf16_f32 v3, v21, v23
	v_lshl_add_u64 v[8:9], v[4:5], 0, v[100:101]
	global_store_dwordx4 v[8:9], v[0:3], off sc1
	ds_read2_b32 v[8:9], v112 offset0:32 offset1:40
	ds_read2_b32 v[10:11], v112 offset0:97 offset1:105
	ds_read2_b32 v[12:13], v112 offset0:162 offset1:170
	ds_read2_b32 v[14:15], v112 offset0:227 offset1:235
	ds_read2_b32 v[16:17], v6 offset0:36 offset1:44
	ds_read2_b32 v[18:19], v6 offset0:101 offset1:109
	ds_read2_b32 v[20:21], v6 offset0:166 offset1:174
	ds_read2_b32 v[22:23], v6 offset0:231 offset1:239
	s_waitcnt lgkmcnt(6)
	v_cvt_pk_bf16_f32 v0, v8, v10
	s_waitcnt lgkmcnt(4)
	v_cvt_pk_bf16_f32 v1, v12, v14
	s_waitcnt lgkmcnt(2)
	v_cvt_pk_bf16_f32 v2, v16, v18
	s_waitcnt lgkmcnt(0)
	v_cvt_pk_bf16_f32 v3, v20, v22
	global_store_dwordx4 v[24:25], v[0:3], off sc1
	s_nop 1
	v_cvt_pk_bf16_f32 v0, v9, v11
	v_cvt_pk_bf16_f32 v1, v13, v15
	v_cvt_pk_bf16_f32 v2, v17, v19
	v_cvt_pk_bf16_f32 v3, v21, v23
	v_lshl_add_u64 v[8:9], v[4:5], 0, v[104:105]
	global_store_dwordx4 v[8:9], v[0:3], off sc1
	ds_read2_b32 v[8:9], v112 offset0:48 offset1:56
	ds_read2_b32 v[10:11], v112 offset0:113 offset1:121
	ds_read2_b32 v[12:13], v112 offset0:178 offset1:186
	ds_read2_b32 v[14:15], v112 offset0:243 offset1:251
	ds_read2_b32 v[16:17], v6 offset0:52 offset1:60
	ds_read2_b32 v[18:19], v6 offset0:117 offset1:125
	ds_read2_b32 v[20:21], v6 offset0:182 offset1:190
	ds_read2_b32 v[6:7], v6 offset0:247 offset1:255
	v_lshl_add_u64 v[22:23], v[4:5], 0, v[106:107]
	s_waitcnt lgkmcnt(6)
	v_cvt_pk_bf16_f32 v0, v8, v10
	s_waitcnt lgkmcnt(4)
	v_cvt_pk_bf16_f32 v1, v12, v14
	s_waitcnt lgkmcnt(2)
	v_cvt_pk_bf16_f32 v2, v16, v18
	s_waitcnt lgkmcnt(0)
	v_cvt_pk_bf16_f32 v3, v20, v6
	global_store_dwordx4 v[22:23], v[0:3], off sc1
	v_lshl_add_u64 v[4:5], v[4:5], 0, v[108:109]
	s_nop 0
	v_cvt_pk_bf16_f32 v0, v9, v11
	v_cvt_pk_bf16_f32 v1, v13, v15
	v_cvt_pk_bf16_f32 v2, v17, v19
	v_cvt_pk_bf16_f32 v3, v21, v7
	global_store_dwordx4 v[4:5], v[0:3], off sc1
	s_waitcnt lgkmcnt(0)
	s_cbranch_scc1 .LBB0_1536

.LBB0_1541:
	s_ashr_i32 s2, s8, 31
	s_lshr_b32 s2, s2, 23
	s_add_i32 s2, s8, s2
	s_ashr_i32 s4, s2, 9
	s_and_b32 s2, s2, 0xfe00
	s_sub_i32 s2, s8, s2
	s_sext_i32_i16 s3, s2
	s_bfe_u32 s3, s3, 0x4001b
	s_add_i32 s3, s2, s3
	s_sext_i32_i16 s5, s3
	s_and_b32 s3, s3, 0xfff0
	s_sub_i32 s2, s2, s3
	s_sext_i32_i16 s11, s2
	s_lshl_b32 s2, s5, 2
	s_ashr_i32 s5, s4, 31
	s_andn2_b32 s2, s2, 63
	s_lshl_b32 s6, s11, 6
	s_lshl_b64 s[4:5], s[4:5], 23
	s_add_u32 s7, s9, s4
	s_addc_u32 s14, s10, s5
	s_ashr_i32 s3, s2, 31
	s_lshl_b64 s[12:13], s[2:3], 12
	s_add_u32 s15, s7, s12
	s_addc_u32 s14, s14, s13
	s_ashr_i32 s7, s6, 31
	s_lshl_b64 s[12:13], s[6:7], 2
	s_add_u32 s12, s15, s12
	s_addc_u32 s13, s14, s13
	v_lshl_add_u64 v[0:1], s[12:13], 0, v[96:97]
	v_lshl_add_u64 v[2:3], v[0:1], 0, v[60:61]
	flat_load_dwordx4 v[114:117], v[2:3] nt
	v_lshl_add_u64 v[2:3], v[0:1], 0, v[62:63]
	flat_load_dwordx4 v[56:59], v[2:3] nt
	v_lshl_add_u64 v[2:3], v[0:1], 0, v[64:65]
	flat_load_dwordx4 v[52:55], v[2:3] nt
	v_lshl_add_u64 v[2:3], v[0:1], 0, v[66:67]
	flat_load_dwordx4 v[48:51], v[2:3] nt
	v_lshl_add_u64 v[2:3], v[0:1], 0, v[68:69]
	flat_load_dwordx4 v[44:47], v[2:3] nt
	v_lshl_add_u64 v[2:3], v[0:1], 0, v[70:71]
	flat_load_dwordx4 v[40:43], v[2:3] nt
	v_lshl_add_u64 v[2:3], v[0:1], 0, v[72:73]
	flat_load_dwordx4 v[36:39], v[2:3] nt
	v_lshl_add_u64 v[2:3], v[0:1], 0, v[74:75]
	flat_load_dwordx4 v[32:35], v[2:3] nt
	v_lshl_add_u64 v[2:3], v[0:1], 0, v[76:77]
	flat_load_dwordx4 v[28:31], v[2:3] nt
	v_lshl_add_u64 v[2:3], v[0:1], 0, v[78:79]
	flat_load_dwordx4 v[24:27], v[2:3] nt
	v_lshl_add_u64 v[2:3], v[0:1], 0, v[80:81]
	flat_load_dwordx4 v[20:23], v[2:3] nt
	v_lshl_add_u64 v[2:3], v[0:1], 0, v[82:83]
	flat_load_dwordx4 v[16:19], v[2:3] nt
	v_lshl_add_u64 v[2:3], v[0:1], 0, v[84:85]
	flat_load_dwordx4 v[12:15], v[2:3] nt
	v_lshl_add_u64 v[2:3], v[0:1], 0, v[86:87]
	flat_load_dwordx4 v[8:11], v[2:3] nt
	v_lshl_add_u64 v[2:3], v[0:1], 0, v[88:89]
	flat_load_dwordx4 v[4:7], v[2:3] nt
	v_lshl_add_u64 v[0:1], v[0:1], 0, v[90:91]
	flat_load_dwordx4 v[0:3], v[0:1] nt
	v_add_u32_e32 v111, 0x410, v113
	s_lshl_b32 s7, s11, 7
	s_and_b32 s7, s7, 0xffffff00
	s_and_b32 s6, s6, 64
	s_or_b32 s6, s7, s6
	s_ashr_i32 s7, s6, 31
	s_add_u32 s11, s16, s4
	s_addc_u32 s12, s18, s5
	s_lshl_b64 s[4:5], s[6:7], 12
	s_add_u32 s4, s11, s4
	s_addc_u32 s5, s12, s5
	s_lshl_b64 s[2:3], s[2:3], 1
	s_add_u32 s2, s4, s2
	s_addc_u32 s3, s5, s3
	s_add_i32 s8, s8, s19
	s_cmpk_gt_i32 s8, 0x1fff
	s_waitcnt vmcnt(0) lgkmcnt(0)
	ds_write2_b32 v113, v114, v115 offset1:1
	ds_write2_b32 v113, v116, v117 offset0:2 offset1:3
	ds_write2_b32 v111, v56, v57 offset1:1
	v_add_u32_e32 v56, 0x418, v113
	ds_write2_b32 v56, v58, v59 offset1:1
	v_add_u32_e32 v56, 0x820, v113
	ds_write2_b32 v56, v52, v53 offset1:1
	v_add_u32_e32 v52, 0x828, v113
	ds_write2_b32 v52, v54, v55 offset1:1
	v_add_u32_e32 v52, 0xc30, v113
	ds_write2_b32 v52, v48, v49 offset1:1
	v_add_u32_e32 v48, 0xc38, v113
	ds_write2_b32 v48, v50, v51 offset1:1
	v_add_u32_e32 v48, 0x1040, v113
	ds_write2_b32 v48, v44, v45 offset1:1
	v_add_u32_e32 v44, 0x1048, v113
	ds_write2_b32 v44, v46, v47 offset1:1
	v_add_u32_e32 v44, 0x1450, v113
	ds_write2_b32 v44, v40, v41 offset1:1
	v_add_u32_e32 v40, 0x1458, v113
	ds_write2_b32 v40, v42, v43 offset1:1
	v_add_u32_e32 v40, 0x1860, v113
	ds_write2_b32 v40, v36, v37 offset1:1
	v_add_u32_e32 v36, 0x1868, v113
	ds_write2_b32 v36, v38, v39 offset1:1
	v_add_u32_e32 v36, 0x1c70, v113
	ds_write2_b32 v36, v32, v33 offset1:1
	v_add_u32_e32 v32, 0x1c78, v113
	ds_write2_b32 v32, v34, v35 offset1:1
	v_add_u32_e32 v32, 0x2080, v113
	ds_write2_b32 v32, v28, v29 offset1:1
	v_add_u32_e32 v28, 0x2088, v113
	ds_write2_b32 v28, v30, v31 offset1:1
	v_add_u32_e32 v28, 0x2490, v113
	ds_write2_b32 v28, v24, v25 offset1:1
	v_add_u32_e32 v24, 0x2498, v113
	ds_write2_b32 v24, v26, v27 offset1:1
	v_add_u32_e32 v24, 0x28a0, v113
	ds_write2_b32 v24, v20, v21 offset1:1
	v_add_u32_e32 v20, 0x28a8, v113
	ds_write2_b32 v20, v22, v23 offset1:1
	v_add_u32_e32 v20, 0x2cb0, v113
	ds_write2_b32 v20, v16, v17 offset1:1
	v_add_u32_e32 v16, 0x2cb8, v113
	ds_write2_b32 v16, v18, v19 offset1:1
	v_add_u32_e32 v16, 0x30c0, v113
	ds_write2_b32 v16, v12, v13 offset1:1
	v_add_u32_e32 v12, 0x30c8, v113
	ds_write2_b32 v12, v14, v15 offset1:1
	v_add_u32_e32 v12, 0x34d0, v113
	ds_write2_b32 v12, v8, v9 offset1:1
	v_add_u32_e32 v8, 0x34d8, v113
	ds_write2_b32 v8, v10, v11 offset1:1
	v_add_u32_e32 v8, 0x38e0, v113
	ds_write2_b32 v8, v4, v5 offset1:1
	v_add_u32_e32 v4, 0x38e8, v113
	ds_write2_b32 v4, v6, v7 offset1:1
	v_add_u32_e32 v4, 0x3cf0, v113
	ds_write2_b32 v4, v0, v1 offset1:1
	v_add_u32_e32 v0, 0x3cf8, v113
	ds_write2_b32 v0, v2, v3 offset1:1
	s_waitcnt lgkmcnt(0)
	ds_read2_b32 v[6:7], v112 offset0:65 offset1:73
	ds_read2_b32 v[8:9], v112 offset1:8
	ds_read2_b32 v[10:11], v112 offset0:130 offset1:138
	ds_read2_b32 v[12:13], v112 offset0:195 offset1:203
	v_mov_b32_e32 v111, v97
	v_lshl_add_u64 v[4:5], s[2:3], 0, v[110:111]
	v_lshl_add_u64 v[22:23], v[4:5], 0, v[92:93]
	s_waitcnt lgkmcnt(2)
	v_cvt_pk_bf16_f32 v0, v8, v6
	v_add_u32_e32 v6, 0x400, v112
	ds_read2_b32 v[14:15], v6 offset0:4 offset1:12
	ds_read2_b32 v[16:17], v6 offset0:69 offset1:77
	ds_read2_b32 v[18:19], v6 offset0:134 offset1:142
	ds_read2_b32 v[20:21], v6 offset0:199 offset1:207
	s_waitcnt lgkmcnt(4)
	v_cvt_pk_bf16_f32 v1, v10, v12
	v_lshl_add_u64 v[24:25], v[4:5], 0, v[98:99]
	s_waitcnt lgkmcnt(2)
	v_cvt_pk_bf16_f32 v2, v14, v16
	s_waitcnt lgkmcnt(0)
	v_cvt_pk_bf16_f32 v3, v18, v20
	global_store_dwordx4 v[22:23], v[0:3], off sc1
	s_nop 1
	v_cvt_pk_bf16_f32 v0, v9, v7
	v_cvt_pk_bf16_f32 v1, v11, v13
	v_cvt_pk_bf16_f32 v2, v15, v17
	v_cvt_pk_bf16_f32 v3, v19, v21
	v_lshl_add_u64 v[8:9], v[4:5], 0, v[94:95]
	global_store_dwordx4 v[8:9], v[0:3], off sc1
	ds_read2_b32 v[8:9], v112 offset0:81 offset1:89
	ds_read2_b32 v[10:11], v112 offset0:16 offset1:24
	ds_read2_b32 v[12:13], v112 offset0:146 offset1:154
	ds_read2_b32 v[14:15], v112 offset0:211 offset1:219
	ds_read2_b32 v[16:17], v6 offset0:20 offset1:28
	ds_read2_b32 v[18:19], v6 offset0:85 offset1:93
	ds_read2_b32 v[20:21], v6 offset0:150 offset1:158
	ds_read2_b32 v[22:23], v6 offset0:215 offset1:223
	s_waitcnt lgkmcnt(6)
	v_cvt_pk_bf16_f32 v0, v10, v8
	s_waitcnt lgkmcnt(4)
	v_cvt_pk_bf16_f32 v1, v12, v14
	s_waitcnt lgkmcnt(2)
	v_cvt_pk_bf16_f32 v2, v16, v18
	s_waitcnt lgkmcnt(0)
	v_cvt_pk_bf16_f32 v3, v20, v22
	global_store_dwordx4 v[24:25], v[0:3], off sc1
	v_lshl_add_u64 v[24:25], v[4:5], 0, v[102:103]
	s_nop 0
	v_cvt_pk_bf16_f32 v0, v11, v9
	v_cvt_pk_bf16_f32 v1, v13, v15
	v_cvt_pk_bf16_f32 v2, v17, v19
	v_cvt_pk_bf16_f32 v3, v21, v23
	v_lshl_add_u64 v[8:9], v[4:5], 0, v[100:101]
	global_store_dwordx4 v[8:9], v[0:3], off sc1
	ds_read2_b32 v[8:9], v112 offset0:32 offset1:40
	ds_read2_b32 v[10:11], v112 offset0:97 offset1:105
	ds_read2_b32 v[12:13], v112 offset0:162 offset1:170
	ds_read2_b32 v[14:15], v112 offset0:227 offset1:235
	ds_read2_b32 v[16:17], v6 offset0:36 offset1:44
	ds_read2_b32 v[18:19], v6 offset0:101 offset1:109
	ds_read2_b32 v[20:21], v6 offset0:166 offset1:174
	ds_read2_b32 v[22:23], v6 offset0:231 offset1:239
	s_waitcnt lgkmcnt(6)
	v_cvt_pk_bf16_f32 v0, v8, v10
	s_waitcnt lgkmcnt(4)
	v_cvt_pk_bf16_f32 v1, v12, v14
	s_waitcnt lgkmcnt(2)
	v_cvt_pk_bf16_f32 v2, v16, v18
	s_waitcnt lgkmcnt(0)
	v_cvt_pk_bf16_f32 v3, v20, v22
	global_store_dwordx4 v[24:25], v[0:3], off sc1
	s_nop 1
	v_cvt_pk_bf16_f32 v0, v9, v11
	v_cvt_pk_bf16_f32 v1, v13, v15
	v_cvt_pk_bf16_f32 v2, v17, v19
	v_cvt_pk_bf16_f32 v3, v21, v23
	v_lshl_add_u64 v[8:9], v[4:5], 0, v[104:105]
	global_store_dwordx4 v[8:9], v[0:3], off sc1
	ds_read2_b32 v[8:9], v112 offset0:48 offset1:56
	ds_read2_b32 v[10:11], v112 offset0:113 offset1:121
	ds_read2_b32 v[12:13], v112 offset0:178 offset1:186
	ds_read2_b32 v[14:15], v112 offset0:243 offset1:251
	ds_read2_b32 v[16:17], v6 offset0:52 offset1:60
	ds_read2_b32 v[18:19], v6 offset0:117 offset1:125
	ds_read2_b32 v[20:21], v6 offset0:182 offset1:190
	ds_read2_b32 v[6:7], v6 offset0:247 offset1:255
	v_lshl_add_u64 v[22:23], v[4:5], 0, v[106:107]
	s_waitcnt lgkmcnt(6)
	v_cvt_pk_bf16_f32 v0, v8, v10
	s_waitcnt lgkmcnt(4)
	v_cvt_pk_bf16_f32 v1, v12, v14
	s_waitcnt lgkmcnt(2)
	v_cvt_pk_bf16_f32 v2, v16, v18
	s_waitcnt lgkmcnt(0)
	v_cvt_pk_bf16_f32 v3, v20, v6
	global_store_dwordx4 v[22:23], v[0:3], off sc1
	v_lshl_add_u64 v[4:5], v[4:5], 0, v[108:109]
	s_nop 0
	v_cvt_pk_bf16_f32 v0, v9, v11
	v_cvt_pk_bf16_f32 v1, v13, v15
	v_cvt_pk_bf16_f32 v2, v17, v19
	v_cvt_pk_bf16_f32 v3, v21, v7
	global_store_dwordx4 v[4:5], v[0:3], off sc1
	s_waitcnt lgkmcnt(0)
	s_cbranch_scc0 .LBB0_1541

.LBB0_1613:
	s_ashr_i32 s2, s8, 31
	s_lshr_b32 s2, s2, 23
	s_add_i32 s3, s8, s2
	s_ashr_i32 s2, s3, 9
	s_and_b32 s3, s3, 0xfe00
	s_sub_i32 s3, s8, s3
	s_sext_i32_i16 s4, s3
	s_bfe_u32 s4, s4, 0x5001a
	s_add_i32 s4, s3, s4
	s_sext_i32_i16 s5, s4
	s_and_b32 s4, s4, 0xffe0
	s_sub_i32 s3, s3, s4
	s_sext_i32_i16 s3, s3
	s_lshl_b32 s4, s5, 1
	s_lshl_b32 s6, s3, 6
	s_ashr_i32 s3, s2, 31
	s_andn2_b32 s4, s4, 63
	s_lshl_b64 s[12:13], s[2:3], 23
	s_add_u32 s7, s9, s12
	s_addc_u32 s11, s10, s13
	s_ashr_i32 s5, s4, 31
	s_lshl_b64 s[12:13], s[4:5], 13
	s_add_u32 s14, s7, s12
	s_addc_u32 s11, s11, s13
	s_ashr_i32 s7, s6, 31
	s_lshl_b64 s[12:13], s[6:7], 2
	s_add_u32 s12, s14, s12
	s_addc_u32 s13, s11, s13
	v_lshl_add_u64 v[0:1], s[12:13], 0, v[96:97]
	v_lshl_add_u64 v[2:3], v[0:1], 0, v[60:61]
	flat_load_dwordx4 v[114:117], v[2:3] nt
	v_lshl_add_u64 v[2:3], v[0:1], 0, v[62:63]
	flat_load_dwordx4 v[56:59], v[2:3] nt
	v_lshl_add_u64 v[2:3], v[0:1], 0, v[64:65]
	flat_load_dwordx4 v[52:55], v[2:3] nt
	v_lshl_add_u64 v[2:3], v[0:1], 0, v[66:67]
	flat_load_dwordx4 v[48:51], v[2:3] nt
	v_lshl_add_u64 v[2:3], v[0:1], 0, v[68:69]
	flat_load_dwordx4 v[44:47], v[2:3] nt
	v_lshl_add_u64 v[2:3], v[0:1], 0, v[70:71]
	flat_load_dwordx4 v[40:43], v[2:3] nt
	v_lshl_add_u64 v[2:3], v[0:1], 0, v[72:73]
	flat_load_dwordx4 v[36:39], v[2:3] nt
	v_lshl_add_u64 v[2:3], v[0:1], 0, v[74:75]
	flat_load_dwordx4 v[32:35], v[2:3] nt
	v_lshl_add_u64 v[2:3], v[0:1], 0, v[76:77]
	flat_load_dwordx4 v[28:31], v[2:3] nt
	v_lshl_add_u64 v[2:3], v[0:1], 0, v[78:79]
	flat_load_dwordx4 v[24:27], v[2:3] nt
	v_lshl_add_u64 v[2:3], v[0:1], 0, v[80:81]
	flat_load_dwordx4 v[20:23], v[2:3] nt
	v_lshl_add_u64 v[2:3], v[0:1], 0, v[82:83]
	flat_load_dwordx4 v[16:19], v[2:3] nt
	v_lshl_add_u64 v[2:3], v[0:1], 0, v[84:85]
	flat_load_dwordx4 v[12:15], v[2:3] nt
	v_lshl_add_u64 v[2:3], v[0:1], 0, v[86:87]
	flat_load_dwordx4 v[8:11], v[2:3] nt
	v_lshl_add_u64 v[2:3], v[0:1], 0, v[88:89]
	flat_load_dwordx4 v[4:7], v[2:3] nt
	v_lshl_add_u64 v[0:1], v[0:1], 0, v[90:91]
	flat_load_dwordx4 v[0:3], v[0:1] nt
	v_add_u32_e32 v111, 0x410, v113
	s_lshl_b64 s[2:3], s[2:3], 22
	s_add_u32 s11, s15, s2
	s_addc_u32 s12, s16, s3
	s_lshl_b64 s[2:3], s[6:7], 11
	s_add_u32 s6, s11, s2
	s_addc_u32 s7, s12, s3
	s_lshl_b64 s[2:3], s[4:5], 1
	s_add_u32 s2, s6, s2
	s_addc_u32 s3, s7, s3
	s_add_i32 s8, s8, s80
	s_cmpk_lt_i32 s8, 0x2000
	s_waitcnt vmcnt(0) lgkmcnt(0)
	ds_write2_b32 v113, v114, v115 offset1:1
	ds_write2_b32 v113, v116, v117 offset0:2 offset1:3
	ds_write2_b32 v111, v56, v57 offset1:1
	v_add_u32_e32 v56, 0x418, v113
	ds_write2_b32 v56, v58, v59 offset1:1
	v_add_u32_e32 v56, 0x820, v113
	ds_write2_b32 v56, v52, v53 offset1:1
	v_add_u32_e32 v52, 0x828, v113
	ds_write2_b32 v52, v54, v55 offset1:1
	v_add_u32_e32 v52, 0xc30, v113
	ds_write2_b32 v52, v48, v49 offset1:1
	v_add_u32_e32 v48, 0xc38, v113
	ds_write2_b32 v48, v50, v51 offset1:1
	v_add_u32_e32 v48, 0x1040, v113
	ds_write2_b32 v48, v44, v45 offset1:1
	v_add_u32_e32 v44, 0x1048, v113
	ds_write2_b32 v44, v46, v47 offset1:1
	v_add_u32_e32 v44, 0x1450, v113
	ds_write2_b32 v44, v40, v41 offset1:1
	v_add_u32_e32 v40, 0x1458, v113
	ds_write2_b32 v40, v42, v43 offset1:1
	v_add_u32_e32 v40, 0x1860, v113
	ds_write2_b32 v40, v36, v37 offset1:1
	v_add_u32_e32 v36, 0x1868, v113
	ds_write2_b32 v36, v38, v39 offset1:1
	v_add_u32_e32 v36, 0x1c70, v113
	ds_write2_b32 v36, v32, v33 offset1:1
	v_add_u32_e32 v32, 0x1c78, v113
	ds_write2_b32 v32, v34, v35 offset1:1
	v_add_u32_e32 v32, 0x2080, v113
	ds_write2_b32 v32, v28, v29 offset1:1
	v_add_u32_e32 v28, 0x2088, v113
	ds_write2_b32 v28, v30, v31 offset1:1
	v_add_u32_e32 v28, 0x2490, v113
	ds_write2_b32 v28, v24, v25 offset1:1
	v_add_u32_e32 v24, 0x2498, v113
	ds_write2_b32 v24, v26, v27 offset1:1
	v_add_u32_e32 v24, 0x28a0, v113
	ds_write2_b32 v24, v20, v21 offset1:1
	v_add_u32_e32 v20, 0x28a8, v113
	ds_write2_b32 v20, v22, v23 offset1:1
	v_add_u32_e32 v20, 0x2cb0, v113
	ds_write2_b32 v20, v16, v17 offset1:1
	v_add_u32_e32 v16, 0x2cb8, v113
	ds_write2_b32 v16, v18, v19 offset1:1
	v_add_u32_e32 v16, 0x30c0, v113
	ds_write2_b32 v16, v12, v13 offset1:1
	v_add_u32_e32 v12, 0x30c8, v113
	ds_write2_b32 v12, v14, v15 offset1:1
	v_add_u32_e32 v12, 0x34d0, v113
	ds_write2_b32 v12, v8, v9 offset1:1
	v_add_u32_e32 v8, 0x34d8, v113
	ds_write2_b32 v8, v10, v11 offset1:1
	v_add_u32_e32 v8, 0x38e0, v113
	ds_write2_b32 v8, v4, v5 offset1:1
	v_add_u32_e32 v4, 0x38e8, v113
	ds_write2_b32 v4, v6, v7 offset1:1
	v_add_u32_e32 v4, 0x3cf0, v113
	ds_write2_b32 v4, v0, v1 offset1:1
	v_add_u32_e32 v0, 0x3cf8, v113
	ds_write2_b32 v0, v2, v3 offset1:1
	s_waitcnt lgkmcnt(0)
	ds_read2_b32 v[6:7], v112 offset0:65 offset1:73
	ds_read2_b32 v[8:9], v112 offset1:8
	ds_read2_b32 v[10:11], v112 offset0:130 offset1:138
	ds_read2_b32 v[12:13], v112 offset0:195 offset1:203
	v_mov_b32_e32 v111, v97
	v_lshl_add_u64 v[4:5], s[2:3], 0, v[110:111]
	v_lshl_add_u64 v[22:23], v[4:5], 0, v[92:93]
	s_waitcnt lgkmcnt(2)
	v_cvt_pk_bf16_f32 v0, v8, v6
	v_add_u32_e32 v6, 0x400, v112
	ds_read2_b32 v[14:15], v6 offset0:4 offset1:12
	ds_read2_b32 v[16:17], v6 offset0:69 offset1:77
	ds_read2_b32 v[18:19], v6 offset0:134 offset1:142
	ds_read2_b32 v[20:21], v6 offset0:199 offset1:207
	s_waitcnt lgkmcnt(4)
	v_cvt_pk_bf16_f32 v1, v10, v12
	v_lshl_add_u64 v[24:25], v[4:5], 0, v[98:99]
	s_waitcnt lgkmcnt(2)
	v_cvt_pk_bf16_f32 v2, v14, v16
	s_waitcnt lgkmcnt(0)
	v_cvt_pk_bf16_f32 v3, v18, v20
	global_store_dwordx4 v[22:23], v[0:3], off sc1
	s_nop 1
	v_cvt_pk_bf16_f32 v0, v9, v7
	v_cvt_pk_bf16_f32 v1, v11, v13
	v_cvt_pk_bf16_f32 v2, v15, v17
	v_cvt_pk_bf16_f32 v3, v19, v21
	v_lshl_add_u64 v[8:9], v[4:5], 0, v[94:95]
	global_store_dwordx4 v[8:9], v[0:3], off sc1
	ds_read2_b32 v[8:9], v112 offset0:81 offset1:89
	ds_read2_b32 v[10:11], v112 offset0:16 offset1:24
	ds_read2_b32 v[12:13], v112 offset0:146 offset1:154
	ds_read2_b32 v[14:15], v112 offset0:211 offset1:219
	ds_read2_b32 v[16:17], v6 offset0:20 offset1:28
	ds_read2_b32 v[18:19], v6 offset0:85 offset1:93
	ds_read2_b32 v[20:21], v6 offset0:150 offset1:158
	ds_read2_b32 v[22:23], v6 offset0:215 offset1:223
	s_waitcnt lgkmcnt(6)
	v_cvt_pk_bf16_f32 v0, v10, v8
	s_waitcnt lgkmcnt(4)
	v_cvt_pk_bf16_f32 v1, v12, v14
	s_waitcnt lgkmcnt(2)
	v_cvt_pk_bf16_f32 v2, v16, v18
	s_waitcnt lgkmcnt(0)
	v_cvt_pk_bf16_f32 v3, v20, v22
	global_store_dwordx4 v[24:25], v[0:3], off sc1
	v_lshl_add_u64 v[24:25], v[4:5], 0, v[102:103]
	s_nop 0
	v_cvt_pk_bf16_f32 v0, v11, v9
	v_cvt_pk_bf16_f32 v1, v13, v15
	v_cvt_pk_bf16_f32 v2, v17, v19
	v_cvt_pk_bf16_f32 v3, v21, v23
	v_lshl_add_u64 v[8:9], v[4:5], 0, v[100:101]
	global_store_dwordx4 v[8:9], v[0:3], off sc1
	ds_read2_b32 v[8:9], v112 offset0:32 offset1:40
	ds_read2_b32 v[10:11], v112 offset0:97 offset1:105
	ds_read2_b32 v[12:13], v112 offset0:162 offset1:170
	ds_read2_b32 v[14:15], v112 offset0:227 offset1:235
	ds_read2_b32 v[16:17], v6 offset0:36 offset1:44
	ds_read2_b32 v[18:19], v6 offset0:101 offset1:109
	ds_read2_b32 v[20:21], v6 offset0:166 offset1:174
	ds_read2_b32 v[22:23], v6 offset0:231 offset1:239
	s_waitcnt lgkmcnt(6)
	v_cvt_pk_bf16_f32 v0, v8, v10
	s_waitcnt lgkmcnt(4)
	v_cvt_pk_bf16_f32 v1, v12, v14
	s_waitcnt lgkmcnt(2)
	v_cvt_pk_bf16_f32 v2, v16, v18
	s_waitcnt lgkmcnt(0)
	v_cvt_pk_bf16_f32 v3, v20, v22
	global_store_dwordx4 v[24:25], v[0:3], off sc1
	s_nop 1
	v_cvt_pk_bf16_f32 v0, v9, v11
	v_cvt_pk_bf16_f32 v1, v13, v15
	v_cvt_pk_bf16_f32 v2, v17, v19
	v_cvt_pk_bf16_f32 v3, v21, v23
	v_lshl_add_u64 v[8:9], v[4:5], 0, v[104:105]
	global_store_dwordx4 v[8:9], v[0:3], off sc1
	ds_read2_b32 v[8:9], v112 offset0:48 offset1:56
	ds_read2_b32 v[10:11], v112 offset0:113 offset1:121
	ds_read2_b32 v[12:13], v112 offset0:178 offset1:186
	ds_read2_b32 v[14:15], v112 offset0:243 offset1:251
	ds_read2_b32 v[16:17], v6 offset0:52 offset1:60
	ds_read2_b32 v[18:19], v6 offset0:117 offset1:125
	ds_read2_b32 v[20:21], v6 offset0:182 offset1:190
	ds_read2_b32 v[6:7], v6 offset0:247 offset1:255
	v_lshl_add_u64 v[22:23], v[4:5], 0, v[106:107]
	s_waitcnt lgkmcnt(6)
	v_cvt_pk_bf16_f32 v0, v8, v10
	s_waitcnt lgkmcnt(4)
	v_cvt_pk_bf16_f32 v1, v12, v14
	s_waitcnt lgkmcnt(2)
	v_cvt_pk_bf16_f32 v2, v16, v18
	s_waitcnt lgkmcnt(0)
	v_cvt_pk_bf16_f32 v3, v20, v6
	global_store_dwordx4 v[22:23], v[0:3], off sc1
	v_lshl_add_u64 v[4:5], v[4:5], 0, v[108:109]
	s_nop 0
	v_cvt_pk_bf16_f32 v0, v9, v11
	v_cvt_pk_bf16_f32 v1, v13, v15
	v_cvt_pk_bf16_f32 v2, v17, v19
	v_cvt_pk_bf16_f32 v3, v21, v7
	global_store_dwordx4 v[4:5], v[0:3], off sc1
	s_waitcnt lgkmcnt(0)
	s_cbranch_scc1 .LBB0_1613

.LBB0_1618:
	s_ashr_i32 s2, s8, 31
	s_lshr_b32 s2, s2, 23
	s_add_i32 s3, s8, s2
	s_ashr_i32 s2, s3, 9
	s_and_b32 s3, s3, 0xfe00
	s_sub_i32 s3, s8, s3
	s_sext_i32_i16 s4, s3
	s_bfe_u32 s4, s4, 0x5001a
	s_add_i32 s4, s3, s4
	s_sext_i32_i16 s5, s4
	s_and_b32 s4, s4, 0xffe0
	s_sub_i32 s3, s3, s4
	s_sext_i32_i16 s3, s3
	s_lshl_b32 s4, s5, 1
	s_lshl_b32 s6, s3, 6
	s_ashr_i32 s3, s2, 31
	s_andn2_b32 s4, s4, 63
	s_lshl_b64 s[12:13], s[2:3], 23
	s_add_u32 s7, s9, s12
	s_addc_u32 s11, s10, s13
	s_ashr_i32 s5, s4, 31
	s_lshl_b64 s[12:13], s[4:5], 13
	s_add_u32 s14, s7, s12
	s_addc_u32 s11, s11, s13
	s_ashr_i32 s7, s6, 31
	s_lshl_b64 s[12:13], s[6:7], 2
	s_add_u32 s12, s14, s12
	s_addc_u32 s13, s11, s13
	v_lshl_add_u64 v[0:1], s[12:13], 0, v[96:97]
	v_lshl_add_u64 v[2:3], v[0:1], 0, v[60:61]
	flat_load_dwordx4 v[114:117], v[2:3] nt
	v_lshl_add_u64 v[2:3], v[0:1], 0, v[62:63]
	flat_load_dwordx4 v[56:59], v[2:3] nt
	v_lshl_add_u64 v[2:3], v[0:1], 0, v[64:65]
	flat_load_dwordx4 v[52:55], v[2:3] nt
	v_lshl_add_u64 v[2:3], v[0:1], 0, v[66:67]
	flat_load_dwordx4 v[48:51], v[2:3] nt
	v_lshl_add_u64 v[2:3], v[0:1], 0, v[68:69]
	flat_load_dwordx4 v[44:47], v[2:3] nt
	v_lshl_add_u64 v[2:3], v[0:1], 0, v[70:71]
	flat_load_dwordx4 v[40:43], v[2:3] nt
	v_lshl_add_u64 v[2:3], v[0:1], 0, v[72:73]
	flat_load_dwordx4 v[36:39], v[2:3] nt
	v_lshl_add_u64 v[2:3], v[0:1], 0, v[74:75]
	flat_load_dwordx4 v[32:35], v[2:3] nt
	v_lshl_add_u64 v[2:3], v[0:1], 0, v[76:77]
	flat_load_dwordx4 v[28:31], v[2:3] nt
	v_lshl_add_u64 v[2:3], v[0:1], 0, v[78:79]
	flat_load_dwordx4 v[24:27], v[2:3] nt
	v_lshl_add_u64 v[2:3], v[0:1], 0, v[80:81]
	flat_load_dwordx4 v[20:23], v[2:3] nt
	v_lshl_add_u64 v[2:3], v[0:1], 0, v[82:83]
	flat_load_dwordx4 v[16:19], v[2:3] nt
	v_lshl_add_u64 v[2:3], v[0:1], 0, v[84:85]
	flat_load_dwordx4 v[12:15], v[2:3] nt
	v_lshl_add_u64 v[2:3], v[0:1], 0, v[86:87]
	flat_load_dwordx4 v[8:11], v[2:3] nt
	v_lshl_add_u64 v[2:3], v[0:1], 0, v[88:89]
	flat_load_dwordx4 v[4:7], v[2:3] nt
	v_lshl_add_u64 v[0:1], v[0:1], 0, v[90:91]
	flat_load_dwordx4 v[0:3], v[0:1] nt
	v_add_u32_e32 v111, 0x410, v113
	s_lshl_b64 s[2:3], s[2:3], 22
	s_add_u32 s11, s15, s2
	s_addc_u32 s12, s16, s3
	s_lshl_b64 s[2:3], s[6:7], 11
	s_add_u32 s6, s11, s2
	s_addc_u32 s7, s12, s3
	s_lshl_b64 s[2:3], s[4:5], 1
	s_add_u32 s2, s6, s2
	s_addc_u32 s3, s7, s3
	s_add_i32 s8, s8, s18
	s_cmpk_gt_i32 s8, 0x1fff
	s_waitcnt vmcnt(0) lgkmcnt(0)
	ds_write2_b32 v113, v114, v115 offset1:1
	ds_write2_b32 v113, v116, v117 offset0:2 offset1:3
	ds_write2_b32 v111, v56, v57 offset1:1
	v_add_u32_e32 v56, 0x418, v113
	ds_write2_b32 v56, v58, v59 offset1:1
	v_add_u32_e32 v56, 0x820, v113
	ds_write2_b32 v56, v52, v53 offset1:1
	v_add_u32_e32 v52, 0x828, v113
	ds_write2_b32 v52, v54, v55 offset1:1
	v_add_u32_e32 v52, 0xc30, v113
	ds_write2_b32 v52, v48, v49 offset1:1
	v_add_u32_e32 v48, 0xc38, v113
	ds_write2_b32 v48, v50, v51 offset1:1
	v_add_u32_e32 v48, 0x1040, v113
	ds_write2_b32 v48, v44, v45 offset1:1
	v_add_u32_e32 v44, 0x1048, v113
	ds_write2_b32 v44, v46, v47 offset1:1
	v_add_u32_e32 v44, 0x1450, v113
	ds_write2_b32 v44, v40, v41 offset1:1
	v_add_u32_e32 v40, 0x1458, v113
	ds_write2_b32 v40, v42, v43 offset1:1
	v_add_u32_e32 v40, 0x1860, v113
	ds_write2_b32 v40, v36, v37 offset1:1
	v_add_u32_e32 v36, 0x1868, v113
	ds_write2_b32 v36, v38, v39 offset1:1
	v_add_u32_e32 v36, 0x1c70, v113
	ds_write2_b32 v36, v32, v33 offset1:1
	v_add_u32_e32 v32, 0x1c78, v113
	ds_write2_b32 v32, v34, v35 offset1:1
	v_add_u32_e32 v32, 0x2080, v113
	ds_write2_b32 v32, v28, v29 offset1:1
	v_add_u32_e32 v28, 0x2088, v113
	ds_write2_b32 v28, v30, v31 offset1:1
	v_add_u32_e32 v28, 0x2490, v113
	ds_write2_b32 v28, v24, v25 offset1:1
	v_add_u32_e32 v24, 0x2498, v113
	ds_write2_b32 v24, v26, v27 offset1:1
	v_add_u32_e32 v24, 0x28a0, v113
	ds_write2_b32 v24, v20, v21 offset1:1
	v_add_u32_e32 v20, 0x28a8, v113
	ds_write2_b32 v20, v22, v23 offset1:1
	v_add_u32_e32 v20, 0x2cb0, v113
	ds_write2_b32 v20, v16, v17 offset1:1
	v_add_u32_e32 v16, 0x2cb8, v113
	ds_write2_b32 v16, v18, v19 offset1:1
	v_add_u32_e32 v16, 0x30c0, v113
	ds_write2_b32 v16, v12, v13 offset1:1
	v_add_u32_e32 v12, 0x30c8, v113
	ds_write2_b32 v12, v14, v15 offset1:1
	v_add_u32_e32 v12, 0x34d0, v113
	ds_write2_b32 v12, v8, v9 offset1:1
	v_add_u32_e32 v8, 0x34d8, v113
	ds_write2_b32 v8, v10, v11 offset1:1
	v_add_u32_e32 v8, 0x38e0, v113
	ds_write2_b32 v8, v4, v5 offset1:1
	v_add_u32_e32 v4, 0x38e8, v113
	ds_write2_b32 v4, v6, v7 offset1:1
	v_add_u32_e32 v4, 0x3cf0, v113
	ds_write2_b32 v4, v0, v1 offset1:1
	v_add_u32_e32 v0, 0x3cf8, v113
	ds_write2_b32 v0, v2, v3 offset1:1
	s_waitcnt lgkmcnt(0)
	ds_read2_b32 v[6:7], v112 offset0:65 offset1:73
	ds_read2_b32 v[8:9], v112 offset1:8
	ds_read2_b32 v[10:11], v112 offset0:130 offset1:138
	ds_read2_b32 v[12:13], v112 offset0:195 offset1:203
	v_mov_b32_e32 v111, v97
	v_lshl_add_u64 v[4:5], s[2:3], 0, v[110:111]
	v_lshl_add_u64 v[22:23], v[4:5], 0, v[92:93]
	s_waitcnt lgkmcnt(2)
	v_cvt_pk_bf16_f32 v0, v8, v6
	v_add_u32_e32 v6, 0x400, v112
	ds_read2_b32 v[14:15], v6 offset0:4 offset1:12
	ds_read2_b32 v[16:17], v6 offset0:69 offset1:77
	ds_read2_b32 v[18:19], v6 offset0:134 offset1:142
	ds_read2_b32 v[20:21], v6 offset0:199 offset1:207
	s_waitcnt lgkmcnt(4)
	v_cvt_pk_bf16_f32 v1, v10, v12
	v_lshl_add_u64 v[24:25], v[4:5], 0, v[98:99]
	s_waitcnt lgkmcnt(2)
	v_cvt_pk_bf16_f32 v2, v14, v16
	s_waitcnt lgkmcnt(0)
	v_cvt_pk_bf16_f32 v3, v18, v20
	global_store_dwordx4 v[22:23], v[0:3], off sc1
	s_nop 1
	v_cvt_pk_bf16_f32 v0, v9, v7
	v_cvt_pk_bf16_f32 v1, v11, v13
	v_cvt_pk_bf16_f32 v2, v15, v17
	v_cvt_pk_bf16_f32 v3, v19, v21
	v_lshl_add_u64 v[8:9], v[4:5], 0, v[94:95]
	global_store_dwordx4 v[8:9], v[0:3], off sc1
	ds_read2_b32 v[8:9], v112 offset0:81 offset1:89
	ds_read2_b32 v[10:11], v112 offset0:16 offset1:24
	ds_read2_b32 v[12:13], v112 offset0:146 offset1:154
	ds_read2_b32 v[14:15], v112 offset0:211 offset1:219
	ds_read2_b32 v[16:17], v6 offset0:20 offset1:28
	ds_read2_b32 v[18:19], v6 offset0:85 offset1:93
	ds_read2_b32 v[20:21], v6 offset0:150 offset1:158
	ds_read2_b32 v[22:23], v6 offset0:215 offset1:223
	s_waitcnt lgkmcnt(6)
	v_cvt_pk_bf16_f32 v0, v10, v8
	s_waitcnt lgkmcnt(4)
	v_cvt_pk_bf16_f32 v1, v12, v14
	s_waitcnt lgkmcnt(2)
	v_cvt_pk_bf16_f32 v2, v16, v18
	s_waitcnt lgkmcnt(0)
	v_cvt_pk_bf16_f32 v3, v20, v22
	global_store_dwordx4 v[24:25], v[0:3], off sc1
	v_lshl_add_u64 v[24:25], v[4:5], 0, v[102:103]
	s_nop 0
	v_cvt_pk_bf16_f32 v0, v11, v9
	v_cvt_pk_bf16_f32 v1, v13, v15
	v_cvt_pk_bf16_f32 v2, v17, v19
	v_cvt_pk_bf16_f32 v3, v21, v23
	v_lshl_add_u64 v[8:9], v[4:5], 0, v[100:101]
	global_store_dwordx4 v[8:9], v[0:3], off sc1
	ds_read2_b32 v[8:9], v112 offset0:32 offset1:40
	ds_read2_b32 v[10:11], v112 offset0:97 offset1:105
	ds_read2_b32 v[12:13], v112 offset0:162 offset1:170
	ds_read2_b32 v[14:15], v112 offset0:227 offset1:235
	ds_read2_b32 v[16:17], v6 offset0:36 offset1:44
	ds_read2_b32 v[18:19], v6 offset0:101 offset1:109
	ds_read2_b32 v[20:21], v6 offset0:166 offset1:174
	ds_read2_b32 v[22:23], v6 offset0:231 offset1:239
	s_waitcnt lgkmcnt(6)
	v_cvt_pk_bf16_f32 v0, v8, v10
	s_waitcnt lgkmcnt(4)
	v_cvt_pk_bf16_f32 v1, v12, v14
	s_waitcnt lgkmcnt(2)
	v_cvt_pk_bf16_f32 v2, v16, v18
	s_waitcnt lgkmcnt(0)
	v_cvt_pk_bf16_f32 v3, v20, v22
	global_store_dwordx4 v[24:25], v[0:3], off sc1
	s_nop 1
	v_cvt_pk_bf16_f32 v0, v9, v11
	v_cvt_pk_bf16_f32 v1, v13, v15
	v_cvt_pk_bf16_f32 v2, v17, v19
	v_cvt_pk_bf16_f32 v3, v21, v23
	v_lshl_add_u64 v[8:9], v[4:5], 0, v[104:105]
	global_store_dwordx4 v[8:9], v[0:3], off sc1
	ds_read2_b32 v[8:9], v112 offset0:48 offset1:56
	ds_read2_b32 v[10:11], v112 offset0:113 offset1:121
	ds_read2_b32 v[12:13], v112 offset0:178 offset1:186
	ds_read2_b32 v[14:15], v112 offset0:243 offset1:251
	ds_read2_b32 v[16:17], v6 offset0:52 offset1:60
	ds_read2_b32 v[18:19], v6 offset0:117 offset1:125
	ds_read2_b32 v[20:21], v6 offset0:182 offset1:190
	ds_read2_b32 v[6:7], v6 offset0:247 offset1:255
	v_lshl_add_u64 v[22:23], v[4:5], 0, v[106:107]
	s_waitcnt lgkmcnt(6)
	v_cvt_pk_bf16_f32 v0, v8, v10
	s_waitcnt lgkmcnt(4)
	v_cvt_pk_bf16_f32 v1, v12, v14
	s_waitcnt lgkmcnt(2)
	v_cvt_pk_bf16_f32 v2, v16, v18
	s_waitcnt lgkmcnt(0)
	v_cvt_pk_bf16_f32 v3, v20, v6
	global_store_dwordx4 v[22:23], v[0:3], off sc1
	v_lshl_add_u64 v[4:5], v[4:5], 0, v[108:109]
	s_nop 0
	v_cvt_pk_bf16_f32 v0, v9, v11
	v_cvt_pk_bf16_f32 v1, v13, v15
	v_cvt_pk_bf16_f32 v2, v17, v19
	v_cvt_pk_bf16_f32 v3, v21, v7
	global_store_dwordx4 v[4:5], v[0:3], off sc1
	s_waitcnt lgkmcnt(0)
	s_cbranch_scc0 .LBB0_1618

.LBB0_1705:
	v_mov_b32_e32 v132, v119
	v_mov_b32_e32 v133, v111
	v_mov_b32_e32 v130, v118
	v_mov_b32_e32 v131, v110
	v_pk_mul_f32 v[132:133], v[132:133], v[132:133]
	v_mov_b32_e32 v134, v121
	v_mov_b32_e32 v135, v113
	v_pk_fma_f32 v[130:131], v[130:131], v[130:131], v[132:133]
	v_mov_b32_e32 v132, v120
	v_mov_b32_e32 v133, v112
	v_pk_mul_f32 v[134:135], v[134:135], v[134:135]
	v_mul_f32_e32 v96, v80, v80
	v_pk_fma_f32 v[132:133], v[132:133], v[132:133], v[134:135]
	v_pk_mul_f32 v[134:135], v[88:89], v[88:89]
	v_pk_add_f32 v[130:131], v[130:131], v[132:133]
	v_pk_mul_f32 v[132:133], v[90:91], v[90:91]
	v_mul_f32_e32 v129, v81, v81
	v_pk_mov_b32 v[136:137], v[134:135], v[132:133] op_sel:[1,0]
	v_mov_b32_e32 v135, v133
	v_pk_add_f32 v[132:133], v[136:137], v[134:135]
	v_pk_add_f32 v[130:131], v[130:131], v[130:131] op_sel:[0,1] op_sel_hi:[1,0]
	v_pk_add_f32 v[132:133], v[132:133], v[132:133] op_sel:[0,1] op_sel_hi:[1,0]
	v_mov_b32_e32 v131, v96
	v_mov_b32_e32 v133, v129
	v_mul_f32_e32 v96, v77, v77
	v_mul_f32_e32 v134, v82, v82
	v_pk_add_f32 v[130:131], v[130:131], v[132:133]
	v_pk_fma_f32 v[132:133], v[76:77], v[76:77], v[96:97] op_sel_hi:[1,1,0]
	v_mul_f32_e32 v96, v79, v79
	v_mul_f32_e32 v136, v83, v83
	v_mov_b32_e32 v133, v134
	v_pk_fma_f32 v[134:135], v[78:79], v[78:79], v[96:97] op_sel_hi:[1,1,0]
	v_mul_f32_e32 v96, v66, v66
	v_mov_b32_e32 v135, v136
	v_pk_add_f32 v[132:133], v[132:133], v[134:135]
	v_pk_mul_f32 v[134:135], v[68:69], v[68:69]
	v_pk_add_f32 v[130:131], v[130:131], v[132:133]
	v_pk_mul_f32 v[132:133], v[70:71], v[70:71]
	v_mul_f32_e32 v129, v67, v67
	v_pk_mov_b32 v[136:137], v[134:135], v[132:133] op_sel:[1,0]
	v_mov_b32_e32 v135, v133
	v_pk_add_f32 v[132:133], v[136:137], v[134:135]
	v_pk_add_f32 v[130:131], v[130:131], v[130:131] op_sel:[0,1] op_sel_hi:[1,0]
	v_pk_add_f32 v[132:133], v[132:133], v[132:133] op_sel:[0,1] op_sel_hi:[1,0]
	v_mov_b32_e32 v131, v96
	v_mov_b32_e32 v133, v129
	v_mul_f32_e32 v96, v73, v73
	v_mul_f32_e32 v134, v64, v64
	v_pk_add_f32 v[130:131], v[130:131], v[132:133]
	v_pk_fma_f32 v[132:133], v[72:73], v[72:73], v[96:97] op_sel_hi:[1,1,0]
	v_mul_f32_e32 v96, v75, v75
	v_mul_f32_e32 v136, v65, v65
	v_mov_b32_e32 v133, v134
	v_pk_fma_f32 v[134:135], v[74:75], v[74:75], v[96:97] op_sel_hi:[1,1,0]
	s_waitcnt vmcnt(3)
	v_and_b32_e32 v137, 0xffff0000, v95
	v_mov_b32_e32 v135, v136
	v_pk_add_f32 v[132:133], v[132:133], v[134:135]
	v_lshlrev_b32_e32 v134, 16, v94
	v_pk_add_f32 v[130:131], v[130:131], v[132:133]
	v_lshlrev_b32_e32 v136, 16, v95
	v_add_f32_e32 v96, v130, v131
	ds_bpermute_b32 v131, v195, v96
	s_waitcnt vmcnt(2)
	v_lshlrev_b32_e32 v138, 16, v92
	v_lshlrev_b32_e32 v140, 16, v93
	v_and_b32_e32 v141, 0xffff0000, v93
	s_waitcnt vmcnt(1)
	v_lshlrev_b32_e32 v142, 16, v86
	s_waitcnt lgkmcnt(0)
	v_add_f32_e32 v96, v96, v131
	ds_bpermute_b32 v133, v218, v96
	v_and_b32_e32 v143, 0xffff0000, v86
	v_lshlrev_b32_e32 v144, 16, v87
	v_and_b32_e32 v145, 0xffff0000, v87
	s_waitcnt vmcnt(0)
	v_lshlrev_b32_e32 v146, 16, v84
	s_waitcnt lgkmcnt(0)
	v_add_f32_e32 v96, v96, v133
	ds_bpermute_b32 v135, v219, v96
	v_and_b32_e32 v147, 0xffff0000, v84
	v_lshlrev_b32_e32 v148, 16, v85
	v_and_b32_e32 v149, 0xffff0000, v85
	v_lshlrev_b32_e32 v126, 16, v124
	s_waitcnt lgkmcnt(0)
	v_add_f32_e32 v96, v96, v135
	ds_bpermute_b32 v139, v220, v96
	v_and_b32_e32 v135, 0xffff0000, v94
	v_and_b32_e32 v127, 0xffff0000, v124
	v_lshlrev_b32_e32 v124, 16, v125
	v_and_b32_e32 v125, 0xffff0000, v125
	s_waitcnt lgkmcnt(0)
	v_add_f32_e32 v94, v96, v139
	ds_bpermute_b32 v95, v221, v94
	v_and_b32_e32 v139, 0xffff0000, v92
	v_lshlrev_b32_e32 v128, 16, v122
	v_and_b32_e32 v129, 0xffff0000, v122
	v_lshlrev_b32_e32 v122, 16, v123
	s_waitcnt lgkmcnt(0)
	v_add_f32_e32 v92, v94, v95
	ds_bpermute_b32 v93, v222, v92
	v_and_b32_e32 v123, 0xffff0000, v123
	v_lshlrev_b32_e32 v130, 16, v116
	v_and_b32_e32 v131, 0xffff0000, v116
	v_lshlrev_b32_e32 v116, 16, v117
	s_waitcnt lgkmcnt(0)
	v_add_f32_e32 v86, v92, v93
	v_fmamk_f32 v86, v86, 0x3a000000, v196
	v_mul_f32_e32 v87, 0x4b800000, v86
	v_cmp_gt_f32_e32 vcc, s35, v86
	v_and_b32_e32 v117, 0xffff0000, v117
	v_lshlrev_b32_e32 v132, 16, v114
	v_cndmask_b32_e32 v86, v86, v87, vcc
	v_rsq_f32_e32 v86, v86
	v_and_b32_e32 v133, 0xffff0000, v114
	v_lshlrev_b32_e32 v114, 16, v115
	v_and_b32_e32 v115, 0xffff0000, v115
	v_mul_f32_e32 v84, 0x45800000, v86
	v_cndmask_b32_e32 v96, v86, v84, vcc
	v_pk_mul_f32 v[84:85], v[120:121], v[96:97] op_sel_hi:[1,0]
	v_pk_mul_f32 v[86:87], v[118:119], v[96:97] op_sel_hi:[1,0]
	v_pk_mul_f32 v[84:85], v[6:7], v[84:85]
	v_pk_mul_f32 v[86:87], v[4:5], v[86:87]
	v_pk_fma_f32 v[94:95], v[2:3], v[84:85], v[124:125]
	v_pk_fma_f32 v[92:93], v[0:1], v[86:87], v[126:127]
	v_pk_mul_f32 v[84:85], v[112:113], v[96:97] op_sel_hi:[1,0]
	v_pk_mul_f32 v[86:87], v[110:111], v[96:97] op_sel_hi:[1,0]
	v_pk_mul_f32 v[84:85], v[14:15], v[84:85]
	v_pk_mul_f32 v[110:111], v[12:13], v[86:87]
	v_pk_mul_f32 v[90:91], v[90:91], v[96:97] op_sel_hi:[1,0]
	v_pk_mul_f32 v[88:89], v[88:89], v[96:97] op_sel_hi:[1,0]
	v_pk_mul_f32 v[78:79], v[78:79], v[96:97] op_sel_hi:[1,0]
	v_pk_mul_f32 v[76:77], v[76:77], v[96:97] op_sel_hi:[1,0]
	v_pk_mul_f32 v[82:83], v[82:83], v[96:97] op_sel_hi:[1,0]
	v_pk_mul_f32 v[80:81], v[80:81], v[96:97] op_sel_hi:[1,0]
	v_pk_mul_f32 v[70:71], v[70:71], v[96:97] op_sel_hi:[1,0]
	v_pk_mul_f32 v[68:69], v[68:69], v[96:97] op_sel_hi:[1,0]
	v_pk_mul_f32 v[74:75], v[74:75], v[96:97] op_sel_hi:[1,0]
	v_pk_mul_f32 v[72:73], v[72:73], v[96:97] op_sel_hi:[1,0]
	v_pk_mul_f32 v[64:65], v[64:65], v[96:97] op_sel_hi:[1,0]
	v_pk_mul_f32 v[66:67], v[66:67], v[96:97] op_sel_hi:[1,0]
	v_pk_fma_f32 v[86:87], v[10:11], v[84:85], v[122:123]
	v_pk_fma_f32 v[84:85], v[8:9], v[110:111], v[128:129]
	v_pk_mul_f32 v[88:89], v[20:21], v[88:89]
	v_pk_mul_f32 v[90:91], v[22:23], v[90:91]
	v_pk_mul_f32 v[76:77], v[28:29], v[76:77]
	v_pk_mul_f32 v[78:79], v[30:31], v[78:79]
	v_pk_mul_f32 v[80:81], v[36:37], v[80:81]
	v_pk_mul_f32 v[82:83], v[38:39], v[82:83]
	v_pk_mul_f32 v[68:69], v[44:45], v[68:69]
	v_pk_mul_f32 v[70:71], v[46:47], v[70:71]
	v_pk_mul_f32 v[72:73], v[52:53], v[72:73]
	v_pk_mul_f32 v[74:75], v[54:55], v[74:75]
	v_pk_mul_f32 v[110:111], v[66:67], v[60:61]
	v_pk_mul_f32 v[64:65], v[64:65], v[62:63]
	s_lshl_b64 s[10:11], s[8:9], 11
	v_pk_fma_f32 v[90:91], v[18:19], v[90:91], v[116:117]
	v_pk_fma_f32 v[88:89], v[16:17], v[88:89], v[130:131]
	v_pk_fma_f32 v[78:79], v[26:27], v[78:79], v[114:115]
	v_pk_fma_f32 v[76:77], v[24:25], v[76:77], v[132:133]
	v_pk_fma_f32 v[82:83], v[34:35], v[82:83], v[136:137]
	v_pk_fma_f32 v[80:81], v[32:33], v[80:81], v[134:135]
	v_pk_fma_f32 v[70:71], v[42:43], v[70:71], v[140:141]
	v_pk_fma_f32 v[68:69], v[40:41], v[68:69], v[138:139]
	v_pk_fma_f32 v[74:75], v[50:51], v[74:75], v[144:145]
	v_pk_fma_f32 v[72:73], v[48:49], v[72:73], v[142:143]
	v_pk_fma_f32 v[66:67], v[58:59], v[64:65], v[148:149]
	v_pk_fma_f32 v[64:65], v[56:57], v[110:111], v[146:147]
	s_and_b64 vcc, exec, s[42:43]
	s_mov_b64 s[12:13], -1
	s_cbranch_vccnz .LBB0_1707
	s_mul_hi_i32 s9, s8, 0x78787879
	s_lshr_b32 s12, s9, 31
	s_ashr_i32 s9, s9, 11
	s_add_i32 s12, s9, s12
	s_mul_i32 s9, s12, 0x1100
	s_sub_i32 s8, s8, s9
	s_ashr_i32 s13, s12, 31
	s_ashr_i32 s9, s8, 31
	s_lshl_b64 s[8:9], s[8:9], 13
	s_lshl_b64 s[12:13], s[12:13], 25
	s_add_u32 s12, s76, s12
	s_addc_u32 s13, s77, s13
	s_add_u32 s8, s12, s8
	s_addc_u32 s9, s13, s9
	s_add_u32 s8, s8, 0xffe00000
	s_addc_u32 s9, s9, -1
	s_mov_b64 s[12:13], 0
	global_store_dwordx4 v190, v[92:95], s[8:9] sc1
	global_store_dwordx4 v190, v[84:87], s[8:9] offset:1024 sc1
	global_store_dwordx4 v190, v[88:91], s[8:9] offset:2048 sc1
	global_store_dwordx4 v190, v[76:79], s[8:9] offset:3072 sc1
	global_store_dwordx4 v191, v[80:83], s[8:9] sc1
	global_store_dwordx4 v192, v[68:71], s[8:9] sc1
	global_store_dwordx4 v193, v[72:75], s[8:9] sc1
	global_store_dwordx4 v194, v[64:67], s[8:9] sc1
